# 8-phase GEMM loops: waves 0-3 (instead of 4-7) run one barrier behind; plus static prio in attention
# baseline (speedup 1.0000x reference)
.LBB0_232:
	v_ashrrev_i32_e32 v1, 31, v8
	v_lshrrev_b32_e32 v1, 26, v1
	v_add_u32_e32 v1, v8, v1
	v_ashrrev_i32_e32 v9, 6, v1
	v_bfe_i32 v1, v8, 27, 1
	v_lshlrev_b32_e32 v0, 4, v8
	v_lshrrev_b32_e32 v1, 22, v1
	v_add_u32_e32 v1, v0, v1
	v_and_b32_e32 v1, 0xfffffc00, v1
	v_sub_u32_e32 v1, v0, v1
	v_lshrrev_b32_e32 v2, 4, v1
	v_bitop3_b32 v1, v2, v1, 32 bitop3:0x6c
	v_ashrrev_i32_e32 v3, 31, v1
	v_lshrrev_b32_e32 v3, 26, v3
	v_add_u32_e32 v3, v1, v3
	v_lshlrev_b32_e32 v2, 3, v9
	v_ashrrev_i32_e32 v10, 6, v3
	v_and_b32_e32 v3, 0xc0, v3
	v_and_b32_e32 v2, -16, v2
	v_sub_u32_e32 v1, v1, v3
	v_mov_b32_e32 v3, 1
	v_add_u32_e32 v2, v10, v2
	v_ashrrev_i16_sdwa v1, v3, sext(v1) dst_sel:DWORD dst_unused:UNUSED_PAD src0_sel:DWORD src1_sel:BYTE_0
	v_lshlrev_b32_e32 v4, 5, v9
	v_bfe_i32 v11, v1, 0, 16
	v_lshlrev_b32_e32 v1, 1, v2
	v_lshrrev_b32_e32 v5, 2, v2
	v_and_b32_e32 v6, 3, v10
	s_mov_b32 s7, 0x1fffe0
	v_and_b32_e32 v4, 32, v4
	v_and_b32_e32 v1, 24, v1
	v_and_b32_e32 v5, 4, v5
	v_and_or_b32 v6, v2, s7, v6
	v_or3_b32 v1, v6, v5, v1
	v_add_lshl_u32 v4, v4, v11, 1
	v_add_u32_e32 v0, 0x2000, v0
	v_lshl_add_u32 v146, v1, 11, v4
	v_ashrrev_i32_e32 v1, 31, v0
	v_lshrrev_b32_e32 v1, 22, v1
	v_add_u32_e32 v1, v0, v1
	v_ashrrev_i32_e32 v12, 10, v1
	v_mul_i32_i24_e32 v1, 0x400, v12
	v_sub_u32_e32 v0, v0, v1
	v_lshrrev_b32_e32 v1, 4, v0
	v_bitop3_b32 v0, v1, v0, 32 bitop3:0x6c
	s_add_u32 s28, s2, 0x3280c000
	v_lshl_add_u32 v144, v2, 11, v4
	v_ashrrev_i32_e32 v2, 31, v0
	s_addc_u32 s29, s3, 0
	v_lshrrev_b32_e32 v2, 26, v2
	s_add_u32 s30, s2, 0x3390c000
	v_add_u32_e32 v2, v0, v2
	s_addc_u32 s31, s3, 0
	s_ashr_i32 s6, s27, 6
	v_lshlrev_b32_e32 v1, 3, v12
	v_ashrrev_i32_e32 v13, 6, v2
	v_and_b32_e32 v2, 0xc0, v2
	v_and_b32_e32 v1, -16, v1
	v_sub_u32_e32 v0, v0, v2
	s_ashr_i32 s16, s27, 8
	s_lshl_b32 s38, s6, 10
	v_add_u32_e32 v1, v13, v1
	v_ashrrev_i16_sdwa v0, v3, sext(v0) dst_sel:DWORD dst_unused:UNUSED_PAD src0_sel:DWORD src1_sel:BYTE_0
	s_add_u32 s4, s30, s4
	v_lshlrev_b32_e32 v4, 5, v12
	v_bfe_i32 v14, v0, 0, 16
	v_lshlrev_b32_e32 v0, 1, v1
	v_lshrrev_b32_e32 v2, 2, v1
	v_and_b32_e32 v3, 3, v13
	s_addc_u32 s5, s31, s5
	s_add_i32 s39, s38, 0
	v_and_b32_e32 v4, 32, v4
	v_and_b32_e32 v0, 24, v0
	v_and_b32_e32 v2, 4, v2
	v_and_or_b32 v3, v1, s7, v3
	s_add_i32 m0, s39, 0x10000
	v_or3_b32 v0, v3, v2, v0
	v_add_lshl_u32 v2, v4, v14, 1
	global_load_lds_dwordx4 v146, s[4:5]
	s_add_i32 m0, s39, 0x12000
	v_lshl_add_u32 v150, v0, 11, v2
	s_add_u32 s22, s28, s0
	global_load_lds_dwordx4 v150, s[4:5]
	s_addc_u32 s23, s29, s1
	s_mov_b32 m0, s39
	s_add_i32 s40, s39, 0x2000
	v_lshl_add_u32 v148, v1, 11, v2
	global_load_lds_dwordx4 v144, s[22:23]
	s_mov_b32 m0, s40
	s_add_u32 s0, s4, 0x40000
	global_load_lds_dwordx4 v148, s[22:23]
	s_addc_u32 s1, s5, 0
	s_add_i32 m0, s39, 0x14000
	v_mov_b32_e32 v153, 0
	global_load_lds_dwordx4 v146, s[0:1]
	s_add_i32 m0, s39, 0x16000
	v_mov_b32_e32 v147, v153
	global_load_lds_dwordx4 v150, s[0:1]
	s_add_u32 s0, s22, 0x40000
	s_addc_u32 s1, s23, 0
	s_add_i32 s41, s39, 0x4000
	s_mov_b32 m0, s41
	s_add_i32 s42, s39, 0x6000
	global_load_lds_dwordx4 v144, s[0:1]
	s_mov_b32 m0, s42
	v_mov_b32_e32 v151, v153
	global_load_lds_dwordx4 v148, s[0:1]
	v_mov_b32_e32 v145, v153
	v_mov_b32_e32 v149, v153
	s_mov_b32 s7, 0
	v_lshl_add_u64 v[6:7], s[4:5], 0, v[146:147]
	v_lshl_add_u64 v[4:5], s[4:5], 0, v[150:151]
	v_lshl_add_u64 v[2:3], s[22:23], 0, v[144:145]
	v_lshl_add_u64 v[0:1], s[22:23], 0, v[148:149]
	s_cmp_lg_u32 s16, 0
	s_movk_i32 s43, 0x4000
	s_cbranch_scc1 .LBB0_234
	s_barrier

.LBB0_302:
	s_waitcnt vmcnt(0)
	s_cmpk_lt_u32 s27, 0x100
	s_cbranch_scc1 .LBB0_304
	s_barrier

.LBB0_361:
	s_waitcnt lgkmcnt(0)
	v_bfe_i32 v2, v8, 27, 1
	v_lshlrev_b32_e32 v0, 4, v8
	v_lshrrev_b32_e32 v2, 22, v2
	v_add_u32_e32 v2, v0, v2
	v_and_b32_e32 v2, 0xfffffc00, v2
	v_sub_u32_e32 v2, v0, v2
	v_ashrrev_i32_e32 v1, 31, v8
	v_lshrrev_b32_e32 v3, 4, v2
	v_lshrrev_b32_e32 v1, 26, v1
	v_bitop3_b32 v2, v3, v2, 32 bitop3:0x6c
	v_add_u32_e32 v1, v8, v1
	v_ashrrev_i32_e32 v4, 31, v2
	v_ashrrev_i32_e32 v1, 6, v1
	v_lshrrev_b32_e32 v4, 26, v4
	v_lshlrev_b32_e32 v3, 3, v1
	v_add_u32_e32 v4, v2, v4
	v_and_b32_e32 v3, -16, v3
	v_ashrrev_i32_e32 v5, 6, v4
	v_and_b32_e32 v4, 0xc0, v4
	v_add_u32_e32 v3, v5, v3
	v_sub_u32_e32 v2, v2, v4
	v_mov_b32_e32 v4, 1
	v_lshlrev_b32_e32 v1, 5, v1
	v_ashrrev_i16_sdwa v2, v4, sext(v2) dst_sel:DWORD dst_unused:UNUSED_PAD src0_sel:DWORD src1_sel:BYTE_0
	v_lshlrev_b32_e32 v6, 1, v3
	v_lshrrev_b32_e32 v7, 2, v3
	v_and_b32_e32 v5, 3, v5
	s_mov_b32 s2, 0x7fffe0
	v_and_b32_e32 v1, 32, v1
	v_bfe_i32 v2, v2, 0, 16
	v_and_b32_e32 v6, 24, v6
	v_and_b32_e32 v7, 4, v7
	v_and_or_b32 v5, v3, s2, v5
	v_or3_b32 v5, v5, v7, v6
	v_add_lshl_u32 v1, v1, v2, 1
	v_add_u32_e32 v0, 0x2000, v0
	v_lshl_add_u32 v136, v3, 10, v1
	v_lshl_add_u32 v138, v5, 9, v1
	v_ashrrev_i32_e32 v1, 31, v0
	v_lshrrev_b32_e32 v1, 22, v1
	v_add_u32_e32 v1, v0, v1
	v_ashrrev_i32_e32 v1, 10, v1
	s_add_u32 s29, s4, 0x3b68c000
	v_mul_i32_i24_e32 v2, 0x400, v1
	s_addc_u32 s30, s5, 0
	v_sub_u32_e32 v0, v0, v2
	s_add_u32 s31, s4, 0x4d58000
	v_lshrrev_b32_e32 v2, 4, v0
	s_addc_u32 s38, s5, 0
	v_bitop3_b32 v0, v2, v0, 32 bitop3:0x6c
	s_add_i32 s0, s3, s0
	v_ashrrev_i32_e32 v3, 31, v0
	s_mul_hi_i32 s3, s0, 0x92492493
	v_lshrrev_b32_e32 v3, 26, v3
	s_add_i32 s3, s3, s0
	v_lshlrev_b32_e32 v2, 3, v1
	v_add_u32_e32 v3, v0, v3
	s_lshr_b32 s8, s3, 31
	s_ashr_i32 s3, s3, 6
	v_and_b32_e32 v2, -16, v2
	v_ashrrev_i32_e32 v5, 6, v3
	v_and_b32_e32 v3, 0xc0, v3
	s_add_i32 s3, s3, s8
	v_add_u32_e32 v2, v5, v2
	v_sub_u32_e32 v0, v0, v3
	s_lshl_b32 s10, s3, 3
	v_lshlrev_b32_e32 v1, 5, v1
	v_ashrrev_i16_sdwa v0, v4, sext(v0) dst_sel:DWORD dst_unused:UNUSED_PAD src0_sel:DWORD src1_sel:BYTE_0
	v_lshlrev_b32_e32 v3, 1, v2
	v_lshrrev_b32_e32 v4, 2, v2
	v_and_b32_e32 v5, 3, v5
	s_sub_i32 s8, 34, s10
	v_and_b32_e32 v1, 32, v1
	v_bfe_i32 v0, v0, 0, 16
	v_and_b32_e32 v3, 24, v3
	v_and_b32_e32 v4, 4, v4
	v_and_or_b32 v5, v2, s2, v5
	s_min_u32 s11, s8, 8
	s_mulk_i32 s3, 0x70
	v_or3_b32 v3, v5, v4, v3
	v_add_lshl_u32 v0, v1, v0, 1
	s_sub_i32 s0, s0, s3
	v_cvt_f32_ubyte0_e32 v1, s11
	v_lshl_add_u32 v140, v2, 10, v0
	v_lshl_add_u32 v142, v3, 9, v0
	v_cvt_f32_i32_e32 v0, s0
	v_rcp_iflag_f32_e32 v2, v1
	s_ashr_i32 s1, s28, 6
	s_ashr_i32 s3, s0, 30
	s_ashr_i32 s2, s28, 8
	v_mul_f32_e32 v2, v0, v2
	v_trunc_f32_e32 v2, v2
	v_fma_f32 v0, -v2, v1, v0
	v_cvt_i32_f32_e32 v2, v2
	s_lshl_b32 s39, s1, 10
	s_or_b32 s3, s3, 1
	v_cmp_ge_f32_e64 s[8:9], |v0|, v1
	s_and_b64 s[8:9], s[8:9], exec
	s_cselect_b32 s3, s3, 0
	v_readfirstlane_b32 s8, v2
	s_add_i32 s3, s8, s3
	s_sext_i32_i8 s59, s3
	s_mul_i32 s3, s3, s11
	s_sub_i32 s0, s0, s3
	s_sext_i32_i8 s0, s0
	s_add_i32 s60, s10, s0
	s_lshl_b32 s0, s60, 18
	s_cmp_lt_i32 s59, 6
	s_cselect_b32 s3, 0, 0x200
	s_or_b32 s0, s0, s3
	s_lshl_b32 s3, s59, 17
	s_add_u32 s26, s31, s3
	s_addc_u32 s27, s38, 0
	s_add_i32 s40, s39, 0
	s_add_i32 m0, s40, 0x10000
	v_mov_b32_e32 v139, 0
	global_load_lds_dwordx4 v138, s[26:27]
	s_add_i32 m0, s40, 0x12000
	s_add_u32 s22, s29, s0
	global_load_lds_dwordx4 v142, s[26:27]
	s_addc_u32 s23, s30, 0
	s_mov_b32 m0, s40
	s_add_i32 s41, s40, 0x2000
	global_load_lds_dwordx4 v136, s[22:23]
	s_mov_b32 m0, s41
	s_add_u32 s8, s26, 0x10000
	global_load_lds_dwordx4 v140, s[22:23]
	s_addc_u32 s9, s27, 0
	s_add_i32 m0, s40, 0x14000
	v_mov_b32_e32 v143, v139
	global_load_lds_dwordx4 v138, s[8:9]
	s_add_i32 m0, s40, 0x16000
	v_mov_b32_e32 v137, v139
	global_load_lds_dwordx4 v142, s[8:9]
	s_add_u32 s8, s22, 0x20000
	s_addc_u32 s9, s23, 0
	s_add_i32 s42, s40, 0x4000
	s_mov_b32 m0, s42
	s_add_i32 s43, s40, 0x6000
	global_load_lds_dwordx4 v136, s[8:9]
	s_mov_b32 m0, s43
	v_mov_b32_e32 v141, v139
	global_load_lds_dwordx4 v140, s[8:9]
	s_mov_b32 s0, 0
	v_lshl_add_u64 v[6:7], s[26:27], 0, v[138:139]
	v_lshl_add_u64 v[4:5], s[26:27], 0, v[142:143]
	v_lshl_add_u64 v[2:3], s[22:23], 0, v[136:137]
	s_cmp_lg_u32 s2, 0
	v_lshl_add_u64 v[0:1], s[22:23], 0, v[140:141]
	s_cbranch_scc1 .LBB0_363
	s_barrier

.LBB0_371:
	s_waitcnt vmcnt(0)
	s_cmpk_lt_u32 s28, 0x100
	s_cbranch_scc1 .LBB0_373
	s_barrier

.LBB0_901:
	v_ashrrev_i32_e32 v1, 31, v8
	v_lshrrev_b32_e32 v1, 26, v1
	v_add_u32_e32 v1, v8, v1
	v_ashrrev_i32_e32 v9, 6, v1
	v_bfe_i32 v1, v8, 27, 1
	v_lshlrev_b32_e32 v0, 4, v8
	v_lshrrev_b32_e32 v1, 22, v1
	v_add_u32_e32 v1, v0, v1
	v_and_b32_e32 v1, 0xfffffc00, v1
	v_sub_u32_e32 v1, v0, v1
	s_waitcnt lgkmcnt(0)
	v_lshrrev_b32_e32 v2, 4, v1
	v_bitop3_b32 v1, v2, v1, 32 bitop3:0x6c
	v_ashrrev_i32_e32 v3, 31, v1
	v_lshrrev_b32_e32 v3, 26, v3
	v_add_u32_e32 v3, v1, v3
	v_lshlrev_b32_e32 v2, 3, v9
	v_ashrrev_i32_e32 v10, 6, v3
	v_and_b32_e32 v3, 0xc0, v3
	v_and_b32_e32 v2, -16, v2
	v_sub_u32_e32 v1, v1, v3
	v_mov_b32_e32 v3, 1
	v_add_u32_e32 v2, v10, v2
	v_ashrrev_i16_sdwa v1, v3, sext(v1) dst_sel:DWORD dst_unused:UNUSED_PAD src0_sel:DWORD src1_sel:BYTE_0
	v_bfe_i32 v11, v1, 0, 16
	v_lshlrev_b32_e32 v1, 1, v2
	v_lshlrev_b32_e32 v4, 5, v9
	v_and_b32_e32 v12, 0xffffffe0, v2
	v_and_b32_e32 v13, 24, v1
	v_lshrrev_b32_e32 v1, 2, v2
	v_and_b32_e32 v15, 3, v10
	v_and_b32_e32 v4, 32, v4
	v_and_b32_e32 v14, 4, v1
	v_or_b32_e32 v1, v12, v15
	s_add_u32 s70, s4, 0x3760c000
	v_or3_b32 v1, v1, v14, v13
	v_add_lshl_u32 v4, v4, v11, 1
	v_add_u32_e32 v0, 0x2000, v0
	s_addc_u32 s71, s5, 0
	v_lshl_add_u32 v150, v1, 11, v4
	v_ashrrev_i32_e32 v1, 31, v0
	s_add_i32 s2, s2, s3
	v_lshrrev_b32_e32 v1, 22, v1
	s_ashr_i32 s3, s2, 31
	v_add_u32_e32 v1, v0, v1
	s_lshr_b32 s3, s3, 26
	v_ashrrev_i32_e32 v16, 10, v1
	s_add_i32 s3, s2, s3
	v_mul_i32_i24_e32 v1, 0x400, v16
	s_ashr_i32 s6, s3, 6
	s_and_b32 s3, s3, 0xffc0
	v_sub_u32_e32 v0, v0, v1
	s_sub_i32 s2, s2, s3
	v_lshrrev_b32_e32 v1, 4, v0
	s_bfe_i32 s3, s2, 0x80000
	v_bitop3_b32 v0, v1, v0, 32 bitop3:0x6c
	s_bfe_u32 s3, s3, 0x3000c
	v_lshl_add_u32 v148, v2, 11, v4
	v_ashrrev_i32_e32 v2, 31, v0
	s_add_i32 s3, s2, s3
	v_lshrrev_b32_e32 v2, 26, v2
	s_bfe_i32 s7, s3, 0x80000
	s_and_b32 s3, s3, 0xf8
	v_add_u32_e32 v2, v0, v2
	s_sub_i32 s2, s2, s3
	v_lshlrev_b32_e32 v1, 3, v16
	v_ashrrev_i32_e32 v4, 6, v2
	v_and_b32_e32 v2, 0xc0, v2
	s_lshl_b32 s6, s6, 3
	s_sext_i32_i16 s7, s7
	s_sext_i32_i8 s2, s2
	s_ashr_i32 s0, s68, 6
	v_and_b32_e32 v1, -16, v1
	v_sub_u32_e32 v0, v0, v2
	s_add_i32 s92, s6, s2
	s_ashr_i32 s91, s7, 3
	v_add_u32_e32 v1, v4, v1
	v_ashrrev_i16_sdwa v0, v3, sext(v0) dst_sel:DWORD dst_unused:UNUSED_PAD src0_sel:DWORD src1_sel:BYTE_0
	s_ashr_i32 s1, s68, 8
	s_lshl_b32 s72, s0, 10
	s_lshl_b32 s2, s91, 19
	s_lshl_b32 s3, s92, 19
	v_bfe_i32 v17, v0, 0, 16
	v_lshlrev_b32_e32 v0, 1, v1
	s_add_u32 s50, s70, s2
	v_lshlrev_b32_e32 v5, 5, v16
	v_and_b32_e32 v18, 0xffffffe0, v1
	v_and_b32_e32 v19, 24, v0
	v_lshrrev_b32_e32 v0, 2, v1
	v_and_b32_e32 v21, 3, v4
	s_addc_u32 s51, s71, 0
	s_add_i32 s73, s72, 0
	v_and_b32_e32 v5, 32, v5
	v_and_b32_e32 v20, 4, v0
	v_or_b32_e32 v0, v18, v21
	s_add_i32 m0, s73, 0x10000
	v_or3_b32 v0, v0, v20, v19
	v_add_lshl_u32 v2, v5, v17, 1
	global_load_lds_dwordx4 v150, s[50:51]
	s_add_i32 m0, s73, 0x12000
	v_lshl_add_u32 v154, v0, 11, v2
	s_add_u32 s48, s65, s3
	global_load_lds_dwordx4 v154, s[50:51]
	s_addc_u32 s49, s66, 0
	s_mov_b32 m0, s73
	s_add_i32 s74, s73, 0x2000
	v_lshl_add_u32 v152, v1, 11, v2
	global_load_lds_dwordx4 v148, s[48:49]
	s_mov_b32 m0, s74
	s_add_u32 s2, s50, 0x40000
	global_load_lds_dwordx4 v152, s[48:49]
	s_addc_u32 s3, s51, 0
	s_add_i32 m0, s73, 0x14000
	v_mov_b32_e32 v157, 0
	global_load_lds_dwordx4 v150, s[2:3]
	s_add_i32 m0, s73, 0x16000
	v_mov_b32_e32 v151, v157
	global_load_lds_dwordx4 v154, s[2:3]
	s_add_u32 s2, s48, 0x40000
	s_addc_u32 s3, s49, 0
	s_add_i32 s75, s73, 0x4000
	s_mov_b32 m0, s75
	s_add_i32 s76, s73, 0x6000
	global_load_lds_dwordx4 v148, s[2:3]
	s_mov_b32 m0, s76
	v_mov_b32_e32 v155, v157
	global_load_lds_dwordx4 v152, s[2:3]
	v_mov_b32_e32 v149, v157
	v_mov_b32_e32 v153, v157
	s_mov_b32 s77, 0
	v_lshl_add_u64 v[6:7], s[50:51], 0, v[150:151]
	v_lshl_add_u64 v[4:5], s[50:51], 0, v[154:155]
	v_lshl_add_u64 v[0:1], s[48:49], 0, v[148:149]
	s_cmp_lg_u32 s1, 0
	v_lshl_add_u64 v[2:3], s[48:49], 0, v[152:153]
	s_cbranch_scc1 .LBB0_903
	s_barrier

.LBB0_911:
	ds_read_b128 v[8:11], v231
	ds_read_b128 v[12:15], v231 offset:1024
	ds_read_b128 v[0:3], v231 offset:2048
	ds_read_b128 v[4:7], v231 offset:3072
	v_lshl_add_u64 v[172:173], v[170:171], 0, s[2:3]
	s_add_i32 s94, s73, 0xc000
	v_lshl_add_u64 v[174:175], v[172:173], 0, s[10:11]
	s_mov_b32 m0, s94
	ds_read_b128 v[180:183], v228
	ds_read_b128 v[184:187], v228 offset:1024
	ds_read_b128 v[188:191], v228 offset:2048
	ds_read_b128 v[192:195], v228 offset:3072
	ds_read_b128 v[196:199], v228 offset:4096
	ds_read_b128 v[200:203], v228 offset:5120
	ds_read_b128 v[204:207], v228 offset:6144
	ds_read_b128 v[208:211], v228 offset:7168
	global_load_lds_dwordx4 v[174:175], off
	v_lshl_add_u64 v[174:175], v[168:169], 0, s[2:3]
	s_add_i32 s93, s73, 0xe000
	v_lshl_add_u64 v[176:177], v[174:175], 0, s[10:11]
	s_mov_b32 m0, s93
	s_nop 0
	global_load_lds_dwordx4 v[176:177], off
	s_waitcnt lgkmcnt(8)
	s_barrier
	s_waitcnt lgkmcnt(0)
	s_setprio 1
	s_waitcnt lgkmcnt(0)
	v_mfma_scale_f32_16x16x128_f8f6f4 v[16:19], v[8:15], v[180:187], v[16:19], v225, v225 op_sel_hi:[0,0,0]
	v_mfma_scale_f32_16x16x128_f8f6f4 v[20:23], v[0:7], v[180:187], v[20:23], v225, v225 op_sel_hi:[0,0,0]
	v_mfma_scale_f32_16x16x128_f8f6f4 v[24:27], v[8:15], v[188:195], v[24:27], v225, v225 op_sel_hi:[0,0,0]
	v_mfma_scale_f32_16x16x128_f8f6f4 v[28:31], v[0:7], v[188:195], v[28:31], v225, v225 op_sel_hi:[0,0,0]
	v_mfma_scale_f32_16x16x128_f8f6f4 v[32:35], v[8:15], v[196:203], v[32:35], v225, v225 op_sel_hi:[0,0,0]
	v_mfma_scale_f32_16x16x128_f8f6f4 v[36:39], v[0:7], v[196:203], v[36:39], v225, v225 op_sel_hi:[0,0,0]
	v_mfma_scale_f32_16x16x128_f8f6f4 v[40:43], v[8:15], v[204:211], v[40:43], v225, v225 op_sel_hi:[0,0,0]
	v_mfma_scale_f32_16x16x128_f8f6f4 v[44:47], v[0:7], v[204:211], v[44:47], v225, v225 op_sel_hi:[0,0,0]
	s_setprio 0
	s_barrier
	v_lshl_add_u64 v[176:177], v[146:147], 0, s[2:3]
	s_add_i32 s96, s83, s72
	v_lshl_add_u64 v[178:179], v[176:177], 0, s[12:13]
	s_mov_b32 m0, s96
	ds_read_b128 v[212:215], v232
	ds_read_b128 v[216:219], v232 offset:1024
	ds_read_b128 v[234:237], v232 offset:2048
	ds_read_b128 v[238:241], v232 offset:3072
	global_load_lds_dwordx4 v[178:179], off
	v_lshl_add_u64 v[178:179], v[144:145], 0, s[2:3]
	s_add_i32 s95, s96, 0x2000
	v_lshl_add_u64 v[220:221], v[178:179], 0, s[12:13]
	s_mov_b32 m0, s95
	s_nop 0
	global_load_lds_dwordx4 v[220:221], off
	s_barrier
	s_waitcnt lgkmcnt(0)
	s_setprio 1
	s_waitcnt lgkmcnt(0)
	v_mfma_scale_f32_16x16x128_f8f6f4 v[48:51], v[212:219], v[180:187], v[48:51], v225, v225 op_sel_hi:[0,0,0]
	v_mfma_scale_f32_16x16x128_f8f6f4 v[52:55], v[234:241], v[180:187], v[52:55], v225, v225 op_sel_hi:[0,0,0]
	v_mfma_scale_f32_16x16x128_f8f6f4 v[56:59], v[212:219], v[188:195], v[56:59], v225, v225 op_sel_hi:[0,0,0]
	v_mfma_scale_f32_16x16x128_f8f6f4 v[60:63], v[234:241], v[188:195], v[60:63], v225, v225 op_sel_hi:[0,0,0]
	v_mfma_scale_f32_16x16x128_f8f6f4 v[64:67], v[212:219], v[196:203], v[64:67], v225, v225 op_sel_hi:[0,0,0]
	v_mfma_scale_f32_16x16x128_f8f6f4 v[68:71], v[234:241], v[196:203], v[68:71], v225, v225 op_sel_hi:[0,0,0]
	v_mfma_scale_f32_16x16x128_f8f6f4 v[72:75], v[212:219], v[204:211], v[72:75], v225, v225 op_sel_hi:[0,0,0]
	v_mfma_scale_f32_16x16x128_f8f6f4 v[76:79], v[234:241], v[204:211], v[76:79], v225, v225 op_sel_hi:[0,0,0]
	s_setprio 0
	s_mov_b32 m0, s73
	v_lshl_add_u64 v[220:221], v[172:173], 0, s[12:13]
	s_barrier
	ds_read_b128 v[180:183], v228 offset:16384
	ds_read_b128 v[184:187], v228 offset:17408
	ds_read_b128 v[188:191], v228 offset:18432
	ds_read_b128 v[192:195], v228 offset:19456
	ds_read_b128 v[196:199], v228 offset:20480
	ds_read_b128 v[200:203], v228 offset:21504
	ds_read_b128 v[204:207], v228 offset:22528
	ds_read_b128 v[208:211], v228 offset:23552
	global_load_lds_dwordx4 v[220:221], off
	v_lshl_add_u64 v[220:221], v[174:175], 0, s[12:13]
	s_mov_b32 m0, s74
	s_nop 0
	global_load_lds_dwordx4 v[220:221], off
	s_barrier
	s_waitcnt lgkmcnt(0)
	s_setprio 1
	s_waitcnt lgkmcnt(0)
	v_mfma_scale_f32_16x16x128_f8f6f4 v[80:83], v[8:15], v[180:187], v[80:83], v225, v225 op_sel_hi:[0,0,0]
	v_mfma_scale_f32_16x16x128_f8f6f4 v[84:87], v[0:7], v[180:187], v[84:87], v225, v225 op_sel_hi:[0,0,0]
	v_mfma_scale_f32_16x16x128_f8f6f4 v[88:91], v[8:15], v[188:195], v[88:91], v225, v225 op_sel_hi:[0,0,0]
	v_mfma_scale_f32_16x16x128_f8f6f4 v[92:95], v[0:7], v[188:195], v[92:95], v225, v225 op_sel_hi:[0,0,0]
	v_mfma_scale_f32_16x16x128_f8f6f4 v[96:99], v[8:15], v[196:203], v[96:99], v225, v225 op_sel_hi:[0,0,0]
	v_mfma_scale_f32_16x16x128_f8f6f4 v[100:103], v[0:7], v[196:203], v[100:103], v225, v225 op_sel_hi:[0,0,0]
	v_mfma_scale_f32_16x16x128_f8f6f4 v[104:107], v[8:15], v[204:211], v[104:107], v225, v225 op_sel_hi:[0,0,0]
	v_mfma_scale_f32_16x16x128_f8f6f4 v[108:111], v[0:7], v[204:211], v[108:111], v225, v225 op_sel_hi:[0,0,0]
	s_setprio 0
	s_barrier
	s_add_i32 s97, s84, s72
	v_lshl_add_u64 v[0:1], v[176:177], 0, s[16:17]
	s_mov_b32 m0, s97
	s_add_i32 s52, s97, 0x2000
	global_load_lds_dwordx4 v[0:1], off
	v_lshl_add_u64 v[0:1], v[178:179], 0, s[16:17]
	s_mov_b32 m0, s52
	s_nop 0
	global_load_lds_dwordx4 v[0:1], off
	s_waitcnt vmcnt(6)
	s_barrier
	s_setprio 1
	v_mfma_scale_f32_16x16x128_f8f6f4 v[112:115], v[212:219], v[180:187], v[112:115], v225, v225 op_sel_hi:[0,0,0]
	v_mfma_scale_f32_16x16x128_f8f6f4 v[116:119], v[234:241], v[180:187], v[116:119], v225, v225 op_sel_hi:[0,0,0]
	v_mfma_scale_f32_16x16x128_f8f6f4 v[120:123], v[212:219], v[188:195], v[120:123], v225, v225 op_sel_hi:[0,0,0]
	v_mfma_scale_f32_16x16x128_f8f6f4 v[124:127], v[234:241], v[188:195], v[124:127], v225, v225 op_sel_hi:[0,0,0]
	v_mfma_scale_f32_16x16x128_f8f6f4 v[128:131], v[212:219], v[196:203], v[128:131], v225, v225 op_sel_hi:[0,0,0]
	v_mfma_scale_f32_16x16x128_f8f6f4 v[132:135], v[234:241], v[196:203], v[132:135], v225, v225 op_sel_hi:[0,0,0]
	v_mfma_scale_f32_16x16x128_f8f6f4 v[136:139], v[212:219], v[204:211], v[136:139], v225, v225 op_sel_hi:[0,0,0]
	v_mfma_scale_f32_16x16x128_f8f6f4 v[140:143], v[234:241], v[204:211], v[140:143], v225, v225 op_sel_hi:[0,0,0]
	s_setprio 0
	s_add_i32 s62, 0, 0x18000
	v_add_u32_e32 v235, s62, v227
	s_barrier
	ds_read_b128 v[0:3], v235
	ds_read_b128 v[4:7], v235 offset:1024
	ds_read_b128 v[8:11], v235 offset:2048
	ds_read_b128 v[12:15], v235 offset:3072
	s_mov_b32 m0, s75
	v_lshl_add_u64 v[212:213], v[172:173], 0, s[16:17]
	ds_read_b128 v[180:183], v228 offset:32768
	ds_read_b128 v[184:187], v228 offset:33792
	ds_read_b128 v[188:191], v228 offset:34816
	ds_read_b128 v[192:195], v228 offset:35840
	ds_read_b128 v[196:199], v228 offset:36864
	ds_read_b128 v[200:203], v228 offset:37888
	ds_read_b128 v[204:207], v228 offset:38912
	ds_read_b128 v[208:211], v228 offset:39936
	global_load_lds_dwordx4 v[212:213], off
	v_lshl_add_u64 v[212:213], v[174:175], 0, s[16:17]
	s_mov_b32 m0, s76
	s_nop 0
	global_load_lds_dwordx4 v[212:213], off
	s_waitcnt lgkmcnt(8)
	s_barrier
	s_waitcnt lgkmcnt(0)
	s_setprio 1
	s_waitcnt lgkmcnt(0)
	v_mfma_scale_f32_16x16x128_f8f6f4 v[16:19], v[0:7], v[180:187], v[16:19], v225, v225 op_sel_hi:[0,0,0]
	v_mfma_scale_f32_16x16x128_f8f6f4 v[20:23], v[8:15], v[180:187], v[20:23], v225, v225 op_sel_hi:[0,0,0]
	v_mfma_scale_f32_16x16x128_f8f6f4 v[24:27], v[0:7], v[188:195], v[24:27], v225, v225 op_sel_hi:[0,0,0]
	v_mfma_scale_f32_16x16x128_f8f6f4 v[28:31], v[8:15], v[188:195], v[28:31], v225, v225 op_sel_hi:[0,0,0]
	v_mfma_scale_f32_16x16x128_f8f6f4 v[32:35], v[0:7], v[196:203], v[32:35], v225, v225 op_sel_hi:[0,0,0]
	v_mfma_scale_f32_16x16x128_f8f6f4 v[36:39], v[8:15], v[196:203], v[36:39], v225, v225 op_sel_hi:[0,0,0]
	v_mfma_scale_f32_16x16x128_f8f6f4 v[40:43], v[0:7], v[204:211], v[40:43], v225, v225 op_sel_hi:[0,0,0]
	v_mfma_scale_f32_16x16x128_f8f6f4 v[44:47], v[8:15], v[204:211], v[44:47], v225, v225 op_sel_hi:[0,0,0]
	s_setprio 0
	s_barrier
	s_add_i32 s53, 0, 0x1c000
	s_add_i32 s62, s62, s72
	v_add_u32_e32 v234, s53, v227
	v_lshl_add_u64 v[220:221], v[176:177], 0, s[18:19]
	s_mov_b32 m0, s62
	s_add_i32 s63, s62, 0x2000
	ds_read_b128 v[212:215], v234
	ds_read_b128 v[216:219], v234 offset:1024
	ds_read_b128 v[236:239], v234 offset:2048
	ds_read_b128 v[240:243], v234 offset:3072
	global_load_lds_dwordx4 v[220:221], off
	v_lshl_add_u64 v[220:221], v[178:179], 0, s[18:19]
	s_mov_b32 m0, s63
	s_nop 0
	global_load_lds_dwordx4 v[220:221], off
	s_barrier
	s_waitcnt lgkmcnt(0)
	s_setprio 1
	s_waitcnt lgkmcnt(0)
	v_mfma_scale_f32_16x16x128_f8f6f4 v[48:51], v[212:219], v[180:187], v[48:51], v225, v225 op_sel_hi:[0,0,0]
	v_mfma_scale_f32_16x16x128_f8f6f4 v[52:55], v[236:243], v[180:187], v[52:55], v225, v225 op_sel_hi:[0,0,0]
	v_mfma_scale_f32_16x16x128_f8f6f4 v[56:59], v[212:219], v[188:195], v[56:59], v225, v225 op_sel_hi:[0,0,0]
	v_mfma_scale_f32_16x16x128_f8f6f4 v[60:63], v[236:243], v[188:195], v[60:63], v225, v225 op_sel_hi:[0,0,0]
	v_mfma_scale_f32_16x16x128_f8f6f4 v[64:67], v[212:219], v[196:203], v[64:67], v225, v225 op_sel_hi:[0,0,0]
	v_mfma_scale_f32_16x16x128_f8f6f4 v[68:71], v[236:243], v[196:203], v[68:71], v225, v225 op_sel_hi:[0,0,0]
	v_mfma_scale_f32_16x16x128_f8f6f4 v[72:75], v[212:219], v[204:211], v[72:75], v225, v225 op_sel_hi:[0,0,0]
	v_mfma_scale_f32_16x16x128_f8f6f4 v[76:79], v[236:243], v[204:211], v[76:79], v225, v225 op_sel_hi:[0,0,0]
	s_setprio 0
	s_mov_b32 m0, s80
	v_lshl_add_u64 v[172:173], v[172:173], 0, s[18:19]
	s_barrier
	ds_read_b128 v[180:183], v228 offset:49152
	ds_read_b128 v[184:187], v228 offset:50176
	ds_read_b128 v[188:191], v228 offset:51200
	ds_read_b128 v[192:195], v228 offset:52224
	ds_read_b128 v[196:199], v228 offset:53248
	ds_read_b128 v[200:203], v228 offset:54272
	ds_read_b128 v[204:207], v228 offset:55296
	ds_read_b128 v[208:211], v228 offset:56320
	global_load_lds_dwordx4 v[172:173], off
	v_lshl_add_u64 v[172:173], v[174:175], 0, s[18:19]
	s_mov_b32 m0, s81
	s_nop 0
	global_load_lds_dwordx4 v[172:173], off
	s_barrier
	s_waitcnt lgkmcnt(0)
	s_setprio 1
	s_waitcnt lgkmcnt(0)
	v_mfma_scale_f32_16x16x128_f8f6f4 v[80:83], v[0:7], v[180:187], v[80:83], v225, v225 op_sel_hi:[0,0,0]
	v_mfma_scale_f32_16x16x128_f8f6f4 v[84:87], v[8:15], v[180:187], v[84:87], v225, v225 op_sel_hi:[0,0,0]
	v_mfma_scale_f32_16x16x128_f8f6f4 v[88:91], v[0:7], v[188:195], v[88:91], v225, v225 op_sel_hi:[0,0,0]
	v_mfma_scale_f32_16x16x128_f8f6f4 v[92:95], v[8:15], v[188:195], v[92:95], v225, v225 op_sel_hi:[0,0,0]
	v_mfma_scale_f32_16x16x128_f8f6f4 v[96:99], v[0:7], v[196:203], v[96:99], v225, v225 op_sel_hi:[0,0,0]
	v_mfma_scale_f32_16x16x128_f8f6f4 v[100:103], v[8:15], v[196:203], v[100:103], v225, v225 op_sel_hi:[0,0,0]
	v_mfma_scale_f32_16x16x128_f8f6f4 v[104:107], v[0:7], v[204:211], v[104:107], v225, v225 op_sel_hi:[0,0,0]
	v_mfma_scale_f32_16x16x128_f8f6f4 v[108:111], v[8:15], v[204:211], v[108:111], v225, v225 op_sel_hi:[0,0,0]
	s_setprio 0
	s_barrier
	s_add_i32 s53, s53, s72
	v_lshl_add_u64 v[0:1], v[176:177], 0, s[20:21]
	s_mov_b32 m0, s53
	s_add_i32 s64, s53, 0x2000
	global_load_lds_dwordx4 v[0:1], off
	v_lshl_add_u64 v[0:1], v[178:179], 0, s[20:21]
	s_mov_b32 m0, s64
	s_nop 0
	global_load_lds_dwordx4 v[0:1], off
	s_waitcnt vmcnt(6)
	s_barrier
	s_setprio 1
	v_mfma_scale_f32_16x16x128_f8f6f4 v[112:115], v[212:219], v[180:187], v[112:115], v225, v225 op_sel_hi:[0,0,0]
	v_mfma_scale_f32_16x16x128_f8f6f4 v[116:119], v[236:243], v[180:187], v[116:119], v225, v225 op_sel_hi:[0,0,0]
	v_mfma_scale_f32_16x16x128_f8f6f4 v[120:123], v[212:219], v[188:195], v[120:123], v225, v225 op_sel_hi:[0,0,0]
	v_mfma_scale_f32_16x16x128_f8f6f4 v[124:127], v[236:243], v[188:195], v[124:127], v225, v225 op_sel_hi:[0,0,0]
	v_mfma_scale_f32_16x16x128_f8f6f4 v[128:131], v[212:219], v[196:203], v[128:131], v225, v225 op_sel_hi:[0,0,0]
	v_mfma_scale_f32_16x16x128_f8f6f4 v[132:135], v[236:243], v[196:203], v[132:135], v225, v225 op_sel_hi:[0,0,0]
	v_mfma_scale_f32_16x16x128_f8f6f4 v[136:139], v[212:219], v[204:211], v[136:139], v225, v225 op_sel_hi:[0,0,0]
	v_mfma_scale_f32_16x16x128_f8f6f4 v[140:143], v[236:243], v[204:211], v[140:143], v225, v225 op_sel_hi:[0,0,0]
	s_setprio 0
	s_add_i32 s44, s44, 2
	s_add_u32 s2, s2, 0x100
	s_addc_u32 s3, s3, 0
	s_cmp_gt_u32 s44, 5
	s_barrier
	s_cbranch_scc0 .LBB0_911
	s_add_u32 s44, s65, s89
	s_addc_u32 s45, s66, 0
	s_add_u32 s46, s70, s90
	s_addc_u32 s47, s71, 0
	s_and_b64 s[2:3], vcc, exec
	s_mul_i32 s2, s92, 24
	s_cselect_b32 s55, s45, s49
	s_cselect_b32 s54, s44, s48
	s_add_i32 s58, s2, s91
	s_ashr_i32 s59, s58, 31
	s_lshl_b64 s[2:3], s[58:59], 16
	s_add_u32 s2, s78, s2
	s_addc_u32 s3, s79, s3
	s_add_i32 s56, s58, 8
	s_ashr_i32 s57, s56, 31
	v_mov_b32_e32 v156, v230
	s_lshl_b64 s[56:57], s[56:57], 16
	s_nop 7
	s_nop 7
	s_nop 7
	s_add_u32 s56, s78, s56
	s_addc_u32 s57, s79, s57
	global_load_dwordx2 v[210:211], v156, s[2:3]
	global_load_dwordx2 v[216:217], v156, s[56:57]
	global_load_dwordx2 v[206:207], v156, s[2:3] offset:512
	global_load_dwordx2 v[208:209], v156, s[56:57] offset:512
	global_load_dwordx2 v[202:203], v156, s[2:3] offset:1024
	global_load_dwordx2 v[204:205], v156, s[56:57] offset:1024
	global_load_dwordx2 v[198:199], v156, s[2:3] offset:1536
	global_load_dwordx2 v[200:201], v156, s[56:57] offset:1536
	global_load_dwordx2 v[194:195], v156, s[2:3] offset:2048
	global_load_dwordx2 v[196:197], v156, s[56:57] offset:2048
	global_load_dwordx2 v[190:191], v156, s[2:3] offset:2560
	global_load_dwordx2 v[192:193], v156, s[56:57] offset:2560
	global_load_dwordx2 v[186:187], v156, s[2:3] offset:3072
	global_load_dwordx2 v[188:189], v156, s[56:57] offset:3072
	global_load_dwordx2 v[182:183], v156, s[2:3] offset:3584
	global_load_dwordx2 v[184:185], v156, s[56:57] offset:3584
	v_lshl_add_u64 v[0:1], s[2:3], 0, v[156:157]
	v_lshl_add_u64 v[2:3], s[56:57], 0, v[156:157]
	v_add_co_u32_e64 v0, s[2:3], s85, v0
	s_waitcnt vmcnt(0)
	v_cvt_f32_ubyte3_e32 v237, v210
	v_cvt_f32_ubyte0_e32 v156, v216
	v_add_f32_e32 v156, 0.5, v156
	v_rcp_f32_e32 v218, v156
	v_cvt_f32_ubyte0_e32 v156, v217
	v_add_f32_e32 v156, 0.5, v156
	v_rcp_f32_e32 v212, v156
	v_cvt_f32_ubyte1_e32 v156, v216
	v_add_f32_e32 v156, 0.5, v156
	v_rcp_f32_e32 v219, v156
	v_cvt_f32_ubyte1_e32 v156, v217
	v_add_f32_e32 v156, 0.5, v156
	v_rcp_f32_e32 v213, v156
	v_cvt_f32_ubyte2_e32 v156, v216
	v_add_f32_e32 v156, 0.5, v156
	v_rcp_f32_e32 v220, v156
	v_cvt_f32_ubyte2_e32 v156, v217
	v_add_f32_e32 v156, 0.5, v156
	v_rcp_f32_e32 v214, v156
	v_cvt_f32_ubyte3_e32 v156, v216
	v_add_f32_e32 v156, 0.5, v156
	v_rcp_f32_e32 v221, v156
	v_cvt_f32_ubyte3_e32 v156, v217
	v_add_f32_e32 v156, 0.5, v156
	v_cvt_f32_ubyte1_e32 v217, v210
	v_cvt_f32_ubyte0_e32 v216, v210
	v_cvt_f32_ubyte2_e32 v236, v210
	v_rcp_f32_e32 v215, v156
	v_pk_add_f32 v[236:237], v[236:237], 0.5 op_sel_hi:[1,0]
	v_pk_add_f32 v[216:217], v[216:217], 0.5 op_sel_hi:[1,0]
	v_cvt_f32_ubyte0_e32 v156, v208
	v_pk_mul_f32 v[216:217], v[216:217], v[218:219]
	v_pk_mul_f32 v[218:219], v[236:237], v[220:221]
	v_pk_mul_f32 v[16:17], v[16:17], v[216:217]
	v_pk_mul_f32 v[18:19], v[18:19], v[218:219]
	v_cvt_f32_ubyte3_e32 v219, v211
	v_cvt_f32_ubyte2_e32 v218, v211
	v_cvt_f32_ubyte1_e32 v217, v211
	v_cvt_f32_ubyte0_e32 v216, v211
	v_pk_add_f32 v[210:211], v[218:219], 0.5 op_sel_hi:[1,0]
	v_add_f32_e32 v156, 0.5, v156
	v_pk_mul_f32 v[210:211], v[210:211], v[214:215]
	v_pk_add_f32 v[216:217], v[216:217], 0.5 op_sel_hi:[1,0]
	v_pk_mul_f32 v[22:23], v[22:23], v[210:211]
	v_rcp_f32_e32 v210, v156
	v_cvt_f32_ubyte0_e32 v156, v209
	v_pk_mul_f32 v[212:213], v[216:217], v[212:213]
	v_add_f32_e32 v156, 0.5, v156
	v_pk_mul_f32 v[20:21], v[20:21], v[212:213]
	v_rcp_f32_e32 v212, v156
	v_cvt_f32_ubyte1_e32 v156, v208
	v_add_f32_e32 v156, 0.5, v156
	v_rcp_f32_e32 v211, v156
	v_cvt_f32_ubyte1_e32 v156, v209
	v_add_f32_e32 v156, 0.5, v156
	v_rcp_f32_e32 v213, v156
	v_cvt_f32_ubyte2_e32 v156, v208
	v_add_f32_e32 v156, 0.5, v156
	v_rcp_f32_e32 v214, v156
	v_cvt_f32_ubyte2_e32 v156, v209
	v_add_f32_e32 v156, 0.5, v156
	v_rcp_f32_e32 v216, v156
	v_cvt_f32_ubyte3_e32 v156, v208
	v_add_f32_e32 v156, 0.5, v156
	v_rcp_f32_e32 v215, v156
	v_cvt_f32_ubyte3_e32 v156, v209
	v_add_f32_e32 v156, 0.5, v156
	v_cvt_f32_ubyte1_e32 v209, v206
	v_cvt_f32_ubyte0_e32 v208, v206
	v_cvt_f32_ubyte3_e32 v219, v206
	v_cvt_f32_ubyte2_e32 v218, v206
	v_rcp_f32_e32 v217, v156
	v_pk_add_f32 v[218:219], v[218:219], 0.5 op_sel_hi:[1,0]
	v_pk_add_f32 v[208:209], v[208:209], 0.5 op_sel_hi:[1,0]
	v_cvt_f32_ubyte0_e32 v156, v204
	v_pk_mul_f32 v[208:209], v[208:209], v[210:211]
	v_pk_mul_f32 v[210:211], v[218:219], v[214:215]
	v_pk_mul_f32 v[48:49], v[48:49], v[208:209]
	v_pk_mul_f32 v[50:51], v[50:51], v[210:211]
	v_cvt_f32_ubyte3_e32 v211, v207
	v_cvt_f32_ubyte2_e32 v210, v207
	v_cvt_f32_ubyte1_e32 v209, v207
	v_cvt_f32_ubyte0_e32 v208, v207
	v_pk_add_f32 v[206:207], v[210:211], 0.5 op_sel_hi:[1,0]
	v_add_f32_e32 v156, 0.5, v156
	v_pk_mul_f32 v[206:207], v[206:207], v[216:217]
	v_pk_add_f32 v[208:209], v[208:209], 0.5 op_sel_hi:[1,0]
	v_pk_mul_f32 v[54:55], v[54:55], v[206:207]
	v_rcp_f32_e32 v206, v156
	v_cvt_f32_ubyte0_e32 v156, v205
	v_pk_mul_f32 v[208:209], v[208:209], v[212:213]
	v_add_f32_e32 v156, 0.5, v156
	v_pk_mul_f32 v[52:53], v[52:53], v[208:209]
	v_rcp_f32_e32 v208, v156
	v_cvt_f32_ubyte1_e32 v156, v204
	v_add_f32_e32 v156, 0.5, v156
	v_rcp_f32_e32 v207, v156
	v_cvt_f32_ubyte1_e32 v156, v205
	v_add_f32_e32 v156, 0.5, v156
	v_rcp_f32_e32 v209, v156
	v_cvt_f32_ubyte2_e32 v156, v204
	v_add_f32_e32 v156, 0.5, v156
	v_rcp_f32_e32 v210, v156
	v_cvt_f32_ubyte2_e32 v156, v205
	v_add_f32_e32 v156, 0.5, v156
	v_rcp_f32_e32 v212, v156
	v_cvt_f32_ubyte3_e32 v156, v204
	v_add_f32_e32 v156, 0.5, v156
	v_rcp_f32_e32 v211, v156
	v_cvt_f32_ubyte3_e32 v156, v205
	v_add_f32_e32 v156, 0.5, v156
	v_cvt_f32_ubyte1_e32 v205, v202
	v_cvt_f32_ubyte0_e32 v204, v202
	v_cvt_f32_ubyte3_e32 v215, v202
	v_cvt_f32_ubyte2_e32 v214, v202
	v_rcp_f32_e32 v213, v156
	v_pk_add_f32 v[214:215], v[214:215], 0.5 op_sel_hi:[1,0]
	v_pk_add_f32 v[204:205], v[204:205], 0.5 op_sel_hi:[1,0]
	v_cvt_f32_ubyte0_e32 v156, v200
	v_pk_mul_f32 v[204:205], v[204:205], v[206:207]
	v_pk_mul_f32 v[206:207], v[214:215], v[210:211]
	v_pk_mul_f32 v[24:25], v[24:25], v[204:205]
	v_pk_mul_f32 v[26:27], v[26:27], v[206:207]
	v_cvt_f32_ubyte3_e32 v207, v203
	v_cvt_f32_ubyte2_e32 v206, v203
	v_cvt_f32_ubyte1_e32 v205, v203
	v_cvt_f32_ubyte0_e32 v204, v203
	v_pk_add_f32 v[202:203], v[206:207], 0.5 op_sel_hi:[1,0]
	v_add_f32_e32 v156, 0.5, v156
	v_pk_mul_f32 v[202:203], v[202:203], v[212:213]
	v_pk_add_f32 v[204:205], v[204:205], 0.5 op_sel_hi:[1,0]
	v_pk_mul_f32 v[30:31], v[30:31], v[202:203]
	v_rcp_f32_e32 v202, v156
	v_cvt_f32_ubyte0_e32 v156, v201
	v_pk_mul_f32 v[204:205], v[204:205], v[208:209]
	v_add_f32_e32 v156, 0.5, v156
	v_pk_mul_f32 v[28:29], v[28:29], v[204:205]
	v_rcp_f32_e32 v204, v156
	v_cvt_f32_ubyte1_e32 v156, v200
	v_add_f32_e32 v156, 0.5, v156
	v_rcp_f32_e32 v203, v156
	v_cvt_f32_ubyte1_e32 v156, v201
	v_add_f32_e32 v156, 0.5, v156
	v_rcp_f32_e32 v205, v156
	v_cvt_f32_ubyte2_e32 v156, v200
	v_add_f32_e32 v156, 0.5, v156
	v_rcp_f32_e32 v206, v156
	v_cvt_f32_ubyte2_e32 v156, v201
	v_add_f32_e32 v156, 0.5, v156
	v_rcp_f32_e32 v208, v156
	v_cvt_f32_ubyte3_e32 v156, v200
	v_add_f32_e32 v156, 0.5, v156
	v_rcp_f32_e32 v207, v156
	v_cvt_f32_ubyte3_e32 v156, v201
	v_add_f32_e32 v156, 0.5, v156
	v_cvt_f32_ubyte1_e32 v201, v198
	v_cvt_f32_ubyte0_e32 v200, v198
	v_cvt_f32_ubyte3_e32 v211, v198
	v_cvt_f32_ubyte2_e32 v210, v198
	v_rcp_f32_e32 v209, v156
	v_pk_add_f32 v[210:211], v[210:211], 0.5 op_sel_hi:[1,0]
	v_pk_add_f32 v[200:201], v[200:201], 0.5 op_sel_hi:[1,0]
	v_cvt_f32_ubyte0_e32 v156, v196
	v_pk_mul_f32 v[200:201], v[200:201], v[202:203]
	v_pk_mul_f32 v[202:203], v[210:211], v[206:207]
	v_pk_mul_f32 v[56:57], v[56:57], v[200:201]
	v_pk_mul_f32 v[58:59], v[58:59], v[202:203]
	v_cvt_f32_ubyte3_e32 v203, v199
	v_cvt_f32_ubyte2_e32 v202, v199
	v_cvt_f32_ubyte1_e32 v201, v199
	v_cvt_f32_ubyte0_e32 v200, v199
	v_pk_add_f32 v[198:199], v[202:203], 0.5 op_sel_hi:[1,0]
	v_add_f32_e32 v156, 0.5, v156
	v_pk_mul_f32 v[198:199], v[198:199], v[208:209]
	v_pk_add_f32 v[200:201], v[200:201], 0.5 op_sel_hi:[1,0]
	v_pk_mul_f32 v[62:63], v[62:63], v[198:199]
	v_rcp_f32_e32 v198, v156
	v_cvt_f32_ubyte0_e32 v156, v197
	v_pk_mul_f32 v[200:201], v[200:201], v[204:205]
	v_add_f32_e32 v156, 0.5, v156
	v_pk_mul_f32 v[60:61], v[60:61], v[200:201]
	v_rcp_f32_e32 v200, v156
	v_cvt_f32_ubyte1_e32 v156, v196
	v_add_f32_e32 v156, 0.5, v156
	v_rcp_f32_e32 v199, v156
	v_cvt_f32_ubyte1_e32 v156, v197
	v_add_f32_e32 v156, 0.5, v156
	v_rcp_f32_e32 v201, v156
	v_cvt_f32_ubyte2_e32 v156, v196
	v_add_f32_e32 v156, 0.5, v156
	v_rcp_f32_e32 v202, v156
	v_cvt_f32_ubyte2_e32 v156, v197
	v_addc_co_u32_e64 v1, s[2:3], 0, v1, s[2:3]
	v_add_f32_e32 v156, 0.5, v156
	v_add_co_u32_e64 v6, s[2:3], s85, v2
	v_rcp_f32_e32 v204, v156
	v_cvt_f32_ubyte3_e32 v156, v196
	v_addc_co_u32_e64 v7, s[2:3], 0, v3, s[2:3]
	v_add_f32_e32 v156, 0.5, v156
	global_load_dwordx2 v[178:179], v[0:1], off
	global_load_dwordx2 v[180:181], v[6:7], off
	global_load_dwordx2 v[174:175], v[0:1], off offset:512
	global_load_dwordx2 v[176:177], v[6:7], off offset:512
	global_load_dwordx2 v[170:171], v[0:1], off offset:1024
	global_load_dwordx2 v[172:173], v[6:7], off offset:1024
	global_load_dwordx2 v[144:145], v[0:1], off offset:1536
	global_load_dwordx2 v[146:147], v[6:7], off offset:1536
	global_load_dwordx2 v[12:13], v[0:1], off offset:2048
	global_load_dwordx2 v[14:15], v[6:7], off offset:2048
	global_load_dwordx2 v[8:9], v[0:1], off offset:2560
	global_load_dwordx2 v[10:11], v[6:7], off offset:2560
	global_load_dwordx2 v[2:3], v[0:1], off offset:3072
	global_load_dwordx2 v[4:5], v[6:7], off offset:3072
	s_nop 0
	global_load_dwordx2 v[0:1], v[0:1], off offset:3584
	s_nop 0
	global_load_dwordx2 v[6:7], v[6:7], off offset:3584
	v_rcp_f32_e32 v203, v156
	v_cvt_f32_ubyte3_e32 v156, v197
	v_add_f32_e32 v156, 0.5, v156
	v_cvt_f32_ubyte1_e32 v197, v194
	v_cvt_f32_ubyte0_e32 v196, v194
	v_cvt_f32_ubyte3_e32 v207, v194
	v_cvt_f32_ubyte2_e32 v206, v194
	v_rcp_f32_e32 v205, v156
	v_pk_add_f32 v[206:207], v[206:207], 0.5 op_sel_hi:[1,0]
	v_pk_add_f32 v[196:197], v[196:197], 0.5 op_sel_hi:[1,0]
	v_cvt_f32_ubyte0_e32 v156, v192
	v_pk_mul_f32 v[196:197], v[196:197], v[198:199]
	v_pk_mul_f32 v[198:199], v[206:207], v[202:203]
	v_pk_mul_f32 v[32:33], v[32:33], v[196:197]
	v_pk_mul_f32 v[34:35], v[34:35], v[198:199]
	v_cvt_f32_ubyte3_e32 v199, v195
	v_cvt_f32_ubyte2_e32 v198, v195
	v_cvt_f32_ubyte1_e32 v197, v195
	v_cvt_f32_ubyte0_e32 v196, v195
	v_pk_add_f32 v[194:195], v[198:199], 0.5 op_sel_hi:[1,0]
	v_add_f32_e32 v156, 0.5, v156
	v_pk_mul_f32 v[194:195], v[194:195], v[204:205]
	v_pk_add_f32 v[196:197], v[196:197], 0.5 op_sel_hi:[1,0]
	v_pk_mul_f32 v[38:39], v[38:39], v[194:195]
	v_rcp_f32_e32 v194, v156
	v_cvt_f32_ubyte0_e32 v156, v193
	v_pk_mul_f32 v[196:197], v[196:197], v[200:201]
	v_add_f32_e32 v156, 0.5, v156
	v_pk_mul_f32 v[36:37], v[36:37], v[196:197]
	v_rcp_f32_e32 v196, v156
	v_cvt_f32_ubyte1_e32 v156, v192
	v_add_f32_e32 v156, 0.5, v156
	v_rcp_f32_e32 v195, v156
	v_cvt_f32_ubyte1_e32 v156, v193
	v_add_f32_e32 v156, 0.5, v156
	v_rcp_f32_e32 v197, v156
	v_cvt_f32_ubyte2_e32 v156, v192
	v_add_f32_e32 v156, 0.5, v156
	v_rcp_f32_e32 v198, v156
	v_cvt_f32_ubyte2_e32 v156, v193
	v_add_f32_e32 v156, 0.5, v156
	v_rcp_f32_e32 v200, v156
	v_cvt_f32_ubyte3_e32 v156, v192
	v_add_f32_e32 v156, 0.5, v156
	v_rcp_f32_e32 v199, v156
	v_cvt_f32_ubyte3_e32 v156, v193
	v_add_f32_e32 v156, 0.5, v156
	v_cvt_f32_ubyte1_e32 v193, v190
	v_cvt_f32_ubyte0_e32 v192, v190
	v_cvt_f32_ubyte3_e32 v203, v190
	v_cvt_f32_ubyte2_e32 v202, v190
	v_rcp_f32_e32 v201, v156
	v_pk_add_f32 v[202:203], v[202:203], 0.5 op_sel_hi:[1,0]
	v_pk_add_f32 v[192:193], v[192:193], 0.5 op_sel_hi:[1,0]
	v_cvt_f32_ubyte0_e32 v156, v188
	v_pk_mul_f32 v[192:193], v[192:193], v[194:195]
	v_pk_mul_f32 v[194:195], v[202:203], v[198:199]
	v_pk_mul_f32 v[64:65], v[64:65], v[192:193]
	v_pk_mul_f32 v[66:67], v[66:67], v[194:195]
	v_cvt_f32_ubyte3_e32 v195, v191
	v_cvt_f32_ubyte2_e32 v194, v191
	v_cvt_f32_ubyte1_e32 v193, v191
	v_cvt_f32_ubyte0_e32 v192, v191
	v_pk_add_f32 v[190:191], v[194:195], 0.5 op_sel_hi:[1,0]
	v_add_f32_e32 v156, 0.5, v156
	v_pk_mul_f32 v[190:191], v[190:191], v[200:201]
	v_pk_add_f32 v[192:193], v[192:193], 0.5 op_sel_hi:[1,0]
	v_pk_mul_f32 v[70:71], v[70:71], v[190:191]
	v_rcp_f32_e32 v190, v156
	v_cvt_f32_ubyte0_e32 v156, v189
	v_pk_mul_f32 v[192:193], v[192:193], v[196:197]
	v_add_f32_e32 v156, 0.5, v156
	v_pk_mul_f32 v[68:69], v[68:69], v[192:193]
	v_rcp_f32_e32 v192, v156
	v_cvt_f32_ubyte1_e32 v156, v188
	v_add_f32_e32 v156, 0.5, v156
	v_rcp_f32_e32 v191, v156
	v_cvt_f32_ubyte1_e32 v156, v189
	v_add_f32_e32 v156, 0.5, v156
	v_rcp_f32_e32 v193, v156
	v_cvt_f32_ubyte2_e32 v156, v188
	v_add_f32_e32 v156, 0.5, v156
	v_rcp_f32_e32 v194, v156
	v_cvt_f32_ubyte2_e32 v156, v189
	v_add_f32_e32 v156, 0.5, v156
	v_rcp_f32_e32 v196, v156
	v_cvt_f32_ubyte3_e32 v156, v188
	v_add_f32_e32 v156, 0.5, v156
	v_rcp_f32_e32 v195, v156
	v_cvt_f32_ubyte3_e32 v156, v189
	v_add_f32_e32 v156, 0.5, v156
	v_cvt_f32_ubyte1_e32 v189, v186
	v_cvt_f32_ubyte0_e32 v188, v186
	v_cvt_f32_ubyte3_e32 v199, v186
	v_cvt_f32_ubyte2_e32 v198, v186
	v_rcp_f32_e32 v197, v156
	v_pk_add_f32 v[198:199], v[198:199], 0.5 op_sel_hi:[1,0]
	v_pk_add_f32 v[188:189], v[188:189], 0.5 op_sel_hi:[1,0]
	v_cvt_f32_ubyte0_e32 v156, v184
	v_pk_mul_f32 v[188:189], v[188:189], v[190:191]
	v_pk_mul_f32 v[190:191], v[198:199], v[194:195]
	v_pk_mul_f32 v[40:41], v[40:41], v[188:189]
	v_pk_mul_f32 v[42:43], v[42:43], v[190:191]
	v_cvt_f32_ubyte3_e32 v191, v187
	v_cvt_f32_ubyte2_e32 v190, v187
	v_cvt_f32_ubyte1_e32 v189, v187
	v_cvt_f32_ubyte0_e32 v188, v187
	v_pk_add_f32 v[186:187], v[190:191], 0.5 op_sel_hi:[1,0]
	v_add_f32_e32 v156, 0.5, v156
	v_pk_mul_f32 v[186:187], v[186:187], v[196:197]
	v_pk_add_f32 v[188:189], v[188:189], 0.5 op_sel_hi:[1,0]
	v_pk_mul_f32 v[46:47], v[46:47], v[186:187]
	v_rcp_f32_e32 v186, v156
	v_cvt_f32_ubyte0_e32 v156, v185
	v_pk_mul_f32 v[188:189], v[188:189], v[192:193]
	v_add_f32_e32 v156, 0.5, v156
	v_pk_mul_f32 v[44:45], v[44:45], v[188:189]
	v_rcp_f32_e32 v188, v156
	v_cvt_f32_ubyte1_e32 v156, v184
	v_add_f32_e32 v156, 0.5, v156
	v_rcp_f32_e32 v187, v156
	v_cvt_f32_ubyte1_e32 v156, v185
	v_add_f32_e32 v156, 0.5, v156
	v_rcp_f32_e32 v189, v156
	v_cvt_f32_ubyte2_e32 v156, v184
	v_add_f32_e32 v156, 0.5, v156
	v_rcp_f32_e32 v190, v156
	v_cvt_f32_ubyte2_e32 v156, v185
	v_add_f32_e32 v156, 0.5, v156
	v_rcp_f32_e32 v192, v156
	v_cvt_f32_ubyte3_e32 v156, v184
	v_add_f32_e32 v156, 0.5, v156
	v_rcp_f32_e32 v191, v156
	v_cvt_f32_ubyte3_e32 v156, v185
	v_add_f32_e32 v156, 0.5, v156
	v_cvt_f32_ubyte1_e32 v185, v182
	v_cvt_f32_ubyte0_e32 v184, v182
	v_cvt_f32_ubyte3_e32 v195, v182
	v_cvt_f32_ubyte2_e32 v194, v182
	v_rcp_f32_e32 v193, v156
	v_pk_add_f32 v[194:195], v[194:195], 0.5 op_sel_hi:[1,0]
	v_pk_add_f32 v[184:185], v[184:185], 0.5 op_sel_hi:[1,0]
	s_waitcnt vmcnt(0)
	v_cvt_f32_ubyte0_e32 v156, v180
	v_pk_mul_f32 v[184:185], v[184:185], v[186:187]
	v_pk_mul_f32 v[186:187], v[194:195], v[190:191]
	v_pk_mul_f32 v[72:73], v[72:73], v[184:185]
	v_pk_mul_f32 v[74:75], v[74:75], v[186:187]
	v_cvt_f32_ubyte3_e32 v187, v183
	v_cvt_f32_ubyte2_e32 v186, v183
	v_cvt_f32_ubyte1_e32 v185, v183
	v_cvt_f32_ubyte0_e32 v184, v183
	v_pk_add_f32 v[182:183], v[186:187], 0.5 op_sel_hi:[1,0]
	v_add_f32_e32 v156, 0.5, v156
	v_pk_mul_f32 v[182:183], v[182:183], v[192:193]
	v_pk_add_f32 v[184:185], v[184:185], 0.5 op_sel_hi:[1,0]
	v_pk_mul_f32 v[78:79], v[78:79], v[182:183]
	v_rcp_f32_e32 v182, v156
	v_cvt_f32_ubyte0_e32 v156, v181
	v_pk_mul_f32 v[184:185], v[184:185], v[188:189]
	v_add_f32_e32 v156, 0.5, v156
	v_pk_mul_f32 v[76:77], v[76:77], v[184:185]
	v_rcp_f32_e32 v184, v156
	v_cvt_f32_ubyte1_e32 v156, v180
	v_add_f32_e32 v156, 0.5, v156
	v_rcp_f32_e32 v183, v156
	v_cvt_f32_ubyte1_e32 v156, v181
	v_add_f32_e32 v156, 0.5, v156
	v_rcp_f32_e32 v185, v156
	v_cvt_f32_ubyte2_e32 v156, v180
	v_add_f32_e32 v156, 0.5, v156
	v_rcp_f32_e32 v186, v156
	v_cvt_f32_ubyte2_e32 v156, v181
	v_add_f32_e32 v156, 0.5, v156
	v_rcp_f32_e32 v188, v156
	v_cvt_f32_ubyte3_e32 v156, v180
	v_add_f32_e32 v156, 0.5, v156
	v_rcp_f32_e32 v187, v156
	v_cvt_f32_ubyte3_e32 v156, v181
	v_add_f32_e32 v156, 0.5, v156
	v_cvt_f32_ubyte1_e32 v181, v178
	v_cvt_f32_ubyte0_e32 v180, v178
	v_cvt_f32_ubyte3_e32 v191, v178
	v_cvt_f32_ubyte2_e32 v190, v178
	v_rcp_f32_e32 v189, v156
	v_pk_add_f32 v[190:191], v[190:191], 0.5 op_sel_hi:[1,0]
	v_pk_add_f32 v[180:181], v[180:181], 0.5 op_sel_hi:[1,0]
	v_cvt_f32_ubyte0_e32 v156, v176
	v_pk_mul_f32 v[180:181], v[180:181], v[182:183]
	v_pk_mul_f32 v[182:183], v[190:191], v[186:187]
	v_pk_mul_f32 v[80:81], v[80:81], v[180:181]
	v_pk_mul_f32 v[82:83], v[82:83], v[182:183]
	v_cvt_f32_ubyte3_e32 v183, v179
	v_cvt_f32_ubyte2_e32 v182, v179
	v_cvt_f32_ubyte1_e32 v181, v179
	v_cvt_f32_ubyte0_e32 v180, v179
	v_pk_add_f32 v[178:179], v[182:183], 0.5 op_sel_hi:[1,0]
	v_add_f32_e32 v156, 0.5, v156
	v_pk_mul_f32 v[178:179], v[178:179], v[188:189]
	v_pk_add_f32 v[180:181], v[180:181], 0.5 op_sel_hi:[1,0]
	v_pk_mul_f32 v[86:87], v[86:87], v[178:179]
	v_rcp_f32_e32 v178, v156
	v_cvt_f32_ubyte0_e32 v156, v177
	v_pk_mul_f32 v[180:181], v[180:181], v[184:185]
	v_add_f32_e32 v156, 0.5, v156
	v_pk_mul_f32 v[84:85], v[84:85], v[180:181]
	v_rcp_f32_e32 v180, v156
	v_cvt_f32_ubyte1_e32 v156, v176
	v_add_f32_e32 v156, 0.5, v156
	v_rcp_f32_e32 v179, v156
	v_cvt_f32_ubyte1_e32 v156, v177
	v_add_f32_e32 v156, 0.5, v156
	v_rcp_f32_e32 v181, v156
	v_cvt_f32_ubyte2_e32 v156, v176
	v_add_f32_e32 v156, 0.5, v156
	v_rcp_f32_e32 v182, v156
	v_cvt_f32_ubyte2_e32 v156, v177
	v_add_f32_e32 v156, 0.5, v156
	v_rcp_f32_e32 v184, v156
	v_cvt_f32_ubyte3_e32 v156, v176
	v_add_f32_e32 v156, 0.5, v156
	v_rcp_f32_e32 v183, v156
	v_cvt_f32_ubyte3_e32 v156, v177
	v_add_f32_e32 v156, 0.5, v156
	v_cvt_f32_ubyte1_e32 v177, v174
	v_cvt_f32_ubyte0_e32 v176, v174
	v_cvt_f32_ubyte3_e32 v187, v174
	v_cvt_f32_ubyte2_e32 v186, v174
	v_rcp_f32_e32 v185, v156
	v_pk_add_f32 v[186:187], v[186:187], 0.5 op_sel_hi:[1,0]
	v_pk_add_f32 v[176:177], v[176:177], 0.5 op_sel_hi:[1,0]
	v_cvt_f32_ubyte0_e32 v156, v172
	v_pk_mul_f32 v[176:177], v[176:177], v[178:179]
	v_pk_mul_f32 v[178:179], v[186:187], v[182:183]
	v_pk_mul_f32 v[112:113], v[112:113], v[176:177]
	v_pk_mul_f32 v[114:115], v[114:115], v[178:179]
	v_cvt_f32_ubyte3_e32 v179, v175
	v_cvt_f32_ubyte2_e32 v178, v175
	v_cvt_f32_ubyte1_e32 v177, v175
	v_cvt_f32_ubyte0_e32 v176, v175
	v_pk_add_f32 v[174:175], v[178:179], 0.5 op_sel_hi:[1,0]
	v_add_f32_e32 v156, 0.5, v156
	v_pk_mul_f32 v[174:175], v[174:175], v[184:185]
	v_pk_add_f32 v[176:177], v[176:177], 0.5 op_sel_hi:[1,0]
	v_pk_mul_f32 v[118:119], v[118:119], v[174:175]
	v_rcp_f32_e32 v174, v156
	v_cvt_f32_ubyte0_e32 v156, v173
	v_pk_mul_f32 v[176:177], v[176:177], v[180:181]
	v_add_f32_e32 v156, 0.5, v156
	v_pk_mul_f32 v[116:117], v[116:117], v[176:177]
	v_rcp_f32_e32 v176, v156
	v_cvt_f32_ubyte1_e32 v156, v172
	v_add_f32_e32 v156, 0.5, v156
	v_rcp_f32_e32 v175, v156
	v_cvt_f32_ubyte1_e32 v156, v173
	v_add_f32_e32 v156, 0.5, v156
	v_rcp_f32_e32 v177, v156
	v_cvt_f32_ubyte2_e32 v156, v172
	v_add_f32_e32 v156, 0.5, v156
	v_rcp_f32_e32 v178, v156
	v_cvt_f32_ubyte2_e32 v156, v173
	v_add_f32_e32 v156, 0.5, v156
	v_rcp_f32_e32 v180, v156
	v_cvt_f32_ubyte3_e32 v156, v172
	v_add_f32_e32 v156, 0.5, v156
	v_rcp_f32_e32 v179, v156
	v_cvt_f32_ubyte3_e32 v156, v173
	v_add_f32_e32 v156, 0.5, v156
	v_cvt_f32_ubyte1_e32 v173, v170
	v_cvt_f32_ubyte0_e32 v172, v170
	v_cvt_f32_ubyte3_e32 v183, v170
	v_cvt_f32_ubyte2_e32 v182, v170
	v_rcp_f32_e32 v181, v156
	v_pk_add_f32 v[182:183], v[182:183], 0.5 op_sel_hi:[1,0]
	v_pk_add_f32 v[172:173], v[172:173], 0.5 op_sel_hi:[1,0]
	v_cvt_f32_ubyte0_e32 v156, v146
	v_pk_mul_f32 v[172:173], v[172:173], v[174:175]
	v_pk_mul_f32 v[174:175], v[182:183], v[178:179]
	v_pk_mul_f32 v[88:89], v[88:89], v[172:173]
	v_pk_mul_f32 v[90:91], v[90:91], v[174:175]
	v_cvt_f32_ubyte3_e32 v175, v171
	v_cvt_f32_ubyte2_e32 v174, v171
	v_cvt_f32_ubyte1_e32 v173, v171
	v_cvt_f32_ubyte0_e32 v172, v171
	v_pk_add_f32 v[170:171], v[174:175], 0.5 op_sel_hi:[1,0]
	v_add_f32_e32 v156, 0.5, v156
	v_pk_mul_f32 v[170:171], v[170:171], v[180:181]
	v_pk_add_f32 v[172:173], v[172:173], 0.5 op_sel_hi:[1,0]
	v_pk_mul_f32 v[94:95], v[94:95], v[170:171]
	v_rcp_f32_e32 v170, v156
	v_cvt_f32_ubyte0_e32 v156, v147
	v_pk_mul_f32 v[172:173], v[172:173], v[176:177]
	v_add_f32_e32 v156, 0.5, v156
	v_pk_mul_f32 v[92:93], v[92:93], v[172:173]
	v_rcp_f32_e32 v172, v156
	v_cvt_f32_ubyte1_e32 v156, v146
	v_add_f32_e32 v156, 0.5, v156
	v_rcp_f32_e32 v171, v156
	v_cvt_f32_ubyte1_e32 v156, v147
	v_add_f32_e32 v156, 0.5, v156
	v_rcp_f32_e32 v173, v156
	v_cvt_f32_ubyte2_e32 v156, v146
	v_cvt_f32_ubyte3_e32 v146, v146
	v_add_f32_e32 v156, 0.5, v156
	v_add_f32_e32 v146, 0.5, v146
	v_rcp_f32_e32 v174, v156
	v_rcp_f32_e32 v175, v146
	v_cvt_f32_ubyte3_e32 v146, v147
	v_cvt_f32_ubyte2_e32 v156, v147
	v_add_f32_e32 v146, 0.5, v146
	v_add_f32_e32 v156, 0.5, v156
	v_rcp_f32_e32 v177, v146
	v_cvt_f32_ubyte1_e32 v147, v144
	v_cvt_f32_ubyte0_e32 v146, v144
	v_cvt_f32_ubyte3_e32 v179, v144
	v_cvt_f32_ubyte2_e32 v178, v144
	v_rcp_f32_e32 v176, v156
	v_pk_add_f32 v[178:179], v[178:179], 0.5 op_sel_hi:[1,0]
	v_pk_add_f32 v[146:147], v[146:147], 0.5 op_sel_hi:[1,0]
	v_cvt_f32_ubyte2_e32 v156, v14
	v_pk_mul_f32 v[146:147], v[146:147], v[170:171]
	v_pk_mul_f32 v[170:171], v[178:179], v[174:175]
	v_pk_mul_f32 v[120:121], v[120:121], v[146:147]
	v_pk_mul_f32 v[122:123], v[122:123], v[170:171]
	v_cvt_f32_ubyte3_e32 v171, v145
	v_cvt_f32_ubyte2_e32 v170, v145
	v_cvt_f32_ubyte1_e32 v147, v145
	v_cvt_f32_ubyte0_e32 v146, v145
	v_pk_add_f32 v[144:145], v[170:171], 0.5 op_sel_hi:[1,0]
	v_pk_add_f32 v[146:147], v[146:147], 0.5 op_sel_hi:[1,0]
	v_pk_mul_f32 v[144:145], v[144:145], v[176:177]
	v_pk_mul_f32 v[146:147], v[146:147], v[172:173]
	v_pk_mul_f32 v[126:127], v[126:127], v[144:145]
	v_cvt_f32_ubyte0_e32 v145, v15
	v_add_f32_e32 v145, 0.5, v145
	v_pk_mul_f32 v[124:125], v[124:125], v[146:147]
	v_cvt_f32_ubyte0_e32 v144, v14
	v_rcp_f32_e32 v146, v145
	v_cvt_f32_ubyte1_e32 v145, v14
	v_cvt_f32_ubyte3_e32 v14, v14
	v_add_f32_e32 v144, 0.5, v144
	v_add_f32_e32 v145, 0.5, v145
	v_add_f32_e32 v156, 0.5, v156
	v_add_f32_e32 v14, 0.5, v14
	v_rcp_f32_e32 v144, v144
	v_rcp_f32_e32 v145, v145
	v_rcp_f32_e32 v170, v156
	v_rcp_f32_e32 v171, v14
	v_cvt_f32_ubyte3_e32 v14, v15
	v_cvt_f32_ubyte2_e32 v156, v15
	v_add_f32_e32 v14, 0.5, v14
	v_cvt_f32_ubyte1_e32 v147, v15
	v_add_f32_e32 v156, 0.5, v156
	v_rcp_f32_e32 v173, v14
	v_cvt_f32_ubyte1_e32 v15, v12
	v_cvt_f32_ubyte0_e32 v14, v12
	v_cvt_f32_ubyte3_e32 v175, v12
	v_cvt_f32_ubyte2_e32 v174, v12
	v_rcp_f32_e32 v172, v156
	v_pk_add_f32 v[174:175], v[174:175], 0.5 op_sel_hi:[1,0]
	v_pk_add_f32 v[14:15], v[14:15], 0.5 op_sel_hi:[1,0]
	v_add_f32_e32 v147, 0.5, v147
	v_pk_mul_f32 v[14:15], v[14:15], v[144:145]
	v_pk_mul_f32 v[144:145], v[174:175], v[170:171]
	v_rcp_f32_e32 v147, v147
	v_pk_mul_f32 v[98:99], v[98:99], v[144:145]
	v_cvt_f32_ubyte3_e32 v145, v13
	v_cvt_f32_ubyte2_e32 v144, v13
	v_pk_mul_f32 v[96:97], v[96:97], v[14:15]
	v_cvt_f32_ubyte1_e32 v15, v13
	v_cvt_f32_ubyte0_e32 v14, v13
	v_pk_add_f32 v[12:13], v[144:145], 0.5 op_sel_hi:[1,0]
	v_pk_add_f32 v[14:15], v[14:15], 0.5 op_sel_hi:[1,0]
	v_pk_mul_f32 v[12:13], v[12:13], v[172:173]
	v_pk_mul_f32 v[14:15], v[14:15], v[146:147]
	v_pk_mul_f32 v[102:103], v[102:103], v[12:13]
	v_cvt_f32_ubyte0_e32 v13, v11
	v_add_f32_e32 v13, 0.5, v13
	v_pk_mul_f32 v[100:101], v[100:101], v[14:15]
	v_cvt_f32_ubyte0_e32 v12, v10
	v_rcp_f32_e32 v14, v13
	v_cvt_f32_ubyte1_e32 v13, v10
	v_cvt_f32_ubyte2_e32 v144, v10
	v_cvt_f32_ubyte2_e32 v145, v11
	v_cvt_f32_ubyte3_e32 v10, v10
	v_add_f32_e32 v12, 0.5, v12
	v_add_f32_e32 v13, 0.5, v13
	v_add_f32_e32 v144, 0.5, v144
	v_add_f32_e32 v145, 0.5, v145
	v_add_f32_e32 v10, 0.5, v10
	v_rcp_f32_e32 v12, v12
	v_rcp_f32_e32 v13, v13
	v_rcp_f32_e32 v144, v144
	v_rcp_f32_e32 v146, v145
	v_rcp_f32_e32 v145, v10
	v_cvt_f32_ubyte3_e32 v10, v11
	v_add_f32_e32 v10, 0.5, v10
	v_cvt_f32_ubyte1_e32 v15, v11
	v_rcp_f32_e32 v147, v10
	v_cvt_f32_ubyte1_e32 v11, v8
	v_cvt_f32_ubyte0_e32 v10, v8
	v_cvt_f32_ubyte3_e32 v171, v8
	v_cvt_f32_ubyte2_e32 v170, v8
	v_pk_add_f32 v[170:171], v[170:171], 0.5 op_sel_hi:[1,0]
	v_pk_add_f32 v[10:11], v[10:11], 0.5 op_sel_hi:[1,0]
	v_add_f32_e32 v15, 0.5, v15
	v_pk_mul_f32 v[10:11], v[10:11], v[12:13]
	v_pk_mul_f32 v[12:13], v[170:171], v[144:145]
	v_rcp_f32_e32 v15, v15
	v_pk_mul_f32 v[130:131], v[130:131], v[12:13]
	v_cvt_f32_ubyte3_e32 v13, v9
	v_cvt_f32_ubyte2_e32 v12, v9
	v_pk_mul_f32 v[128:129], v[128:129], v[10:11]
	v_cvt_f32_ubyte1_e32 v11, v9
	v_cvt_f32_ubyte0_e32 v10, v9
	v_pk_add_f32 v[8:9], v[12:13], 0.5 op_sel_hi:[1,0]
	v_pk_add_f32 v[10:11], v[10:11], 0.5 op_sel_hi:[1,0]
	v_pk_mul_f32 v[8:9], v[8:9], v[146:147]
	v_pk_mul_f32 v[10:11], v[10:11], v[14:15]
	v_pk_mul_f32 v[134:135], v[134:135], v[8:9]
	v_cvt_f32_ubyte0_e32 v9, v5
	v_add_f32_e32 v9, 0.5, v9
	v_pk_mul_f32 v[132:133], v[132:133], v[10:11]
	v_cvt_f32_ubyte0_e32 v8, v4
	v_rcp_f32_e32 v10, v9
	v_cvt_f32_ubyte1_e32 v9, v4
	v_cvt_f32_ubyte2_e32 v12, v4
	v_cvt_f32_ubyte2_e32 v13, v5
	v_cvt_f32_ubyte3_e32 v4, v4
	v_add_f32_e32 v8, 0.5, v8
	v_add_f32_e32 v9, 0.5, v9
	v_add_f32_e32 v12, 0.5, v12
	v_add_f32_e32 v13, 0.5, v13
	v_add_f32_e32 v4, 0.5, v4
	v_rcp_f32_e32 v8, v8
	v_rcp_f32_e32 v9, v9
	v_rcp_f32_e32 v12, v12
	v_rcp_f32_e32 v14, v13
	v_rcp_f32_e32 v13, v4
	v_cvt_f32_ubyte3_e32 v4, v5
	v_add_f32_e32 v4, 0.5, v4
	v_cvt_f32_ubyte1_e32 v11, v5
	v_rcp_f32_e32 v15, v4
	v_cvt_f32_ubyte1_e32 v5, v2
	v_cvt_f32_ubyte0_e32 v4, v2
	v_cvt_f32_ubyte3_e32 v145, v2
	v_cvt_f32_ubyte2_e32 v144, v2
	v_pk_add_f32 v[144:145], v[144:145], 0.5 op_sel_hi:[1,0]
	v_pk_add_f32 v[4:5], v[4:5], 0.5 op_sel_hi:[1,0]
	v_add_f32_e32 v11, 0.5, v11
	v_pk_mul_f32 v[4:5], v[4:5], v[8:9]
	v_pk_mul_f32 v[8:9], v[144:145], v[12:13]
	v_rcp_f32_e32 v11, v11
	v_pk_mul_f32 v[106:107], v[106:107], v[8:9]
	v_cvt_f32_ubyte3_e32 v9, v3
	v_cvt_f32_ubyte2_e32 v8, v3
	v_pk_mul_f32 v[104:105], v[104:105], v[4:5]
	v_cvt_f32_ubyte1_e32 v5, v3
	v_cvt_f32_ubyte0_e32 v4, v3
	v_pk_add_f32 v[2:3], v[8:9], 0.5 op_sel_hi:[1,0]
	v_pk_add_f32 v[4:5], v[4:5], 0.5 op_sel_hi:[1,0]
	v_pk_mul_f32 v[2:3], v[2:3], v[14:15]
	v_pk_mul_f32 v[4:5], v[4:5], v[10:11]
	v_pk_mul_f32 v[110:111], v[110:111], v[2:3]
	v_cvt_f32_ubyte0_e32 v3, v7
	v_add_f32_e32 v3, 0.5, v3
	v_pk_mul_f32 v[108:109], v[108:109], v[4:5]
	v_cvt_f32_ubyte0_e32 v2, v6
	v_rcp_f32_e32 v4, v3
	v_cvt_f32_ubyte1_e32 v3, v6
	v_cvt_f32_ubyte2_e32 v8, v6
	v_cvt_f32_ubyte2_e32 v9, v7
	v_cvt_f32_ubyte3_e32 v6, v6
	v_add_f32_e32 v2, 0.5, v2
	v_add_f32_e32 v3, 0.5, v3
	v_add_f32_e32 v8, 0.5, v8
	v_add_f32_e32 v9, 0.5, v9
	v_add_f32_e32 v6, 0.5, v6
	v_rcp_f32_e32 v2, v2
	v_rcp_f32_e32 v3, v3
	v_rcp_f32_e32 v8, v8
	v_rcp_f32_e32 v10, v9
	v_rcp_f32_e32 v9, v6
	v_cvt_f32_ubyte3_e32 v6, v7
	v_cvt_f32_ubyte1_e32 v5, v7
	v_add_f32_e32 v6, 0.5, v6
	v_add_f32_e32 v5, 0.5, v5
	v_rcp_f32_e32 v11, v6
	v_cvt_f32_ubyte1_e32 v7, v0
	v_cvt_f32_ubyte0_e32 v6, v0
	v_cvt_f32_ubyte3_e32 v13, v0
	v_cvt_f32_ubyte2_e32 v12, v0
	v_rcp_f32_e32 v5, v5
	v_pk_add_f32 v[12:13], v[12:13], 0.5 op_sel_hi:[1,0]
	v_pk_add_f32 v[6:7], v[6:7], 0.5 op_sel_hi:[1,0]
	s_nop 0
	v_pk_mul_f32 v[2:3], v[6:7], v[2:3]
	v_pk_mul_f32 v[6:7], v[12:13], v[8:9]
	v_pk_mul_f32 v[136:137], v[136:137], v[2:3]
	v_pk_mul_f32 v[138:139], v[138:139], v[6:7]
	v_cvt_f32_ubyte1_e32 v3, v1
	v_cvt_f32_ubyte0_e32 v2, v1
	v_cvt_f32_ubyte3_e32 v7, v1
	v_cvt_f32_ubyte2_e32 v6, v1
	v_pk_add_f32 v[0:1], v[6:7], 0.5 op_sel_hi:[1,0]
	v_pk_add_f32 v[2:3], v[2:3], 0.5 op_sel_hi:[1,0]
	v_pk_mul_f32 v[0:1], v[0:1], v[10:11]
	v_pk_mul_f32 v[2:3], v[2:3], v[4:5]
	v_pk_mul_f32 v[142:143], v[142:143], v[0:1]
	v_pk_mul_f32 v[140:141], v[140:141], v[2:3]
	ds_read_b128 v[8:11], v231
	ds_read_b128 v[12:15], v231 offset:1024
	ds_read_b128 v[0:3], v231 offset:2048
	ds_read_b128 v[4:7], v231 offset:3072
	s_add_u32 s2, s48, 0x40480
	s_addc_u32 s3, s49, 0
	s_mov_b32 m0, s94
	v_lshl_add_u64 v[144:145], s[2:3], 0, v[148:149]
	ds_read_b128 v[174:177], v228
	ds_read_b128 v[178:181], v228 offset:1024
	ds_read_b128 v[182:185], v228 offset:2048
	ds_read_b128 v[186:189], v228 offset:3072
	ds_read_b128 v[190:193], v228 offset:4096
	ds_read_b128 v[194:197], v228 offset:5120
	ds_read_b128 v[198:201], v228 offset:6144
	ds_read_b128 v[202:205], v228 offset:7168
	global_load_lds_dwordx4 v[144:145], off
	v_lshl_add_u64 v[144:145], s[2:3], 0, v[152:153]
	s_mov_b32 m0, s93
	s_nop 0
	global_load_lds_dwordx4 v[144:145], off
	s_waitcnt lgkmcnt(8)
	s_barrier
	s_waitcnt lgkmcnt(0)
	s_setprio 1
	s_waitcnt lgkmcnt(0)
	v_mfma_scale_f32_16x16x128_f8f6f4 v[16:19], v[8:15], v[174:181], v[16:19], v225, v225 op_sel_hi:[0,0,0]
	v_mfma_scale_f32_16x16x128_f8f6f4 v[20:23], v[0:7], v[174:181], v[20:23], v225, v225 op_sel_hi:[0,0,0]
	v_mfma_scale_f32_16x16x128_f8f6f4 v[24:27], v[8:15], v[182:189], v[24:27], v225, v225 op_sel_hi:[0,0,0]
	v_mfma_scale_f32_16x16x128_f8f6f4 v[28:31], v[0:7], v[182:189], v[28:31], v225, v225 op_sel_hi:[0,0,0]
	v_mfma_scale_f32_16x16x128_f8f6f4 v[32:35], v[8:15], v[190:197], v[32:35], v225, v225 op_sel_hi:[0,0,0]
	v_mfma_scale_f32_16x16x128_f8f6f4 v[36:39], v[0:7], v[190:197], v[36:39], v225, v225 op_sel_hi:[0,0,0]
	v_mfma_scale_f32_16x16x128_f8f6f4 v[40:43], v[8:15], v[198:205], v[40:43], v225, v225 op_sel_hi:[0,0,0]
	v_mfma_scale_f32_16x16x128_f8f6f4 v[44:47], v[0:7], v[198:205], v[44:47], v225, v225 op_sel_hi:[0,0,0]
	s_setprio 0
	s_barrier
	v_lshl_add_u64 v[170:171], s[50:51], 0, v[150:151]
	s_mov_b32 m0, s96
	v_lshl_add_u64 v[144:145], v[170:171], 0, s[22:23]
	v_lshl_add_u64 v[172:173], s[50:51], 0, v[154:155]
	ds_read_b128 v[206:209], v232
	ds_read_b128 v[210:213], v232 offset:1024
	ds_read_b128 v[214:217], v232 offset:2048
	ds_read_b128 v[218:221], v232 offset:3072
	global_load_lds_dwordx4 v[144:145], off
	v_lshl_add_u64 v[144:145], v[172:173], 0, s[22:23]
	s_mov_b32 m0, s95
	s_nop 0
	global_load_lds_dwordx4 v[144:145], off
	s_barrier
	s_waitcnt lgkmcnt(0)
	s_setprio 1
	s_waitcnt lgkmcnt(0)
	v_mfma_scale_f32_16x16x128_f8f6f4 v[48:51], v[206:213], v[174:181], v[48:51], v225, v225 op_sel_hi:[0,0,0]
	v_mfma_scale_f32_16x16x128_f8f6f4 v[52:55], v[214:221], v[174:181], v[52:55], v225, v225 op_sel_hi:[0,0,0]
	v_mfma_scale_f32_16x16x128_f8f6f4 v[56:59], v[206:213], v[182:189], v[56:59], v225, v225 op_sel_hi:[0,0,0]
	v_mfma_scale_f32_16x16x128_f8f6f4 v[60:63], v[214:221], v[182:189], v[60:63], v225, v225 op_sel_hi:[0,0,0]
	v_mfma_scale_f32_16x16x128_f8f6f4 v[64:67], v[206:213], v[190:197], v[64:67], v225, v225 op_sel_hi:[0,0,0]
	v_mfma_scale_f32_16x16x128_f8f6f4 v[68:71], v[214:221], v[190:197], v[68:71], v225, v225 op_sel_hi:[0,0,0]
	v_mfma_scale_f32_16x16x128_f8f6f4 v[72:75], v[206:213], v[198:205], v[72:75], v225, v225 op_sel_hi:[0,0,0]
	v_mfma_scale_f32_16x16x128_f8f6f4 v[76:79], v[214:221], v[198:205], v[76:79], v225, v225 op_sel_hi:[0,0,0]
	s_setprio 0
	v_lshl_add_u64 v[174:175], s[48:49], 0, v[148:149]
	s_mov_b32 m0, s73
	v_lshl_add_u64 v[144:145], v[174:175], 0, s[22:23]
	s_barrier
	ds_read_b128 v[176:179], v228 offset:16384
	ds_read_b128 v[180:183], v228 offset:17408
	ds_read_b128 v[184:187], v228 offset:18432
	ds_read_b128 v[188:191], v228 offset:19456
	ds_read_b128 v[192:195], v228 offset:20480
	ds_read_b128 v[196:199], v228 offset:21504
	ds_read_b128 v[236:239], v228 offset:22528
	ds_read_b128 v[240:243], v228 offset:23552
	global_load_lds_dwordx4 v[144:145], off
	v_lshl_add_u64 v[144:145], v[168:169], 0, s[22:23]
	s_mov_b32 m0, s74
	s_nop 0
	global_load_lds_dwordx4 v[144:145], off
	s_barrier
	s_waitcnt lgkmcnt(0)
	s_setprio 1
	s_waitcnt lgkmcnt(0)
	v_mfma_scale_f32_16x16x128_f8f6f4 v[80:83], v[8:15], v[176:183], v[80:83], v225, v225 op_sel_hi:[0,0,0]
	v_mfma_scale_f32_16x16x128_f8f6f4 v[84:87], v[0:7], v[176:183], v[84:87], v225, v225 op_sel_hi:[0,0,0]
	v_mfma_scale_f32_16x16x128_f8f6f4 v[88:91], v[8:15], v[184:191], v[88:91], v225, v225 op_sel_hi:[0,0,0]
	v_mfma_scale_f32_16x16x128_f8f6f4 v[92:95], v[0:7], v[184:191], v[92:95], v225, v225 op_sel_hi:[0,0,0]
	v_mfma_scale_f32_16x16x128_f8f6f4 v[96:99], v[8:15], v[192:199], v[96:99], v225, v225 op_sel_hi:[0,0,0]
	v_mfma_scale_f32_16x16x128_f8f6f4 v[100:103], v[0:7], v[192:199], v[100:103], v225, v225 op_sel_hi:[0,0,0]
	v_mfma_scale_f32_16x16x128_f8f6f4 v[104:107], v[8:15], v[236:243], v[104:107], v225, v225 op_sel_hi:[0,0,0]
	v_mfma_scale_f32_16x16x128_f8f6f4 v[108:111], v[0:7], v[236:243], v[108:111], v225, v225 op_sel_hi:[0,0,0]
	s_setprio 0
	s_barrier
	s_add_u32 s2, s50, 0x40500
	s_addc_u32 s3, s51, 0
	s_mov_b32 m0, s97
	v_lshl_add_u64 v[0:1], s[2:3], 0, v[150:151]
	global_load_lds_dwordx4 v[0:1], off
	v_lshl_add_u64 v[0:1], s[2:3], 0, v[154:155]
	s_mov_b32 m0, s52
	s_nop 0
	global_load_lds_dwordx4 v[0:1], off
	s_waitcnt vmcnt(6)
	s_barrier
	s_setprio 1
	v_mfma_scale_f32_16x16x128_f8f6f4 v[112:115], v[206:213], v[176:183], v[112:115], v225, v225 op_sel_hi:[0,0,0]
	v_mfma_scale_f32_16x16x128_f8f6f4 v[116:119], v[214:221], v[176:183], v[116:119], v225, v225 op_sel_hi:[0,0,0]
	v_mfma_scale_f32_16x16x128_f8f6f4 v[120:123], v[206:213], v[184:191], v[120:123], v225, v225 op_sel_hi:[0,0,0]
	v_mfma_scale_f32_16x16x128_f8f6f4 v[124:127], v[214:221], v[184:191], v[124:127], v225, v225 op_sel_hi:[0,0,0]
	v_mfma_scale_f32_16x16x128_f8f6f4 v[128:131], v[206:213], v[192:199], v[128:131], v225, v225 op_sel_hi:[0,0,0]
	v_mfma_scale_f32_16x16x128_f8f6f4 v[132:135], v[214:221], v[192:199], v[132:135], v225, v225 op_sel_hi:[0,0,0]
	v_mfma_scale_f32_16x16x128_f8f6f4 v[136:139], v[206:213], v[236:243], v[136:139], v225, v225 op_sel_hi:[0,0,0]
	v_mfma_scale_f32_16x16x128_f8f6f4 v[140:143], v[214:221], v[236:243], v[140:143], v225, v225 op_sel_hi:[0,0,0]
	s_setprio 0
	s_barrier
	ds_read_b128 v[0:3], v235
	ds_read_b128 v[4:7], v235 offset:1024
	ds_read_b128 v[8:11], v235 offset:2048
	ds_read_b128 v[12:15], v235 offset:3072
	s_add_u32 s2, s48, 0x40500
	s_addc_u32 s3, s49, 0
	s_mov_b32 m0, s75
	v_lshl_add_u64 v[144:145], s[2:3], 0, v[148:149]
	ds_read_b128 v[176:179], v228 offset:32768
	ds_read_b128 v[180:183], v228 offset:33792
	ds_read_b128 v[184:187], v228 offset:34816
	ds_read_b128 v[188:191], v228 offset:35840
	ds_read_b128 v[192:195], v228 offset:36864
	ds_read_b128 v[196:199], v228 offset:37888
	ds_read_b128 v[200:203], v228 offset:38912
	ds_read_b128 v[204:207], v228 offset:39936
	global_load_lds_dwordx4 v[144:145], off
	v_lshl_add_u64 v[144:145], s[2:3], 0, v[152:153]
	s_mov_b32 m0, s76
	s_nop 0
	global_load_lds_dwordx4 v[144:145], off
	s_waitcnt lgkmcnt(8)
	s_barrier
	s_waitcnt lgkmcnt(0)
	s_setprio 1
	s_waitcnt lgkmcnt(0)
	v_mfma_scale_f32_16x16x128_f8f6f4 v[16:19], v[0:7], v[176:183], v[16:19], v225, v225 op_sel_hi:[0,0,0]
	v_mfma_scale_f32_16x16x128_f8f6f4 v[20:23], v[8:15], v[176:183], v[20:23], v225, v225 op_sel_hi:[0,0,0]
	v_mfma_scale_f32_16x16x128_f8f6f4 v[24:27], v[0:7], v[184:191], v[24:27], v225, v225 op_sel_hi:[0,0,0]
	v_mfma_scale_f32_16x16x128_f8f6f4 v[28:31], v[8:15], v[184:191], v[28:31], v225, v225 op_sel_hi:[0,0,0]
	v_mfma_scale_f32_16x16x128_f8f6f4 v[32:35], v[0:7], v[192:199], v[32:35], v225, v225 op_sel_hi:[0,0,0]
	v_mfma_scale_f32_16x16x128_f8f6f4 v[36:39], v[8:15], v[192:199], v[36:39], v225, v225 op_sel_hi:[0,0,0]
	v_mfma_scale_f32_16x16x128_f8f6f4 v[40:43], v[0:7], v[200:207], v[40:43], v225, v225 op_sel_hi:[0,0,0]
	v_mfma_scale_f32_16x16x128_f8f6f4 v[44:47], v[8:15], v[200:207], v[44:47], v225, v225 op_sel_hi:[0,0,0]
	s_setprio 0
	s_barrier
	s_mov_b32 m0, s62
	v_lshl_add_u64 v[144:145], v[170:171], 0, s[24:25]
	ds_read_b128 v[208:211], v234
	ds_read_b128 v[212:215], v234 offset:1024
	ds_read_b128 v[236:239], v234 offset:2048
	ds_read_b128 v[240:243], v234 offset:3072
	global_load_lds_dwordx4 v[144:145], off
	v_lshl_add_u64 v[144:145], v[172:173], 0, s[24:25]
	s_mov_b32 m0, s63
	s_nop 0
	global_load_lds_dwordx4 v[144:145], off
	s_barrier
	s_waitcnt lgkmcnt(0)
	s_setprio 1
	s_waitcnt lgkmcnt(0)
	v_mfma_scale_f32_16x16x128_f8f6f4 v[48:51], v[208:215], v[176:183], v[48:51], v225, v225 op_sel_hi:[0,0,0]
	v_mfma_scale_f32_16x16x128_f8f6f4 v[52:55], v[236:243], v[176:183], v[52:55], v225, v225 op_sel_hi:[0,0,0]
	v_mfma_scale_f32_16x16x128_f8f6f4 v[56:59], v[208:215], v[184:191], v[56:59], v225, v225 op_sel_hi:[0,0,0]
	v_mfma_scale_f32_16x16x128_f8f6f4 v[60:63], v[236:243], v[184:191], v[60:63], v225, v225 op_sel_hi:[0,0,0]
	v_mfma_scale_f32_16x16x128_f8f6f4 v[64:67], v[208:215], v[192:199], v[64:67], v225, v225 op_sel_hi:[0,0,0]
	v_mfma_scale_f32_16x16x128_f8f6f4 v[68:71], v[236:243], v[192:199], v[68:71], v225, v225 op_sel_hi:[0,0,0]
	v_mfma_scale_f32_16x16x128_f8f6f4 v[72:75], v[208:215], v[200:207], v[72:75], v225, v225 op_sel_hi:[0,0,0]
	v_mfma_scale_f32_16x16x128_f8f6f4 v[76:79], v[236:243], v[200:207], v[76:79], v225, v225 op_sel_hi:[0,0,0]
	s_setprio 0
	s_mov_b32 m0, s80
	v_lshl_add_u64 v[144:145], v[174:175], 0, s[24:25]
	s_barrier
	ds_read_b128 v[176:179], v228 offset:49152
	ds_read_b128 v[180:183], v228 offset:50176
	ds_read_b128 v[184:187], v228 offset:51200
	ds_read_b128 v[188:191], v228 offset:52224
	ds_read_b128 v[192:195], v228 offset:53248
	ds_read_b128 v[196:199], v228 offset:54272
	ds_read_b128 v[200:203], v228 offset:55296
	ds_read_b128 v[204:207], v228 offset:56320
	global_load_lds_dwordx4 v[144:145], off
	v_lshl_add_u64 v[144:145], v[168:169], 0, s[24:25]
	s_mov_b32 m0, s81
	s_nop 0
	global_load_lds_dwordx4 v[144:145], off
	s_barrier
	s_waitcnt lgkmcnt(0)
	s_setprio 1
	s_waitcnt lgkmcnt(0)
	v_mfma_scale_f32_16x16x128_f8f6f4 v[80:83], v[0:7], v[176:183], v[80:83], v225, v225 op_sel_hi:[0,0,0]
	v_mfma_scale_f32_16x16x128_f8f6f4 v[84:87], v[8:15], v[176:183], v[84:87], v225, v225 op_sel_hi:[0,0,0]
	v_mfma_scale_f32_16x16x128_f8f6f4 v[88:91], v[0:7], v[184:191], v[88:91], v225, v225 op_sel_hi:[0,0,0]
	v_mfma_scale_f32_16x16x128_f8f6f4 v[92:95], v[8:15], v[184:191], v[92:95], v225, v225 op_sel_hi:[0,0,0]
	v_mfma_scale_f32_16x16x128_f8f6f4 v[96:99], v[0:7], v[192:199], v[96:99], v225, v225 op_sel_hi:[0,0,0]
	v_mfma_scale_f32_16x16x128_f8f6f4 v[100:103], v[8:15], v[192:199], v[100:103], v225, v225 op_sel_hi:[0,0,0]
	v_mfma_scale_f32_16x16x128_f8f6f4 v[104:107], v[0:7], v[200:207], v[104:107], v225, v225 op_sel_hi:[0,0,0]
	v_mfma_scale_f32_16x16x128_f8f6f4 v[108:111], v[8:15], v[200:207], v[108:111], v225, v225 op_sel_hi:[0,0,0]
	s_setprio 0
	s_barrier
	s_add_u32 s2, s50, 0x40580
	s_addc_u32 s3, s51, 0
	s_mov_b32 m0, s53
	v_lshl_add_u64 v[0:1], s[2:3], 0, v[150:151]
	global_load_lds_dwordx4 v[0:1], off
	v_lshl_add_u64 v[0:1], s[2:3], 0, v[154:155]
	s_mov_b32 m0, s64
	s_nop 0
	global_load_lds_dwordx4 v[0:1], off
	s_waitcnt vmcnt(6)
	s_barrier
	s_setprio 1
	v_mfma_scale_f32_16x16x128_f8f6f4 v[112:115], v[208:215], v[176:183], v[112:115], v225, v225 op_sel_hi:[0,0,0]
	v_mfma_scale_f32_16x16x128_f8f6f4 v[116:119], v[236:243], v[176:183], v[116:119], v225, v225 op_sel_hi:[0,0,0]
	v_mfma_scale_f32_16x16x128_f8f6f4 v[120:123], v[208:215], v[184:191], v[120:123], v225, v225 op_sel_hi:[0,0,0]
	v_mfma_scale_f32_16x16x128_f8f6f4 v[124:127], v[236:243], v[184:191], v[124:127], v225, v225 op_sel_hi:[0,0,0]
	v_mfma_scale_f32_16x16x128_f8f6f4 v[128:131], v[208:215], v[192:199], v[128:131], v225, v225 op_sel_hi:[0,0,0]
	v_mfma_scale_f32_16x16x128_f8f6f4 v[132:135], v[236:243], v[192:199], v[132:135], v225, v225 op_sel_hi:[0,0,0]
	v_mfma_scale_f32_16x16x128_f8f6f4 v[136:139], v[208:215], v[200:207], v[136:139], v225, v225 op_sel_hi:[0,0,0]
	v_mfma_scale_f32_16x16x128_f8f6f4 v[140:143], v[236:243], v[200:207], v[140:143], v225, v225 op_sel_hi:[0,0,0]
	s_setprio 0
	s_barrier
	ds_read_b128 v[0:3], v231
	ds_read_b128 v[4:7], v231 offset:1024
	ds_read_b128 v[8:11], v231 offset:2048
	ds_read_b128 v[12:15], v231 offset:3072
	s_add_u32 s2, s48, 0x40580
	s_addc_u32 s3, s49, 0
	s_mov_b32 m0, s94
	v_lshl_add_u64 v[144:145], s[2:3], 0, v[148:149]
	ds_read_b128 v[176:179], v228
	ds_read_b128 v[180:183], v228 offset:1024
	ds_read_b128 v[184:187], v228 offset:2048
	ds_read_b128 v[188:191], v228 offset:3072
	ds_read_b128 v[192:195], v228 offset:4096
	ds_read_b128 v[196:199], v228 offset:5120
	ds_read_b128 v[200:203], v228 offset:6144
	ds_read_b128 v[204:207], v228 offset:7168
	global_load_lds_dwordx4 v[144:145], off
	v_lshl_add_u64 v[144:145], s[2:3], 0, v[152:153]
	s_mov_b32 m0, s93
	s_nop 0
	global_load_lds_dwordx4 v[144:145], off
	s_waitcnt lgkmcnt(8)
	s_barrier
	s_waitcnt lgkmcnt(0)
	s_setprio 1
	s_waitcnt lgkmcnt(0)
	v_mfma_scale_f32_16x16x128_f8f6f4 v[16:19], v[0:7], v[176:183], v[16:19], v225, v225 op_sel_hi:[0,0,0]
	v_mfma_scale_f32_16x16x128_f8f6f4 v[20:23], v[8:15], v[176:183], v[20:23], v225, v225 op_sel_hi:[0,0,0]
	v_mfma_scale_f32_16x16x128_f8f6f4 v[24:27], v[0:7], v[184:191], v[24:27], v225, v225 op_sel_hi:[0,0,0]
	v_mfma_scale_f32_16x16x128_f8f6f4 v[28:31], v[8:15], v[184:191], v[28:31], v225, v225 op_sel_hi:[0,0,0]
	v_mfma_scale_f32_16x16x128_f8f6f4 v[32:35], v[0:7], v[192:199], v[32:35], v225, v225 op_sel_hi:[0,0,0]
	v_mfma_scale_f32_16x16x128_f8f6f4 v[36:39], v[8:15], v[192:199], v[36:39], v225, v225 op_sel_hi:[0,0,0]
	v_mfma_scale_f32_16x16x128_f8f6f4 v[40:43], v[0:7], v[200:207], v[40:43], v225, v225 op_sel_hi:[0,0,0]
	v_mfma_scale_f32_16x16x128_f8f6f4 v[44:47], v[8:15], v[200:207], v[44:47], v225, v225 op_sel_hi:[0,0,0]
	s_setprio 0
	s_barrier
	s_mov_b32 m0, s96
	v_lshl_add_u64 v[144:145], v[170:171], 0, s[26:27]
	ds_read_b128 v[208:211], v232
	ds_read_b128 v[212:215], v232 offset:1024
	ds_read_b128 v[236:239], v232 offset:2048
	ds_read_b128 v[240:243], v232 offset:3072
	global_load_lds_dwordx4 v[144:145], off
	v_lshl_add_u64 v[144:145], v[172:173], 0, s[26:27]
	s_mov_b32 m0, s95
	s_nop 0
	global_load_lds_dwordx4 v[144:145], off
	s_barrier
	s_waitcnt lgkmcnt(0)
	s_setprio 1
	s_waitcnt lgkmcnt(0)
	v_mfma_scale_f32_16x16x128_f8f6f4 v[48:51], v[208:215], v[176:183], v[48:51], v225, v225 op_sel_hi:[0,0,0]
	v_mfma_scale_f32_16x16x128_f8f6f4 v[52:55], v[236:243], v[176:183], v[52:55], v225, v225 op_sel_hi:[0,0,0]
	v_mfma_scale_f32_16x16x128_f8f6f4 v[56:59], v[208:215], v[184:191], v[56:59], v225, v225 op_sel_hi:[0,0,0]
	v_mfma_scale_f32_16x16x128_f8f6f4 v[60:63], v[236:243], v[184:191], v[60:63], v225, v225 op_sel_hi:[0,0,0]
	v_mfma_scale_f32_16x16x128_f8f6f4 v[64:67], v[208:215], v[192:199], v[64:67], v225, v225 op_sel_hi:[0,0,0]
	v_mfma_scale_f32_16x16x128_f8f6f4 v[68:71], v[236:243], v[192:199], v[68:71], v225, v225 op_sel_hi:[0,0,0]
	v_mfma_scale_f32_16x16x128_f8f6f4 v[72:75], v[208:215], v[200:207], v[72:75], v225, v225 op_sel_hi:[0,0,0]
	v_mfma_scale_f32_16x16x128_f8f6f4 v[76:79], v[236:243], v[200:207], v[76:79], v225, v225 op_sel_hi:[0,0,0]
	s_setprio 0
	s_mov_b32 m0, s73
	v_lshl_add_u64 v[144:145], v[174:175], 0, s[26:27]
	s_barrier
	ds_read_b128 v[176:179], v228 offset:16384
	ds_read_b128 v[180:183], v228 offset:17408
	ds_read_b128 v[184:187], v228 offset:18432
	ds_read_b128 v[188:191], v228 offset:19456
	ds_read_b128 v[192:195], v228 offset:20480
	ds_read_b128 v[196:199], v228 offset:21504
	ds_read_b128 v[200:203], v228 offset:22528
	ds_read_b128 v[204:207], v228 offset:23552
	global_load_lds_dwordx4 v[144:145], off
	v_lshl_add_u64 v[144:145], v[168:169], 0, s[26:27]
	s_mov_b32 m0, s74
	s_nop 0
	global_load_lds_dwordx4 v[144:145], off
	s_barrier
	s_waitcnt lgkmcnt(0)
	s_setprio 1
	s_waitcnt lgkmcnt(0)
	v_mfma_scale_f32_16x16x128_f8f6f4 v[80:83], v[0:7], v[176:183], v[80:83], v225, v225 op_sel_hi:[0,0,0]
	v_mfma_scale_f32_16x16x128_f8f6f4 v[84:87], v[8:15], v[176:183], v[84:87], v225, v225 op_sel_hi:[0,0,0]
	v_mfma_scale_f32_16x16x128_f8f6f4 v[88:91], v[0:7], v[184:191], v[88:91], v225, v225 op_sel_hi:[0,0,0]
	v_mfma_scale_f32_16x16x128_f8f6f4 v[92:95], v[8:15], v[184:191], v[92:95], v225, v225 op_sel_hi:[0,0,0]
	v_mfma_scale_f32_16x16x128_f8f6f4 v[96:99], v[0:7], v[192:199], v[96:99], v225, v225 op_sel_hi:[0,0,0]
	v_mfma_scale_f32_16x16x128_f8f6f4 v[100:103], v[8:15], v[192:199], v[100:103], v225, v225 op_sel_hi:[0,0,0]
	v_mfma_scale_f32_16x16x128_f8f6f4 v[104:107], v[0:7], v[200:207], v[104:107], v225, v225 op_sel_hi:[0,0,0]
	v_mfma_scale_f32_16x16x128_f8f6f4 v[108:111], v[8:15], v[200:207], v[108:111], v225, v225 op_sel_hi:[0,0,0]
	s_setprio 0
	s_barrier
	s_add_u32 s2, s50, 0x40600
	s_addc_u32 s3, s51, 0
	s_mov_b32 m0, s97
	v_lshl_add_u64 v[0:1], s[2:3], 0, v[150:151]
	global_load_lds_dwordx4 v[0:1], off
	v_lshl_add_u64 v[0:1], s[2:3], 0, v[154:155]
	s_mov_b32 m0, s52
	s_nop 0
	global_load_lds_dwordx4 v[0:1], off
	s_waitcnt vmcnt(6)
	s_barrier
	s_setprio 1
	v_mfma_scale_f32_16x16x128_f8f6f4 v[112:115], v[208:215], v[176:183], v[112:115], v225, v225 op_sel_hi:[0,0,0]
	v_mfma_scale_f32_16x16x128_f8f6f4 v[116:119], v[236:243], v[176:183], v[116:119], v225, v225 op_sel_hi:[0,0,0]
	v_mfma_scale_f32_16x16x128_f8f6f4 v[120:123], v[208:215], v[184:191], v[120:123], v225, v225 op_sel_hi:[0,0,0]
	v_mfma_scale_f32_16x16x128_f8f6f4 v[124:127], v[236:243], v[184:191], v[124:127], v225, v225 op_sel_hi:[0,0,0]
	v_mfma_scale_f32_16x16x128_f8f6f4 v[128:131], v[208:215], v[192:199], v[128:131], v225, v225 op_sel_hi:[0,0,0]
	v_mfma_scale_f32_16x16x128_f8f6f4 v[132:135], v[236:243], v[192:199], v[132:135], v225, v225 op_sel_hi:[0,0,0]
	v_mfma_scale_f32_16x16x128_f8f6f4 v[136:139], v[208:215], v[200:207], v[136:139], v225, v225 op_sel_hi:[0,0,0]
	v_mfma_scale_f32_16x16x128_f8f6f4 v[140:143], v[236:243], v[200:207], v[140:143], v225, v225 op_sel_hi:[0,0,0]
	s_setprio 0
	s_barrier
	ds_read_b128 v[0:3], v235
	ds_read_b128 v[4:7], v235 offset:1024
	ds_read_b128 v[8:11], v235 offset:2048
	ds_read_b128 v[12:15], v235 offset:3072
	s_add_u32 s2, s48, 0x40600
	s_addc_u32 s3, s49, 0
	s_mov_b32 m0, s75
	v_lshl_add_u64 v[144:145], s[2:3], 0, v[148:149]
	ds_read_b128 v[176:179], v228 offset:32768
	ds_read_b128 v[180:183], v228 offset:33792
	ds_read_b128 v[184:187], v228 offset:34816
	ds_read_b128 v[188:191], v228 offset:35840
	ds_read_b128 v[192:195], v228 offset:36864
	ds_read_b128 v[196:199], v228 offset:37888
	ds_read_b128 v[200:203], v228 offset:38912
	ds_read_b128 v[204:207], v228 offset:39936
	global_load_lds_dwordx4 v[144:145], off
	v_lshl_add_u64 v[144:145], s[2:3], 0, v[152:153]
	s_mov_b32 m0, s76
	s_nop 0
	global_load_lds_dwordx4 v[144:145], off
	s_waitcnt lgkmcnt(8)
	s_barrier
	s_waitcnt lgkmcnt(0)
	s_setprio 1
	s_waitcnt lgkmcnt(0)
	v_mfma_scale_f32_16x16x128_f8f6f4 v[16:19], v[0:7], v[176:183], v[16:19], v225, v225 op_sel_hi:[0,0,0]
	v_mfma_scale_f32_16x16x128_f8f6f4 v[20:23], v[8:15], v[176:183], v[20:23], v225, v225 op_sel_hi:[0,0,0]
	v_mfma_scale_f32_16x16x128_f8f6f4 v[24:27], v[0:7], v[184:191], v[24:27], v225, v225 op_sel_hi:[0,0,0]
	v_mfma_scale_f32_16x16x128_f8f6f4 v[28:31], v[8:15], v[184:191], v[28:31], v225, v225 op_sel_hi:[0,0,0]
	v_mfma_scale_f32_16x16x128_f8f6f4 v[32:35], v[0:7], v[192:199], v[32:35], v225, v225 op_sel_hi:[0,0,0]
	v_mfma_scale_f32_16x16x128_f8f6f4 v[36:39], v[8:15], v[192:199], v[36:39], v225, v225 op_sel_hi:[0,0,0]
	v_mfma_scale_f32_16x16x128_f8f6f4 v[40:43], v[0:7], v[200:207], v[40:43], v225, v225 op_sel_hi:[0,0,0]
	v_mfma_scale_f32_16x16x128_f8f6f4 v[44:47], v[8:15], v[200:207], v[44:47], v225, v225 op_sel_hi:[0,0,0]
	s_setprio 0
	s_barrier
	s_mov_b32 m0, s62
	v_lshl_add_u64 v[144:145], v[170:171], 0, s[28:29]
	ds_read_b128 v[208:211], v234
	ds_read_b128 v[212:215], v234 offset:1024
	ds_read_b128 v[236:239], v234 offset:2048
	ds_read_b128 v[240:243], v234 offset:3072
	global_load_lds_dwordx4 v[144:145], off
	v_lshl_add_u64 v[144:145], v[172:173], 0, s[28:29]
	s_mov_b32 m0, s63
	s_nop 0
	global_load_lds_dwordx4 v[144:145], off
	s_barrier
	s_waitcnt lgkmcnt(0)
	s_setprio 1
	s_waitcnt lgkmcnt(0)
	v_mfma_scale_f32_16x16x128_f8f6f4 v[48:51], v[208:215], v[176:183], v[48:51], v225, v225 op_sel_hi:[0,0,0]
	v_mfma_scale_f32_16x16x128_f8f6f4 v[52:55], v[236:243], v[176:183], v[52:55], v225, v225 op_sel_hi:[0,0,0]
	v_mfma_scale_f32_16x16x128_f8f6f4 v[56:59], v[208:215], v[184:191], v[56:59], v225, v225 op_sel_hi:[0,0,0]
	v_mfma_scale_f32_16x16x128_f8f6f4 v[60:63], v[236:243], v[184:191], v[60:63], v225, v225 op_sel_hi:[0,0,0]
	v_mfma_scale_f32_16x16x128_f8f6f4 v[64:67], v[208:215], v[192:199], v[64:67], v225, v225 op_sel_hi:[0,0,0]
	v_mfma_scale_f32_16x16x128_f8f6f4 v[68:71], v[236:243], v[192:199], v[68:71], v225, v225 op_sel_hi:[0,0,0]
	v_mfma_scale_f32_16x16x128_f8f6f4 v[72:75], v[208:215], v[200:207], v[72:75], v225, v225 op_sel_hi:[0,0,0]
	v_mfma_scale_f32_16x16x128_f8f6f4 v[76:79], v[236:243], v[200:207], v[76:79], v225, v225 op_sel_hi:[0,0,0]
	s_setprio 0
	s_mov_b32 m0, s80
	v_lshl_add_u64 v[144:145], v[174:175], 0, s[28:29]
	s_barrier
	ds_read_b128 v[176:179], v228 offset:49152
	ds_read_b128 v[180:183], v228 offset:50176
	ds_read_b128 v[184:187], v228 offset:51200
	ds_read_b128 v[188:191], v228 offset:52224
	ds_read_b128 v[192:195], v228 offset:53248
	ds_read_b128 v[196:199], v228 offset:54272
	ds_read_b128 v[200:203], v228 offset:55296
	ds_read_b128 v[204:207], v228 offset:56320
	global_load_lds_dwordx4 v[144:145], off
	v_lshl_add_u64 v[144:145], v[168:169], 0, s[28:29]
	s_mov_b32 m0, s81
	s_nop 0
	global_load_lds_dwordx4 v[144:145], off
	s_barrier
	s_waitcnt lgkmcnt(0)
	s_setprio 1
	s_waitcnt lgkmcnt(0)
	v_mfma_scale_f32_16x16x128_f8f6f4 v[80:83], v[0:7], v[176:183], v[80:83], v225, v225 op_sel_hi:[0,0,0]
	v_mfma_scale_f32_16x16x128_f8f6f4 v[84:87], v[8:15], v[176:183], v[84:87], v225, v225 op_sel_hi:[0,0,0]
	v_mfma_scale_f32_16x16x128_f8f6f4 v[88:91], v[0:7], v[184:191], v[88:91], v225, v225 op_sel_hi:[0,0,0]
	v_mfma_scale_f32_16x16x128_f8f6f4 v[92:95], v[8:15], v[184:191], v[92:95], v225, v225 op_sel_hi:[0,0,0]
	v_mfma_scale_f32_16x16x128_f8f6f4 v[96:99], v[0:7], v[192:199], v[96:99], v225, v225 op_sel_hi:[0,0,0]
	v_mfma_scale_f32_16x16x128_f8f6f4 v[100:103], v[8:15], v[192:199], v[100:103], v225, v225 op_sel_hi:[0,0,0]
	v_mfma_scale_f32_16x16x128_f8f6f4 v[104:107], v[0:7], v[200:207], v[104:107], v225, v225 op_sel_hi:[0,0,0]
	v_mfma_scale_f32_16x16x128_f8f6f4 v[108:111], v[8:15], v[200:207], v[108:111], v225, v225 op_sel_hi:[0,0,0]
	s_setprio 0
	s_barrier
	s_add_u32 s2, s50, 0x40680
	s_addc_u32 s3, s51, 0
	s_mov_b32 m0, s53
	v_lshl_add_u64 v[0:1], s[2:3], 0, v[150:151]
	global_load_lds_dwordx4 v[0:1], off
	v_lshl_add_u64 v[0:1], s[2:3], 0, v[154:155]
	s_mov_b32 m0, s64
	s_nop 0
	global_load_lds_dwordx4 v[0:1], off
	s_waitcnt vmcnt(6)
	s_barrier
	s_setprio 1
	v_mfma_scale_f32_16x16x128_f8f6f4 v[112:115], v[208:215], v[176:183], v[112:115], v225, v225 op_sel_hi:[0,0,0]
	v_mfma_scale_f32_16x16x128_f8f6f4 v[116:119], v[236:243], v[176:183], v[116:119], v225, v225 op_sel_hi:[0,0,0]
	v_mfma_scale_f32_16x16x128_f8f6f4 v[120:123], v[208:215], v[184:191], v[120:123], v225, v225 op_sel_hi:[0,0,0]
	v_mfma_scale_f32_16x16x128_f8f6f4 v[124:127], v[236:243], v[184:191], v[124:127], v225, v225 op_sel_hi:[0,0,0]
	v_mfma_scale_f32_16x16x128_f8f6f4 v[128:131], v[208:215], v[192:199], v[128:131], v225, v225 op_sel_hi:[0,0,0]
	v_mfma_scale_f32_16x16x128_f8f6f4 v[132:135], v[236:243], v[192:199], v[132:135], v225, v225 op_sel_hi:[0,0,0]
	v_mfma_scale_f32_16x16x128_f8f6f4 v[136:139], v[208:215], v[200:207], v[136:139], v225, v225 op_sel_hi:[0,0,0]
	v_mfma_scale_f32_16x16x128_f8f6f4 v[140:143], v[236:243], v[200:207], v[140:143], v225, v225 op_sel_hi:[0,0,0]
	s_setprio 0
	s_and_b64 s[2:3], vcc, exec
	s_cselect_b32 s61, s47, s51
	s_cselect_b32 s60, s46, s50
	s_add_i32 s2, s58, 16
	s_ashr_i32 s3, s2, 31
	v_mov_b32_e32 v156, v230
	s_lshl_b64 s[2:3], s[2:3], 16
	s_barrier
	s_nop 7
	s_nop 7
	s_nop 7
	s_add_u32 s2, s78, s2
	s_addc_u32 s3, s79, s3
	global_load_dwordx2 v[216:217], v156, s[56:57]
	global_load_dwordx2 v[236:237], v156, s[2:3]
	global_load_dwordx2 v[212:213], v156, s[56:57] offset:512
	global_load_dwordx2 v[214:215], v156, s[2:3] offset:512
	global_load_dwordx2 v[208:209], v156, s[56:57] offset:1024
	global_load_dwordx2 v[210:211], v156, s[2:3] offset:1024
	global_load_dwordx2 v[204:205], v156, s[56:57] offset:1536
	global_load_dwordx2 v[206:207], v156, s[2:3] offset:1536
	global_load_dwordx2 v[200:201], v156, s[56:57] offset:2048
	global_load_dwordx2 v[202:203], v156, s[2:3] offset:2048
	global_load_dwordx2 v[196:197], v156, s[56:57] offset:2560
	global_load_dwordx2 v[198:199], v156, s[2:3] offset:2560
	global_load_dwordx2 v[192:193], v156, s[56:57] offset:3072
	global_load_dwordx2 v[194:195], v156, s[2:3] offset:3072
	global_load_dwordx2 v[188:189], v156, s[56:57] offset:3584
	global_load_dwordx2 v[190:191], v156, s[2:3] offset:3584
	v_lshl_add_u64 v[0:1], s[56:57], 0, v[156:157]
	v_lshl_add_u64 v[2:3], s[2:3], 0, v[156:157]
	v_add_co_u32_e32 v0, vcc, s85, v0
	s_waitcnt vmcnt(0)
	v_cvt_f32_ubyte3_e32 v243, v216
	v_cvt_f32_ubyte0_e32 v156, v236
	v_add_f32_e32 v156, 0.5, v156
	v_rcp_f32_e32 v238, v156
	v_cvt_f32_ubyte0_e32 v156, v237
	v_add_f32_e32 v156, 0.5, v156
	v_rcp_f32_e32 v218, v156
	v_cvt_f32_ubyte1_e32 v156, v236
	v_add_f32_e32 v156, 0.5, v156
	v_rcp_f32_e32 v239, v156
	v_cvt_f32_ubyte1_e32 v156, v237
	v_add_f32_e32 v156, 0.5, v156
	v_rcp_f32_e32 v219, v156
	v_cvt_f32_ubyte2_e32 v156, v236
	v_add_f32_e32 v156, 0.5, v156
	v_rcp_f32_e32 v240, v156
	v_cvt_f32_ubyte2_e32 v156, v237
	v_add_f32_e32 v156, 0.5, v156
	v_rcp_f32_e32 v220, v156
	v_cvt_f32_ubyte3_e32 v156, v236
	v_add_f32_e32 v156, 0.5, v156
	v_rcp_f32_e32 v241, v156
	v_cvt_f32_ubyte3_e32 v156, v237
	v_add_f32_e32 v156, 0.5, v156
	v_cvt_f32_ubyte1_e32 v237, v216
	v_cvt_f32_ubyte0_e32 v236, v216
	v_cvt_f32_ubyte2_e32 v242, v216
	v_rcp_f32_e32 v221, v156
	v_pk_add_f32 v[242:243], v[242:243], 0.5 op_sel_hi:[1,0]
	v_pk_add_f32 v[236:237], v[236:237], 0.5 op_sel_hi:[1,0]
	v_cvt_f32_ubyte0_e32 v156, v214
	v_pk_mul_f32 v[236:237], v[236:237], v[238:239]
	v_pk_mul_f32 v[238:239], v[242:243], v[240:241]
	v_pk_mul_f32 v[16:17], v[16:17], v[236:237]
	v_pk_mul_f32 v[18:19], v[18:19], v[238:239]
	v_cvt_f32_ubyte3_e32 v239, v217
	v_cvt_f32_ubyte2_e32 v238, v217
	v_cvt_f32_ubyte1_e32 v237, v217
	v_cvt_f32_ubyte0_e32 v236, v217
	v_pk_add_f32 v[216:217], v[238:239], 0.5 op_sel_hi:[1,0]
	v_add_f32_e32 v156, 0.5, v156
	v_pk_mul_f32 v[216:217], v[216:217], v[220:221]
	v_pk_add_f32 v[236:237], v[236:237], 0.5 op_sel_hi:[1,0]
	v_pk_mul_f32 v[22:23], v[22:23], v[216:217]
	v_rcp_f32_e32 v216, v156
	v_cvt_f32_ubyte0_e32 v156, v215
	v_pk_mul_f32 v[218:219], v[236:237], v[218:219]
	v_add_f32_e32 v156, 0.5, v156
	v_pk_mul_f32 v[20:21], v[20:21], v[218:219]
	v_rcp_f32_e32 v218, v156
	v_cvt_f32_ubyte1_e32 v156, v214
	v_add_f32_e32 v156, 0.5, v156
	v_rcp_f32_e32 v217, v156
	v_cvt_f32_ubyte1_e32 v156, v215
	v_add_f32_e32 v156, 0.5, v156
	v_rcp_f32_e32 v219, v156
	v_cvt_f32_ubyte2_e32 v156, v214
	v_add_f32_e32 v156, 0.5, v156
	v_rcp_f32_e32 v220, v156
	v_cvt_f32_ubyte2_e32 v156, v215
	v_add_f32_e32 v156, 0.5, v156
	v_rcp_f32_e32 v236, v156
	v_cvt_f32_ubyte3_e32 v156, v214
	v_add_f32_e32 v156, 0.5, v156
	v_rcp_f32_e32 v221, v156
	v_cvt_f32_ubyte3_e32 v156, v215
	v_add_f32_e32 v156, 0.5, v156
	v_cvt_f32_ubyte1_e32 v215, v212
	v_cvt_f32_ubyte0_e32 v214, v212
	v_cvt_f32_ubyte3_e32 v239, v212
	v_cvt_f32_ubyte2_e32 v238, v212
	v_rcp_f32_e32 v237, v156
	v_pk_add_f32 v[238:239], v[238:239], 0.5 op_sel_hi:[1,0]
	v_pk_add_f32 v[214:215], v[214:215], 0.5 op_sel_hi:[1,0]
	v_cvt_f32_ubyte0_e32 v156, v210
	v_pk_mul_f32 v[214:215], v[214:215], v[216:217]
	v_pk_mul_f32 v[216:217], v[238:239], v[220:221]
	v_pk_mul_f32 v[48:49], v[48:49], v[214:215]
	v_pk_mul_f32 v[50:51], v[50:51], v[216:217]
	v_cvt_f32_ubyte3_e32 v217, v213
	v_cvt_f32_ubyte2_e32 v216, v213
	v_cvt_f32_ubyte1_e32 v215, v213
	v_cvt_f32_ubyte0_e32 v214, v213
	v_pk_add_f32 v[212:213], v[216:217], 0.5 op_sel_hi:[1,0]
	v_add_f32_e32 v156, 0.5, v156
	v_pk_mul_f32 v[212:213], v[212:213], v[236:237]
	v_pk_add_f32 v[214:215], v[214:215], 0.5 op_sel_hi:[1,0]
	v_pk_mul_f32 v[54:55], v[54:55], v[212:213]
	v_rcp_f32_e32 v212, v156
	v_cvt_f32_ubyte0_e32 v156, v211
	v_pk_mul_f32 v[214:215], v[214:215], v[218:219]
	v_add_f32_e32 v156, 0.5, v156
	v_pk_mul_f32 v[52:53], v[52:53], v[214:215]
	v_rcp_f32_e32 v214, v156
	v_cvt_f32_ubyte1_e32 v156, v210
	v_add_f32_e32 v156, 0.5, v156
	v_rcp_f32_e32 v213, v156
	v_cvt_f32_ubyte1_e32 v156, v211
	v_add_f32_e32 v156, 0.5, v156
	v_rcp_f32_e32 v215, v156
	v_cvt_f32_ubyte2_e32 v156, v210
	v_add_f32_e32 v156, 0.5, v156
	v_rcp_f32_e32 v216, v156
	v_cvt_f32_ubyte2_e32 v156, v211
	v_add_f32_e32 v156, 0.5, v156
	v_rcp_f32_e32 v218, v156
	v_cvt_f32_ubyte3_e32 v156, v210
	v_add_f32_e32 v156, 0.5, v156
	v_rcp_f32_e32 v217, v156
	v_cvt_f32_ubyte3_e32 v156, v211
	v_add_f32_e32 v156, 0.5, v156
	v_cvt_f32_ubyte1_e32 v211, v208
	v_cvt_f32_ubyte0_e32 v210, v208
	v_cvt_f32_ubyte3_e32 v221, v208
	v_cvt_f32_ubyte2_e32 v220, v208
	v_rcp_f32_e32 v219, v156
	v_pk_add_f32 v[220:221], v[220:221], 0.5 op_sel_hi:[1,0]
	v_pk_add_f32 v[210:211], v[210:211], 0.5 op_sel_hi:[1,0]
	v_cvt_f32_ubyte0_e32 v156, v206
	v_pk_mul_f32 v[210:211], v[210:211], v[212:213]
	v_pk_mul_f32 v[212:213], v[220:221], v[216:217]
	v_pk_mul_f32 v[24:25], v[24:25], v[210:211]
	v_pk_mul_f32 v[26:27], v[26:27], v[212:213]
	v_cvt_f32_ubyte3_e32 v213, v209
	v_cvt_f32_ubyte2_e32 v212, v209
	v_cvt_f32_ubyte1_e32 v211, v209
	v_cvt_f32_ubyte0_e32 v210, v209
	v_pk_add_f32 v[208:209], v[212:213], 0.5 op_sel_hi:[1,0]
	v_add_f32_e32 v156, 0.5, v156
	v_pk_mul_f32 v[208:209], v[208:209], v[218:219]
	v_pk_add_f32 v[210:211], v[210:211], 0.5 op_sel_hi:[1,0]
	v_pk_mul_f32 v[30:31], v[30:31], v[208:209]
	v_rcp_f32_e32 v208, v156
	v_cvt_f32_ubyte0_e32 v156, v207
	v_pk_mul_f32 v[210:211], v[210:211], v[214:215]
	v_add_f32_e32 v156, 0.5, v156
	v_pk_mul_f32 v[28:29], v[28:29], v[210:211]
	v_rcp_f32_e32 v210, v156
	v_cvt_f32_ubyte1_e32 v156, v206
	v_add_f32_e32 v156, 0.5, v156
	v_rcp_f32_e32 v209, v156
	v_cvt_f32_ubyte1_e32 v156, v207
	v_add_f32_e32 v156, 0.5, v156
	v_rcp_f32_e32 v211, v156
	v_cvt_f32_ubyte2_e32 v156, v206
	v_add_f32_e32 v156, 0.5, v156
	v_rcp_f32_e32 v212, v156
	v_cvt_f32_ubyte2_e32 v156, v207
	v_add_f32_e32 v156, 0.5, v156
	v_rcp_f32_e32 v214, v156
	v_cvt_f32_ubyte3_e32 v156, v206
	v_add_f32_e32 v156, 0.5, v156
	v_rcp_f32_e32 v213, v156
	v_cvt_f32_ubyte3_e32 v156, v207
	v_add_f32_e32 v156, 0.5, v156
	v_cvt_f32_ubyte1_e32 v207, v204
	v_cvt_f32_ubyte0_e32 v206, v204
	v_cvt_f32_ubyte3_e32 v217, v204
	v_cvt_f32_ubyte2_e32 v216, v204
	v_rcp_f32_e32 v215, v156
	v_pk_add_f32 v[216:217], v[216:217], 0.5 op_sel_hi:[1,0]
	v_pk_add_f32 v[206:207], v[206:207], 0.5 op_sel_hi:[1,0]
	v_cvt_f32_ubyte0_e32 v156, v202
	v_pk_mul_f32 v[206:207], v[206:207], v[208:209]
	v_pk_mul_f32 v[208:209], v[216:217], v[212:213]
	v_pk_mul_f32 v[56:57], v[56:57], v[206:207]
	v_pk_mul_f32 v[58:59], v[58:59], v[208:209]
	v_cvt_f32_ubyte3_e32 v209, v205
	v_cvt_f32_ubyte2_e32 v208, v205
	v_cvt_f32_ubyte1_e32 v207, v205
	v_cvt_f32_ubyte0_e32 v206, v205
	v_pk_add_f32 v[204:205], v[208:209], 0.5 op_sel_hi:[1,0]
	v_add_f32_e32 v156, 0.5, v156
	v_pk_mul_f32 v[204:205], v[204:205], v[214:215]
	v_pk_add_f32 v[206:207], v[206:207], 0.5 op_sel_hi:[1,0]
	v_pk_mul_f32 v[62:63], v[62:63], v[204:205]
	v_rcp_f32_e32 v204, v156
	v_cvt_f32_ubyte0_e32 v156, v203
	v_pk_mul_f32 v[206:207], v[206:207], v[210:211]
	v_add_f32_e32 v156, 0.5, v156
	v_pk_mul_f32 v[60:61], v[60:61], v[206:207]
	v_rcp_f32_e32 v206, v156
	v_cvt_f32_ubyte1_e32 v156, v202
	v_add_f32_e32 v156, 0.5, v156
	v_rcp_f32_e32 v205, v156
	v_cvt_f32_ubyte1_e32 v156, v203
	v_add_f32_e32 v156, 0.5, v156
	v_rcp_f32_e32 v207, v156
	v_cvt_f32_ubyte2_e32 v156, v202
	v_add_f32_e32 v156, 0.5, v156
	v_rcp_f32_e32 v208, v156
	v_cvt_f32_ubyte2_e32 v156, v203
	v_addc_co_u32_e32 v1, vcc, 0, v1, vcc
	v_add_f32_e32 v156, 0.5, v156
	v_add_co_u32_e32 v6, vcc, s85, v2
	v_rcp_f32_e32 v210, v156
	v_cvt_f32_ubyte3_e32 v156, v202
	v_addc_co_u32_e32 v7, vcc, 0, v3, vcc
	v_add_f32_e32 v156, 0.5, v156
	global_load_dwordx2 v[184:185], v[0:1], off
	global_load_dwordx2 v[186:187], v[6:7], off
	global_load_dwordx2 v[180:181], v[0:1], off offset:512
	global_load_dwordx2 v[182:183], v[6:7], off offset:512
	global_load_dwordx2 v[176:177], v[0:1], off offset:1024
	global_load_dwordx2 v[178:179], v[6:7], off offset:1024
	global_load_dwordx2 v[144:145], v[0:1], off offset:1536
	global_load_dwordx2 v[146:147], v[6:7], off offset:1536
	global_load_dwordx2 v[12:13], v[0:1], off offset:2048
	global_load_dwordx2 v[14:15], v[6:7], off offset:2048
	global_load_dwordx2 v[8:9], v[0:1], off offset:2560
	global_load_dwordx2 v[10:11], v[6:7], off offset:2560
	global_load_dwordx2 v[2:3], v[0:1], off offset:3072
	global_load_dwordx2 v[4:5], v[6:7], off offset:3072
	s_nop 0
	global_load_dwordx2 v[0:1], v[0:1], off offset:3584
	s_nop 0
	global_load_dwordx2 v[6:7], v[6:7], off offset:3584
	v_rcp_f32_e32 v209, v156
	v_cvt_f32_ubyte3_e32 v156, v203
	v_add_f32_e32 v156, 0.5, v156
	v_cvt_f32_ubyte1_e32 v203, v200
	v_cvt_f32_ubyte0_e32 v202, v200
	v_cvt_f32_ubyte3_e32 v213, v200
	v_cvt_f32_ubyte2_e32 v212, v200
	v_rcp_f32_e32 v211, v156
	v_pk_add_f32 v[212:213], v[212:213], 0.5 op_sel_hi:[1,0]
	v_pk_add_f32 v[202:203], v[202:203], 0.5 op_sel_hi:[1,0]
	v_cvt_f32_ubyte0_e32 v156, v198
	v_pk_mul_f32 v[202:203], v[202:203], v[204:205]
	v_pk_mul_f32 v[204:205], v[212:213], v[208:209]
	v_pk_mul_f32 v[32:33], v[32:33], v[202:203]
	v_pk_mul_f32 v[34:35], v[34:35], v[204:205]
	v_cvt_f32_ubyte3_e32 v205, v201
	v_cvt_f32_ubyte2_e32 v204, v201
	v_cvt_f32_ubyte1_e32 v203, v201
	v_cvt_f32_ubyte0_e32 v202, v201
	v_pk_add_f32 v[200:201], v[204:205], 0.5 op_sel_hi:[1,0]
	v_add_f32_e32 v156, 0.5, v156
	v_pk_mul_f32 v[200:201], v[200:201], v[210:211]
	v_pk_add_f32 v[202:203], v[202:203], 0.5 op_sel_hi:[1,0]
	v_pk_mul_f32 v[38:39], v[38:39], v[200:201]
	v_rcp_f32_e32 v200, v156
	v_cvt_f32_ubyte0_e32 v156, v199
	v_pk_mul_f32 v[202:203], v[202:203], v[206:207]
	v_add_f32_e32 v156, 0.5, v156
	v_pk_mul_f32 v[36:37], v[36:37], v[202:203]
	v_rcp_f32_e32 v202, v156
	v_cvt_f32_ubyte1_e32 v156, v198
	v_add_f32_e32 v156, 0.5, v156
	v_rcp_f32_e32 v201, v156
	v_cvt_f32_ubyte1_e32 v156, v199
	v_add_f32_e32 v156, 0.5, v156
	v_rcp_f32_e32 v203, v156
	v_cvt_f32_ubyte2_e32 v156, v198
	v_add_f32_e32 v156, 0.5, v156
	v_rcp_f32_e32 v204, v156
	v_cvt_f32_ubyte2_e32 v156, v199
	v_add_f32_e32 v156, 0.5, v156
	v_rcp_f32_e32 v206, v156
	v_cvt_f32_ubyte3_e32 v156, v198
	v_add_f32_e32 v156, 0.5, v156
	v_rcp_f32_e32 v205, v156
	v_cvt_f32_ubyte3_e32 v156, v199
	v_add_f32_e32 v156, 0.5, v156
	v_cvt_f32_ubyte1_e32 v199, v196
	v_cvt_f32_ubyte0_e32 v198, v196
	v_cvt_f32_ubyte3_e32 v209, v196
	v_cvt_f32_ubyte2_e32 v208, v196
	v_rcp_f32_e32 v207, v156
	v_pk_add_f32 v[208:209], v[208:209], 0.5 op_sel_hi:[1,0]
	v_pk_add_f32 v[198:199], v[198:199], 0.5 op_sel_hi:[1,0]
	v_cvt_f32_ubyte0_e32 v156, v194
	v_pk_mul_f32 v[198:199], v[198:199], v[200:201]
	v_pk_mul_f32 v[200:201], v[208:209], v[204:205]
	v_pk_mul_f32 v[64:65], v[64:65], v[198:199]
	v_pk_mul_f32 v[66:67], v[66:67], v[200:201]
	v_cvt_f32_ubyte3_e32 v201, v197
	v_cvt_f32_ubyte2_e32 v200, v197
	v_cvt_f32_ubyte1_e32 v199, v197
	v_cvt_f32_ubyte0_e32 v198, v197
	v_pk_add_f32 v[196:197], v[200:201], 0.5 op_sel_hi:[1,0]
	v_add_f32_e32 v156, 0.5, v156
	v_pk_mul_f32 v[196:197], v[196:197], v[206:207]
	v_pk_add_f32 v[198:199], v[198:199], 0.5 op_sel_hi:[1,0]
	v_pk_mul_f32 v[70:71], v[70:71], v[196:197]
	v_rcp_f32_e32 v196, v156
	v_cvt_f32_ubyte0_e32 v156, v195
	v_pk_mul_f32 v[198:199], v[198:199], v[202:203]
	v_add_f32_e32 v156, 0.5, v156
	v_pk_mul_f32 v[68:69], v[68:69], v[198:199]
	v_rcp_f32_e32 v198, v156
	v_cvt_f32_ubyte1_e32 v156, v194
	v_add_f32_e32 v156, 0.5, v156
	v_rcp_f32_e32 v197, v156
	v_cvt_f32_ubyte1_e32 v156, v195
	v_add_f32_e32 v156, 0.5, v156
	v_rcp_f32_e32 v199, v156
	v_cvt_f32_ubyte2_e32 v156, v194
	v_add_f32_e32 v156, 0.5, v156
	v_rcp_f32_e32 v200, v156
	v_cvt_f32_ubyte2_e32 v156, v195
	v_add_f32_e32 v156, 0.5, v156
	v_rcp_f32_e32 v202, v156
	v_cvt_f32_ubyte3_e32 v156, v194
	v_add_f32_e32 v156, 0.5, v156
	v_rcp_f32_e32 v201, v156
	v_cvt_f32_ubyte3_e32 v156, v195
	v_add_f32_e32 v156, 0.5, v156
	v_cvt_f32_ubyte1_e32 v195, v192
	v_cvt_f32_ubyte0_e32 v194, v192
	v_cvt_f32_ubyte3_e32 v205, v192
	v_cvt_f32_ubyte2_e32 v204, v192
	v_rcp_f32_e32 v203, v156
	v_pk_add_f32 v[204:205], v[204:205], 0.5 op_sel_hi:[1,0]
	v_pk_add_f32 v[194:195], v[194:195], 0.5 op_sel_hi:[1,0]
	v_cvt_f32_ubyte0_e32 v156, v190
	v_pk_mul_f32 v[194:195], v[194:195], v[196:197]
	v_pk_mul_f32 v[196:197], v[204:205], v[200:201]
	v_pk_mul_f32 v[40:41], v[40:41], v[194:195]
	v_pk_mul_f32 v[42:43], v[42:43], v[196:197]
	v_cvt_f32_ubyte3_e32 v197, v193
	v_cvt_f32_ubyte2_e32 v196, v193
	v_cvt_f32_ubyte1_e32 v195, v193
	v_cvt_f32_ubyte0_e32 v194, v193
	v_pk_add_f32 v[192:193], v[196:197], 0.5 op_sel_hi:[1,0]
	v_add_f32_e32 v156, 0.5, v156
	v_pk_mul_f32 v[192:193], v[192:193], v[202:203]
	v_pk_add_f32 v[194:195], v[194:195], 0.5 op_sel_hi:[1,0]
	v_pk_mul_f32 v[46:47], v[46:47], v[192:193]
	v_rcp_f32_e32 v192, v156
	v_cvt_f32_ubyte0_e32 v156, v191
	v_pk_mul_f32 v[194:195], v[194:195], v[198:199]
	v_add_f32_e32 v156, 0.5, v156
	v_pk_mul_f32 v[44:45], v[44:45], v[194:195]
	v_rcp_f32_e32 v194, v156
	v_cvt_f32_ubyte1_e32 v156, v190
	v_add_f32_e32 v156, 0.5, v156
	v_rcp_f32_e32 v193, v156
	v_cvt_f32_ubyte1_e32 v156, v191
	v_add_f32_e32 v156, 0.5, v156
	v_rcp_f32_e32 v195, v156
	v_cvt_f32_ubyte2_e32 v156, v190
	v_add_f32_e32 v156, 0.5, v156
	v_rcp_f32_e32 v196, v156
	v_cvt_f32_ubyte2_e32 v156, v191
	v_add_f32_e32 v156, 0.5, v156
	v_rcp_f32_e32 v198, v156
	v_cvt_f32_ubyte3_e32 v156, v190
	v_add_f32_e32 v156, 0.5, v156
	v_rcp_f32_e32 v197, v156
	v_cvt_f32_ubyte3_e32 v156, v191
	v_add_f32_e32 v156, 0.5, v156
	v_cvt_f32_ubyte1_e32 v191, v188
	v_cvt_f32_ubyte0_e32 v190, v188
	v_cvt_f32_ubyte3_e32 v201, v188
	v_cvt_f32_ubyte2_e32 v200, v188
	v_rcp_f32_e32 v199, v156
	v_pk_add_f32 v[200:201], v[200:201], 0.5 op_sel_hi:[1,0]
	v_pk_add_f32 v[190:191], v[190:191], 0.5 op_sel_hi:[1,0]
	s_waitcnt vmcnt(0)
	v_cvt_f32_ubyte0_e32 v156, v186
	v_pk_mul_f32 v[190:191], v[190:191], v[192:193]
	v_pk_mul_f32 v[192:193], v[200:201], v[196:197]
	v_pk_mul_f32 v[72:73], v[72:73], v[190:191]
	v_pk_mul_f32 v[74:75], v[74:75], v[192:193]
	v_cvt_f32_ubyte3_e32 v193, v189
	v_cvt_f32_ubyte2_e32 v192, v189
	v_cvt_f32_ubyte1_e32 v191, v189
	v_cvt_f32_ubyte0_e32 v190, v189
	v_pk_add_f32 v[188:189], v[192:193], 0.5 op_sel_hi:[1,0]
	v_add_f32_e32 v156, 0.5, v156
	v_pk_mul_f32 v[188:189], v[188:189], v[198:199]
	v_pk_add_f32 v[190:191], v[190:191], 0.5 op_sel_hi:[1,0]
	v_pk_mul_f32 v[78:79], v[78:79], v[188:189]
	v_rcp_f32_e32 v188, v156
	v_cvt_f32_ubyte0_e32 v156, v187
	v_pk_mul_f32 v[190:191], v[190:191], v[194:195]
	v_add_f32_e32 v156, 0.5, v156
	v_pk_mul_f32 v[76:77], v[76:77], v[190:191]
	v_rcp_f32_e32 v190, v156
	v_cvt_f32_ubyte1_e32 v156, v186
	v_add_f32_e32 v156, 0.5, v156
	v_rcp_f32_e32 v189, v156
	v_cvt_f32_ubyte1_e32 v156, v187
	v_add_f32_e32 v156, 0.5, v156
	v_rcp_f32_e32 v191, v156
	v_cvt_f32_ubyte2_e32 v156, v186
	v_add_f32_e32 v156, 0.5, v156
	v_rcp_f32_e32 v192, v156
	v_cvt_f32_ubyte2_e32 v156, v187
	v_add_f32_e32 v156, 0.5, v156
	v_rcp_f32_e32 v194, v156
	v_cvt_f32_ubyte3_e32 v156, v186
	v_add_f32_e32 v156, 0.5, v156
	v_rcp_f32_e32 v193, v156
	v_cvt_f32_ubyte3_e32 v156, v187
	v_add_f32_e32 v156, 0.5, v156
	v_cvt_f32_ubyte1_e32 v187, v184
	v_cvt_f32_ubyte0_e32 v186, v184
	v_cvt_f32_ubyte3_e32 v197, v184
	v_cvt_f32_ubyte2_e32 v196, v184
	v_rcp_f32_e32 v195, v156
	v_pk_add_f32 v[196:197], v[196:197], 0.5 op_sel_hi:[1,0]
	v_pk_add_f32 v[186:187], v[186:187], 0.5 op_sel_hi:[1,0]
	v_cvt_f32_ubyte0_e32 v156, v182
	v_pk_mul_f32 v[186:187], v[186:187], v[188:189]
	v_pk_mul_f32 v[188:189], v[196:197], v[192:193]
	v_pk_mul_f32 v[80:81], v[80:81], v[186:187]
	v_pk_mul_f32 v[82:83], v[82:83], v[188:189]
	v_cvt_f32_ubyte3_e32 v189, v185
	v_cvt_f32_ubyte2_e32 v188, v185
	v_cvt_f32_ubyte1_e32 v187, v185
	v_cvt_f32_ubyte0_e32 v186, v185
	v_pk_add_f32 v[184:185], v[188:189], 0.5 op_sel_hi:[1,0]
	v_add_f32_e32 v156, 0.5, v156
	v_pk_mul_f32 v[184:185], v[184:185], v[194:195]
	v_pk_add_f32 v[186:187], v[186:187], 0.5 op_sel_hi:[1,0]
	v_pk_mul_f32 v[86:87], v[86:87], v[184:185]
	v_rcp_f32_e32 v184, v156
	v_cvt_f32_ubyte0_e32 v156, v183
	v_pk_mul_f32 v[186:187], v[186:187], v[190:191]
	v_add_f32_e32 v156, 0.5, v156
	v_pk_mul_f32 v[84:85], v[84:85], v[186:187]
	v_rcp_f32_e32 v186, v156
	v_cvt_f32_ubyte1_e32 v156, v182
	v_add_f32_e32 v156, 0.5, v156
	v_rcp_f32_e32 v185, v156
	v_cvt_f32_ubyte1_e32 v156, v183
	v_add_f32_e32 v156, 0.5, v156
	v_rcp_f32_e32 v187, v156
	v_cvt_f32_ubyte2_e32 v156, v182
	v_add_f32_e32 v156, 0.5, v156
	v_rcp_f32_e32 v188, v156
	v_cvt_f32_ubyte2_e32 v156, v183
	v_add_f32_e32 v156, 0.5, v156
	v_rcp_f32_e32 v190, v156
	v_cvt_f32_ubyte3_e32 v156, v182
	v_add_f32_e32 v156, 0.5, v156
	v_rcp_f32_e32 v189, v156
	v_cvt_f32_ubyte3_e32 v156, v183
	v_add_f32_e32 v156, 0.5, v156
	v_cvt_f32_ubyte1_e32 v183, v180
	v_cvt_f32_ubyte0_e32 v182, v180
	v_cvt_f32_ubyte3_e32 v193, v180
	v_cvt_f32_ubyte2_e32 v192, v180
	v_rcp_f32_e32 v191, v156
	v_pk_add_f32 v[192:193], v[192:193], 0.5 op_sel_hi:[1,0]
	v_pk_add_f32 v[182:183], v[182:183], 0.5 op_sel_hi:[1,0]
	v_cvt_f32_ubyte0_e32 v156, v178
	v_pk_mul_f32 v[182:183], v[182:183], v[184:185]
	v_pk_mul_f32 v[184:185], v[192:193], v[188:189]
	v_pk_mul_f32 v[112:113], v[112:113], v[182:183]
	v_pk_mul_f32 v[114:115], v[114:115], v[184:185]
	v_cvt_f32_ubyte3_e32 v185, v181
	v_cvt_f32_ubyte2_e32 v184, v181
	v_cvt_f32_ubyte1_e32 v183, v181
	v_cvt_f32_ubyte0_e32 v182, v181
	v_pk_add_f32 v[180:181], v[184:185], 0.5 op_sel_hi:[1,0]
	v_add_f32_e32 v156, 0.5, v156
	v_pk_mul_f32 v[180:181], v[180:181], v[190:191]
	v_pk_add_f32 v[182:183], v[182:183], 0.5 op_sel_hi:[1,0]
	v_pk_mul_f32 v[118:119], v[118:119], v[180:181]
	v_rcp_f32_e32 v180, v156
	v_cvt_f32_ubyte0_e32 v156, v179
	v_pk_mul_f32 v[182:183], v[182:183], v[186:187]
	v_add_f32_e32 v156, 0.5, v156
	v_pk_mul_f32 v[116:117], v[116:117], v[182:183]
	v_rcp_f32_e32 v182, v156
	v_cvt_f32_ubyte1_e32 v156, v178
	v_add_f32_e32 v156, 0.5, v156
	v_rcp_f32_e32 v181, v156
	v_cvt_f32_ubyte1_e32 v156, v179
	v_add_f32_e32 v156, 0.5, v156
	v_rcp_f32_e32 v183, v156
	v_cvt_f32_ubyte2_e32 v156, v178
	v_add_f32_e32 v156, 0.5, v156
	v_rcp_f32_e32 v184, v156
	v_cvt_f32_ubyte2_e32 v156, v179
	v_add_f32_e32 v156, 0.5, v156
	v_rcp_f32_e32 v186, v156
	v_cvt_f32_ubyte3_e32 v156, v178
	v_add_f32_e32 v156, 0.5, v156
	v_rcp_f32_e32 v185, v156
	v_cvt_f32_ubyte3_e32 v156, v179
	v_add_f32_e32 v156, 0.5, v156
	v_cvt_f32_ubyte1_e32 v179, v176
	v_cvt_f32_ubyte0_e32 v178, v176
	v_cvt_f32_ubyte3_e32 v189, v176
	v_cvt_f32_ubyte2_e32 v188, v176
	v_rcp_f32_e32 v187, v156
	v_pk_add_f32 v[188:189], v[188:189], 0.5 op_sel_hi:[1,0]
	v_pk_add_f32 v[178:179], v[178:179], 0.5 op_sel_hi:[1,0]
	v_cvt_f32_ubyte0_e32 v156, v146
	v_pk_mul_f32 v[178:179], v[178:179], v[180:181]
	v_pk_mul_f32 v[180:181], v[188:189], v[184:185]
	v_pk_mul_f32 v[88:89], v[88:89], v[178:179]
	v_pk_mul_f32 v[90:91], v[90:91], v[180:181]
	v_cvt_f32_ubyte3_e32 v181, v177
	v_cvt_f32_ubyte2_e32 v180, v177
	v_cvt_f32_ubyte1_e32 v179, v177
	v_cvt_f32_ubyte0_e32 v178, v177
	v_pk_add_f32 v[176:177], v[180:181], 0.5 op_sel_hi:[1,0]
	v_add_f32_e32 v156, 0.5, v156
	v_pk_mul_f32 v[176:177], v[176:177], v[186:187]
	v_pk_add_f32 v[178:179], v[178:179], 0.5 op_sel_hi:[1,0]
	v_pk_mul_f32 v[94:95], v[94:95], v[176:177]
	v_rcp_f32_e32 v176, v156
	v_cvt_f32_ubyte0_e32 v156, v147
	v_pk_mul_f32 v[178:179], v[178:179], v[182:183]
	v_add_f32_e32 v156, 0.5, v156
	v_pk_mul_f32 v[92:93], v[92:93], v[178:179]
	v_rcp_f32_e32 v178, v156
	v_cvt_f32_ubyte1_e32 v156, v146
	v_add_f32_e32 v156, 0.5, v156
	v_rcp_f32_e32 v177, v156
	v_cvt_f32_ubyte1_e32 v156, v147
	v_add_f32_e32 v156, 0.5, v156
	v_rcp_f32_e32 v179, v156
	v_cvt_f32_ubyte2_e32 v156, v146
	v_cvt_f32_ubyte3_e32 v146, v146
	v_add_f32_e32 v156, 0.5, v156
	v_add_f32_e32 v146, 0.5, v146
	v_rcp_f32_e32 v180, v156
	v_rcp_f32_e32 v181, v146
	v_cvt_f32_ubyte3_e32 v146, v147
	v_cvt_f32_ubyte2_e32 v156, v147
	v_add_f32_e32 v146, 0.5, v146
	v_add_f32_e32 v156, 0.5, v156
	v_rcp_f32_e32 v183, v146
	v_cvt_f32_ubyte1_e32 v147, v144
	v_cvt_f32_ubyte0_e32 v146, v144
	v_cvt_f32_ubyte3_e32 v185, v144
	v_cvt_f32_ubyte2_e32 v184, v144
	v_rcp_f32_e32 v182, v156
	v_pk_add_f32 v[184:185], v[184:185], 0.5 op_sel_hi:[1,0]
	v_pk_add_f32 v[146:147], v[146:147], 0.5 op_sel_hi:[1,0]
	v_cvt_f32_ubyte2_e32 v156, v14
	v_pk_mul_f32 v[146:147], v[146:147], v[176:177]
	v_pk_mul_f32 v[176:177], v[184:185], v[180:181]
	v_pk_mul_f32 v[120:121], v[120:121], v[146:147]
	v_pk_mul_f32 v[122:123], v[122:123], v[176:177]
	v_cvt_f32_ubyte3_e32 v177, v145
	v_cvt_f32_ubyte2_e32 v176, v145
	v_cvt_f32_ubyte1_e32 v147, v145
	v_cvt_f32_ubyte0_e32 v146, v145
	v_pk_add_f32 v[144:145], v[176:177], 0.5 op_sel_hi:[1,0]
	v_pk_add_f32 v[146:147], v[146:147], 0.5 op_sel_hi:[1,0]
	v_pk_mul_f32 v[144:145], v[144:145], v[182:183]
	v_pk_mul_f32 v[146:147], v[146:147], v[178:179]
	v_pk_mul_f32 v[126:127], v[126:127], v[144:145]
	v_cvt_f32_ubyte0_e32 v145, v15
	v_add_f32_e32 v145, 0.5, v145
	v_pk_mul_f32 v[124:125], v[124:125], v[146:147]
	v_cvt_f32_ubyte0_e32 v144, v14
	v_rcp_f32_e32 v146, v145
	v_cvt_f32_ubyte1_e32 v145, v14
	v_cvt_f32_ubyte3_e32 v14, v14
	v_add_f32_e32 v144, 0.5, v144
	v_add_f32_e32 v145, 0.5, v145
	v_add_f32_e32 v156, 0.5, v156
	v_add_f32_e32 v14, 0.5, v14
	v_rcp_f32_e32 v144, v144
	v_rcp_f32_e32 v145, v145
	v_rcp_f32_e32 v176, v156
	v_rcp_f32_e32 v177, v14
	v_cvt_f32_ubyte3_e32 v14, v15
	v_cvt_f32_ubyte2_e32 v156, v15
	v_add_f32_e32 v14, 0.5, v14
	v_cvt_f32_ubyte1_e32 v147, v15
	v_add_f32_e32 v156, 0.5, v156
	v_rcp_f32_e32 v179, v14
	v_cvt_f32_ubyte1_e32 v15, v12
	v_cvt_f32_ubyte0_e32 v14, v12
	v_cvt_f32_ubyte3_e32 v181, v12
	v_cvt_f32_ubyte2_e32 v180, v12
	v_rcp_f32_e32 v178, v156
	v_pk_add_f32 v[180:181], v[180:181], 0.5 op_sel_hi:[1,0]
	v_pk_add_f32 v[14:15], v[14:15], 0.5 op_sel_hi:[1,0]
	v_add_f32_e32 v147, 0.5, v147
	v_pk_mul_f32 v[14:15], v[14:15], v[144:145]
	v_pk_mul_f32 v[144:145], v[180:181], v[176:177]
	v_rcp_f32_e32 v147, v147
	v_pk_mul_f32 v[98:99], v[98:99], v[144:145]
	v_cvt_f32_ubyte3_e32 v145, v13
	v_cvt_f32_ubyte2_e32 v144, v13
	v_pk_mul_f32 v[96:97], v[96:97], v[14:15]
	v_cvt_f32_ubyte1_e32 v15, v13
	v_cvt_f32_ubyte0_e32 v14, v13
	v_pk_add_f32 v[12:13], v[144:145], 0.5 op_sel_hi:[1,0]
	v_pk_add_f32 v[14:15], v[14:15], 0.5 op_sel_hi:[1,0]
	v_pk_mul_f32 v[12:13], v[12:13], v[178:179]
	v_pk_mul_f32 v[14:15], v[14:15], v[146:147]
	v_pk_mul_f32 v[102:103], v[102:103], v[12:13]
	v_cvt_f32_ubyte0_e32 v13, v11
	v_add_f32_e32 v13, 0.5, v13
	v_pk_mul_f32 v[100:101], v[100:101], v[14:15]
	v_cvt_f32_ubyte0_e32 v12, v10
	v_rcp_f32_e32 v14, v13
	v_cvt_f32_ubyte1_e32 v13, v10
	v_cvt_f32_ubyte2_e32 v144, v10
	v_cvt_f32_ubyte2_e32 v145, v11
	v_cvt_f32_ubyte3_e32 v10, v10
	v_add_f32_e32 v12, 0.5, v12
	v_add_f32_e32 v13, 0.5, v13
	v_add_f32_e32 v144, 0.5, v144
	v_add_f32_e32 v145, 0.5, v145
	v_add_f32_e32 v10, 0.5, v10
	v_rcp_f32_e32 v12, v12
	v_rcp_f32_e32 v13, v13
	v_rcp_f32_e32 v144, v144
	v_rcp_f32_e32 v146, v145
	v_rcp_f32_e32 v145, v10
	v_cvt_f32_ubyte3_e32 v10, v11
	v_add_f32_e32 v10, 0.5, v10
	v_cvt_f32_ubyte1_e32 v15, v11
	v_rcp_f32_e32 v147, v10
	v_cvt_f32_ubyte1_e32 v11, v8
	v_cvt_f32_ubyte0_e32 v10, v8
	v_cvt_f32_ubyte3_e32 v177, v8
	v_cvt_f32_ubyte2_e32 v176, v8
	v_pk_add_f32 v[176:177], v[176:177], 0.5 op_sel_hi:[1,0]
	v_pk_add_f32 v[10:11], v[10:11], 0.5 op_sel_hi:[1,0]
	v_add_f32_e32 v15, 0.5, v15
	v_pk_mul_f32 v[10:11], v[10:11], v[12:13]
	v_pk_mul_f32 v[12:13], v[176:177], v[144:145]
	v_rcp_f32_e32 v15, v15
	v_pk_mul_f32 v[130:131], v[130:131], v[12:13]
	v_cvt_f32_ubyte3_e32 v13, v9
	v_cvt_f32_ubyte2_e32 v12, v9
	v_pk_mul_f32 v[128:129], v[128:129], v[10:11]
	v_cvt_f32_ubyte1_e32 v11, v9
	v_cvt_f32_ubyte0_e32 v10, v9
	v_pk_add_f32 v[8:9], v[12:13], 0.5 op_sel_hi:[1,0]
	v_pk_add_f32 v[10:11], v[10:11], 0.5 op_sel_hi:[1,0]
	v_pk_mul_f32 v[8:9], v[8:9], v[146:147]
	v_pk_mul_f32 v[10:11], v[10:11], v[14:15]
	v_pk_mul_f32 v[134:135], v[134:135], v[8:9]
	v_cvt_f32_ubyte0_e32 v9, v5
	v_add_f32_e32 v9, 0.5, v9
	v_pk_mul_f32 v[132:133], v[132:133], v[10:11]
	v_cvt_f32_ubyte0_e32 v8, v4
	v_rcp_f32_e32 v10, v9
	v_cvt_f32_ubyte1_e32 v9, v4
	v_cvt_f32_ubyte2_e32 v12, v4
	v_cvt_f32_ubyte2_e32 v13, v5
	v_cvt_f32_ubyte3_e32 v4, v4
	v_add_f32_e32 v8, 0.5, v8
	v_add_f32_e32 v9, 0.5, v9
	v_add_f32_e32 v12, 0.5, v12
	v_add_f32_e32 v13, 0.5, v13
	v_add_f32_e32 v4, 0.5, v4
	v_rcp_f32_e32 v8, v8
	v_rcp_f32_e32 v9, v9
	v_rcp_f32_e32 v12, v12
	v_rcp_f32_e32 v14, v13
	v_rcp_f32_e32 v13, v4
	v_cvt_f32_ubyte3_e32 v4, v5
	v_add_f32_e32 v4, 0.5, v4
	v_cvt_f32_ubyte1_e32 v11, v5
	v_rcp_f32_e32 v15, v4
	v_cvt_f32_ubyte1_e32 v5, v2
	v_cvt_f32_ubyte0_e32 v4, v2
	v_cvt_f32_ubyte3_e32 v145, v2
	v_cvt_f32_ubyte2_e32 v144, v2
	v_pk_add_f32 v[144:145], v[144:145], 0.5 op_sel_hi:[1,0]
	v_pk_add_f32 v[4:5], v[4:5], 0.5 op_sel_hi:[1,0]
	v_add_f32_e32 v11, 0.5, v11
	v_pk_mul_f32 v[4:5], v[4:5], v[8:9]
	v_pk_mul_f32 v[8:9], v[144:145], v[12:13]
	v_rcp_f32_e32 v11, v11
	v_pk_mul_f32 v[106:107], v[106:107], v[8:9]
	v_cvt_f32_ubyte3_e32 v9, v3
	v_cvt_f32_ubyte2_e32 v8, v3
	v_pk_mul_f32 v[104:105], v[104:105], v[4:5]
	v_cvt_f32_ubyte1_e32 v5, v3
	v_cvt_f32_ubyte0_e32 v4, v3
	v_pk_add_f32 v[2:3], v[8:9], 0.5 op_sel_hi:[1,0]
	v_pk_add_f32 v[4:5], v[4:5], 0.5 op_sel_hi:[1,0]
	v_pk_mul_f32 v[2:3], v[2:3], v[14:15]
	v_pk_mul_f32 v[4:5], v[4:5], v[10:11]
	v_pk_mul_f32 v[110:111], v[110:111], v[2:3]
	v_cvt_f32_ubyte0_e32 v3, v7
	v_add_f32_e32 v3, 0.5, v3
	v_pk_mul_f32 v[108:109], v[108:109], v[4:5]
	v_cvt_f32_ubyte0_e32 v2, v6
	v_rcp_f32_e32 v4, v3
	v_cvt_f32_ubyte1_e32 v3, v6
	v_cvt_f32_ubyte2_e32 v8, v6
	v_cvt_f32_ubyte2_e32 v9, v7
	v_cvt_f32_ubyte3_e32 v6, v6
	v_add_f32_e32 v2, 0.5, v2
	v_add_f32_e32 v3, 0.5, v3
	v_add_f32_e32 v8, 0.5, v8
	v_add_f32_e32 v9, 0.5, v9
	v_add_f32_e32 v6, 0.5, v6
	v_rcp_f32_e32 v2, v2
	v_rcp_f32_e32 v3, v3
	v_rcp_f32_e32 v8, v8
	v_rcp_f32_e32 v10, v9
	v_rcp_f32_e32 v9, v6
	v_cvt_f32_ubyte3_e32 v6, v7
	v_cvt_f32_ubyte1_e32 v5, v7
	v_add_f32_e32 v6, 0.5, v6
	v_add_f32_e32 v5, 0.5, v5
	v_rcp_f32_e32 v11, v6
	v_cvt_f32_ubyte1_e32 v7, v0
	v_cvt_f32_ubyte0_e32 v6, v0
	v_cvt_f32_ubyte3_e32 v13, v0
	v_cvt_f32_ubyte2_e32 v12, v0
	v_rcp_f32_e32 v5, v5
	v_pk_add_f32 v[12:13], v[12:13], 0.5 op_sel_hi:[1,0]
	v_pk_add_f32 v[6:7], v[6:7], 0.5 op_sel_hi:[1,0]
	s_nop 0
	v_pk_mul_f32 v[2:3], v[6:7], v[2:3]
	v_pk_mul_f32 v[6:7], v[12:13], v[8:9]
	v_pk_mul_f32 v[144:145], v[136:137], v[2:3]
	v_pk_mul_f32 v[146:147], v[138:139], v[6:7]
	v_cvt_f32_ubyte1_e32 v3, v1
	v_cvt_f32_ubyte0_e32 v2, v1
	v_cvt_f32_ubyte3_e32 v7, v1
	v_cvt_f32_ubyte2_e32 v6, v1
	v_pk_add_f32 v[0:1], v[6:7], 0.5 op_sel_hi:[1,0]
	v_pk_add_f32 v[2:3], v[2:3], 0.5 op_sel_hi:[1,0]
	v_pk_mul_f32 v[0:1], v[0:1], v[10:11]
	v_pk_mul_f32 v[2:3], v[2:3], v[4:5]
	v_pk_mul_f32 v[138:139], v[142:143], v[0:1]
	v_pk_mul_f32 v[136:137], v[140:141], v[2:3]
	ds_read_b128 v[8:11], v231
	ds_read_b128 v[12:15], v231 offset:1024
	ds_read_b128 v[0:3], v231 offset:2048
	ds_read_b128 v[4:7], v231 offset:3072
	s_add_u32 s56, s48, 0x40680
	s_addc_u32 s57, s49, 0
	s_mov_b32 m0, s94
	v_lshl_add_u64 v[140:141], s[56:57], 0, v[148:149]
	ds_read_b128 v[176:179], v228
	ds_read_b128 v[180:183], v228 offset:1024
	ds_read_b128 v[184:187], v228 offset:2048
	ds_read_b128 v[188:191], v228 offset:3072
	ds_read_b128 v[192:195], v228 offset:4096
	ds_read_b128 v[196:199], v228 offset:5120
	ds_read_b128 v[200:203], v228 offset:6144
	ds_read_b128 v[204:207], v228 offset:7168
	global_load_lds_dwordx4 v[140:141], off
	v_lshl_add_u64 v[140:141], s[56:57], 0, v[152:153]
	s_mov_b32 m0, s93
	s_nop 0
	global_load_lds_dwordx4 v[140:141], off
	s_waitcnt lgkmcnt(8)
	s_barrier
	s_waitcnt lgkmcnt(0)
	s_setprio 1
	s_waitcnt lgkmcnt(0)
	v_mfma_scale_f32_16x16x128_f8f6f4 v[16:19], v[8:15], v[176:183], v[16:19], v225, v225 op_sel_hi:[0,0,0]
	v_mfma_scale_f32_16x16x128_f8f6f4 v[20:23], v[0:7], v[176:183], v[20:23], v225, v225 op_sel_hi:[0,0,0]
	v_mfma_scale_f32_16x16x128_f8f6f4 v[24:27], v[8:15], v[184:191], v[24:27], v225, v225 op_sel_hi:[0,0,0]
	v_mfma_scale_f32_16x16x128_f8f6f4 v[28:31], v[0:7], v[184:191], v[28:31], v225, v225 op_sel_hi:[0,0,0]
	v_mfma_scale_f32_16x16x128_f8f6f4 v[32:35], v[8:15], v[192:199], v[32:35], v225, v225 op_sel_hi:[0,0,0]
	v_mfma_scale_f32_16x16x128_f8f6f4 v[36:39], v[0:7], v[192:199], v[36:39], v225, v225 op_sel_hi:[0,0,0]
	v_mfma_scale_f32_16x16x128_f8f6f4 v[40:43], v[8:15], v[200:207], v[40:43], v225, v225 op_sel_hi:[0,0,0]
	v_mfma_scale_f32_16x16x128_f8f6f4 v[44:47], v[0:7], v[200:207], v[44:47], v225, v225 op_sel_hi:[0,0,0]
	s_setprio 0
	s_barrier
	s_mov_b32 m0, s96
	v_lshl_add_u64 v[140:141], v[170:171], 0, s[30:31]
	ds_read_b128 v[208:211], v232
	ds_read_b128 v[212:215], v232 offset:1024
	ds_read_b128 v[236:239], v232 offset:2048
	ds_read_b128 v[240:243], v232 offset:3072
	global_load_lds_dwordx4 v[140:141], off
	v_lshl_add_u64 v[140:141], v[172:173], 0, s[30:31]
	s_mov_b32 m0, s95
	s_nop 0
	global_load_lds_dwordx4 v[140:141], off
	s_barrier
	s_waitcnt lgkmcnt(0)
	s_setprio 1
	s_waitcnt lgkmcnt(0)
	v_mfma_scale_f32_16x16x128_f8f6f4 v[48:51], v[208:215], v[176:183], v[48:51], v225, v225 op_sel_hi:[0,0,0]
	v_mfma_scale_f32_16x16x128_f8f6f4 v[52:55], v[236:243], v[176:183], v[52:55], v225, v225 op_sel_hi:[0,0,0]
	v_mfma_scale_f32_16x16x128_f8f6f4 v[56:59], v[208:215], v[184:191], v[56:59], v225, v225 op_sel_hi:[0,0,0]
	v_mfma_scale_f32_16x16x128_f8f6f4 v[60:63], v[236:243], v[184:191], v[60:63], v225, v225 op_sel_hi:[0,0,0]
	v_mfma_scale_f32_16x16x128_f8f6f4 v[64:67], v[208:215], v[192:199], v[64:67], v225, v225 op_sel_hi:[0,0,0]
	v_mfma_scale_f32_16x16x128_f8f6f4 v[68:71], v[236:243], v[192:199], v[68:71], v225, v225 op_sel_hi:[0,0,0]
	v_mfma_scale_f32_16x16x128_f8f6f4 v[72:75], v[208:215], v[200:207], v[72:75], v225, v225 op_sel_hi:[0,0,0]
	v_mfma_scale_f32_16x16x128_f8f6f4 v[76:79], v[236:243], v[200:207], v[76:79], v225, v225 op_sel_hi:[0,0,0]
	s_setprio 0
	s_mov_b32 m0, s73
	v_lshl_add_u64 v[140:141], v[174:175], 0, s[30:31]
	s_barrier
	ds_read_b128 v[176:179], v228 offset:16384
	ds_read_b128 v[180:183], v228 offset:17408
	ds_read_b128 v[184:187], v228 offset:18432
	ds_read_b128 v[188:191], v228 offset:19456
	ds_read_b128 v[192:195], v228 offset:20480
	ds_read_b128 v[196:199], v228 offset:21504
	ds_read_b128 v[200:203], v228 offset:22528
	ds_read_b128 v[204:207], v228 offset:23552
	global_load_lds_dwordx4 v[140:141], off
	v_lshl_add_u64 v[140:141], v[168:169], 0, s[30:31]
	s_mov_b32 m0, s74
	s_nop 0
	global_load_lds_dwordx4 v[140:141], off
	s_barrier
	s_waitcnt lgkmcnt(0)
	s_setprio 1
	s_waitcnt lgkmcnt(0)
	v_mfma_scale_f32_16x16x128_f8f6f4 v[80:83], v[8:15], v[176:183], v[80:83], v225, v225 op_sel_hi:[0,0,0]
	v_mfma_scale_f32_16x16x128_f8f6f4 v[84:87], v[0:7], v[176:183], v[84:87], v225, v225 op_sel_hi:[0,0,0]
	v_mfma_scale_f32_16x16x128_f8f6f4 v[88:91], v[8:15], v[184:191], v[88:91], v225, v225 op_sel_hi:[0,0,0]
	v_mfma_scale_f32_16x16x128_f8f6f4 v[92:95], v[0:7], v[184:191], v[92:95], v225, v225 op_sel_hi:[0,0,0]
	v_mfma_scale_f32_16x16x128_f8f6f4 v[96:99], v[8:15], v[192:199], v[96:99], v225, v225 op_sel_hi:[0,0,0]
	v_mfma_scale_f32_16x16x128_f8f6f4 v[100:103], v[0:7], v[192:199], v[100:103], v225, v225 op_sel_hi:[0,0,0]
	v_mfma_scale_f32_16x16x128_f8f6f4 v[104:107], v[8:15], v[200:207], v[104:107], v225, v225 op_sel_hi:[0,0,0]
	v_mfma_scale_f32_16x16x128_f8f6f4 v[108:111], v[0:7], v[200:207], v[108:111], v225, v225 op_sel_hi:[0,0,0]
	s_setprio 0
	s_barrier
	s_add_u32 s56, s50, 0x40700
	s_addc_u32 s57, s51, 0
	s_mov_b32 m0, s97
	v_lshl_add_u64 v[0:1], s[56:57], 0, v[150:151]
	global_load_lds_dwordx4 v[0:1], off
	v_lshl_add_u64 v[0:1], s[56:57], 0, v[154:155]
	s_mov_b32 m0, s52
	s_nop 0
	global_load_lds_dwordx4 v[0:1], off
	s_waitcnt vmcnt(6)
	s_barrier
	s_setprio 1
	v_mfma_scale_f32_16x16x128_f8f6f4 v[112:115], v[208:215], v[176:183], v[112:115], v225, v225 op_sel_hi:[0,0,0]
	v_mfma_scale_f32_16x16x128_f8f6f4 v[116:119], v[236:243], v[176:183], v[116:119], v225, v225 op_sel_hi:[0,0,0]
	v_mfma_scale_f32_16x16x128_f8f6f4 v[120:123], v[208:215], v[184:191], v[120:123], v225, v225 op_sel_hi:[0,0,0]
	v_mfma_scale_f32_16x16x128_f8f6f4 v[124:127], v[236:243], v[184:191], v[124:127], v225, v225 op_sel_hi:[0,0,0]
	v_mfma_scale_f32_16x16x128_f8f6f4 v[128:131], v[208:215], v[192:199], v[128:131], v225, v225 op_sel_hi:[0,0,0]
	v_mfma_scale_f32_16x16x128_f8f6f4 v[132:135], v[236:243], v[192:199], v[132:135], v225, v225 op_sel_hi:[0,0,0]
	v_mfma_scale_f32_16x16x128_f8f6f4 v[144:147], v[208:215], v[200:207], v[144:147], v225, v225 op_sel_hi:[0,0,0]
	v_mfma_scale_f32_16x16x128_f8f6f4 v[136:139], v[236:243], v[200:207], v[136:139], v225, v225 op_sel_hi:[0,0,0]
	s_setprio 0
	s_barrier
	ds_read_b128 v[0:3], v235
	ds_read_b128 v[4:7], v235 offset:1024
	ds_read_b128 v[8:11], v235 offset:2048
	ds_read_b128 v[12:15], v235 offset:3072
	s_add_u32 s56, s48, 0x40700
	s_addc_u32 s57, s49, 0
	s_mov_b32 m0, s75
	v_lshl_add_u64 v[140:141], s[56:57], 0, v[148:149]
	ds_read_b128 v[176:179], v228 offset:32768
	ds_read_b128 v[180:183], v228 offset:33792
	ds_read_b128 v[184:187], v228 offset:34816
	ds_read_b128 v[188:191], v228 offset:35840
	ds_read_b128 v[192:195], v228 offset:36864
	ds_read_b128 v[196:199], v228 offset:37888
	ds_read_b128 v[200:203], v228 offset:38912
	ds_read_b128 v[204:207], v228 offset:39936
	global_load_lds_dwordx4 v[140:141], off
	v_lshl_add_u64 v[140:141], s[56:57], 0, v[152:153]
	s_mov_b32 m0, s76
	s_nop 0
	global_load_lds_dwordx4 v[140:141], off
	s_waitcnt lgkmcnt(8)
	s_barrier
	s_waitcnt lgkmcnt(0)
	s_setprio 1
	s_waitcnt lgkmcnt(0)
	v_mfma_scale_f32_16x16x128_f8f6f4 v[16:19], v[0:7], v[176:183], v[16:19], v225, v225 op_sel_hi:[0,0,0]
	v_mfma_scale_f32_16x16x128_f8f6f4 v[20:23], v[8:15], v[176:183], v[20:23], v225, v225 op_sel_hi:[0,0,0]
	v_mfma_scale_f32_16x16x128_f8f6f4 v[24:27], v[0:7], v[184:191], v[24:27], v225, v225 op_sel_hi:[0,0,0]
	v_mfma_scale_f32_16x16x128_f8f6f4 v[28:31], v[8:15], v[184:191], v[28:31], v225, v225 op_sel_hi:[0,0,0]
	v_mfma_scale_f32_16x16x128_f8f6f4 v[32:35], v[0:7], v[192:199], v[32:35], v225, v225 op_sel_hi:[0,0,0]
	v_mfma_scale_f32_16x16x128_f8f6f4 v[36:39], v[8:15], v[192:199], v[36:39], v225, v225 op_sel_hi:[0,0,0]
	v_mfma_scale_f32_16x16x128_f8f6f4 v[40:43], v[0:7], v[200:207], v[40:43], v225, v225 op_sel_hi:[0,0,0]
	v_mfma_scale_f32_16x16x128_f8f6f4 v[44:47], v[8:15], v[200:207], v[44:47], v225, v225 op_sel_hi:[0,0,0]
	s_setprio 0
	s_barrier
	s_mov_b32 m0, s62
	v_lshl_add_u64 v[140:141], v[170:171], 0, s[38:39]
	ds_read_b128 v[208:211], v234
	ds_read_b128 v[212:215], v234 offset:1024
	ds_read_b128 v[236:239], v234 offset:2048
	ds_read_b128 v[240:243], v234 offset:3072
	global_load_lds_dwordx4 v[140:141], off
	v_lshl_add_u64 v[140:141], v[172:173], 0, s[38:39]
	s_mov_b32 m0, s63
	s_nop 0
	global_load_lds_dwordx4 v[140:141], off
	s_barrier
	s_waitcnt lgkmcnt(0)
	s_setprio 1
	s_waitcnt lgkmcnt(0)
	v_mfma_scale_f32_16x16x128_f8f6f4 v[48:51], v[208:215], v[176:183], v[48:51], v225, v225 op_sel_hi:[0,0,0]
	v_mfma_scale_f32_16x16x128_f8f6f4 v[52:55], v[236:243], v[176:183], v[52:55], v225, v225 op_sel_hi:[0,0,0]
	v_mfma_scale_f32_16x16x128_f8f6f4 v[56:59], v[208:215], v[184:191], v[56:59], v225, v225 op_sel_hi:[0,0,0]
	v_mfma_scale_f32_16x16x128_f8f6f4 v[60:63], v[236:243], v[184:191], v[60:63], v225, v225 op_sel_hi:[0,0,0]
	v_mfma_scale_f32_16x16x128_f8f6f4 v[64:67], v[208:215], v[192:199], v[64:67], v225, v225 op_sel_hi:[0,0,0]
	v_mfma_scale_f32_16x16x128_f8f6f4 v[68:71], v[236:243], v[192:199], v[68:71], v225, v225 op_sel_hi:[0,0,0]
	v_mfma_scale_f32_16x16x128_f8f6f4 v[72:75], v[208:215], v[200:207], v[72:75], v225, v225 op_sel_hi:[0,0,0]
	v_mfma_scale_f32_16x16x128_f8f6f4 v[76:79], v[236:243], v[200:207], v[76:79], v225, v225 op_sel_hi:[0,0,0]
	s_setprio 0
	s_mov_b32 m0, s80
	v_lshl_add_u64 v[140:141], v[174:175], 0, s[38:39]
	s_barrier
	ds_read_b128 v[176:179], v228 offset:49152
	ds_read_b128 v[180:183], v228 offset:50176
	ds_read_b128 v[184:187], v228 offset:51200
	ds_read_b128 v[188:191], v228 offset:52224
	ds_read_b128 v[192:195], v228 offset:53248
	ds_read_b128 v[196:199], v228 offset:54272
	ds_read_b128 v[200:203], v228 offset:55296
	ds_read_b128 v[204:207], v228 offset:56320
	global_load_lds_dwordx4 v[140:141], off
	v_lshl_add_u64 v[140:141], v[168:169], 0, s[38:39]
	s_mov_b32 m0, s81
	s_nop 0
	global_load_lds_dwordx4 v[140:141], off
	s_barrier
	s_waitcnt lgkmcnt(0)
	s_setprio 1
	s_waitcnt lgkmcnt(0)
	v_mfma_scale_f32_16x16x128_f8f6f4 v[80:83], v[0:7], v[176:183], v[80:83], v225, v225 op_sel_hi:[0,0,0]
	v_mfma_scale_f32_16x16x128_f8f6f4 v[84:87], v[8:15], v[176:183], v[84:87], v225, v225 op_sel_hi:[0,0,0]
	v_mfma_scale_f32_16x16x128_f8f6f4 v[88:91], v[0:7], v[184:191], v[88:91], v225, v225 op_sel_hi:[0,0,0]
	v_mfma_scale_f32_16x16x128_f8f6f4 v[92:95], v[8:15], v[184:191], v[92:95], v225, v225 op_sel_hi:[0,0,0]
	v_mfma_scale_f32_16x16x128_f8f6f4 v[96:99], v[0:7], v[192:199], v[96:99], v225, v225 op_sel_hi:[0,0,0]
	v_mfma_scale_f32_16x16x128_f8f6f4 v[100:103], v[8:15], v[192:199], v[100:103], v225, v225 op_sel_hi:[0,0,0]
	v_mfma_scale_f32_16x16x128_f8f6f4 v[104:107], v[0:7], v[200:207], v[104:107], v225, v225 op_sel_hi:[0,0,0]
	v_mfma_scale_f32_16x16x128_f8f6f4 v[108:111], v[8:15], v[200:207], v[108:111], v225, v225 op_sel_hi:[0,0,0]
	s_setprio 0
	s_barrier
	s_add_u32 s50, s50, 0x40780
	s_addc_u32 s51, s51, 0
	s_mov_b32 m0, s53
	v_lshl_add_u64 v[0:1], s[50:51], 0, v[150:151]
	global_load_lds_dwordx4 v[0:1], off
	v_lshl_add_u64 v[0:1], s[50:51], 0, v[154:155]
	s_mov_b32 m0, s64
	s_nop 0
	global_load_lds_dwordx4 v[0:1], off
	s_waitcnt vmcnt(6)
	s_barrier
	s_setprio 1
	v_mfma_scale_f32_16x16x128_f8f6f4 v[112:115], v[208:215], v[176:183], v[112:115], v225, v225 op_sel_hi:[0,0,0]
	v_mfma_scale_f32_16x16x128_f8f6f4 v[116:119], v[236:243], v[176:183], v[116:119], v225, v225 op_sel_hi:[0,0,0]
	v_mfma_scale_f32_16x16x128_f8f6f4 v[120:123], v[208:215], v[184:191], v[120:123], v225, v225 op_sel_hi:[0,0,0]
	v_mfma_scale_f32_16x16x128_f8f6f4 v[124:127], v[236:243], v[184:191], v[124:127], v225, v225 op_sel_hi:[0,0,0]
	v_mfma_scale_f32_16x16x128_f8f6f4 v[128:131], v[208:215], v[192:199], v[128:131], v225, v225 op_sel_hi:[0,0,0]
	v_mfma_scale_f32_16x16x128_f8f6f4 v[132:135], v[236:243], v[192:199], v[132:135], v225, v225 op_sel_hi:[0,0,0]
	v_mfma_scale_f32_16x16x128_f8f6f4 v[144:147], v[208:215], v[200:207], v[144:147], v225, v225 op_sel_hi:[0,0,0]
	v_mfma_scale_f32_16x16x128_f8f6f4 v[136:139], v[236:243], v[200:207], v[136:139], v225, v225 op_sel_hi:[0,0,0]
	s_setprio 0
	s_barrier
	ds_read_b128 v[8:11], v231
	ds_read_b128 v[12:15], v231 offset:1024
	ds_read_b128 v[168:171], v231 offset:2048
	ds_read_b128 v[172:175], v231 offset:3072
	s_add_u32 s48, s48, 0x40780
	s_addc_u32 s49, s49, 0
	s_mov_b32 m0, s94
	v_lshl_add_u64 v[0:1], s[48:49], 0, v[148:149]
	ds_read_b128 v[176:179], v228
	ds_read_b128 v[180:183], v228 offset:1024
	ds_read_b128 v[184:187], v228 offset:2048
	ds_read_b128 v[188:191], v228 offset:3072
	ds_read_b128 v[192:195], v228 offset:4096
	ds_read_b128 v[196:199], v228 offset:5120
	ds_read_b128 v[200:203], v228 offset:6144
	ds_read_b128 v[204:207], v228 offset:7168
	global_load_lds_dwordx4 v[0:1], off
	v_lshl_add_u64 v[0:1], s[48:49], 0, v[152:153]
	s_mov_b32 m0, s93
	s_nop 0
	global_load_lds_dwordx4 v[0:1], off
	s_waitcnt lgkmcnt(8)
	s_barrier
	s_waitcnt lgkmcnt(0)
	s_setprio 1
	s_waitcnt lgkmcnt(0)
	v_mfma_scale_f32_16x16x128_f8f6f4 v[16:19], v[8:15], v[176:183], v[16:19], v225, v225 op_sel_hi:[0,0,0]
	v_mfma_scale_f32_16x16x128_f8f6f4 v[20:23], v[168:175], v[176:183], v[20:23], v225, v225 op_sel_hi:[0,0,0]
	v_mfma_scale_f32_16x16x128_f8f6f4 v[24:27], v[8:15], v[184:191], v[24:27], v225, v225 op_sel_hi:[0,0,0]
	v_mfma_scale_f32_16x16x128_f8f6f4 v[28:31], v[168:175], v[184:191], v[28:31], v225, v225 op_sel_hi:[0,0,0]
	v_mfma_scale_f32_16x16x128_f8f6f4 v[32:35], v[8:15], v[192:199], v[32:35], v225, v225 op_sel_hi:[0,0,0]
	v_mfma_scale_f32_16x16x128_f8f6f4 v[36:39], v[168:175], v[192:199], v[36:39], v225, v225 op_sel_hi:[0,0,0]
	v_mfma_scale_f32_16x16x128_f8f6f4 v[40:43], v[8:15], v[200:207], v[40:43], v225, v225 op_sel_hi:[0,0,0]
	v_mfma_scale_f32_16x16x128_f8f6f4 v[44:47], v[168:175], v[200:207], v[44:47], v225, v225 op_sel_hi:[0,0,0]
	s_setprio 0
	s_barrier
	s_mov_b32 m0, s96
	v_lshl_add_u64 v[0:1], s[60:61], 0, v[150:151]
	ds_read_b128 v[208:211], v232
	ds_read_b128 v[212:215], v232 offset:1024
	ds_read_b128 v[236:239], v232 offset:2048
	ds_read_b128 v[240:243], v232 offset:3072
	global_load_lds_dwordx4 v[0:1], off
	v_lshl_add_u64 v[2:3], s[60:61], 0, v[154:155]
	s_mov_b32 m0, s95
	s_nop 0
	global_load_lds_dwordx4 v[2:3], off
	s_barrier
	s_waitcnt lgkmcnt(0)
	s_setprio 1
	s_waitcnt lgkmcnt(0)
	v_mfma_scale_f32_16x16x128_f8f6f4 v[48:51], v[208:215], v[176:183], v[48:51], v225, v225 op_sel_hi:[0,0,0]
	v_mfma_scale_f32_16x16x128_f8f6f4 v[52:55], v[236:243], v[176:183], v[52:55], v225, v225 op_sel_hi:[0,0,0]
	v_mfma_scale_f32_16x16x128_f8f6f4 v[56:59], v[208:215], v[184:191], v[56:59], v225, v225 op_sel_hi:[0,0,0]
	v_mfma_scale_f32_16x16x128_f8f6f4 v[60:63], v[236:243], v[184:191], v[60:63], v225, v225 op_sel_hi:[0,0,0]
	v_mfma_scale_f32_16x16x128_f8f6f4 v[64:67], v[208:215], v[192:199], v[64:67], v225, v225 op_sel_hi:[0,0,0]
	v_mfma_scale_f32_16x16x128_f8f6f4 v[68:71], v[236:243], v[192:199], v[68:71], v225, v225 op_sel_hi:[0,0,0]
	v_mfma_scale_f32_16x16x128_f8f6f4 v[72:75], v[208:215], v[200:207], v[72:75], v225, v225 op_sel_hi:[0,0,0]
	v_mfma_scale_f32_16x16x128_f8f6f4 v[76:79], v[236:243], v[200:207], v[76:79], v225, v225 op_sel_hi:[0,0,0]
	s_setprio 0
	s_mov_b32 m0, s73
	v_lshl_add_u64 v[4:5], s[54:55], 0, v[148:149]
	s_barrier
	ds_read_b128 v[176:179], v228 offset:16384
	ds_read_b128 v[180:183], v228 offset:17408
	ds_read_b128 v[184:187], v228 offset:18432
	ds_read_b128 v[188:191], v228 offset:19456
	ds_read_b128 v[192:195], v228 offset:20480
	ds_read_b128 v[196:199], v228 offset:21504
	ds_read_b128 v[200:203], v228 offset:22528
	ds_read_b128 v[204:207], v228 offset:23552
	global_load_lds_dwordx4 v[4:5], off
	v_lshl_add_u64 v[6:7], s[54:55], 0, v[152:153]
	s_mov_b32 m0, s74
	s_nop 0
	global_load_lds_dwordx4 v[6:7], off
	s_barrier
	s_waitcnt lgkmcnt(0)
	s_setprio 1
	s_waitcnt lgkmcnt(0)
	v_mfma_scale_f32_16x16x128_f8f6f4 v[80:83], v[8:15], v[176:183], v[80:83], v225, v225 op_sel_hi:[0,0,0]
	v_mfma_scale_f32_16x16x128_f8f6f4 v[84:87], v[168:175], v[176:183], v[84:87], v225, v225 op_sel_hi:[0,0,0]
	v_mfma_scale_f32_16x16x128_f8f6f4 v[88:91], v[8:15], v[184:191], v[88:91], v225, v225 op_sel_hi:[0,0,0]
	v_mfma_scale_f32_16x16x128_f8f6f4 v[92:95], v[168:175], v[184:191], v[92:95], v225, v225 op_sel_hi:[0,0,0]
	v_mfma_scale_f32_16x16x128_f8f6f4 v[96:99], v[8:15], v[192:199], v[96:99], v225, v225 op_sel_hi:[0,0,0]
	v_mfma_scale_f32_16x16x128_f8f6f4 v[100:103], v[168:175], v[192:199], v[100:103], v225, v225 op_sel_hi:[0,0,0]
	v_mfma_scale_f32_16x16x128_f8f6f4 v[104:107], v[8:15], v[200:207], v[104:107], v225, v225 op_sel_hi:[0,0,0]
	v_mfma_scale_f32_16x16x128_f8f6f4 v[108:111], v[168:175], v[200:207], v[108:111], v225, v225 op_sel_hi:[0,0,0]
	s_setprio 0
	s_barrier
	s_add_u32 s48, s60, 0x40000
	s_addc_u32 s49, s61, 0
	s_mov_b32 m0, s97
	v_lshl_add_u64 v[8:9], s[48:49], 0, v[150:151]
	global_load_lds_dwordx4 v[8:9], off
	v_lshl_add_u64 v[8:9], s[48:49], 0, v[154:155]
	s_mov_b32 m0, s52
	s_nop 0
	global_load_lds_dwordx4 v[8:9], off
	s_waitcnt vmcnt(6)
	s_barrier
	s_setprio 1
	v_mfma_scale_f32_16x16x128_f8f6f4 v[112:115], v[208:215], v[176:183], v[112:115], v225, v225 op_sel_hi:[0,0,0]
	v_mfma_scale_f32_16x16x128_f8f6f4 v[116:119], v[236:243], v[176:183], v[116:119], v225, v225 op_sel_hi:[0,0,0]
	v_mfma_scale_f32_16x16x128_f8f6f4 v[120:123], v[208:215], v[184:191], v[120:123], v225, v225 op_sel_hi:[0,0,0]
	v_mfma_scale_f32_16x16x128_f8f6f4 v[124:127], v[236:243], v[184:191], v[124:127], v225, v225 op_sel_hi:[0,0,0]
	v_mfma_scale_f32_16x16x128_f8f6f4 v[128:131], v[208:215], v[192:199], v[128:131], v225, v225 op_sel_hi:[0,0,0]
	v_mfma_scale_f32_16x16x128_f8f6f4 v[132:135], v[236:243], v[192:199], v[132:135], v225, v225 op_sel_hi:[0,0,0]
	v_mfma_scale_f32_16x16x128_f8f6f4 v[144:147], v[208:215], v[200:207], v[144:147], v225, v225 op_sel_hi:[0,0,0]
	v_mfma_scale_f32_16x16x128_f8f6f4 v[136:139], v[236:243], v[200:207], v[136:139], v225, v225 op_sel_hi:[0,0,0]
	s_setprio 0
	s_barrier
	ds_read_b128 v[8:11], v235
	ds_read_b128 v[12:15], v235 offset:1024
	ds_read_b128 v[168:171], v235 offset:2048
	ds_read_b128 v[172:175], v235 offset:3072
	s_add_u32 s48, s54, 0x40000
	s_addc_u32 s49, s55, 0
	s_mov_b32 m0, s75
	v_lshl_add_u64 v[140:141], s[48:49], 0, v[148:149]
	ds_read_b128 v[176:179], v228 offset:32768
	ds_read_b128 v[180:183], v228 offset:33792
	ds_read_b128 v[184:187], v228 offset:34816
	ds_read_b128 v[188:191], v228 offset:35840
	ds_read_b128 v[192:195], v228 offset:36864
	ds_read_b128 v[196:199], v228 offset:37888
	ds_read_b128 v[200:203], v228 offset:38912
	ds_read_b128 v[204:207], v228 offset:39936
	global_load_lds_dwordx4 v[140:141], off
	v_lshl_add_u64 v[140:141], s[48:49], 0, v[152:153]
	s_mov_b32 m0, s76
	s_nop 0
	global_load_lds_dwordx4 v[140:141], off
	s_waitcnt lgkmcnt(8)
	s_barrier
	s_waitcnt lgkmcnt(0)
	s_setprio 1
	s_waitcnt lgkmcnt(0)
	v_mfma_scale_f32_16x16x128_f8f6f4 v[16:19], v[8:15], v[176:183], v[16:19], v225, v225 op_sel_hi:[0,0,0]
	v_mfma_scale_f32_16x16x128_f8f6f4 v[20:23], v[168:175], v[176:183], v[20:23], v225, v225 op_sel_hi:[0,0,0]
	v_mfma_scale_f32_16x16x128_f8f6f4 v[24:27], v[8:15], v[184:191], v[24:27], v225, v225 op_sel_hi:[0,0,0]
	v_mfma_scale_f32_16x16x128_f8f6f4 v[28:31], v[168:175], v[184:191], v[28:31], v225, v225 op_sel_hi:[0,0,0]
	v_mfma_scale_f32_16x16x128_f8f6f4 v[32:35], v[8:15], v[192:199], v[32:35], v225, v225 op_sel_hi:[0,0,0]
	v_mfma_scale_f32_16x16x128_f8f6f4 v[36:39], v[168:175], v[192:199], v[36:39], v225, v225 op_sel_hi:[0,0,0]
	v_mfma_scale_f32_16x16x128_f8f6f4 v[40:43], v[8:15], v[200:207], v[40:43], v225, v225 op_sel_hi:[0,0,0]
	v_mfma_scale_f32_16x16x128_f8f6f4 v[44:47], v[168:175], v[200:207], v[44:47], v225, v225 op_sel_hi:[0,0,0]
	s_setprio 0
	s_barrier
	s_mov_b32 m0, s62
	v_lshl_add_u64 v[0:1], v[0:1], 0, s[8:9]
	ds_read_b128 v[208:211], v234
	ds_read_b128 v[212:215], v234 offset:1024
	ds_read_b128 v[236:239], v234 offset:2048
	ds_read_b128 v[240:243], v234 offset:3072
	global_load_lds_dwordx4 v[0:1], off
	v_lshl_add_u64 v[0:1], v[2:3], 0, s[8:9]
	s_mov_b32 m0, s63
	s_nop 0
	global_load_lds_dwordx4 v[0:1], off
	s_barrier
	s_waitcnt lgkmcnt(0)
	s_setprio 1
	s_waitcnt lgkmcnt(0)
	v_mfma_scale_f32_16x16x128_f8f6f4 v[48:51], v[208:215], v[176:183], v[48:51], v225, v225 op_sel_hi:[0,0,0]
	v_mfma_scale_f32_16x16x128_f8f6f4 v[52:55], v[236:243], v[176:183], v[52:55], v225, v225 op_sel_hi:[0,0,0]
	v_mfma_scale_f32_16x16x128_f8f6f4 v[56:59], v[208:215], v[184:191], v[56:59], v225, v225 op_sel_hi:[0,0,0]
	v_mfma_scale_f32_16x16x128_f8f6f4 v[60:63], v[236:243], v[184:191], v[60:63], v225, v225 op_sel_hi:[0,0,0]
	v_mfma_scale_f32_16x16x128_f8f6f4 v[64:67], v[208:215], v[192:199], v[64:67], v225, v225 op_sel_hi:[0,0,0]
	v_mfma_scale_f32_16x16x128_f8f6f4 v[68:71], v[236:243], v[192:199], v[68:71], v225, v225 op_sel_hi:[0,0,0]
	v_mfma_scale_f32_16x16x128_f8f6f4 v[72:75], v[208:215], v[200:207], v[72:75], v225, v225 op_sel_hi:[0,0,0]
	v_mfma_scale_f32_16x16x128_f8f6f4 v[76:79], v[236:243], v[200:207], v[76:79], v225, v225 op_sel_hi:[0,0,0]
	s_setprio 0
	s_mov_b32 m0, s80
	v_lshl_add_u64 v[0:1], v[4:5], 0, s[8:9]
	s_barrier
	ds_read_b128 v[176:179], v228 offset:49152
	ds_read_b128 v[180:183], v228 offset:50176
	ds_read_b128 v[184:187], v228 offset:51200
	ds_read_b128 v[188:191], v228 offset:52224
	ds_read_b128 v[192:195], v228 offset:53248
	ds_read_b128 v[196:199], v228 offset:54272
	ds_read_b128 v[200:203], v228 offset:55296
	ds_read_b128 v[204:207], v228 offset:56320
	global_load_lds_dwordx4 v[0:1], off
	v_lshl_add_u64 v[0:1], v[6:7], 0, s[8:9]
	s_mov_b32 m0, s81
	s_nop 0
	global_load_lds_dwordx4 v[0:1], off
	s_barrier
	s_waitcnt lgkmcnt(0)
	s_setprio 1
	s_waitcnt lgkmcnt(0)
	v_mfma_scale_f32_16x16x128_f8f6f4 v[80:83], v[8:15], v[176:183], v[80:83], v225, v225 op_sel_hi:[0,0,0]
	v_mfma_scale_f32_16x16x128_f8f6f4 v[84:87], v[168:175], v[176:183], v[84:87], v225, v225 op_sel_hi:[0,0,0]
	v_mfma_scale_f32_16x16x128_f8f6f4 v[88:91], v[8:15], v[184:191], v[88:91], v225, v225 op_sel_hi:[0,0,0]
	v_mfma_scale_f32_16x16x128_f8f6f4 v[92:95], v[168:175], v[184:191], v[92:95], v225, v225 op_sel_hi:[0,0,0]
	v_mfma_scale_f32_16x16x128_f8f6f4 v[96:99], v[8:15], v[192:199], v[96:99], v225, v225 op_sel_hi:[0,0,0]
	v_mfma_scale_f32_16x16x128_f8f6f4 v[100:103], v[168:175], v[192:199], v[100:103], v225, v225 op_sel_hi:[0,0,0]
	v_mfma_scale_f32_16x16x128_f8f6f4 v[104:107], v[8:15], v[200:207], v[104:107], v225, v225 op_sel_hi:[0,0,0]
	v_mfma_scale_f32_16x16x128_f8f6f4 v[108:111], v[168:175], v[200:207], v[108:111], v225, v225 op_sel_hi:[0,0,0]
	s_setprio 0
	s_barrier
	s_add_u32 s48, s60, 0x40080
	s_addc_u32 s49, s61, 0
	s_mov_b32 m0, s53
	v_lshl_add_u64 v[0:1], s[48:49], 0, v[150:151]
	global_load_lds_dwordx4 v[0:1], off
	v_lshl_add_u64 v[0:1], s[48:49], 0, v[154:155]
	s_mov_b32 m0, s64
	s_nop 0
	global_load_lds_dwordx4 v[0:1], off
	s_waitcnt vmcnt(6)
	s_barrier
	s_setprio 1
	v_mfma_scale_f32_16x16x128_f8f6f4 v[112:115], v[208:215], v[176:183], v[112:115], v225, v225 op_sel_hi:[0,0,0]
	v_mfma_scale_f32_16x16x128_f8f6f4 v[116:119], v[236:243], v[176:183], v[116:119], v225, v225 op_sel_hi:[0,0,0]
	v_mfma_scale_f32_16x16x128_f8f6f4 v[120:123], v[208:215], v[184:191], v[120:123], v225, v225 op_sel_hi:[0,0,0]
	v_mfma_scale_f32_16x16x128_f8f6f4 v[124:127], v[236:243], v[184:191], v[124:127], v225, v225 op_sel_hi:[0,0,0]
	v_mfma_scale_f32_16x16x128_f8f6f4 v[128:131], v[208:215], v[192:199], v[128:131], v225, v225 op_sel_hi:[0,0,0]
	v_mfma_scale_f32_16x16x128_f8f6f4 v[132:135], v[236:243], v[192:199], v[132:135], v225, v225 op_sel_hi:[0,0,0]
	v_mfma_scale_f32_16x16x128_f8f6f4 v[144:147], v[208:215], v[200:207], v[144:147], v225, v225 op_sel_hi:[0,0,0]
	v_mfma_scale_f32_16x16x128_f8f6f4 v[136:139], v[236:243], v[200:207], v[136:139], v225, v225 op_sel_hi:[0,0,0]
	s_setprio 0
	v_mov_b32_e32 v156, v230
	s_barrier
	s_nop 7
	s_nop 7
	s_nop 7
	global_load_dwordx2 v[4:5], v156, s[2:3]
	global_load_dwordx2 v[6:7], v156, s[2:3] offset:512
	global_load_dwordx2 v[8:9], v156, s[2:3] offset:1024
	global_load_dwordx2 v[10:11], v156, s[2:3] offset:1536
	global_load_dwordx2 v[168:169], v156, s[2:3] offset:2048
	global_load_dwordx2 v[202:203], v156, s[2:3] offset:2560
	global_load_dwordx2 v[200:201], v156, s[2:3] offset:3072
	global_load_dwordx2 v[198:199], v156, s[2:3] offset:3584
	v_lshl_add_u64 v[0:1], s[2:3], 0, v[156:157]
	v_add_co_u32_e32 v0, vcc, s85, v0
	s_mov_b64 s[2:3], 0x40000
	s_nop 0
	v_addc_co_u32_e32 v1, vcc, 0, v1, vcc
	global_load_dwordx2 v[196:197], v[0:1], off
	global_load_dwordx2 v[194:195], v[0:1], off offset:512
	global_load_dwordx2 v[192:193], v[0:1], off offset:1024
	global_load_dwordx2 v[190:191], v[0:1], off offset:1536
	global_load_dwordx2 v[180:181], v[0:1], off offset:2048
	global_load_dwordx2 v[170:171], v[0:1], off offset:2560
	global_load_dwordx2 v[2:3], v[0:1], off offset:3072
	s_nop 0
	global_load_dwordx2 v[0:1], v[0:1], off offset:3584
	s_mov_b64 s[50:51], s[46:47]
	s_mov_b64 s[48:49], s[44:45]
	s_waitcnt vmcnt(0)
	v_cvt_f32_ubyte1_e32 v13, v4
	v_cvt_f32_ubyte0_e32 v12, v4
	v_cvt_f32_ubyte3_e32 v15, v4
	v_cvt_f32_ubyte2_e32 v14, v4
	v_cvt_f32_ubyte1_e32 v141, v5
	v_cvt_f32_ubyte0_e32 v140, v5
	v_cvt_f32_ubyte3_e32 v143, v5
	v_cvt_f32_ubyte2_e32 v142, v5
	v_cvt_f32_ubyte1_e32 v5, v6
	v_cvt_f32_ubyte0_e32 v4, v6
	v_cvt_f32_ubyte1_e32 v175, v7
	v_cvt_f32_ubyte0_e32 v174, v7
	v_pk_add_f32 v[4:5], v[4:5], 0.5 op_sel_hi:[1,0]
	v_cvt_f32_ubyte3_e32 v173, v6
	v_cvt_f32_ubyte2_e32 v172, v6
	v_cvt_f32_ubyte3_e32 v177, v7
	v_cvt_f32_ubyte2_e32 v176, v7
	v_cvt_f32_ubyte1_e32 v7, v8
	v_cvt_f32_ubyte0_e32 v6, v8
	v_pk_add_f32 v[174:175], v[174:175], 0.5 op_sel_hi:[1,0]
	v_pk_mul_f32 v[4:5], v[4:5], s[40:41] op_sel_hi:[1,0]
	v_pk_add_f32 v[172:173], v[172:173], 0.5 op_sel_hi:[1,0]
	v_pk_add_f32 v[6:7], v[6:7], 0.5 op_sel_hi:[1,0]
	v_pk_mul_f32 v[204:205], v[174:175], s[40:41] op_sel_hi:[1,0]
	v_pk_mul_f32 v[174:175], v[48:49], v[4:5]
	v_cvt_f32_ubyte3_e32 v5, v10
	v_cvt_f32_ubyte2_e32 v4, v10
	v_cvt_f32_ubyte3_e32 v179, v8
	v_cvt_f32_ubyte2_e32 v178, v8
	v_cvt_f32_ubyte1_e32 v183, v9
	v_cvt_f32_ubyte0_e32 v182, v9
	v_cvt_f32_ubyte3_e32 v185, v9
	v_cvt_f32_ubyte2_e32 v184, v9
	v_cvt_f32_ubyte1_e32 v9, v10
	v_pk_add_f32 v[12:13], v[12:13], 0.5 op_sel_hi:[1,0]
	v_pk_mul_f32 v[172:173], v[172:173], s[40:41] op_sel_hi:[1,0]
	v_pk_mul_f32 v[6:7], v[6:7], s[40:41] op_sel_hi:[1,0]
	v_cvt_f32_ubyte0_e32 v8, v10
	v_pk_add_f32 v[4:5], v[4:5], 0.5 op_sel_hi:[1,0]
	v_pk_add_f32 v[14:15], v[14:15], 0.5 op_sel_hi:[1,0]
	v_pk_add_f32 v[184:185], v[184:185], 0.5 op_sel_hi:[1,0]
	v_pk_mul_f32 v[12:13], v[12:13], s[40:41] op_sel_hi:[1,0]
	v_pk_mul_f32 v[172:173], v[50:51], v[172:173]
	v_pk_mul_f32 v[50:51], v[24:25], v[6:7]
	v_pk_add_f32 v[6:7], v[8:9], 0.5 op_sel_hi:[1,0]
	v_pk_mul_f32 v[4:5], v[4:5], s[40:41] op_sel_hi:[1,0]
	v_pk_add_f32 v[182:183], v[182:183], 0.5 op_sel_hi:[1,0]
	v_pk_mul_f32 v[14:15], v[14:15], s[40:41] op_sel_hi:[1,0]
	v_pk_mul_f32 v[210:211], v[184:185], s[40:41] op_sel_hi:[1,0]
	v_pk_mul_f32 v[184:185], v[16:17], v[12:13]
	v_pk_mul_f32 v[6:7], v[6:7], s[40:41] op_sel_hi:[1,0]
	v_pk_mul_f32 v[12:13], v[58:59], v[4:5]
	v_cvt_f32_ubyte1_e32 v5, v11
	v_cvt_f32_ubyte0_e32 v4, v11
	v_pk_add_f32 v[142:143], v[142:143], 0.5 op_sel_hi:[1,0]
	v_pk_mul_f32 v[208:209], v[182:183], s[40:41] op_sel_hi:[1,0]
	v_pk_mul_f32 v[182:183], v[18:19], v[14:15]
	v_pk_mul_f32 v[14:15], v[56:57], v[6:7]
	v_cvt_f32_ubyte3_e32 v7, v11
	v_cvt_f32_ubyte2_e32 v6, v11
	v_pk_add_f32 v[4:5], v[4:5], 0.5 op_sel_hi:[1,0]
	v_pk_add_f32 v[140:141], v[140:141], 0.5 op_sel_hi:[1,0]
	v_pk_mul_f32 v[142:143], v[142:143], s[40:41] op_sel_hi:[1,0]
	v_pk_add_f32 v[6:7], v[6:7], 0.5 op_sel_hi:[1,0]
	v_pk_mul_f32 v[4:5], v[4:5], s[40:41] op_sel_hi:[1,0]
	v_pk_mul_f32 v[140:141], v[140:141], s[40:41] op_sel_hi:[1,0]
	v_pk_mul_f32 v[186:187], v[22:23], v[142:143]
	v_pk_mul_f32 v[6:7], v[6:7], s[40:41] op_sel_hi:[1,0]
	v_pk_mul_f32 v[142:143], v[60:61], v[4:5]
	v_cvt_f32_ubyte1_e32 v5, v168
	v_cvt_f32_ubyte0_e32 v4, v168
	v_pk_mul_f32 v[188:189], v[20:21], v[140:141]
	v_pk_mul_f32 v[140:141], v[62:63], v[6:7]
	v_cvt_f32_ubyte3_e32 v7, v168
	v_cvt_f32_ubyte2_e32 v6, v168
	v_pk_add_f32 v[4:5], v[4:5], 0.5 op_sel_hi:[1,0]
	v_pk_add_f32 v[6:7], v[6:7], 0.5 op_sel_hi:[1,0]
	v_pk_mul_f32 v[8:9], v[4:5], s[40:41] op_sel_hi:[1,0]
	v_pk_mul_f32 v[4:5], v[6:7], s[40:41] op_sel_hi:[1,0]
	v_pk_mul_f32 v[6:7], v[32:33], v[8:9]
	v_cvt_f32_ubyte1_e32 v9, v169
	v_cvt_f32_ubyte0_e32 v8, v169
	v_cvt_f32_ubyte3_e32 v11, v169
	v_cvt_f32_ubyte2_e32 v10, v169
	v_pk_add_f32 v[8:9], v[8:9], 0.5 op_sel_hi:[1,0]
	v_pk_add_f32 v[10:11], v[10:11], 0.5 op_sel_hi:[1,0]
	v_pk_mul_f32 v[8:9], v[8:9], s[40:41] op_sel_hi:[1,0]
	v_pk_mul_f32 v[10:11], v[10:11], s[40:41] op_sel_hi:[1,0]
	v_pk_mul_f32 v[58:59], v[36:37], v[8:9]
	v_cvt_f32_ubyte1_e32 v9, v202
	v_cvt_f32_ubyte0_e32 v8, v202
	v_pk_mul_f32 v[56:57], v[38:39], v[10:11]
	v_cvt_f32_ubyte3_e32 v11, v202
	v_cvt_f32_ubyte2_e32 v10, v202
	v_pk_add_f32 v[8:9], v[8:9], 0.5 op_sel_hi:[1,0]
	v_pk_add_f32 v[10:11], v[10:11], 0.5 op_sel_hi:[1,0]
	v_pk_mul_f32 v[8:9], v[8:9], s[40:41] op_sel_hi:[1,0]
	v_pk_mul_f32 v[10:11], v[10:11], s[40:41] op_sel_hi:[1,0]
	v_pk_mul_f32 v[18:19], v[64:65], v[8:9]
	v_cvt_f32_ubyte1_e32 v9, v203
	v_cvt_f32_ubyte0_e32 v8, v203
	v_pk_mul_f32 v[16:17], v[66:67], v[10:11]
	v_cvt_f32_ubyte3_e32 v11, v203
	v_cvt_f32_ubyte2_e32 v10, v203
	v_pk_add_f32 v[8:9], v[8:9], 0.5 op_sel_hi:[1,0]
	v_pk_add_f32 v[10:11], v[10:11], 0.5 op_sel_hi:[1,0]
	v_pk_mul_f32 v[8:9], v[8:9], s[40:41] op_sel_hi:[1,0]
	v_pk_mul_f32 v[10:11], v[10:11], s[40:41] op_sel_hi:[1,0]
	v_pk_mul_f32 v[168:169], v[68:69], v[8:9]
	v_cvt_f32_ubyte1_e32 v9, v200
	v_cvt_f32_ubyte0_e32 v8, v200
	v_pk_mul_f32 v[70:71], v[70:71], v[10:11]
	v_cvt_f32_ubyte3_e32 v11, v200
	v_cvt_f32_ubyte2_e32 v10, v200
	v_pk_add_f32 v[8:9], v[8:9], 0.5 op_sel_hi:[1,0]
	v_pk_add_f32 v[10:11], v[10:11], 0.5 op_sel_hi:[1,0]
	v_pk_mul_f32 v[20:21], v[8:9], s[40:41] op_sel_hi:[1,0]
	v_pk_mul_f32 v[8:9], v[10:11], s[40:41] op_sel_hi:[1,0]
	v_pk_mul_f32 v[10:11], v[40:41], v[20:21]
	v_cvt_f32_ubyte1_e32 v21, v201
	v_cvt_f32_ubyte0_e32 v20, v201
	v_cvt_f32_ubyte3_e32 v23, v201
	v_cvt_f32_ubyte2_e32 v22, v201
	v_pk_add_f32 v[20:21], v[20:21], 0.5 op_sel_hi:[1,0]
	v_pk_add_f32 v[22:23], v[22:23], 0.5 op_sel_hi:[1,0]
	v_pk_mul_f32 v[20:21], v[20:21], s[40:41] op_sel_hi:[1,0]
	v_pk_mul_f32 v[22:23], v[22:23], s[40:41] op_sel_hi:[1,0]
	v_pk_mul_f32 v[66:67], v[44:45], v[20:21]
	v_cvt_f32_ubyte1_e32 v21, v198
	v_cvt_f32_ubyte0_e32 v20, v198
	v_pk_mul_f32 v[64:65], v[46:47], v[22:23]
	v_cvt_f32_ubyte3_e32 v23, v198
	v_cvt_f32_ubyte2_e32 v22, v198
	v_pk_add_f32 v[20:21], v[20:21], 0.5 op_sel_hi:[1,0]
	v_pk_add_f32 v[178:179], v[178:179], 0.5 op_sel_hi:[1,0]
	v_pk_add_f32 v[22:23], v[22:23], 0.5 op_sel_hi:[1,0]
	v_pk_mul_f32 v[24:25], v[20:21], s[40:41] op_sel_hi:[1,0]
	v_pk_mul_f32 v[206:207], v[178:179], s[40:41] op_sel_hi:[1,0]
	v_pk_mul_f32 v[20:21], v[22:23], s[40:41] op_sel_hi:[1,0]
	v_pk_mul_f32 v[22:23], v[72:73], v[24:25]
	v_cvt_f32_ubyte1_e32 v25, v199
	v_cvt_f32_ubyte0_e32 v24, v199
	v_pk_mul_f32 v[48:49], v[26:27], v[206:207]
	v_cvt_f32_ubyte3_e32 v27, v199
	v_cvt_f32_ubyte2_e32 v26, v199
	v_pk_add_f32 v[24:25], v[24:25], 0.5 op_sel_hi:[1,0]
	v_pk_add_f32 v[26:27], v[26:27], 0.5 op_sel_hi:[1,0]
	v_pk_mul_f32 v[24:25], v[24:25], s[40:41] op_sel_hi:[1,0]
	v_pk_add_f32 v[176:177], v[176:177], 0.5 op_sel_hi:[1,0]
	v_pk_mul_f32 v[20:21], v[74:75], v[20:21]
	v_pk_mul_f32 v[26:27], v[26:27], s[40:41] op_sel_hi:[1,0]
	v_pk_mul_f32 v[74:75], v[76:77], v[24:25]
	v_cvt_f32_ubyte1_e32 v25, v196
	v_cvt_f32_ubyte0_e32 v24, v196
	v_pk_mul_f32 v[176:177], v[176:177], s[40:41] op_sel_hi:[1,0]
	v_pk_mul_f32 v[72:73], v[78:79], v[26:27]
	v_cvt_f32_ubyte3_e32 v27, v196
	v_cvt_f32_ubyte2_e32 v26, v196
	v_pk_add_f32 v[24:25], v[24:25], 0.5 op_sel_hi:[1,0]
	v_pk_mul_f32 v[176:177], v[54:55], v[176:177]
	v_pk_mul_f32 v[54:55], v[28:29], v[208:209]
	v_pk_add_f32 v[26:27], v[26:27], 0.5 op_sel_hi:[1,0]
	v_pk_mul_f32 v[28:29], v[24:25], s[40:41] op_sel_hi:[1,0]
	v_pk_mul_f32 v[24:25], v[26:27], s[40:41] op_sel_hi:[1,0]
	v_pk_mul_f32 v[26:27], v[80:81], v[28:29]
	v_cvt_f32_ubyte1_e32 v29, v197
	v_cvt_f32_ubyte0_e32 v28, v197
	v_pk_mul_f32 v[178:179], v[52:53], v[204:205]
	v_pk_mul_f32 v[52:53], v[30:31], v[210:211]
	v_cvt_f32_ubyte3_e32 v31, v197
	v_cvt_f32_ubyte2_e32 v30, v197
	v_pk_add_f32 v[28:29], v[28:29], 0.5 op_sel_hi:[1,0]
	v_pk_add_f32 v[30:31], v[30:31], 0.5 op_sel_hi:[1,0]
	v_pk_mul_f32 v[28:29], v[28:29], s[40:41] op_sel_hi:[1,0]
	v_pk_mul_f32 v[30:31], v[30:31], s[40:41] op_sel_hi:[1,0]
	v_pk_mul_f32 v[78:79], v[84:85], v[28:29]
	v_cvt_f32_ubyte1_e32 v29, v194
	v_cvt_f32_ubyte0_e32 v28, v194
	v_pk_mul_f32 v[76:77], v[86:87], v[30:31]
	v_cvt_f32_ubyte3_e32 v31, v194
	v_cvt_f32_ubyte2_e32 v30, v194
	v_pk_add_f32 v[28:29], v[28:29], 0.5 op_sel_hi:[1,0]
	v_pk_add_f32 v[30:31], v[30:31], 0.5 op_sel_hi:[1,0]
	v_pk_mul_f32 v[32:33], v[28:29], s[40:41] op_sel_hi:[1,0]
	v_pk_mul_f32 v[28:29], v[30:31], s[40:41] op_sel_hi:[1,0]
	v_pk_mul_f32 v[30:31], v[112:113], v[32:33]
	v_cvt_f32_ubyte1_e32 v33, v195
	v_cvt_f32_ubyte0_e32 v32, v195
	v_pk_mul_f32 v[4:5], v[34:35], v[4:5]
	v_cvt_f32_ubyte3_e32 v35, v195
	v_cvt_f32_ubyte2_e32 v34, v195
	v_pk_add_f32 v[32:33], v[32:33], 0.5 op_sel_hi:[1,0]
	v_pk_add_f32 v[34:35], v[34:35], 0.5 op_sel_hi:[1,0]
	v_pk_mul_f32 v[32:33], v[32:33], s[40:41] op_sel_hi:[1,0]
	v_pk_mul_f32 v[24:25], v[82:83], v[24:25]
	v_pk_mul_f32 v[34:35], v[34:35], s[40:41] op_sel_hi:[1,0]
	v_pk_mul_f32 v[82:83], v[116:117], v[32:33]
	v_cvt_f32_ubyte1_e32 v33, v192
	v_cvt_f32_ubyte0_e32 v32, v192
	v_pk_mul_f32 v[80:81], v[118:119], v[34:35]
	v_cvt_f32_ubyte3_e32 v35, v192
	v_cvt_f32_ubyte2_e32 v34, v192
	v_pk_add_f32 v[32:33], v[32:33], 0.5 op_sel_hi:[1,0]
	v_pk_add_f32 v[34:35], v[34:35], 0.5 op_sel_hi:[1,0]
	v_pk_mul_f32 v[36:37], v[32:33], s[40:41] op_sel_hi:[1,0]
	v_pk_mul_f32 v[32:33], v[34:35], s[40:41] op_sel_hi:[1,0]
	v_pk_mul_f32 v[34:35], v[88:89], v[36:37]
	v_cvt_f32_ubyte1_e32 v37, v193
	v_cvt_f32_ubyte0_e32 v36, v193
	v_cvt_f32_ubyte3_e32 v39, v193
	v_cvt_f32_ubyte2_e32 v38, v193
	v_pk_add_f32 v[36:37], v[36:37], 0.5 op_sel_hi:[1,0]
	v_pk_add_f32 v[38:39], v[38:39], 0.5 op_sel_hi:[1,0]
	v_pk_mul_f32 v[36:37], v[36:37], s[40:41] op_sel_hi:[1,0]
	v_pk_mul_f32 v[38:39], v[38:39], s[40:41] op_sel_hi:[1,0]
	v_pk_mul_f32 v[86:87], v[92:93], v[36:37]
	v_cvt_f32_ubyte1_e32 v37, v190
	v_cvt_f32_ubyte0_e32 v36, v190
	v_pk_mul_f32 v[84:85], v[94:95], v[38:39]
	v_cvt_f32_ubyte3_e32 v39, v190
	v_cvt_f32_ubyte2_e32 v38, v190
	v_pk_add_f32 v[36:37], v[36:37], 0.5 op_sel_hi:[1,0]
	v_pk_add_f32 v[38:39], v[38:39], 0.5 op_sel_hi:[1,0]
	v_pk_mul_f32 v[40:41], v[36:37], s[40:41] op_sel_hi:[1,0]
	v_pk_mul_f32 v[36:37], v[38:39], s[40:41] op_sel_hi:[1,0]
	v_pk_mul_f32 v[38:39], v[120:121], v[40:41]
	v_cvt_f32_ubyte1_e32 v41, v191
	v_cvt_f32_ubyte0_e32 v40, v191
	v_pk_mul_f32 v[8:9], v[42:43], v[8:9]
	v_cvt_f32_ubyte3_e32 v43, v191
	v_cvt_f32_ubyte2_e32 v42, v191
	v_pk_add_f32 v[40:41], v[40:41], 0.5 op_sel_hi:[1,0]
	v_pk_add_f32 v[42:43], v[42:43], 0.5 op_sel_hi:[1,0]
	v_pk_mul_f32 v[40:41], v[40:41], s[40:41] op_sel_hi:[1,0]
	v_pk_mul_f32 v[32:33], v[90:91], v[32:33]
	v_pk_mul_f32 v[42:43], v[42:43], s[40:41] op_sel_hi:[1,0]
	v_pk_mul_f32 v[90:91], v[124:125], v[40:41]
	v_cvt_f32_ubyte1_e32 v41, v180
	v_cvt_f32_ubyte0_e32 v40, v180
	v_pk_mul_f32 v[88:89], v[126:127], v[42:43]
	v_cvt_f32_ubyte3_e32 v43, v180
	v_cvt_f32_ubyte2_e32 v42, v180
	v_pk_add_f32 v[40:41], v[40:41], 0.5 op_sel_hi:[1,0]
	v_pk_add_f32 v[42:43], v[42:43], 0.5 op_sel_hi:[1,0]
	v_pk_mul_f32 v[44:45], v[40:41], s[40:41] op_sel_hi:[1,0]
	v_pk_mul_f32 v[40:41], v[42:43], s[40:41] op_sel_hi:[1,0]
	v_pk_mul_f32 v[42:43], v[96:97], v[44:45]
	v_cvt_f32_ubyte1_e32 v45, v181
	v_cvt_f32_ubyte0_e32 v44, v181
	v_cvt_f32_ubyte3_e32 v47, v181
	v_cvt_f32_ubyte2_e32 v46, v181
	v_pk_add_f32 v[44:45], v[44:45], 0.5 op_sel_hi:[1,0]
	v_pk_add_f32 v[46:47], v[46:47], 0.5 op_sel_hi:[1,0]
	v_pk_mul_f32 v[44:45], v[44:45], s[40:41] op_sel_hi:[1,0]
	v_pk_mul_f32 v[46:47], v[46:47], s[40:41] op_sel_hi:[1,0]
	v_pk_mul_f32 v[94:95], v[100:101], v[44:45]
	v_cvt_f32_ubyte1_e32 v45, v170
	v_cvt_f32_ubyte0_e32 v44, v170
	v_pk_mul_f32 v[92:93], v[102:103], v[46:47]
	v_cvt_f32_ubyte3_e32 v47, v170
	v_cvt_f32_ubyte2_e32 v46, v170
	v_pk_add_f32 v[44:45], v[44:45], 0.5 op_sel_hi:[1,0]
	v_pk_add_f32 v[46:47], v[46:47], 0.5 op_sel_hi:[1,0]
	v_pk_mul_f32 v[60:61], v[44:45], s[40:41] op_sel_hi:[1,0]
	v_pk_mul_f32 v[44:45], v[46:47], s[40:41] op_sel_hi:[1,0]
	v_pk_mul_f32 v[46:47], v[128:129], v[60:61]
	v_cvt_f32_ubyte1_e32 v61, v171
	v_cvt_f32_ubyte0_e32 v60, v171
	v_cvt_f32_ubyte3_e32 v63, v171
	v_cvt_f32_ubyte2_e32 v62, v171
	v_pk_add_f32 v[60:61], v[60:61], 0.5 op_sel_hi:[1,0]
	v_pk_add_f32 v[62:63], v[62:63], 0.5 op_sel_hi:[1,0]
	v_pk_mul_f32 v[60:61], v[60:61], s[40:41] op_sel_hi:[1,0]
	v_pk_mul_f32 v[40:41], v[98:99], v[40:41]
	v_pk_mul_f32 v[62:63], v[62:63], s[40:41] op_sel_hi:[1,0]
	v_pk_mul_f32 v[98:99], v[132:133], v[60:61]
	v_cvt_f32_ubyte1_e32 v61, v2
	v_cvt_f32_ubyte0_e32 v60, v2
	v_pk_mul_f32 v[96:97], v[134:135], v[62:63]
	v_cvt_f32_ubyte3_e32 v63, v2
	v_cvt_f32_ubyte2_e32 v62, v2
	v_pk_add_f32 v[60:61], v[60:61], 0.5 op_sel_hi:[1,0]
	v_pk_add_f32 v[62:63], v[62:63], 0.5 op_sel_hi:[1,0]
	v_pk_mul_f32 v[68:69], v[60:61], s[40:41] op_sel_hi:[1,0]
	v_cvt_f32_ubyte3_e32 v101, v3
	v_cvt_f32_ubyte2_e32 v100, v3
	v_pk_mul_f32 v[60:61], v[62:63], s[40:41] op_sel_hi:[1,0]
	v_pk_mul_f32 v[62:63], v[104:105], v[68:69]
	v_cvt_f32_ubyte1_e32 v69, v3
	v_cvt_f32_ubyte0_e32 v68, v3
	v_pk_add_f32 v[2:3], v[100:101], 0.5 op_sel_hi:[1,0]
	v_pk_add_f32 v[68:69], v[68:69], 0.5 op_sel_hi:[1,0]
	v_pk_mul_f32 v[2:3], v[2:3], s[40:41] op_sel_hi:[1,0]
	v_pk_mul_f32 v[68:69], v[68:69], s[40:41] op_sel_hi:[1,0]
	v_pk_mul_f32 v[100:101], v[110:111], v[2:3]
	v_cvt_f32_ubyte1_e32 v3, v0
	v_cvt_f32_ubyte0_e32 v2, v0
	v_pk_mul_f32 v[102:103], v[108:109], v[68:69]
	v_cvt_f32_ubyte3_e32 v69, v0
	v_cvt_f32_ubyte2_e32 v68, v0
	v_pk_add_f32 v[2:3], v[2:3], 0.5 op_sel_hi:[1,0]
	v_lshl_add_u32 v108, s92, 8, v226
	v_pk_mul_f32 v[28:29], v[114:115], v[28:29]
	v_pk_mul_f32 v[60:61], v[106:107], v[60:61]
	v_pk_add_f32 v[68:69], v[68:69], 0.5 op_sel_hi:[1,0]
	v_pk_mul_f32 v[104:105], v[2:3], s[40:41] op_sel_hi:[1,0]
	v_cvt_f32_ubyte3_e32 v107, v1
	v_cvt_f32_ubyte2_e32 v106, v1
	v_ashrrev_i32_e32 v109, 31, v108
	v_pk_mul_f32 v[112:113], v[182:183], s[42:43] op_sel_hi:[1,0]
	v_pk_mul_f32 v[114:115], v[184:185], s[42:43] op_sel_hi:[1,0]
	v_pk_mul_f32 v[2:3], v[68:69], s[40:41] op_sel_hi:[1,0]
	v_pk_mul_f32 v[68:69], v[144:145], v[104:105]
	v_cvt_f32_ubyte1_e32 v105, v1
	v_cvt_f32_ubyte0_e32 v104, v1
	v_pk_add_f32 v[0:1], v[106:107], 0.5 op_sel_hi:[1,0]
	v_lshlrev_b64 v[106:107], 11, v[108:109]
	v_pk_mul_f32 v[118:119], v[188:189], s[42:43] op_sel_hi:[1,0]
	v_med3_f32 v109, v114, s86, v233
	v_med3_f32 v114, v115, s86, v233
	v_med3_f32 v115, v112, s86, v233
	v_mov_b32_e32 v112, v157
	v_med3_f32 v120, v113, s86, v233
	v_cvt_pk_fp8_f32 v112, v109, v114
	v_med3_f32 v109, v118, s86, v233
	v_med3_f32 v114, v119, s86, v233
	v_mov_b32_e32 v113, v157
	v_cvt_pk_fp8_f32 v113, v109, v114
	v_pk_mul_f32 v[116:117], v[186:187], s[42:43] op_sel_hi:[1,0]
	v_cvt_pk_fp8_f32 v112, v115, v120 op_sel:[0,0,1]
	v_med3_f32 v109, v116, s86, v233
	v_med3_f32 v114, v117, s86, v233
	v_cvt_pk_fp8_f32 v113, v109, v114 op_sel:[0,0,1]
	v_pk_mul_f32 v[114:115], v[172:173], s[42:43] op_sel_hi:[1,0]
	v_pk_mul_f32 v[116:117], v[174:175], s[42:43] op_sel_hi:[1,0]
	v_pk_mul_f32 v[120:121], v[178:179], s[42:43] op_sel_hi:[1,0]
	v_med3_f32 v109, v116, s86, v233
	v_med3_f32 v116, v117, s86, v233
	v_med3_f32 v117, v114, s86, v233
	v_mov_b32_e32 v114, v157
	v_pk_mul_f32 v[36:37], v[122:123], v[36:37]
	v_med3_f32 v122, v115, s86, v233
	v_cvt_pk_fp8_f32 v114, v109, v116
	v_med3_f32 v109, v120, s86, v233
	v_med3_f32 v116, v121, s86, v233
	v_mov_b32_e32 v115, v157
	v_cvt_pk_fp8_f32 v115, v109, v116
	v_pk_mul_f32 v[118:119], v[176:177], s[42:43] op_sel_hi:[1,0]
	v_lshl_or_b32 v110, s91, 8, v229
	v_med3_f32 v109, v118, s86, v233
	v_med3_f32 v116, v119, s86, v233
	v_cvt_pk_fp8_f32 v114, v117, v122 op_sel:[0,0,1]
	v_cvt_pk_fp8_f32 v115, v109, v116 op_sel:[0,0,1]
	v_ashrrev_i32_e32 v111, 31, v110
	v_lshl_add_u64 v[106:107], s[6:7], 0, v[106:107]
	v_pk_mul_f32 v[48:49], v[48:49], s[42:43] op_sel_hi:[1,0]
	v_pk_mul_f32 v[50:51], v[50:51], s[42:43] op_sel_hi:[1,0]
	v_lshl_add_u64 v[106:107], v[106:107], 0, v[110:111]
	v_pk_mul_f32 v[54:55], v[54:55], s[42:43] op_sel_hi:[1,0]
	v_med3_f32 v50, v50, s86, v233
	v_med3_f32 v51, v51, s86, v233
	v_med3_f32 v109, v48, s86, v233
	v_mov_b32_e32 v48, v157
	global_store_dwordx2 v[106:107], v[112:113], off
	global_store_dwordx2 v[106:107], v[114:115], off offset:128
	v_pk_mul_f32 v[52:53], v[52:53], s[42:43] op_sel_hi:[1,0]
	v_med3_f32 v114, v49, s86, v233
	v_cvt_pk_fp8_f32 v48, v50, v51
	v_med3_f32 v50, v54, s86, v233
	v_med3_f32 v51, v55, s86, v233
	v_mov_b32_e32 v49, v157
	v_pk_mul_f32 v[12:13], v[12:13], s[42:43] op_sel_hi:[1,0]
	v_pk_mul_f32 v[14:15], v[14:15], s[42:43] op_sel_hi:[1,0]
	v_cvt_pk_fp8_f32 v49, v50, v51
	v_med3_f32 v50, v52, s86, v233
	v_med3_f32 v51, v53, s86, v233
	v_pk_mul_f32 v[52:53], v[142:143], s[42:43] op_sel_hi:[1,0]
	v_med3_f32 v14, v14, s86, v233
	v_med3_f32 v15, v15, s86, v233
	v_med3_f32 v54, v12, s86, v233
	v_mov_b32_e32 v12, v157
	v_med3_f32 v55, v13, s86, v233
	v_cvt_pk_fp8_f32 v12, v14, v15
	v_med3_f32 v14, v52, s86, v233
	v_med3_f32 v15, v53, s86, v233
	v_mov_b32_e32 v13, v157
	v_cvt_pk_fp8_f32 v13, v14, v15
	v_or_b32_e32 v112, 16, v108
	v_cvt_pk_fp8_f32 v49, v50, v51 op_sel:[0,0,1]
	v_pk_mul_f32 v[50:51], v[140:141], s[42:43] op_sel_hi:[1,0]
	v_ashrrev_i32_e32 v113, 31, v112
	v_cvt_pk_fp8_f32 v48, v109, v114 op_sel:[0,0,1]
	v_med3_f32 v14, v50, s86, v233
	v_med3_f32 v15, v51, s86, v233
	v_lshlrev_b64 v[112:113], 11, v[112:113]
	v_cvt_pk_fp8_f32 v12, v54, v55 op_sel:[0,0,1]
	v_cvt_pk_fp8_f32 v13, v14, v15 op_sel:[0,0,1]
	v_lshl_add_u64 v[14:15], s[6:7], 0, v[112:113]
	v_lshl_add_u64 v[14:15], v[14:15], 0, v[110:111]
	v_pk_mul_f32 v[4:5], v[4:5], s[42:43] op_sel_hi:[1,0]
	v_pk_mul_f32 v[6:7], v[6:7], s[42:43] op_sel_hi:[1,0]
	global_store_dwordx2 v[14:15], v[48:49], off
	global_store_dwordx2 v[14:15], v[12:13], off offset:128
	v_pk_mul_f32 v[48:49], v[58:59], s[42:43] op_sel_hi:[1,0]
	v_med3_f32 v6, v6, s86, v233
	v_med3_f32 v7, v7, s86, v233
	v_med3_f32 v50, v4, s86, v233
	v_mov_b32_e32 v4, v157
	v_med3_f32 v51, v5, s86, v233
	v_cvt_pk_fp8_f32 v4, v6, v7
	v_med3_f32 v6, v48, s86, v233
	v_med3_f32 v7, v49, s86, v233
	v_mov_b32_e32 v5, v157
	v_cvt_pk_fp8_f32 v5, v6, v7
	v_pk_mul_f32 v[14:15], v[56:57], s[42:43] op_sel_hi:[1,0]
	v_or_b32_e32 v12, 32, v108
	v_med3_f32 v6, v14, s86, v233
	v_med3_f32 v7, v15, s86, v233
	v_cvt_pk_fp8_f32 v5, v6, v7 op_sel:[0,0,1]
	v_pk_mul_f32 v[6:7], v[16:17], s[42:43] op_sel_hi:[1,0]
	v_pk_mul_f32 v[14:15], v[18:19], s[42:43] op_sel_hi:[1,0]
	v_pk_mul_f32 v[18:19], v[168:169], s[42:43] op_sel_hi:[1,0]
	v_med3_f32 v14, v14, s86, v233
	v_med3_f32 v15, v15, s86, v233
	v_med3_f32 v48, v6, s86, v233
	v_mov_b32_e32 v6, v157
	v_med3_f32 v49, v7, s86, v233
	v_cvt_pk_fp8_f32 v6, v14, v15
	v_med3_f32 v14, v18, s86, v233
	v_med3_f32 v15, v19, s86, v233
	v_mov_b32_e32 v7, v157
	v_cvt_pk_fp8_f32 v7, v14, v15
	v_pk_mul_f32 v[16:17], v[70:71], s[42:43] op_sel_hi:[1,0]
	v_ashrrev_i32_e32 v13, 31, v12
	v_cvt_pk_fp8_f32 v4, v50, v51 op_sel:[0,0,1]
	v_med3_f32 v14, v16, s86, v233
	v_med3_f32 v15, v17, s86, v233
	v_lshlrev_b64 v[12:13], 11, v[12:13]
	v_cvt_pk_fp8_f32 v6, v48, v49 op_sel:[0,0,1]
	v_cvt_pk_fp8_f32 v7, v14, v15 op_sel:[0,0,1]
	v_lshl_add_u64 v[12:13], s[6:7], 0, v[12:13]
	v_lshl_add_u64 v[12:13], v[12:13], 0, v[110:111]
	global_store_dwordx2 v[12:13], v[4:5], off
	global_store_dwordx2 v[12:13], v[6:7], off offset:128
	v_pk_mul_f32 v[6:7], v[8:9], s[42:43] op_sel_hi:[1,0]
	v_pk_mul_f32 v[8:9], v[10:11], s[42:43] op_sel_hi:[1,0]
	v_pk_mul_f32 v[12:13], v[66:67], s[42:43] op_sel_hi:[1,0]
	v_med3_f32 v8, v8, s86, v233
	v_med3_f32 v9, v9, s86, v233
	v_med3_f32 v14, v6, s86, v233
	v_mov_b32_e32 v6, v157
	v_med3_f32 v15, v7, s86, v233
	v_cvt_pk_fp8_f32 v6, v8, v9
	v_med3_f32 v8, v12, s86, v233
	v_med3_f32 v9, v13, s86, v233
	v_mov_b32_e32 v7, v157
	v_cvt_pk_fp8_f32 v7, v8, v9
	v_pk_mul_f32 v[10:11], v[64:65], s[42:43] op_sel_hi:[1,0]
	v_cvt_pk_fp8_f32 v6, v14, v15 op_sel:[0,0,1]
	v_med3_f32 v8, v10, s86, v233
	v_med3_f32 v9, v11, s86, v233
	v_cvt_pk_fp8_f32 v7, v8, v9 op_sel:[0,0,1]
	v_pk_mul_f32 v[8:9], v[20:21], s[42:43] op_sel_hi:[1,0]
	v_pk_mul_f32 v[10:11], v[22:23], s[42:43] op_sel_hi:[1,0]
	v_pk_mul_f32 v[14:15], v[74:75], s[42:43] op_sel_hi:[1,0]
	v_med3_f32 v10, v10, s86, v233
	v_med3_f32 v11, v11, s86, v233
	v_med3_f32 v16, v8, s86, v233
	v_mov_b32_e32 v8, v157
	v_med3_f32 v17, v9, s86, v233
	v_cvt_pk_fp8_f32 v8, v10, v11
	v_med3_f32 v10, v14, s86, v233
	v_med3_f32 v11, v15, s86, v233
	v_mov_b32_e32 v9, v157
	v_cvt_pk_fp8_f32 v9, v10, v11
	v_or_b32_e32 v4, 48, v108
	v_pk_mul_f32 v[12:13], v[72:73], s[42:43] op_sel_hi:[1,0]
	v_ashrrev_i32_e32 v5, 31, v4
	v_med3_f32 v10, v12, s86, v233
	v_med3_f32 v11, v13, s86, v233
	v_lshlrev_b64 v[4:5], 11, v[4:5]
	v_cvt_pk_fp8_f32 v8, v16, v17 op_sel:[0,0,1]
	v_cvt_pk_fp8_f32 v9, v10, v11 op_sel:[0,0,1]
	v_lshl_add_u64 v[4:5], s[6:7], 0, v[4:5]
	v_lshl_add_u64 v[4:5], v[4:5], 0, v[110:111]
	global_store_dwordx2 v[4:5], v[6:7], off
	global_store_dwordx2 v[4:5], v[8:9], off offset:128
	v_pk_mul_f32 v[6:7], v[24:25], s[42:43] op_sel_hi:[1,0]
	v_pk_mul_f32 v[8:9], v[26:27], s[42:43] op_sel_hi:[1,0]
	v_pk_mul_f32 v[12:13], v[78:79], s[42:43] op_sel_hi:[1,0]
	v_med3_f32 v8, v8, s86, v233
	v_med3_f32 v9, v9, s86, v233
	v_med3_f32 v14, v6, s86, v233
	v_mov_b32_e32 v6, v157
	v_med3_f32 v15, v7, s86, v233
	v_cvt_pk_fp8_f32 v6, v8, v9
	v_med3_f32 v8, v12, s86, v233
	v_med3_f32 v9, v13, s86, v233
	v_mov_b32_e32 v7, v157
	v_cvt_pk_fp8_f32 v7, v8, v9
	v_pk_mul_f32 v[10:11], v[76:77], s[42:43] op_sel_hi:[1,0]
	v_cvt_pk_fp8_f32 v6, v14, v15 op_sel:[0,0,1]
	v_med3_f32 v8, v10, s86, v233
	v_med3_f32 v9, v11, s86, v233
	v_cvt_pk_fp8_f32 v7, v8, v9 op_sel:[0,0,1]
	v_pk_mul_f32 v[8:9], v[28:29], s[42:43] op_sel_hi:[1,0]
	v_pk_mul_f32 v[10:11], v[30:31], s[42:43] op_sel_hi:[1,0]
	v_pk_mul_f32 v[14:15], v[82:83], s[42:43] op_sel_hi:[1,0]
	v_med3_f32 v10, v10, s86, v233
	v_med3_f32 v11, v11, s86, v233
	v_med3_f32 v16, v8, s86, v233
	v_mov_b32_e32 v8, v157
	v_med3_f32 v17, v9, s86, v233
	v_cvt_pk_fp8_f32 v8, v10, v11
	v_med3_f32 v10, v14, s86, v233
	v_med3_f32 v11, v15, s86, v233
	v_mov_b32_e32 v9, v157
	v_cvt_pk_fp8_f32 v9, v10, v11
	v_pk_mul_f32 v[12:13], v[80:81], s[42:43] op_sel_hi:[1,0]
	v_lshl_add_u64 v[4:5], v[106:107], 0, s[2:3]
	v_med3_f32 v10, v12, s86, v233
	v_med3_f32 v11, v13, s86, v233
	v_cvt_pk_fp8_f32 v8, v16, v17 op_sel:[0,0,1]
	v_cvt_pk_fp8_f32 v9, v10, v11 op_sel:[0,0,1]
	s_mov_b32 s2, 0x40000
	v_add_co_u32_e32 v10, vcc, s2, v106
	v_pk_mul_f32 v[12:13], v[86:87], s[42:43] op_sel_hi:[1,0]
	s_nop 0
	v_addc_co_u32_e32 v11, vcc, 0, v107, vcc
	global_store_dwordx2 v[10:11], v[6:7], off
	global_store_dwordx2 v[4:5], v[8:9], off offset:128
	v_pk_mul_f32 v[6:7], v[32:33], s[42:43] op_sel_hi:[1,0]
	v_pk_mul_f32 v[8:9], v[34:35], s[42:43] op_sel_hi:[1,0]
	v_med3_f32 v14, v6, s86, v233
	v_med3_f32 v8, v8, s86, v233
	v_med3_f32 v9, v9, s86, v233
	v_mov_b32_e32 v6, v157
	v_med3_f32 v15, v7, s86, v233
	v_cvt_pk_fp8_f32 v6, v8, v9
	v_med3_f32 v8, v12, s86, v233
	v_med3_f32 v9, v13, s86, v233
	v_mov_b32_e32 v7, v157
	v_cvt_pk_fp8_f32 v7, v8, v9
	v_pk_mul_f32 v[10:11], v[84:85], s[42:43] op_sel_hi:[1,0]
	v_cvt_pk_fp8_f32 v6, v14, v15 op_sel:[0,0,1]
	v_med3_f32 v8, v10, s86, v233
	v_med3_f32 v9, v11, s86, v233
	v_cvt_pk_fp8_f32 v7, v8, v9 op_sel:[0,0,1]
	v_pk_mul_f32 v[8:9], v[36:37], s[42:43] op_sel_hi:[1,0]
	v_pk_mul_f32 v[10:11], v[38:39], s[42:43] op_sel_hi:[1,0]
	v_pk_mul_f32 v[14:15], v[90:91], s[42:43] op_sel_hi:[1,0]
	v_med3_f32 v10, v10, s86, v233
	v_med3_f32 v11, v11, s86, v233
	v_med3_f32 v16, v8, s86, v233
	v_mov_b32_e32 v8, v157
	v_med3_f32 v17, v9, s86, v233
	v_cvt_pk_fp8_f32 v8, v10, v11
	v_med3_f32 v10, v14, s86, v233
	v_med3_f32 v11, v15, s86, v233
	v_mov_b32_e32 v9, v157
	v_cvt_pk_fp8_f32 v9, v10, v11
	v_pk_mul_f32 v[12:13], v[88:89], s[42:43] op_sel_hi:[1,0]
	s_mov_b64 s[2:3], 0x48000
	v_med3_f32 v10, v12, s86, v233
	v_med3_f32 v11, v13, s86, v233
	v_lshl_add_u64 v[4:5], v[106:107], 0, s[2:3]
	v_cvt_pk_fp8_f32 v8, v16, v17 op_sel:[0,0,1]
	v_cvt_pk_fp8_f32 v9, v10, v11 op_sel:[0,0,1]
	s_mov_b32 s2, 0x48000
	v_add_co_u32_e32 v10, vcc, s2, v106
	v_pk_mul_f32 v[12:13], v[94:95], s[42:43] op_sel_hi:[1,0]
	s_nop 0
	v_addc_co_u32_e32 v11, vcc, 0, v107, vcc
	global_store_dwordx2 v[10:11], v[6:7], off
	global_store_dwordx2 v[4:5], v[8:9], off offset:128
	v_pk_mul_f32 v[6:7], v[40:41], s[42:43] op_sel_hi:[1,0]
	v_pk_mul_f32 v[8:9], v[42:43], s[42:43] op_sel_hi:[1,0]
	v_med3_f32 v14, v6, s86, v233
	v_med3_f32 v8, v8, s86, v233
	v_med3_f32 v9, v9, s86, v233
	v_mov_b32_e32 v6, v157
	v_med3_f32 v15, v7, s86, v233
	v_cvt_pk_fp8_f32 v6, v8, v9
	v_med3_f32 v8, v12, s86, v233
	v_med3_f32 v9, v13, s86, v233
	v_mov_b32_e32 v7, v157
	v_cvt_pk_fp8_f32 v7, v8, v9
	v_pk_mul_f32 v[10:11], v[92:93], s[42:43] op_sel_hi:[1,0]
	v_pk_mul_f32 v[44:45], v[130:131], v[44:45]
	v_med3_f32 v8, v10, s86, v233
	v_med3_f32 v9, v11, s86, v233
	v_cvt_pk_fp8_f32 v7, v8, v9 op_sel:[0,0,1]
	v_pk_mul_f32 v[8:9], v[44:45], s[42:43] op_sel_hi:[1,0]
	v_pk_mul_f32 v[10:11], v[46:47], s[42:43] op_sel_hi:[1,0]
	v_cvt_pk_fp8_f32 v6, v14, v15 op_sel:[0,0,1]
	v_pk_mul_f32 v[14:15], v[98:99], s[42:43] op_sel_hi:[1,0]
	v_med3_f32 v10, v10, s86, v233
	v_med3_f32 v11, v11, s86, v233
	v_med3_f32 v16, v8, s86, v233
	v_mov_b32_e32 v8, v157
	v_med3_f32 v17, v9, s86, v233
	v_cvt_pk_fp8_f32 v8, v10, v11
	v_med3_f32 v10, v14, s86, v233
	v_med3_f32 v11, v15, s86, v233
	v_mov_b32_e32 v9, v157
	v_cvt_pk_fp8_f32 v9, v10, v11
	v_pk_mul_f32 v[12:13], v[96:97], s[42:43] op_sel_hi:[1,0]
	s_mov_b64 s[2:3], 0x50000
	v_med3_f32 v10, v12, s86, v233
	v_med3_f32 v11, v13, s86, v233
	v_lshl_add_u64 v[4:5], v[106:107], 0, s[2:3]
	v_cvt_pk_fp8_f32 v8, v16, v17 op_sel:[0,0,1]
	v_cvt_pk_fp8_f32 v9, v10, v11 op_sel:[0,0,1]
	s_mov_b32 s2, 0x50000
	v_add_co_u32_e32 v10, vcc, s2, v106
	v_pk_mul_f32 v[12:13], v[102:103], s[42:43] op_sel_hi:[1,0]
	s_nop 0
	v_addc_co_u32_e32 v11, vcc, 0, v107, vcc
	global_store_dwordx2 v[10:11], v[6:7], off
	global_store_dwordx2 v[4:5], v[8:9], off offset:128
	v_pk_mul_f32 v[6:7], v[60:61], s[42:43] op_sel_hi:[1,0]
	v_pk_mul_f32 v[8:9], v[62:63], s[42:43] op_sel_hi:[1,0]
	v_med3_f32 v14, v6, s86, v233
	v_med3_f32 v8, v8, s86, v233
	v_med3_f32 v9, v9, s86, v233
	v_mov_b32_e32 v6, v157
	v_med3_f32 v15, v7, s86, v233
	v_cvt_pk_fp8_f32 v6, v8, v9
	v_med3_f32 v8, v12, s86, v233
	v_med3_f32 v9, v13, s86, v233
	v_mov_b32_e32 v7, v157
	v_cvt_pk_fp8_f32 v7, v8, v9
	v_pk_add_f32 v[104:105], v[104:105], 0.5 op_sel_hi:[1,0]
	v_pk_mul_f32 v[10:11], v[100:101], s[42:43] op_sel_hi:[1,0]
	v_pk_mul_f32 v[2:3], v[146:147], v[2:3]
	v_pk_mul_f32 v[104:105], v[104:105], s[40:41] op_sel_hi:[1,0]
	v_med3_f32 v8, v10, s86, v233
	v_med3_f32 v9, v11, s86, v233
	v_pk_mul_f32 v[104:105], v[136:137], v[104:105]
	v_cvt_pk_fp8_f32 v7, v8, v9 op_sel:[0,0,1]
	v_pk_mul_f32 v[2:3], v[2:3], s[42:43] op_sel_hi:[1,0]
	v_pk_mul_f32 v[8:9], v[68:69], s[42:43] op_sel_hi:[1,0]
	v_pk_mul_f32 v[10:11], v[104:105], s[42:43] op_sel_hi:[1,0]
	v_med3_f32 v8, v8, s86, v233
	v_med3_f32 v9, v9, s86, v233
	v_med3_f32 v12, v2, s86, v233
	v_mov_b32_e32 v2, v157
	v_med3_f32 v13, v3, s86, v233
	v_cvt_pk_fp8_f32 v2, v8, v9
	v_med3_f32 v8, v10, s86, v233
	v_med3_f32 v9, v11, s86, v233
	v_mov_b32_e32 v3, v157
	v_pk_mul_f32 v[0:1], v[0:1], s[40:41] op_sel_hi:[1,0]
	v_cvt_pk_fp8_f32 v3, v8, v9
	v_pk_mul_f32 v[0:1], v[138:139], v[0:1]
	s_mov_b64 s[2:3], 0x58000
	v_pk_mul_f32 v[0:1], v[0:1], s[42:43] op_sel_hi:[1,0]
	v_lshl_add_u64 v[4:5], v[106:107], 0, s[2:3]
	v_cvt_pk_fp8_f32 v6, v14, v15 op_sel:[0,0,1]
	v_med3_f32 v0, v0, s86, v233
	v_med3_f32 v1, v1, s86, v233
	s_mov_b32 s2, 0x58000
	v_cvt_pk_fp8_f32 v2, v12, v13 op_sel:[0,0,1]
	v_cvt_pk_fp8_f32 v3, v0, v1 op_sel:[0,0,1]
	v_add_co_u32_e32 v0, vcc, s2, v106
	s_mov_b32 s91, s87
	s_nop 0
	v_addc_co_u32_e32 v1, vcc, 0, v107, vcc
	s_and_b64 vcc, exec, s[0:1]
	s_mov_b32 s92, s88
	global_store_dwordx2 v[0:1], v[6:7], off
	global_store_dwordx2 v[4:5], v[2:3], off offset:128
	s_cbranch_vccz .LBB0_904
	s_waitcnt vmcnt(0)
	s_cmpk_lt_u32 s68, 0x100
	s_cbranch_scc1 .LBB0_915
	s_barrier

.LBB0_975:
	v_ashrrev_i32_e32 v1, 31, v8
	v_lshrrev_b32_e32 v1, 26, v1
	v_add_u32_e32 v1, v8, v1
	v_ashrrev_i32_e32 v9, 6, v1
	v_bfe_i32 v1, v8, 27, 1
	v_lshlrev_b32_e32 v0, 4, v8
	v_lshrrev_b32_e32 v1, 22, v1
	v_add_u32_e32 v1, v0, v1
	v_and_b32_e32 v1, 0xfffffc00, v1
	v_sub_u32_e32 v1, v0, v1
	v_lshrrev_b32_e32 v2, 4, v1
	v_bitop3_b32 v1, v2, v1, 32 bitop3:0x6c
	v_ashrrev_i32_e32 v3, 31, v1
	v_lshrrev_b32_e32 v3, 26, v3
	v_add_u32_e32 v3, v1, v3
	v_lshlrev_b32_e32 v2, 3, v9
	v_ashrrev_i32_e32 v10, 6, v3
	v_and_b32_e32 v3, 0xc0, v3
	v_and_b32_e32 v2, -16, v2
	v_sub_u32_e32 v1, v1, v3
	v_mov_b32_e32 v3, 1
	v_add_u32_e32 v2, v10, v2
	v_ashrrev_i16_sdwa v1, v3, sext(v1) dst_sel:DWORD dst_unused:UNUSED_PAD src0_sel:DWORD src1_sel:BYTE_0
	v_lshlrev_b32_e32 v4, 5, v9
	v_bfe_i32 v11, v1, 0, 16
	v_lshlrev_b32_e32 v1, 1, v2
	v_lshrrev_b32_e32 v5, 2, v2
	v_and_b32_e32 v6, 3, v10
	s_mov_b32 s1, 0x1fffe0
	v_and_b32_e32 v4, 32, v4
	v_and_b32_e32 v1, 24, v1
	v_and_b32_e32 v5, 4, v5
	v_and_or_b32 v6, v2, s1, v6
	s_add_u32 s39, s4, 0x3660c000
	v_or3_b32 v1, v6, v5, v1
	v_add_lshl_u32 v4, v4, v11, 1
	v_add_u32_e32 v0, 0x2000, v0
	s_addc_u32 s40, s5, 0
	v_lshl_add_u32 v146, v1, 11, v4
	v_ashrrev_i32_e32 v1, 31, v0
	s_add_u32 s41, s4, 0x35e0c000
	v_lshrrev_b32_e32 v1, 22, v1
	s_addc_u32 s42, s5, 0
	v_add_u32_e32 v1, v0, v1
	s_add_i32 s6, s6, s7
	v_ashrrev_i32_e32 v12, 10, v1
	s_ashr_i32 s7, s6, 31
	v_mul_i32_i24_e32 v1, 0x400, v12
	s_lshr_b32 s7, s7, 26
	v_sub_u32_e32 v0, v0, v1
	s_add_i32 s7, s6, s7
	v_lshrrev_b32_e32 v1, 4, v0
	s_ashr_i32 s8, s7, 6
	s_and_b32 s7, s7, 0xffc0
	v_bitop3_b32 v0, v1, v0, 32 bitop3:0x6c
	s_sub_i32 s6, s6, s7
	v_lshl_add_u32 v144, v2, 11, v4
	v_ashrrev_i32_e32 v2, 31, v0
	s_bfe_i32 s7, s6, 0x80000
	v_lshrrev_b32_e32 v2, 26, v2
	s_bfe_u32 s7, s7, 0x3000c
	v_add_u32_e32 v2, v0, v2
	s_add_i32 s7, s6, s7
	v_lshlrev_b32_e32 v1, 3, v12
	v_ashrrev_i32_e32 v13, 6, v2
	v_and_b32_e32 v2, 0xc0, v2
	s_bfe_i32 s9, s7, 0x80000
	s_and_b32 s7, s7, 0xf8
	v_and_b32_e32 v1, -16, v1
	v_sub_u32_e32 v0, v0, v2
	s_sub_i32 s6, s6, s7
	v_add_u32_e32 v1, v13, v1
	v_ashrrev_i16_sdwa v0, v3, sext(v0) dst_sel:DWORD dst_unused:UNUSED_PAD src0_sel:DWORD src1_sel:BYTE_0
	v_and_b32_e32 v3, 3, v13
	s_lshl_b32 s8, s8, 3
	s_sext_i32_i16 s9, s9
	s_sext_i32_i8 s6, s6
	v_and_or_b32 v3, v1, s1, v3
	s_ashr_i32 s1, s31, 6
	s_add_i32 s60, s8, s6
	s_ashr_i32 s59, s9, 3
	s_ashr_i32 s0, s31, 8
	s_lshl_b32 s43, s1, 10
	s_lshl_b32 s6, s59, 19
	s_lshl_b32 s7, s60, 19
	s_add_u32 s18, s41, s6
	v_lshlrev_b32_e32 v4, 5, v12
	v_bfe_i32 v14, v0, 0, 16
	v_lshlrev_b32_e32 v0, 1, v1
	v_lshrrev_b32_e32 v2, 2, v1
	s_addc_u32 s19, s42, 0
	s_add_i32 s44, s43, 0
	v_and_b32_e32 v4, 32, v4
	v_and_b32_e32 v0, 24, v0
	v_and_b32_e32 v2, 4, v2
	s_add_i32 m0, s44, 0x10000
	v_or3_b32 v0, v3, v2, v0
	v_add_lshl_u32 v2, v4, v14, 1
	global_load_lds_dwordx4 v146, s[18:19]
	s_add_i32 m0, s44, 0x12000
	v_lshl_add_u32 v150, v0, 11, v2
	s_add_u32 s20, s39, s7
	global_load_lds_dwordx4 v150, s[18:19]
	s_addc_u32 s21, s40, 0
	s_mov_b32 m0, s44
	s_add_i32 s45, s44, 0x2000
	v_lshl_add_u32 v148, v1, 11, v2
	global_load_lds_dwordx4 v144, s[20:21]
	s_mov_b32 m0, s45
	s_add_u32 s6, s18, 0x40000
	global_load_lds_dwordx4 v148, s[20:21]
	s_addc_u32 s7, s19, 0
	s_add_i32 m0, s44, 0x14000
	v_mov_b32_e32 v153, 0
	global_load_lds_dwordx4 v146, s[6:7]
	s_add_i32 m0, s44, 0x16000
	v_mov_b32_e32 v147, v153
	global_load_lds_dwordx4 v150, s[6:7]
	s_add_u32 s6, s20, 0x40000
	s_addc_u32 s7, s21, 0
	s_add_i32 s46, s44, 0x4000
	s_mov_b32 m0, s46
	s_add_i32 s47, s44, 0x6000
	global_load_lds_dwordx4 v144, s[6:7]
	s_mov_b32 m0, s47
	v_mov_b32_e32 v151, v153
	global_load_lds_dwordx4 v148, s[6:7]
	v_mov_b32_e32 v145, v153
	v_mov_b32_e32 v149, v153
	s_mov_b32 s48, 0
	v_lshl_add_u64 v[6:7], s[18:19], 0, v[146:147]
	v_lshl_add_u64 v[4:5], s[18:19], 0, v[150:151]
	v_lshl_add_u64 v[2:3], s[20:21], 0, v[144:145]
	v_lshl_add_u64 v[0:1], s[20:21], 0, v[148:149]
	s_cmp_lg_u32 s0, 0
	s_mov_b32 s49, 0x14000
	s_cbranch_scc1 .LBB0_977
	s_barrier

.LBB0_985:
	ds_read_b128 v[8:11], v176
	ds_read_b128 v[12:15], v176 offset:1024
	ds_read_b128 v[0:3], v176 offset:2048
	ds_read_b128 v[4:7], v176 offset:3072
	s_add_u32 s20, s18, 0xfffc0080
	s_addc_u32 s21, s19, -1
	s_cmp_eq_u32 s67, 12
	s_cselect_b32 s23, s61, s21
	s_cselect_b32 s22, s62, s20
	s_cselect_b32 s21, s63, s66
	s_cselect_b32 s20, s64, s65
	v_lshl_add_u64 v[158:159], s[18:19], 0, v[156:157]
	s_add_i32 m0, s44, 0xc000
	ds_read_b128 v[180:183], v177
	ds_read_b128 v[184:187], v177 offset:1024
	ds_read_b128 v[188:191], v177 offset:2048
	ds_read_b128 v[192:195], v177 offset:3072
	ds_read_b128 v[196:199], v177 offset:4096
	ds_read_b128 v[200:203], v177 offset:5120
	ds_read_b128 v[204:207], v177 offset:6144
	ds_read_b128 v[208:211], v177 offset:7168
	global_load_lds_dwordx4 v[158:159], off
	v_lshl_add_u64 v[158:159], s[18:19], 0, v[154:155]
	s_add_i32 m0, s44, 0xe000
	s_nop 0
	global_load_lds_dwordx4 v[158:159], off
	s_waitcnt lgkmcnt(8)
	s_barrier
	s_waitcnt lgkmcnt(0)
	s_setprio 1
	s_waitcnt lgkmcnt(0)
	v_mfma_scale_f32_16x16x128_f8f6f4 v[140:143], v[8:15], v[180:187], v[140:143], v172, v172 op_sel_hi:[0,0,0]
	v_mfma_scale_f32_16x16x128_f8f6f4 v[136:139], v[0:7], v[180:187], v[136:139], v172, v172 op_sel_hi:[0,0,0]
	v_mfma_scale_f32_16x16x128_f8f6f4 v[128:131], v[8:15], v[188:195], v[128:131], v172, v172 op_sel_hi:[0,0,0]
	v_mfma_scale_f32_16x16x128_f8f6f4 v[120:123], v[0:7], v[188:195], v[120:123], v172, v172 op_sel_hi:[0,0,0]
	v_mfma_scale_f32_16x16x128_f8f6f4 v[112:115], v[8:15], v[196:203], v[112:115], v172, v172 op_sel_hi:[0,0,0]
	v_mfma_scale_f32_16x16x128_f8f6f4 v[104:107], v[0:7], v[196:203], v[104:107], v172, v172 op_sel_hi:[0,0,0]
	v_mfma_scale_f32_16x16x128_f8f6f4 v[96:99], v[8:15], v[204:211], v[96:99], v172, v172 op_sel_hi:[0,0,0]
	v_mfma_scale_f32_16x16x128_f8f6f4 v[88:91], v[0:7], v[204:211], v[88:91], v172, v172 op_sel_hi:[0,0,0]
	s_setprio 0
	s_barrier
	s_add_i32 s68, s53, s43
	v_lshl_add_u64 v[162:163], s[20:21], 0, v[146:147]
	s_mov_b32 m0, s68
	ds_read_b128 v[212:215], v178
	ds_read_b128 v[216:219], v178 offset:1024
	ds_read_b128 v[224:227], v178 offset:2048
	ds_read_b128 v[228:231], v178 offset:3072
	global_load_lds_dwordx4 v[162:163], off
	v_lshl_add_u64 v[164:165], s[20:21], 0, v[150:151]
	s_add_i32 m0, s68, 0x2000
	s_nop 0
	global_load_lds_dwordx4 v[164:165], off
	s_barrier
	s_waitcnt lgkmcnt(0)
	s_setprio 1
	s_waitcnt lgkmcnt(0)
	v_mfma_scale_f32_16x16x128_f8f6f4 v[132:135], v[212:219], v[180:187], v[132:135], v172, v172 op_sel_hi:[0,0,0]
	v_mfma_scale_f32_16x16x128_f8f6f4 v[124:127], v[224:231], v[180:187], v[124:127], v172, v172 op_sel_hi:[0,0,0]
	v_mfma_scale_f32_16x16x128_f8f6f4 v[116:119], v[212:219], v[188:195], v[116:119], v172, v172 op_sel_hi:[0,0,0]
	v_mfma_scale_f32_16x16x128_f8f6f4 v[108:111], v[224:231], v[188:195], v[108:111], v172, v172 op_sel_hi:[0,0,0]
	v_mfma_scale_f32_16x16x128_f8f6f4 v[100:103], v[212:219], v[196:203], v[100:103], v172, v172 op_sel_hi:[0,0,0]
	v_mfma_scale_f32_16x16x128_f8f6f4 v[92:95], v[224:231], v[196:203], v[92:95], v172, v172 op_sel_hi:[0,0,0]
	v_mfma_scale_f32_16x16x128_f8f6f4 v[84:87], v[212:219], v[204:211], v[84:87], v172, v172 op_sel_hi:[0,0,0]
	v_mfma_scale_f32_16x16x128_f8f6f4 v[80:83], v[224:231], v[204:211], v[80:83], v172, v172 op_sel_hi:[0,0,0]
	s_setprio 0
	s_mov_b32 m0, s44
	v_lshl_add_u64 v[166:167], s[22:23], 0, v[144:145]
	s_barrier
	ds_read_b128 v[180:183], v177 offset:16384
	ds_read_b128 v[184:187], v177 offset:17408
	ds_read_b128 v[188:191], v177 offset:18432
	ds_read_b128 v[192:195], v177 offset:19456
	ds_read_b128 v[196:199], v177 offset:20480
	ds_read_b128 v[200:203], v177 offset:21504
	ds_read_b128 v[204:207], v177 offset:22528
	ds_read_b128 v[208:211], v177 offset:23552
	global_load_lds_dwordx4 v[166:167], off
	v_lshl_add_u64 v[168:169], s[22:23], 0, v[148:149]
	s_mov_b32 m0, s45
	s_nop 0
	global_load_lds_dwordx4 v[168:169], off
	s_barrier
	s_waitcnt lgkmcnt(0)
	s_setprio 1
	s_waitcnt lgkmcnt(0)
	v_mfma_scale_f32_16x16x128_f8f6f4 v[76:79], v[8:15], v[180:187], v[76:79], v172, v172 op_sel_hi:[0,0,0]
	v_mfma_scale_f32_16x16x128_f8f6f4 v[72:75], v[0:7], v[180:187], v[72:75], v172, v172 op_sel_hi:[0,0,0]
	v_mfma_scale_f32_16x16x128_f8f6f4 v[64:67], v[8:15], v[188:195], v[64:67], v172, v172 op_sel_hi:[0,0,0]
	v_mfma_scale_f32_16x16x128_f8f6f4 v[56:59], v[0:7], v[188:195], v[56:59], v172, v172 op_sel_hi:[0,0,0]
	v_mfma_scale_f32_16x16x128_f8f6f4 v[48:51], v[8:15], v[196:203], v[48:51], v172, v172 op_sel_hi:[0,0,0]
	v_mfma_scale_f32_16x16x128_f8f6f4 v[40:43], v[0:7], v[196:203], v[40:43], v172, v172 op_sel_hi:[0,0,0]
	v_mfma_scale_f32_16x16x128_f8f6f4 v[32:35], v[8:15], v[204:211], v[32:35], v172, v172 op_sel_hi:[0,0,0]
	v_mfma_scale_f32_16x16x128_f8f6f4 v[24:27], v[0:7], v[204:211], v[24:27], v172, v172 op_sel_hi:[0,0,0]
	s_setprio 0
	s_barrier
	s_add_u32 s68, s20, 0x40000
	s_addc_u32 s69, s21, 0
	s_add_i32 s70, s54, s43
	v_lshl_add_u64 v[0:1], s[68:69], 0, v[146:147]
	s_mov_b32 m0, s70
	s_nop 0
	global_load_lds_dwordx4 v[0:1], off
	v_lshl_add_u64 v[0:1], s[68:69], 0, v[150:151]
	s_add_i32 m0, s70, 0x2000
	s_nop 0
	global_load_lds_dwordx4 v[0:1], off
	s_waitcnt vmcnt(6)
	s_barrier
	s_setprio 1
	v_mfma_scale_f32_16x16x128_f8f6f4 v[68:71], v[212:219], v[180:187], v[68:71], v172, v172 op_sel_hi:[0,0,0]
	v_mfma_scale_f32_16x16x128_f8f6f4 v[60:63], v[224:231], v[180:187], v[60:63], v172, v172 op_sel_hi:[0,0,0]
	v_mfma_scale_f32_16x16x128_f8f6f4 v[52:55], v[212:219], v[188:195], v[52:55], v172, v172 op_sel_hi:[0,0,0]
	v_mfma_scale_f32_16x16x128_f8f6f4 v[44:47], v[224:231], v[188:195], v[44:47], v172, v172 op_sel_hi:[0,0,0]
	v_mfma_scale_f32_16x16x128_f8f6f4 v[36:39], v[212:219], v[196:203], v[36:39], v172, v172 op_sel_hi:[0,0,0]
	v_mfma_scale_f32_16x16x128_f8f6f4 v[28:31], v[224:231], v[196:203], v[28:31], v172, v172 op_sel_hi:[0,0,0]
	v_mfma_scale_f32_16x16x128_f8f6f4 v[20:23], v[212:219], v[204:211], v[20:23], v172, v172 op_sel_hi:[0,0,0]
	v_mfma_scale_f32_16x16x128_f8f6f4 v[16:19], v[224:231], v[204:211], v[16:19], v172, v172 op_sel_hi:[0,0,0]
	s_setprio 0
	s_add_i32 s68, 0, 0x18000
	v_add_u32_e32 v12, s68, v173
	s_barrier
	ds_read_b128 v[0:3], v12
	ds_read_b128 v[4:7], v12 offset:1024
	ds_read_b128 v[8:11], v12 offset:2048
	ds_read_b128 v[12:15], v12 offset:3072
	s_add_u32 s22, s22, 0x40000
	s_addc_u32 s23, s23, 0
	s_mov_b32 m0, s46
	v_lshl_add_u64 v[158:159], s[22:23], 0, v[144:145]
	ds_read_b128 v[180:183], v177 offset:32768
	ds_read_b128 v[184:187], v177 offset:33792
	ds_read_b128 v[188:191], v177 offset:34816
	ds_read_b128 v[192:195], v177 offset:35840
	ds_read_b128 v[196:199], v177 offset:36864
	ds_read_b128 v[200:203], v177 offset:37888
	ds_read_b128 v[204:207], v177 offset:38912
	ds_read_b128 v[208:211], v177 offset:39936
	global_load_lds_dwordx4 v[158:159], off
	v_lshl_add_u64 v[158:159], s[22:23], 0, v[148:149]
	s_mov_b32 m0, s47
	s_nop 0
	global_load_lds_dwordx4 v[158:159], off
	s_waitcnt lgkmcnt(8)
	s_barrier
	s_waitcnt lgkmcnt(0)
	s_setprio 1
	s_waitcnt lgkmcnt(0)
	v_mfma_scale_f32_16x16x128_f8f6f4 v[140:143], v[0:7], v[180:187], v[140:143], v172, v172 op_sel_hi:[0,0,0]
	v_mfma_scale_f32_16x16x128_f8f6f4 v[136:139], v[8:15], v[180:187], v[136:139], v172, v172 op_sel_hi:[0,0,0]
	v_mfma_scale_f32_16x16x128_f8f6f4 v[128:131], v[0:7], v[188:195], v[128:131], v172, v172 op_sel_hi:[0,0,0]
	v_mfma_scale_f32_16x16x128_f8f6f4 v[120:123], v[8:15], v[188:195], v[120:123], v172, v172 op_sel_hi:[0,0,0]
	v_mfma_scale_f32_16x16x128_f8f6f4 v[112:115], v[0:7], v[196:203], v[112:115], v172, v172 op_sel_hi:[0,0,0]
	v_mfma_scale_f32_16x16x128_f8f6f4 v[104:107], v[8:15], v[196:203], v[104:107], v172, v172 op_sel_hi:[0,0,0]
	v_mfma_scale_f32_16x16x128_f8f6f4 v[96:99], v[0:7], v[204:211], v[96:99], v172, v172 op_sel_hi:[0,0,0]
	v_mfma_scale_f32_16x16x128_f8f6f4 v[88:91], v[8:15], v[204:211], v[88:91], v172, v172 op_sel_hi:[0,0,0]
	s_setprio 0
	s_barrier
	s_add_i32 s22, 0, 0x1c000
	s_add_i32 s23, s68, s43
	v_add_u32_e32 v152, s22, v173
	v_lshl_add_u64 v[158:159], v[162:163], 0, s[6:7]
	s_mov_b32 m0, s23
	ds_read_b128 v[212:215], v152
	ds_read_b128 v[216:219], v152 offset:1024
	ds_read_b128 v[224:227], v152 offset:2048
	ds_read_b128 v[228:231], v152 offset:3072
	global_load_lds_dwordx4 v[158:159], off
	v_lshl_add_u64 v[158:159], v[164:165], 0, s[6:7]
	s_add_i32 m0, s23, 0x2000
	s_nop 0
	global_load_lds_dwordx4 v[158:159], off
	s_barrier
	s_waitcnt lgkmcnt(0)
	s_setprio 1
	s_waitcnt lgkmcnt(0)
	v_mfma_scale_f32_16x16x128_f8f6f4 v[132:135], v[212:219], v[180:187], v[132:135], v172, v172 op_sel_hi:[0,0,0]
	v_mfma_scale_f32_16x16x128_f8f6f4 v[124:127], v[224:231], v[180:187], v[124:127], v172, v172 op_sel_hi:[0,0,0]
	v_mfma_scale_f32_16x16x128_f8f6f4 v[116:119], v[212:219], v[188:195], v[116:119], v172, v172 op_sel_hi:[0,0,0]
	v_mfma_scale_f32_16x16x128_f8f6f4 v[108:111], v[224:231], v[188:195], v[108:111], v172, v172 op_sel_hi:[0,0,0]
	v_mfma_scale_f32_16x16x128_f8f6f4 v[100:103], v[212:219], v[196:203], v[100:103], v172, v172 op_sel_hi:[0,0,0]
	v_mfma_scale_f32_16x16x128_f8f6f4 v[92:95], v[224:231], v[196:203], v[92:95], v172, v172 op_sel_hi:[0,0,0]
	v_mfma_scale_f32_16x16x128_f8f6f4 v[84:87], v[212:219], v[204:211], v[84:87], v172, v172 op_sel_hi:[0,0,0]
	v_mfma_scale_f32_16x16x128_f8f6f4 v[80:83], v[224:231], v[204:211], v[80:83], v172, v172 op_sel_hi:[0,0,0]
	s_setprio 0
	s_mov_b32 m0, s50
	v_lshl_add_u64 v[158:159], v[166:167], 0, s[6:7]
	s_barrier
	ds_read_b128 v[180:183], v177 offset:49152
	ds_read_b128 v[184:187], v177 offset:50176
	ds_read_b128 v[188:191], v177 offset:51200
	ds_read_b128 v[192:195], v177 offset:52224
	ds_read_b128 v[196:199], v177 offset:53248
	ds_read_b128 v[200:203], v177 offset:54272
	ds_read_b128 v[204:207], v177 offset:55296
	ds_read_b128 v[208:211], v177 offset:56320
	global_load_lds_dwordx4 v[158:159], off
	v_lshl_add_u64 v[158:159], v[168:169], 0, s[6:7]
	s_mov_b32 m0, s51
	s_nop 0
	global_load_lds_dwordx4 v[158:159], off
	s_barrier
	s_waitcnt lgkmcnt(0)
	s_setprio 1
	s_waitcnt lgkmcnt(0)
	v_mfma_scale_f32_16x16x128_f8f6f4 v[76:79], v[0:7], v[180:187], v[76:79], v172, v172 op_sel_hi:[0,0,0]
	v_mfma_scale_f32_16x16x128_f8f6f4 v[72:75], v[8:15], v[180:187], v[72:75], v172, v172 op_sel_hi:[0,0,0]
	v_mfma_scale_f32_16x16x128_f8f6f4 v[64:67], v[0:7], v[188:195], v[64:67], v172, v172 op_sel_hi:[0,0,0]
	v_mfma_scale_f32_16x16x128_f8f6f4 v[56:59], v[8:15], v[188:195], v[56:59], v172, v172 op_sel_hi:[0,0,0]
	v_mfma_scale_f32_16x16x128_f8f6f4 v[48:51], v[0:7], v[196:203], v[48:51], v172, v172 op_sel_hi:[0,0,0]
	v_mfma_scale_f32_16x16x128_f8f6f4 v[40:43], v[8:15], v[196:203], v[40:43], v172, v172 op_sel_hi:[0,0,0]
	v_mfma_scale_f32_16x16x128_f8f6f4 v[32:35], v[0:7], v[204:211], v[32:35], v172, v172 op_sel_hi:[0,0,0]
	v_mfma_scale_f32_16x16x128_f8f6f4 v[24:27], v[8:15], v[204:211], v[24:27], v172, v172 op_sel_hi:[0,0,0]
	s_setprio 0
	s_barrier
	s_add_u32 s20, s20, 0x40080
	s_addc_u32 s21, s21, 0
	s_add_i32 s22, s22, s43
	v_lshl_add_u64 v[0:1], s[20:21], 0, v[146:147]
	s_mov_b32 m0, s22
	s_nop 0
	global_load_lds_dwordx4 v[0:1], off
	v_lshl_add_u64 v[0:1], s[20:21], 0, v[150:151]
	s_add_i32 m0, s22, 0x2000
	s_nop 0
	global_load_lds_dwordx4 v[0:1], off
	s_waitcnt vmcnt(6)
	s_barrier
	s_setprio 1
	v_mfma_scale_f32_16x16x128_f8f6f4 v[68:71], v[212:219], v[180:187], v[68:71], v172, v172 op_sel_hi:[0,0,0]
	v_mfma_scale_f32_16x16x128_f8f6f4 v[60:63], v[224:231], v[180:187], v[60:63], v172, v172 op_sel_hi:[0,0,0]
	v_mfma_scale_f32_16x16x128_f8f6f4 v[52:55], v[212:219], v[188:195], v[52:55], v172, v172 op_sel_hi:[0,0,0]
	v_mfma_scale_f32_16x16x128_f8f6f4 v[44:47], v[224:231], v[188:195], v[44:47], v172, v172 op_sel_hi:[0,0,0]
	v_mfma_scale_f32_16x16x128_f8f6f4 v[36:39], v[212:219], v[196:203], v[36:39], v172, v172 op_sel_hi:[0,0,0]
	v_mfma_scale_f32_16x16x128_f8f6f4 v[28:31], v[224:231], v[196:203], v[28:31], v172, v172 op_sel_hi:[0,0,0]
	v_mfma_scale_f32_16x16x128_f8f6f4 v[20:23], v[212:219], v[204:211], v[20:23], v172, v172 op_sel_hi:[0,0,0]
	v_mfma_scale_f32_16x16x128_f8f6f4 v[16:19], v[224:231], v[204:211], v[16:19], v172, v172 op_sel_hi:[0,0,0]
	s_setprio 0
	s_add_i32 s67, s67, 2
	s_add_u32 s65, s65, 0x100
	s_addc_u32 s66, s66, 0
	s_add_u32 s18, s18, 0x100
	s_addc_u32 s19, s19, 0
	s_cmp_gt_u32 s67, 13
	s_barrier
	s_cbranch_scc0 .LBB0_985
	s_lshl_b32 s18, s60, 8
	s_min_i32 s19, s60, 32
	s_ashr_i32 s22, s19, 4
	s_add_i32 s19, s18, 0xffffe000
	s_cmp_lt_i32 s60, 32
	s_cselect_b32 s20, s18, s19
	s_mul_i32 s22, s22, 6
	s_cselect_b32 s60, s28, s30
	s_cselect_b32 s61, s27, s29
	s_ashr_i32 s21, s20, 31
	s_ashr_i32 s19, s18, 31
	s_ashr_i32 s23, s22, 31
	s_lshl_b64 s[20:21], s[20:21], 13
	s_lshl_b64 s[18:19], s[18:19], 12
	s_lshl_b64 s[22:23], s[22:23], 13
	v_lshl_or_b32 v8, s59, 8, v175
	s_add_u32 s22, s4, s22
	s_addc_u32 s23, s5, s23
	v_ashrrev_i32_e32 v9, 31, v8
	v_lshl_add_u64 v[0:1], v[8:9], 2, s[22:23]
	v_lshl_add_u64 v[10:11], v[0:1], 0, s[8:9]
	v_add_co_u32_e32 v0, vcc, s49, v0
	s_add_u32 s20, s61, s20
	s_nop 7
	s_nop 7
	s_nop 7
	s_nop 0
	v_addc_co_u32_e32 v1, vcc, 0, v1, vcc
	s_addc_u32 s21, s60, s21
	v_add_u32_e32 v152, v174, v8
	global_load_dwordx4 v[0:3], v[0:1], off
	s_nop 0
	global_load_dwordx4 v[164:167], v[10:11], off offset:528
	global_load_dwordx4 v[4:7], v[10:11], off offset:16
	global_load_dwordx4 v[180:183], v[10:11], off offset:512
	v_mov_b32_e32 v169, v153
	v_lshl_add_u64 v[8:9], v[152:153], 2, s[20:21]
	v_add_u32_e32 v168, 0x80, v152
	global_load_dwordx4 v[184:187], v[8:9], off
	global_load_dwordx4 v[188:191], v[8:9], off offset:16
	v_lshl_add_u64 v[8:9], v[168:169], 2, s[20:21]
	global_load_dwordx4 v[192:195], v[8:9], off
	global_load_dwordx4 v[196:199], v[8:9], off offset:16
	v_add_u32_e32 v220, 0x8000, v152
	v_mov_b32_e32 v221, v153
	v_lshl_add_u64 v[8:9], v[220:221], 2, s[20:21]
	v_add_u32_e32 v252, 0x8080, v152
	v_mov_b32_e32 v253, v153
	global_load_dwordx4 v[200:203], v[8:9], off
	global_load_dwordx4 v[204:207], v[8:9], off offset:16
	v_lshl_add_u64 v[8:9], v[252:253], 2, s[20:21]
	global_load_dwordx4 v[208:211], v[8:9], off
	global_load_dwordx4 v[212:215], v[8:9], off offset:16
	v_mov_b32_e32 v223, v153
	v_add_u32_e32 v222, 0x10000, v152
	v_lshl_add_u64 v[8:9], v[222:223], 2, s[20:21]
	v_mov_b32_e32 v171, v153
	v_add_u32_e32 v170, 0x10080, v152
	global_load_dwordx4 v[216:219], v[8:9], off
	global_load_dwordx4 v[224:227], v[8:9], off offset:16
	v_lshl_add_u64 v[8:9], v[170:171], 2, s[20:21]
	v_mov_b32_e32 v159, v153
	v_add_u32_e32 v158, 0x18000, v152
	global_load_dwordx4 v[228:231], v[8:9], off
	global_load_dwordx4 v[232:235], v[8:9], off offset:16
	v_lshl_add_u64 v[8:9], v[158:159], 2, s[20:21]
	v_mov_b32_e32 v163, v153
	v_add_u32_e32 v162, 0x18080, v152
	global_load_dwordx4 v[236:239], v[8:9], off
	global_load_dwordx4 v[240:243], v[8:9], off offset:16
	v_lshl_add_u64 v[8:9], v[162:163], 2, s[20:21]
	global_load_dwordx4 v[244:247], v[8:9], off offset:16
	global_load_dwordx4 v[248:251], v[8:9], off
	s_add_u32 s18, s2, s18
	s_addc_u32 s19, s3, s19
	v_lshl_add_u64 v[160:161], v[152:153], 1, s[18:19]
	s_and_b64 vcc, exec, s[0:1]
	s_mov_b32 s59, s55
	s_mov_b32 s60, s56
	s_waitcnt vmcnt(0)
	v_pk_mul_f32 v[14:15], v[0:1], s[10:11] op_sel_hi:[1,0]
	v_pk_mul_f32 v[12:13], v[2:3], s[10:11] op_sel_hi:[1,0]
	v_pk_mul_f32 v[8:9], v[6:7], s[10:11] op_sel_hi:[1,0]
	v_pk_mul_f32 v[10:11], v[4:5], s[10:11] op_sel_hi:[1,0]
	v_pk_mul_f32 v[6:7], v[180:181], s[10:11] op_sel_hi:[1,0]
	v_pk_mul_f32 v[4:5], v[182:183], s[10:11] op_sel_hi:[1,0]
	v_pk_mul_f32 v[0:1], v[166:167], s[10:11] op_sel_hi:[1,0]
	v_pk_mul_f32 v[2:3], v[164:165], s[10:11] op_sel_hi:[1,0]
	v_pk_fma_f32 v[140:141], v[140:141], v[14:15], v[184:185]
	v_pk_fma_f32 v[164:165], v[138:139], v[8:9], v[190:191]
	v_pk_fma_f32 v[138:139], v[136:137], v[10:11], v[188:189]
	v_pk_fma_f32 v[132:133], v[132:133], v[6:7], v[192:193]
	v_pk_fma_f32 v[142:143], v[142:143], v[12:13], v[186:187]
	v_cvt_pk_bf16_f32 v136, v140, v141
	v_pk_fma_f32 v[134:135], v[134:135], v[4:5], v[194:195]
	v_cvt_pk_bf16_f32 v137, v142, v143
	v_cvt_pk_bf16_f32 v138, v138, v139
	v_cvt_pk_bf16_f32 v139, v164, v165
	v_pk_fma_f32 v[140:141], v[126:127], v[0:1], v[198:199]
	global_store_dwordx4 v[160:161], v[136:139], off
	v_pk_fma_f32 v[126:127], v[124:125], v[2:3], v[196:197]
	v_cvt_pk_bf16_f32 v124, v132, v133
	v_cvt_pk_bf16_f32 v125, v134, v135
	v_lshl_add_u64 v[132:133], v[168:169], 1, s[18:19]
	v_cvt_pk_bf16_f32 v126, v126, v127
	v_cvt_pk_bf16_f32 v127, v140, v141
	global_store_dwordx4 v[132:133], v[124:127], off
	v_pk_fma_f32 v[116:117], v[116:117], v[6:7], v[208:209]
	v_pk_fma_f32 v[118:119], v[118:119], v[4:5], v[210:211]
	v_pk_fma_f32 v[124:125], v[130:131], v[12:13], v[202:203]
	v_pk_fma_f32 v[126:127], v[128:129], v[14:15], v[200:201]
	v_pk_fma_f32 v[128:129], v[122:123], v[8:9], v[206:207]
	v_pk_fma_f32 v[122:123], v[120:121], v[10:11], v[204:205]
	v_cvt_pk_bf16_f32 v120, v126, v127
	v_cvt_pk_bf16_f32 v121, v124, v125
	v_lshl_add_u64 v[124:125], v[220:221], 1, s[18:19]
	v_cvt_pk_bf16_f32 v122, v122, v123
	v_cvt_pk_bf16_f32 v123, v128, v129
	global_store_dwordx4 v[124:125], v[120:123], off
	v_pk_fma_f32 v[100:101], v[100:101], v[6:7], v[228:229]
	v_pk_fma_f32 v[102:103], v[102:103], v[4:5], v[230:231]
	v_pk_fma_f32 v[120:121], v[110:111], v[0:1], v[214:215]
	v_pk_fma_f32 v[110:111], v[108:109], v[2:3], v[212:213]
	v_cvt_pk_bf16_f32 v108, v116, v117
	v_cvt_pk_bf16_f32 v109, v118, v119
	v_lshl_add_u64 v[116:117], v[252:253], 1, s[18:19]
	v_cvt_pk_bf16_f32 v110, v110, v111
	v_cvt_pk_bf16_f32 v111, v120, v121
	global_store_dwordx4 v[116:117], v[108:111], off
	v_pk_fma_f32 v[84:85], v[84:85], v[6:7], v[248:249]
	v_pk_fma_f32 v[86:87], v[86:87], v[4:5], v[250:251]
	v_pk_fma_f32 v[108:109], v[114:115], v[12:13], v[218:219]
	v_pk_fma_f32 v[110:111], v[112:113], v[14:15], v[216:217]
	v_pk_fma_f32 v[112:113], v[106:107], v[8:9], v[226:227]
	v_pk_fma_f32 v[106:107], v[104:105], v[10:11], v[224:225]
	v_cvt_pk_bf16_f32 v104, v110, v111
	v_cvt_pk_bf16_f32 v105, v108, v109
	v_lshl_add_u64 v[108:109], v[222:223], 1, s[18:19]
	v_cvt_pk_bf16_f32 v106, v106, v107
	v_cvt_pk_bf16_f32 v107, v112, v113
	global_store_dwordx4 v[108:109], v[104:107], off
	v_add_u32_e32 v160, 0x40080, v152
	v_mov_b32_e32 v161, v153
	v_pk_fma_f32 v[104:105], v[94:95], v[0:1], v[234:235]
	v_pk_fma_f32 v[94:95], v[92:93], v[2:3], v[232:233]
	v_cvt_pk_bf16_f32 v92, v100, v101
	v_cvt_pk_bf16_f32 v93, v102, v103
	v_lshl_add_u64 v[100:101], v[170:171], 1, s[18:19]
	v_cvt_pk_bf16_f32 v94, v94, v95
	v_cvt_pk_bf16_f32 v95, v104, v105
	global_store_dwordx4 v[100:101], v[92:95], off
	v_add_u32_e32 v164, 0x48080, v152
	v_mov_b32_e32 v165, v153
	v_pk_fma_f32 v[92:93], v[98:99], v[12:13], v[238:239]
	v_pk_fma_f32 v[94:95], v[96:97], v[14:15], v[236:237]
	v_pk_fma_f32 v[96:97], v[90:91], v[8:9], v[242:243]
	v_pk_fma_f32 v[90:91], v[88:89], v[10:11], v[240:241]
	v_cvt_pk_bf16_f32 v88, v94, v95
	v_cvt_pk_bf16_f32 v89, v92, v93
	v_lshl_add_u64 v[92:93], v[158:159], 1, s[18:19]
	v_cvt_pk_bf16_f32 v90, v90, v91
	v_cvt_pk_bf16_f32 v91, v96, v97
	global_store_dwordx4 v[92:93], v[88:91], off
	v_add_u32_e32 v158, 0x40000, v152
	v_lshl_add_u64 v[92:93], v[160:161], 2, s[20:21]
	v_pk_fma_f32 v[88:89], v[82:83], v[0:1], v[246:247]
	v_pk_fma_f32 v[82:83], v[80:81], v[2:3], v[244:245]
	v_cvt_pk_bf16_f32 v80, v84, v85
	v_lshl_add_u64 v[84:85], v[162:163], 1, s[18:19]
	v_cvt_pk_bf16_f32 v81, v86, v87
	v_cvt_pk_bf16_f32 v82, v82, v83
	v_cvt_pk_bf16_f32 v83, v88, v89
	global_store_dwordx4 v[84:85], v[80:83], off
	v_lshl_add_u64 v[84:85], v[158:159], 2, s[20:21]
	global_load_dwordx4 v[80:83], v[84:85], off
	s_nop 0
	global_load_dwordx4 v[84:87], v[84:85], off offset:16
	s_nop 0
	global_load_dwordx4 v[88:91], v[92:93], off
	s_nop 0
	global_load_dwordx4 v[92:95], v[92:93], off offset:16
	v_add_u32_e32 v162, 0x48000, v152
	v_lshl_add_u64 v[100:101], v[162:163], 2, s[20:21]
	global_load_dwordx4 v[96:99], v[100:101], off
	s_nop 0
	global_load_dwordx4 v[100:103], v[100:101], off offset:16
	v_lshl_add_u64 v[108:109], v[164:165], 2, s[20:21]
	global_load_dwordx4 v[104:107], v[108:109], off
	s_nop 0
	global_load_dwordx4 v[108:111], v[108:109], off offset:16
	v_add_u32_e32 v166, 0x50000, v152
	v_mov_b32_e32 v167, v153
	v_lshl_add_u64 v[116:117], v[166:167], 2, s[20:21]
	v_add_u32_e32 v168, 0x50080, v152
	global_load_dwordx4 v[112:115], v[116:117], off
	s_nop 0
	global_load_dwordx4 v[116:119], v[116:117], off offset:16
	v_lshl_add_u64 v[124:125], v[168:169], 2, s[20:21]
	v_add_u32_e32 v170, 0x58000, v152
	global_load_dwordx4 v[120:123], v[124:125], off
	s_nop 0
	global_load_dwordx4 v[124:127], v[124:125], off offset:16
	v_lshl_add_u64 v[132:133], v[170:171], 2, s[20:21]
	v_add_u32_e32 v152, 0x58080, v152
	global_load_dwordx4 v[128:131], v[132:133], off
	s_nop 0
	global_load_dwordx4 v[132:135], v[132:133], off offset:16
	v_lshl_add_u64 v[140:141], v[152:153], 2, s[20:21]
	global_load_dwordx4 v[136:139], v[140:141], off
	s_nop 0
	global_load_dwordx4 v[140:143], v[140:141], off offset:16
	s_mov_b64 s[20:21], s[12:13]
	s_waitcnt vmcnt(0)
	v_pk_fma_f32 v[76:77], v[76:77], v[14:15], v[80:81]
	v_pk_fma_f32 v[78:79], v[78:79], v[12:13], v[82:83]
	v_pk_fma_f32 v[80:81], v[74:75], v[8:9], v[86:87]
	v_pk_fma_f32 v[74:75], v[72:73], v[10:11], v[84:85]
	v_cvt_pk_bf16_f32 v72, v76, v77
	v_cvt_pk_bf16_f32 v73, v78, v79
	v_lshl_add_u64 v[76:77], v[158:159], 1, s[18:19]
	v_pk_fma_f32 v[68:69], v[68:69], v[6:7], v[88:89]
	v_cvt_pk_bf16_f32 v74, v74, v75
	v_cvt_pk_bf16_f32 v75, v80, v81
	global_store_dwordx4 v[76:77], v[72:75], off
	v_pk_fma_f32 v[70:71], v[70:71], v[4:5], v[90:91]
	v_pk_fma_f32 v[52:53], v[52:53], v[6:7], v[104:105]
	v_pk_fma_f32 v[72:73], v[62:63], v[0:1], v[94:95]
	v_pk_fma_f32 v[62:63], v[60:61], v[2:3], v[92:93]
	v_cvt_pk_bf16_f32 v60, v68, v69
	v_cvt_pk_bf16_f32 v61, v70, v71
	v_lshl_add_u64 v[68:69], v[160:161], 1, s[18:19]
	v_cvt_pk_bf16_f32 v62, v62, v63
	v_cvt_pk_bf16_f32 v63, v72, v73
	global_store_dwordx4 v[68:69], v[60:63], off
	v_pk_fma_f32 v[54:55], v[54:55], v[4:5], v[106:107]
	v_pk_fma_f32 v[36:37], v[36:37], v[6:7], v[120:121]
	v_pk_fma_f32 v[60:61], v[66:67], v[12:13], v[98:99]
	v_pk_fma_f32 v[62:63], v[64:65], v[14:15], v[96:97]
	v_pk_fma_f32 v[64:65], v[58:59], v[8:9], v[102:103]
	v_pk_fma_f32 v[58:59], v[56:57], v[10:11], v[100:101]
	v_cvt_pk_bf16_f32 v56, v62, v63
	v_cvt_pk_bf16_f32 v57, v60, v61
	v_lshl_add_u64 v[60:61], v[162:163], 1, s[18:19]
	v_cvt_pk_bf16_f32 v58, v58, v59
	v_cvt_pk_bf16_f32 v59, v64, v65
	global_store_dwordx4 v[60:61], v[56:59], off
	v_pk_fma_f32 v[38:39], v[38:39], v[4:5], v[122:123]
	v_pk_fma_f32 v[26:27], v[26:27], v[8:9], v[134:135]
	v_pk_fma_f32 v[56:57], v[46:47], v[0:1], v[110:111]
	v_pk_fma_f32 v[46:47], v[44:45], v[2:3], v[108:109]
	v_cvt_pk_bf16_f32 v44, v52, v53
	v_cvt_pk_bf16_f32 v45, v54, v55
	v_lshl_add_u64 v[52:53], v[164:165], 1, s[18:19]
	v_cvt_pk_bf16_f32 v46, v46, v47
	v_cvt_pk_bf16_f32 v47, v56, v57
	global_store_dwordx4 v[52:53], v[44:47], off
	v_pk_fma_f32 v[4:5], v[22:23], v[4:5], v[138:139]
	v_pk_fma_f32 v[6:7], v[20:21], v[6:7], v[136:137]
	v_pk_fma_f32 v[44:45], v[50:51], v[12:13], v[114:115]
	v_pk_fma_f32 v[46:47], v[48:49], v[14:15], v[112:113]
	v_pk_fma_f32 v[48:49], v[42:43], v[8:9], v[118:119]
	v_pk_fma_f32 v[42:43], v[40:41], v[10:11], v[116:117]
	v_cvt_pk_bf16_f32 v40, v46, v47
	v_cvt_pk_bf16_f32 v41, v44, v45
	v_lshl_add_u64 v[44:45], v[166:167], 1, s[18:19]
	v_cvt_pk_bf16_f32 v42, v42, v43
	v_cvt_pk_bf16_f32 v43, v48, v49
	global_store_dwordx4 v[44:45], v[40:43], off
	v_pk_fma_f32 v[12:13], v[34:35], v[12:13], v[130:131]
	v_pk_fma_f32 v[14:15], v[32:33], v[14:15], v[128:129]
	v_pk_fma_f32 v[40:41], v[30:31], v[0:1], v[126:127]
	v_pk_fma_f32 v[30:31], v[28:29], v[2:3], v[124:125]
	v_cvt_pk_bf16_f32 v28, v36, v37
	v_lshl_add_u64 v[36:37], v[168:169], 1, s[18:19]
	v_cvt_pk_bf16_f32 v29, v38, v39
	v_cvt_pk_bf16_f32 v30, v30, v31
	v_cvt_pk_bf16_f32 v31, v40, v41
	global_store_dwordx4 v[36:37], v[28:31], off
	v_pk_fma_f32 v[10:11], v[24:25], v[10:11], v[132:133]
	v_cvt_pk_bf16_f32 v8, v14, v15
	v_cvt_pk_bf16_f32 v9, v12, v13
	v_lshl_add_u64 v[12:13], v[170:171], 1, s[18:19]
	v_cvt_pk_bf16_f32 v10, v10, v11
	v_cvt_pk_bf16_f32 v11, v26, v27
	global_store_dwordx4 v[12:13], v[8:11], off
	v_pk_fma_f32 v[2:3], v[16:17], v[2:3], v[140:141]
	s_nop 0
	v_pk_fma_f32 v[8:9], v[18:19], v[0:1], v[142:143]
	v_cvt_pk_bf16_f32 v0, v6, v7
	v_cvt_pk_bf16_f32 v1, v4, v5
	v_lshl_add_u64 v[4:5], v[152:153], 1, s[18:19]
	v_cvt_pk_bf16_f32 v2, v2, v3
	v_cvt_pk_bf16_f32 v3, v8, v9
	global_store_dwordx4 v[4:5], v[0:3], off
	s_mov_b64 s[18:19], s[16:17]
	s_cbranch_vccz .LBB0_978
	s_waitcnt vmcnt(0)
	s_cmpk_lt_u32 s31, 0x100
	s_cbranch_scc1 .LBB0_989
	s_barrier

.LBB0_1198:
	s_cmp_gt_i32 s36, 12
	s_cselect_b64 s[0:1], -1, 0
	s_cmp_lt_i32 s37, 13
	s_cselect_b64 s[2:3], -1, 0
	s_or_b64 s[0:1], s[0:1], s[2:3]
	s_and_b64 vcc, exec, s[0:1]
	s_cbranch_vccnz .LBB0_1342
	s_and_b32 s0, s81, 0xffffffc0
	v_mbcnt_hi_u32_b32 v186, -1, v253
	v_add_u32_e32 v187, s0, v186
	s_mov_b32 s23, s15
	s_mov_b64 s[4:5], s[34:35]
	s_mov_b32 s6, s14
	v_mov_b32_e32 v0, 0x4000
	global_load_dword v0, v0, s[4:5] offset:1536
	v_readfirstlane_b32 s42, v187
	s_add_u32 s40, s4, 0x7458000
	s_addc_u32 s41, s5, 0
	s_and_b32 s0, s42, 0xffffffc0
	s_waitcnt vmcnt(0) lgkmcnt(0)
	v_add_u32_e32 v4, s0, v186
	s_ashr_i32 s7, s6, 31
	s_mov_b32 s2, 0
	v_mov_b32_e32 v188, 0x7f7f7f7f
	v_readfirstlane_b32 s0, v0
	s_ashr_i32 s1, s0, 31
	s_lshl_b64 s[0:1], s[0:1], 2
	v_mov_b64_e32 v[0:1], s[6:7]
	v_cmp_le_i64_e32 vcc, s[0:1], v[0:1]
	v_readfirstlane_b32 s43, v4
	s_cbranch_vccnz .LBB0_1215
	s_add_u32 s44, s4, 0x4400
	s_addc_u32 s45, s5, 0
	s_add_u32 s46, s4, 0x3bf0c000
	s_addc_u32 s47, s5, 0
	s_add_u32 s48, s4, 0x4000
	s_addc_u32 s49, s5, 0
	s_add_u32 s8, s4, 0x3280c000
	s_addc_u32 s9, s5, 0
	s_ashr_i32 s16, s43, 6
	s_ashr_i32 s20, s43, 8
	s_lshl_b32 s50, s16, 10
	s_ashr_i64 s[28:29], s[6:7], 2
	s_and_b32 s66, s6, 3
	s_and_b32 s3, s6, -4
	s_add_u32 s10, s44, s3
	s_addc_u32 s11, s45, s7
	v_mov_b32_e32 v161, 0
	global_load_dword v0, v161, s[10:11]
	s_lshl_b32 s11, s66, 19
	s_add_i32 s3, s28, 0xa0
	s_ashr_i64 s[2:3], s[2:3], 30
	v_lshlrev_b32_e32 v2, 4, v4
	v_ashrrev_i32_e32 v3, 31, v4
	v_bfe_i32 v5, v4, 27, 1
	v_lshrrev_b32_e32 v3, 26, v3
	v_lshrrev_b32_e32 v5, 22, v5
	v_add_u32_e32 v6, 0x2000, v2
	v_add_u32_e32 v3, v4, v3
	v_add_u32_e32 v5, v2, v5
	v_ashrrev_i32_e32 v7, 31, v6
	v_ashrrev_i32_e32 v10, 6, v3
	v_and_b32_e32 v3, 0xfffffc00, v5
	v_lshrrev_b32_e32 v5, 22, v7
	v_sub_u32_e32 v2, v2, v3
	v_add_u32_e32 v5, v6, v5
	v_lshrrev_b32_e32 v7, 4, v2
	v_ashrrev_i32_e32 v5, 10, v5
	v_bitop3_b32 v11, v7, v2, 32 bitop3:0x6c
	v_mul_i32_i24_e32 v2, 0x400, v5
	v_lshlrev_b32_e32 v7, 3, v5
	v_ashrrev_i32_e32 v8, 31, v11
	v_sub_u32_e32 v2, v6, v2
	v_and_b32_e32 v6, -16, v7
	v_lshrrev_b32_e32 v7, 26, v8
	v_lshrrev_b32_e32 v8, 4, v2
	v_bitop3_b32 v13, v8, v2, 32 bitop3:0x6c
	v_ashrrev_i32_e32 v2, 31, v13
	v_lshlrev_b32_e32 v3, 3, v10
	v_add_u32_e32 v12, v11, v7
	v_lshrrev_b32_e32 v2, 26, v2
	v_and_b32_e32 v3, -16, v3
	v_ashrrev_i32_e32 v14, 6, v12
	v_add_u32_e32 v15, v13, v2
	v_add_u32_e32 v189, v14, v3
	v_ashrrev_i32_e32 v16, 6, v15
	v_add_u32_e32 v190, v16, v6
	v_mov_b32_e32 v163, v161
	v_mov_b32_e32 v165, v161
	s_mov_b32 s54, 0x10000
	s_mov_b32 s55, 0x12000
	v_mov_b32_e32 v173, v161
	s_mov_b32 s56, 0x14000
	s_waitcnt vmcnt(0)
	v_readfirstlane_b32 s10, v0
	s_lshl_b32 s12, s10, 21
	s_or_b32 s12, s12, s11
	s_add_u32 s2, s44, s2
	s_addc_u32 s3, s45, s3
	s_ashr_i32 s11, s10, 31
	global_load_dword v0, v161, s[2:3]
	s_lshl_b64 s[2:3], s[10:11], 2
	s_add_u32 s2, s48, s2
	s_addc_u32 s3, s49, s3
	global_load_dword v1, v161, s[2:3]
	s_mul_i32 s2, s10, 0x8800
	s_mul_hi_i32 s3, s10, 0x8800
	s_waitcnt vmcnt(1)
	v_readfirstlane_b32 s21, v0
	s_lshl_b32 s11, s21, 8
	s_add_u32 s2, s46, s2
	v_add_u32_e32 v0, s11, v189
	s_waitcnt vmcnt(0)
	v_readfirstlane_b32 s25, v1
	v_add_u32_e32 v2, s11, v190
	s_addc_u32 s3, s47, s3
	s_bitset1_b32 s11, 7
	v_cmp_gt_i32_e32 vcc, s25, v0
	v_add_u32_e32 v6, s11, v189
	v_add_u32_e32 v7, s11, v190
	v_cndmask_b32_e32 v0, 0, v0, vcc
	v_cmp_gt_i32_e32 vcc, s25, v2
	v_ashrrev_i32_e32 v1, 31, v0
	v_lshl_add_u64 v[0:1], v[0:1], 2, s[2:3]
	v_cndmask_b32_e32 v2, 0, v2, vcc
	v_cmp_gt_i32_e32 vcc, s25, v6
	v_ashrrev_i32_e32 v3, 31, v2
	v_lshl_add_u64 v[2:3], v[2:3], 2, s[2:3]
	v_cndmask_b32_e32 v6, 0, v6, vcc
	v_cmp_gt_i32_e32 vcc, s25, v7
	s_add_u32 s30, s40, s12
	s_addc_u32 s31, s41, 0
	v_cndmask_b32_e32 v8, 0, v7, vcc
	v_ashrrev_i32_e32 v7, 31, v6
	v_ashrrev_i32_e32 v9, 31, v8
	v_lshl_add_u64 v[6:7], v[6:7], 2, s[2:3]
	v_lshl_add_u64 v[8:9], v[8:9], 2, s[2:3]
	global_load_dword v17, v[0:1], off
	global_load_dword v18, v[2:3], off
	global_load_dword v19, v[6:7], off
	global_load_dword v20, v[8:9], off
	v_and_b32_e32 v3, 0xc0, v12
	v_mov_b32_e32 v0, 1
	v_sub_u32_e32 v3, v11, v3
	v_lshlrev_b32_e32 v1, 5, v10
	v_ashrrev_i16_sdwa v3, v0, sext(v3) dst_sel:DWORD dst_unused:UNUSED_PAD src0_sel:DWORD src1_sel:BYTE_0
	s_mov_b32 s2, 0x1fffe0
	v_and_b32_e32 v1, 32, v1
	v_lshlrev_b32_e32 v2, 5, v5
	v_and_b32_e32 v5, 3, v14
	v_lshrrev_b32_e32 v6, 2, v189
	v_lshlrev_b32_e32 v7, 1, v189
	v_bfe_i32 v3, v3, 0, 16
	v_and_b32_e32 v8, 0xc0, v15
	v_and_or_b32 v5, v189, s2, v5
	v_and_b32_e32 v6, 4, v6
	v_and_b32_e32 v7, 24, v7
	v_add_lshl_u32 v191, v1, v3, 1
	v_sub_u32_e32 v1, v13, v8
	v_and_b32_e32 v3, 3, v16
	v_or3_b32 v5, v5, v6, v7
	v_ashrrev_i16_sdwa v0, v0, sext(v1) dst_sel:DWORD dst_unused:UNUSED_PAD src0_sel:DWORD src1_sel:BYTE_0
	v_and_or_b32 v1, v190, s2, v3
	v_lshrrev_b32_e32 v3, 2, v190
	v_lshlrev_b32_e32 v6, 1, v190
	v_and_b32_e32 v2, 32, v2
	v_lshl_add_u32 v162, v5, 11, v191
	v_bfe_i32 v0, v0, 0, 16
	v_and_b32_e32 v3, 4, v3
	v_and_b32_e32 v5, 24, v6
	s_add_i32 s29, s50, 0
	v_add_lshl_u32 v192, v2, v0, 1
	v_or3_b32 v0, v1, v3, v5
	s_add_i32 m0, s29, 0x10000
	v_lshl_add_u32 v164, v0, 11, v192
	global_load_lds_dwordx4 v162, s[30:31]
	s_add_i32 m0, s29, 0x12000
	s_add_i32 s51, s29, 0x2000
	global_load_lds_dwordx4 v164, s[30:31]
	s_mov_b32 m0, s29
	s_add_u32 s2, s30, 0x40000
	s_addc_u32 s3, s31, 0
	s_add_i32 s52, s29, 0x4000
	s_add_i32 s53, s29, 0x6000
	v_lshl_add_u64 v[2:3], s[30:31], 0, v[162:163]
	v_lshl_add_u64 v[0:1], s[30:31], 0, v[164:165]
	s_waitcnt vmcnt(0)
	v_lshl_add_u32 v160, v17, 11, v191
	v_lshl_add_u32 v172, v18, 11, v192
	global_load_lds_dwordx4 v160, s[8:9]
	s_mov_b32 m0, s51
	v_lshl_add_u32 v170, v19, 11, v191
	global_load_lds_dwordx4 v172, s[8:9]
	s_add_i32 m0, s29, 0x14000
	v_lshl_add_u32 v168, v20, 11, v192
	global_load_lds_dwordx4 v162, s[2:3]
	s_add_i32 m0, s29, 0x16000
	s_cmp_lg_u32 s20, 0
	global_load_lds_dwordx4 v164, s[2:3]
	s_mov_b32 m0, s52
	s_nop 0
	global_load_lds_dwordx4 v170, s[8:9]
	s_mov_b32 m0, s53
	s_nop 0
	global_load_lds_dwordx4 v168, s[8:9]
	s_cbranch_scc1 .LBB0_1202
	s_barrier

.LBB0_1212:
	s_waitcnt vmcnt(0)
	s_cmpk_lt_u32 s43, 0x100
	s_cbranch_scc1 .LBB0_1214
	s_barrier

.LBB0_1342:
	s_cmp_gt_i32 s36, 13
	s_cselect_b64 s[0:1], -1, 0
	s_cmp_lt_i32 s37, 14
	s_cselect_b64 s[2:3], -1, 0
	s_or_b64 s[0:1], s[0:1], s[2:3]
	s_and_b64 vcc, exec, s[0:1]
	s_cbranch_vccnz .LBB0_1403
	s_and_b32 s0, s81, 0xffffffc0
	v_mbcnt_hi_u32_b32 v152, -1, v253
	v_add_u32_e32 v0, s0, v152
	s_mov_b64 s[2:3], s[34:35]
	s_mov_b32 s8, s14
	s_mov_b32 s19, s15
	v_mov_b32_e32 v1, 0x4000
	global_load_dword v1, v1, s[2:3] offset:1536
	v_readfirstlane_b32 s0, v0
	s_andn2_b32 s0, s0, 63
	s_ashr_i32 s9, s8, 31
	s_waitcnt vmcnt(0)
	v_add_u32_e32 v8, s0, v152
	v_mov_b32_e32 v153, 0x7f7f7f7f
	v_readfirstlane_b32 s0, v1
	s_ashr_i32 s1, s0, 31
	s_lshl_b64 s[0:1], s[0:1], 3
	v_mov_b64_e32 v[0:1], s[8:9]
	v_cmp_le_i64_e32 vcc, s[0:1], v[0:1]
	v_readfirstlane_b32 s40, v8
	s_cbranch_vccnz .LBB0_1353
	s_add_u32 s41, s2, 0x4400
	s_addc_u32 s42, s3, 0
	s_add_u32 s43, s2, 0x4241c000
	s_addc_u32 s44, s3, 0
	s_add_u32 s45, s2, 0x17458000
	s_addc_u32 s46, s3, 0
	s_ashr_i32 s5, s40, 6
	s_ashr_i64 s[26:27], s[8:9], 3
	s_ashr_i32 s4, s40, 8
	s_lshl_b32 s47, s5, 10
	s_and_b32 s68, s8, 7
	s_lshl_b64 s[6:7], s[26:27], 2
	s_add_u32 s6, s41, s6
	s_addc_u32 s7, s42, s7
	v_mov_b32_e32 v133, 0
	global_load_dword v0, v133, s[6:7]
	v_lshlrev_b32_e32 v1, 4, v8
	v_bfe_i32 v3, v8, 27, 1
	v_add_u32_e32 v5, 0x2000, v1
	v_lshrrev_b32_e32 v3, 22, v3
	v_ashrrev_i32_e32 v6, 31, v5
	v_add_u32_e32 v3, v1, v3
	v_lshrrev_b32_e32 v6, 22, v6
	v_and_b32_e32 v3, 0xfffffc00, v3
	v_add_u32_e32 v6, v5, v6
	v_sub_u32_e32 v1, v1, v3
	v_ashrrev_i32_e32 v6, 10, v6
	v_lshrrev_b32_e32 v7, 4, v1
	v_mul_i32_i24_e32 v9, 0x400, v6
	v_lshlrev_b32_e32 v10, 3, v6
	v_bitop3_b32 v1, v7, v1, 32 bitop3:0x6c
	v_sub_u32_e32 v5, v5, v9
	s_waitcnt lgkmcnt(0)
	v_ashrrev_i32_e32 v4, 31, v8
	v_and_b32_e32 v7, -16, v10
	v_ashrrev_i32_e32 v9, 31, v1
	v_lshrrev_b32_e32 v10, 4, v5
	v_lshrrev_b32_e32 v4, 26, v4
	v_lshrrev_b32_e32 v9, 26, v9
	v_bitop3_b32 v5, v10, v5, 32 bitop3:0x6c
	v_add_u32_e32 v4, v8, v4
	v_add_u32_e32 v9, v1, v9
	v_ashrrev_i32_e32 v10, 31, v5
	v_ashrrev_i32_e32 v4, 6, v4
	v_ashrrev_i32_e32 v11, 6, v9
	v_and_b32_e32 v9, 0xc0, v9
	v_lshrrev_b32_e32 v10, 26, v10
	v_mov_b32_e32 v2, 1
	v_lshlrev_b32_e32 v3, 3, v4
	v_sub_u32_e32 v1, v1, v9
	v_add_u32_e32 v9, v5, v10
	v_lshlrev_b32_e32 v4, 5, v4
	v_and_b32_e32 v3, -16, v3
	v_ashrrev_i16_sdwa v1, v2, sext(v1) dst_sel:DWORD dst_unused:UNUSED_PAD src0_sel:DWORD src1_sel:BYTE_0
	v_ashrrev_i32_e32 v13, 6, v9
	s_mov_b32 s6, 0x7fffe0
	v_and_b32_e32 v4, 32, v4
	v_add_u32_e32 v3, v11, v3
	v_and_b32_e32 v11, 3, v11
	v_bfe_i32 v1, v1, 0, 16
	v_add_u32_e32 v7, v13, v7
	v_and_b32_e32 v13, 3, v13
	v_and_or_b32 v10, v3, s6, v11
	v_add_lshl_u32 v1, v4, v1, 1
	v_and_or_b32 v4, v7, s6, v13
	s_lshl_b32 s10, s68, 17
	s_lshl_b32 s7, s26, 17
	v_lshrrev_b32_e32 v11, 2, v3
	v_lshlrev_b32_e32 v12, 1, v3
	v_and_b32_e32 v9, 0xc0, v9
	v_and_b32_e32 v11, 4, v11
	v_and_b32_e32 v12, 24, v12
	v_sub_u32_e32 v5, v5, v9
	v_lshlrev_b32_e32 v6, 5, v6
	v_or3_b32 v9, v10, v11, v12
	v_lshrrev_b32_e32 v10, 2, v7
	v_lshlrev_b32_e32 v11, 1, v7
	v_ashrrev_i16_sdwa v2, v2, sext(v5) dst_sel:DWORD dst_unused:UNUSED_PAD src0_sel:DWORD src1_sel:BYTE_0
	v_and_b32_e32 v6, 32, v6
	v_lshl_add_u32 v132, v9, 9, v1
	v_lshl_add_u32 v134, v3, 9, v1
	v_and_b32_e32 v1, 4, v10
	v_and_b32_e32 v3, 24, v11
	v_bfe_i32 v2, v2, 0, 16
	v_or3_b32 v1, v4, v1, v3
	v_add_lshl_u32 v2, v6, v2, 1
	v_lshl_add_u32 v136, v1, 9, v2
	v_lshl_add_u32 v138, v7, 9, v2
	v_mov_b32_e32 v137, v133
	v_mov_b32_e32 v135, v133
	v_mov_b32_e32 v139, v133
	s_mov_b32 s51, 0x10000
	s_waitcnt vmcnt(0)
	v_readfirstlane_b32 s6, v0
	s_lshl_b32 s6, s6, 20
	s_or_b32 s6, s6, s10
	s_add_u32 s38, s45, s6
	s_addc_u32 s39, s46, 0
	s_add_i32 s27, s47, 0
	s_add_i32 m0, s27, 0x10000
	v_lshl_add_u64 v[6:7], s[38:39], 0, v[132:133]
	global_load_lds_dwordx4 v132, s[38:39]
	s_add_i32 m0, s27, 0x12000
	s_add_u32 s30, s43, s7
	global_load_lds_dwordx4 v136, s[38:39]
	s_addc_u32 s31, s44, 0
	s_mov_b32 m0, s27
	s_add_i32 s48, s27, 0x2000
	global_load_lds_dwordx4 v134, s[30:31]
	s_mov_b32 m0, s48
	s_add_u32 s6, s38, 0x10000
	global_load_lds_dwordx4 v138, s[30:31]
	s_addc_u32 s7, s39, 0
	s_add_i32 m0, s27, 0x14000
	v_lshl_add_u64 v[4:5], s[38:39], 0, v[136:137]
	global_load_lds_dwordx4 v132, s[6:7]
	s_add_i32 m0, s27, 0x16000
	v_lshl_add_u64 v[2:3], s[30:31], 0, v[134:135]
	global_load_lds_dwordx4 v136, s[6:7]
	s_add_u32 s6, s30, 0x10000
	s_addc_u32 s7, s31, 0
	s_add_i32 s49, s27, 0x4000
	s_mov_b32 m0, s49
	s_add_i32 s50, s27, 0x6000
	global_load_lds_dwordx4 v134, s[6:7]
	s_mov_b32 m0, s50
	s_cmp_lg_u32 s4, 0
	global_load_lds_dwordx4 v138, s[6:7]
	v_lshl_add_u64 v[0:1], s[30:31], 0, v[138:139]
	s_cbranch_scc1 .LBB0_1346
	s_barrier

.LBB0_1350:
	s_waitcnt vmcnt(0)
	s_cmpk_lt_u32 s40, 0x100
	s_cbranch_scc1 .LBB0_1352
	s_barrier

.LBB0_1547:
	v_ashrrev_i32_e32 v1, 31, v8
	v_lshrrev_b32_e32 v1, 26, v1
	v_add_u32_e32 v1, v8, v1
	v_ashrrev_i32_e32 v9, 6, v1
	v_bfe_i32 v1, v8, 27, 1
	v_lshlrev_b32_e32 v0, 4, v8
	v_lshrrev_b32_e32 v1, 22, v1
	v_add_u32_e32 v1, v0, v1
	v_and_b32_e32 v1, 0xfffffc00, v1
	v_sub_u32_e32 v1, v0, v1
	s_waitcnt lgkmcnt(0)
	v_lshrrev_b32_e32 v2, 4, v1
	v_bitop3_b32 v1, v2, v1, 32 bitop3:0x6c
	v_ashrrev_i32_e32 v3, 31, v1
	v_lshrrev_b32_e32 v3, 26, v3
	v_add_u32_e32 v3, v1, v3
	v_lshlrev_b32_e32 v2, 3, v9
	v_ashrrev_i32_e32 v10, 6, v3
	v_and_b32_e32 v3, 0xc0, v3
	v_and_b32_e32 v2, -16, v2
	v_sub_u32_e32 v1, v1, v3
	v_mov_b32_e32 v3, 1
	v_add_u32_e32 v2, v10, v2
	v_ashrrev_i16_sdwa v1, v3, sext(v1) dst_sel:DWORD dst_unused:UNUSED_PAD src0_sel:DWORD src1_sel:BYTE_0
	v_lshlrev_b32_e32 v4, 5, v9
	v_bfe_i32 v11, v1, 0, 16
	v_lshlrev_b32_e32 v1, 1, v2
	v_lshrrev_b32_e32 v5, 2, v2
	v_and_b32_e32 v6, 3, v10
	s_mov_b32 s7, 0x1fffe0
	v_and_b32_e32 v4, 32, v4
	v_and_b32_e32 v1, 24, v1
	v_and_b32_e32 v5, 4, v5
	v_and_or_b32 v6, v2, s7, v6
	v_or3_b32 v1, v6, v5, v1
	v_add_lshl_u32 v4, v4, v11, 1
	v_add_u32_e32 v0, 0x2000, v0
	v_lshl_add_u32 v146, v1, 11, v4
	v_ashrrev_i32_e32 v1, 31, v0
	v_lshrrev_b32_e32 v1, 22, v1
	v_add_u32_e32 v1, v0, v1
	v_ashrrev_i32_e32 v12, 10, v1
	v_mul_i32_i24_e32 v1, 0x400, v12
	v_sub_u32_e32 v0, v0, v1
	v_lshrrev_b32_e32 v1, 4, v0
	v_bitop3_b32 v0, v1, v0, 32 bitop3:0x6c
	s_add_u32 s28, s2, 0x3280c000
	v_lshl_add_u32 v144, v2, 11, v4
	v_ashrrev_i32_e32 v2, 31, v0
	s_addc_u32 s29, s3, 0
	v_lshrrev_b32_e32 v2, 26, v2
	s_add_u32 s30, s2, 0x34b8c000
	v_add_u32_e32 v2, v0, v2
	s_addc_u32 s31, s3, 0
	s_ashr_i32 s6, s27, 6
	v_lshlrev_b32_e32 v1, 3, v12
	v_ashrrev_i32_e32 v13, 6, v2
	v_and_b32_e32 v2, 0xc0, v2
	v_and_b32_e32 v1, -16, v1
	v_sub_u32_e32 v0, v0, v2
	s_ashr_i32 s16, s27, 8
	s_lshl_b32 s38, s6, 10
	v_add_u32_e32 v1, v13, v1
	v_ashrrev_i16_sdwa v0, v3, sext(v0) dst_sel:DWORD dst_unused:UNUSED_PAD src0_sel:DWORD src1_sel:BYTE_0
	s_add_u32 s4, s30, s4
	v_lshlrev_b32_e32 v4, 5, v12
	v_bfe_i32 v14, v0, 0, 16
	v_lshlrev_b32_e32 v0, 1, v1
	v_lshrrev_b32_e32 v2, 2, v1
	v_and_b32_e32 v3, 3, v13
	s_addc_u32 s5, s31, s5
	s_add_i32 s39, s38, 0
	v_and_b32_e32 v4, 32, v4
	v_and_b32_e32 v0, 24, v0
	v_and_b32_e32 v2, 4, v2
	v_and_or_b32 v3, v1, s7, v3
	s_add_i32 m0, s39, 0x10000
	v_or3_b32 v0, v3, v2, v0
	v_add_lshl_u32 v2, v4, v14, 1
	global_load_lds_dwordx4 v146, s[4:5]
	s_add_i32 m0, s39, 0x12000
	v_lshl_add_u32 v150, v0, 11, v2
	s_add_u32 s22, s28, s0
	global_load_lds_dwordx4 v150, s[4:5]
	s_addc_u32 s23, s29, s1
	s_mov_b32 m0, s39
	s_add_i32 s40, s39, 0x2000
	v_lshl_add_u32 v148, v1, 11, v2
	global_load_lds_dwordx4 v144, s[22:23]
	s_mov_b32 m0, s40
	s_add_u32 s0, s4, 0x40000
	global_load_lds_dwordx4 v148, s[22:23]
	s_addc_u32 s1, s5, 0
	s_add_i32 m0, s39, 0x14000
	v_mov_b32_e32 v153, 0
	global_load_lds_dwordx4 v146, s[0:1]
	s_add_i32 m0, s39, 0x16000
	v_mov_b32_e32 v147, v153
	global_load_lds_dwordx4 v150, s[0:1]
	s_add_u32 s0, s22, 0x40000
	s_addc_u32 s1, s23, 0
	s_add_i32 s41, s39, 0x4000
	s_mov_b32 m0, s41
	s_add_i32 s42, s39, 0x6000
	global_load_lds_dwordx4 v144, s[0:1]
	s_mov_b32 m0, s42
	v_mov_b32_e32 v151, v153
	global_load_lds_dwordx4 v148, s[0:1]
	v_mov_b32_e32 v145, v153
	v_mov_b32_e32 v149, v153
	s_mov_b32 s7, 0
	v_lshl_add_u64 v[6:7], s[4:5], 0, v[146:147]
	v_lshl_add_u64 v[4:5], s[4:5], 0, v[150:151]
	v_lshl_add_u64 v[2:3], s[22:23], 0, v[144:145]
	v_lshl_add_u64 v[0:1], s[22:23], 0, v[148:149]
	s_cmp_lg_u32 s16, 0
	s_movk_i32 s43, 0x4000
	s_cbranch_scc1 .LBB0_1549
	s_barrier

.LBB0_1676:
	s_waitcnt lgkmcnt(0)
	v_bfe_i32 v2, v8, 27, 1
	v_lshlrev_b32_e32 v0, 4, v8
	v_lshrrev_b32_e32 v2, 22, v2
	v_add_u32_e32 v2, v0, v2
	v_and_b32_e32 v2, 0xfffffc00, v2
	v_sub_u32_e32 v2, v0, v2
	v_ashrrev_i32_e32 v1, 31, v8
	v_lshrrev_b32_e32 v3, 4, v2
	v_lshrrev_b32_e32 v1, 26, v1
	v_bitop3_b32 v2, v3, v2, 32 bitop3:0x6c
	v_add_u32_e32 v1, v8, v1
	v_ashrrev_i32_e32 v4, 31, v2
	v_ashrrev_i32_e32 v1, 6, v1
	v_lshrrev_b32_e32 v4, 26, v4
	v_lshlrev_b32_e32 v3, 3, v1
	v_add_u32_e32 v4, v2, v4
	v_and_b32_e32 v3, -16, v3
	v_ashrrev_i32_e32 v5, 6, v4
	v_and_b32_e32 v4, 0xc0, v4
	v_add_u32_e32 v3, v5, v3
	v_sub_u32_e32 v2, v2, v4
	v_mov_b32_e32 v4, 1
	v_lshlrev_b32_e32 v1, 5, v1
	v_ashrrev_i16_sdwa v2, v4, sext(v2) dst_sel:DWORD dst_unused:UNUSED_PAD src0_sel:DWORD src1_sel:BYTE_0
	v_lshlrev_b32_e32 v6, 1, v3
	v_lshrrev_b32_e32 v7, 2, v3
	v_and_b32_e32 v5, 3, v5
	s_mov_b32 s2, 0x7fffe0
	v_and_b32_e32 v1, 32, v1
	v_bfe_i32 v2, v2, 0, 16
	v_and_b32_e32 v6, 24, v6
	v_and_b32_e32 v7, 4, v7
	v_and_or_b32 v5, v3, s2, v5
	v_or3_b32 v5, v5, v7, v6
	v_add_lshl_u32 v1, v1, v2, 1
	v_add_u32_e32 v0, 0x2000, v0
	v_lshl_add_u32 v136, v3, 10, v1
	v_lshl_add_u32 v138, v5, 9, v1
	v_ashrrev_i32_e32 v1, 31, v0
	v_lshrrev_b32_e32 v1, 22, v1
	v_add_u32_e32 v1, v0, v1
	v_ashrrev_i32_e32 v1, 10, v1
	s_add_u32 s29, s4, 0x3b68c000
	v_mul_i32_i24_e32 v2, 0x400, v1
	s_addc_u32 s30, s5, 0
	v_sub_u32_e32 v0, v0, v2
	s_add_u32 s31, s4, 0x50d8000
	v_lshrrev_b32_e32 v2, 4, v0
	s_addc_u32 s38, s5, 0
	v_bitop3_b32 v0, v2, v0, 32 bitop3:0x6c
	s_add_i32 s0, s3, s0
	v_ashrrev_i32_e32 v3, 31, v0
	s_mul_hi_i32 s3, s0, 0x92492493
	v_lshrrev_b32_e32 v3, 26, v3
	s_add_i32 s3, s3, s0
	v_lshlrev_b32_e32 v2, 3, v1
	v_add_u32_e32 v3, v0, v3
	s_lshr_b32 s8, s3, 31
	s_ashr_i32 s3, s3, 6
	v_and_b32_e32 v2, -16, v2
	v_ashrrev_i32_e32 v5, 6, v3
	v_and_b32_e32 v3, 0xc0, v3
	s_add_i32 s3, s3, s8
	v_add_u32_e32 v2, v5, v2
	v_sub_u32_e32 v0, v0, v3
	s_lshl_b32 s10, s3, 3
	v_lshlrev_b32_e32 v1, 5, v1
	v_ashrrev_i16_sdwa v0, v4, sext(v0) dst_sel:DWORD dst_unused:UNUSED_PAD src0_sel:DWORD src1_sel:BYTE_0
	v_lshlrev_b32_e32 v3, 1, v2
	v_lshrrev_b32_e32 v4, 2, v2
	v_and_b32_e32 v5, 3, v5
	s_sub_i32 s8, 34, s10
	v_and_b32_e32 v1, 32, v1
	v_bfe_i32 v0, v0, 0, 16
	v_and_b32_e32 v3, 24, v3
	v_and_b32_e32 v4, 4, v4
	v_and_or_b32 v5, v2, s2, v5
	s_min_u32 s11, s8, 8
	s_mulk_i32 s3, 0x70
	v_or3_b32 v3, v5, v4, v3
	v_add_lshl_u32 v0, v1, v0, 1
	s_sub_i32 s0, s0, s3
	v_cvt_f32_ubyte0_e32 v1, s11
	v_lshl_add_u32 v140, v2, 10, v0
	v_lshl_add_u32 v142, v3, 9, v0
	v_cvt_f32_i32_e32 v0, s0
	v_rcp_iflag_f32_e32 v2, v1
	s_ashr_i32 s1, s28, 6
	s_ashr_i32 s3, s0, 30
	s_ashr_i32 s2, s28, 8
	v_mul_f32_e32 v2, v0, v2
	v_trunc_f32_e32 v2, v2
	v_fma_f32 v0, -v2, v1, v0
	v_cvt_i32_f32_e32 v2, v2
	s_lshl_b32 s39, s1, 10
	s_or_b32 s3, s3, 1
	v_cmp_ge_f32_e64 s[8:9], |v0|, v1
	s_and_b64 s[8:9], s[8:9], exec
	s_cselect_b32 s3, s3, 0
	v_readfirstlane_b32 s8, v2
	s_add_i32 s3, s8, s3
	s_sext_i32_i8 s59, s3
	s_mul_i32 s3, s3, s11
	s_sub_i32 s0, s0, s3
	s_sext_i32_i8 s0, s0
	s_add_i32 s60, s10, s0
	s_lshl_b32 s0, s60, 18
	s_cmp_lt_i32 s59, 6
	s_cselect_b32 s3, 0, 0x200
	s_or_b32 s0, s0, s3
	s_lshl_b32 s3, s59, 17
	s_add_u32 s26, s31, s3
	s_addc_u32 s27, s38, 0
	s_add_i32 s40, s39, 0
	s_add_i32 m0, s40, 0x10000
	v_mov_b32_e32 v139, 0
	global_load_lds_dwordx4 v138, s[26:27]
	s_add_i32 m0, s40, 0x12000
	s_add_u32 s22, s29, s0
	global_load_lds_dwordx4 v142, s[26:27]
	s_addc_u32 s23, s30, 0
	s_mov_b32 m0, s40
	s_add_i32 s41, s40, 0x2000
	global_load_lds_dwordx4 v136, s[22:23]
	s_mov_b32 m0, s41
	s_add_u32 s8, s26, 0x10000
	global_load_lds_dwordx4 v140, s[22:23]
	s_addc_u32 s9, s27, 0
	s_add_i32 m0, s40, 0x14000
	v_mov_b32_e32 v143, v139
	global_load_lds_dwordx4 v138, s[8:9]
	s_add_i32 m0, s40, 0x16000
	v_mov_b32_e32 v137, v139
	global_load_lds_dwordx4 v142, s[8:9]
	s_add_u32 s8, s22, 0x20000
	s_addc_u32 s9, s23, 0
	s_add_i32 s42, s40, 0x4000
	s_mov_b32 m0, s42
	s_add_i32 s43, s40, 0x6000
	global_load_lds_dwordx4 v136, s[8:9]
	s_mov_b32 m0, s43
	v_mov_b32_e32 v141, v139
	global_load_lds_dwordx4 v140, s[8:9]
	s_mov_b32 s0, 0
	v_lshl_add_u64 v[6:7], s[26:27], 0, v[138:139]
	v_lshl_add_u64 v[4:5], s[26:27], 0, v[142:143]
	v_lshl_add_u64 v[2:3], s[22:23], 0, v[136:137]
	s_cmp_lg_u32 s2, 0
	v_lshl_add_u64 v[0:1], s[22:23], 0, v[140:141]
	s_cbranch_scc1 .LBB0_1678
	s_barrier

.LBB0_2181:
	v_ashrrev_i32_e32 v1, 31, v8
	v_lshrrev_b32_e32 v1, 26, v1
	v_add_u32_e32 v1, v8, v1
	v_ashrrev_i32_e32 v9, 6, v1
	v_bfe_i32 v1, v8, 27, 1
	v_lshlrev_b32_e32 v0, 4, v8
	v_lshrrev_b32_e32 v1, 22, v1
	v_add_u32_e32 v1, v0, v1
	v_and_b32_e32 v1, 0xfffffc00, v1
	v_sub_u32_e32 v1, v0, v1
	s_waitcnt lgkmcnt(0)
	v_lshrrev_b32_e32 v2, 4, v1
	v_bitop3_b32 v1, v2, v1, 32 bitop3:0x6c
	v_ashrrev_i32_e32 v3, 31, v1
	v_lshrrev_b32_e32 v3, 26, v3
	v_add_u32_e32 v3, v1, v3
	v_lshlrev_b32_e32 v2, 3, v9
	v_ashrrev_i32_e32 v10, 6, v3
	v_and_b32_e32 v3, 0xc0, v3
	v_and_b32_e32 v2, -16, v2
	v_sub_u32_e32 v1, v1, v3
	v_mov_b32_e32 v3, 1
	v_add_u32_e32 v2, v10, v2
	v_ashrrev_i16_sdwa v1, v3, sext(v1) dst_sel:DWORD dst_unused:UNUSED_PAD src0_sel:DWORD src1_sel:BYTE_0
	v_bfe_i32 v11, v1, 0, 16
	v_lshlrev_b32_e32 v1, 1, v2
	s_add_u32 s65, s0, 0x216b8000
	v_lshlrev_b32_e32 v4, 5, v9
	v_and_b32_e32 v12, 0xffffffe0, v2
	v_and_b32_e32 v13, 24, v1
	v_lshrrev_b32_e32 v1, 2, v2
	v_and_b32_e32 v15, 3, v10
	s_addc_u32 s66, s1, 0
	v_and_b32_e32 v4, 32, v4
	v_and_b32_e32 v14, 4, v1
	v_or_b32_e32 v1, v12, v15
	s_add_u32 s67, s0, 0x37a0c000
	v_or3_b32 v1, v1, v14, v13
	v_add_lshl_u32 v4, v4, v11, 1
	v_add_u32_e32 v0, 0x2000, v0
	s_addc_u32 s68, s1, 0
	v_lshl_add_u32 v150, v1, 11, v4
	v_ashrrev_i32_e32 v1, 31, v0
	s_add_i32 s4, s4, s5
	v_lshrrev_b32_e32 v1, 22, v1
	s_ashr_i32 s5, s4, 31
	v_add_u32_e32 v1, v0, v1
	s_lshr_b32 s5, s5, 26
	v_ashrrev_i32_e32 v16, 10, v1
	s_add_i32 s5, s4, s5
	v_mul_i32_i24_e32 v1, 0x400, v16
	s_ashr_i32 s6, s5, 6
	s_and_b32 s5, s5, 0xffc0
	v_sub_u32_e32 v0, v0, v1
	s_sub_i32 s4, s4, s5
	v_lshrrev_b32_e32 v1, 4, v0
	s_bfe_i32 s5, s4, 0x80000
	v_bitop3_b32 v0, v1, v0, 32 bitop3:0x6c
	s_bfe_u32 s5, s5, 0x3000c
	v_lshl_add_u32 v148, v2, 11, v4
	v_ashrrev_i32_e32 v2, 31, v0
	s_add_i32 s5, s4, s5
	v_lshrrev_b32_e32 v2, 26, v2
	s_bfe_i32 s7, s5, 0x80000
	s_and_b32 s5, s5, 0xf8
	v_add_u32_e32 v2, v0, v2
	s_sub_i32 s4, s4, s5
	v_lshlrev_b32_e32 v1, 3, v16
	v_ashrrev_i32_e32 v4, 6, v2
	v_and_b32_e32 v2, 0xc0, v2
	s_lshl_b32 s6, s6, 3
	s_sext_i32_i16 s7, s7
	s_sext_i32_i8 s4, s4
	s_ashr_i32 s2, s60, 6
	v_and_b32_e32 v1, -16, v1
	v_sub_u32_e32 v0, v0, v2
	s_add_i32 s90, s6, s4
	s_ashr_i32 s89, s7, 3
	v_add_u32_e32 v1, v4, v1
	v_ashrrev_i16_sdwa v0, v3, sext(v0) dst_sel:DWORD dst_unused:UNUSED_PAD src0_sel:DWORD src1_sel:BYTE_0
	s_ashr_i32 s3, s60, 8
	s_lshl_b32 s69, s2, 10
	s_lshl_b32 s4, s89, 19
	s_lshl_b32 s5, s90, 19
	v_bfe_i32 v17, v0, 0, 16
	v_lshlrev_b32_e32 v0, 1, v1
	s_add_u32 s48, s67, s4
	v_lshlrev_b32_e32 v5, 5, v16
	v_and_b32_e32 v18, 0xffffffe0, v1
	v_and_b32_e32 v19, 24, v0
	v_lshrrev_b32_e32 v0, 2, v1
	v_and_b32_e32 v21, 3, v4
	s_addc_u32 s49, s68, 0
	s_add_i32 s70, s69, 0
	v_and_b32_e32 v5, 32, v5
	v_and_b32_e32 v20, 4, v0
	v_or_b32_e32 v0, v18, v21
	s_add_i32 m0, s70, 0x10000
	v_or3_b32 v0, v0, v20, v19
	v_add_lshl_u32 v2, v5, v17, 1
	global_load_lds_dwordx4 v150, s[48:49]
	s_add_i32 m0, s70, 0x12000
	v_lshl_add_u32 v154, v0, 11, v2
	s_add_u32 s46, s65, s5
	global_load_lds_dwordx4 v154, s[48:49]
	s_addc_u32 s47, s66, 0
	s_mov_b32 m0, s70
	s_add_i32 s71, s70, 0x2000
	v_lshl_add_u32 v152, v1, 11, v2
	global_load_lds_dwordx4 v148, s[46:47]
	s_mov_b32 m0, s71
	s_add_u32 s4, s48, 0x40000
	global_load_lds_dwordx4 v152, s[46:47]
	s_addc_u32 s5, s49, 0
	s_add_i32 m0, s70, 0x14000
	v_mov_b32_e32 v157, 0
	global_load_lds_dwordx4 v150, s[4:5]
	s_add_i32 m0, s70, 0x16000
	v_mov_b32_e32 v151, v157
	global_load_lds_dwordx4 v154, s[4:5]
	s_add_u32 s4, s46, 0x40000
	s_addc_u32 s5, s47, 0
	s_add_i32 s72, s70, 0x4000
	s_mov_b32 m0, s72
	s_add_i32 s73, s70, 0x6000
	global_load_lds_dwordx4 v148, s[4:5]
	s_mov_b32 m0, s73
	v_mov_b32_e32 v155, v157
	global_load_lds_dwordx4 v152, s[4:5]
	v_mov_b32_e32 v149, v157
	v_mov_b32_e32 v153, v157
	s_mov_b32 s74, 0
	v_lshl_add_u64 v[6:7], s[48:49], 0, v[150:151]
	v_lshl_add_u64 v[4:5], s[48:49], 0, v[154:155]
	v_lshl_add_u64 v[0:1], s[46:47], 0, v[148:149]
	s_cmp_lg_u32 s3, 0
	v_lshl_add_u64 v[2:3], s[46:47], 0, v[152:153]
	s_cbranch_scc1 .LBB0_2183
	s_barrier

.LBB0_2191:
	ds_read_b128 v[8:11], v230
	ds_read_b128 v[12:15], v230 offset:1024
	ds_read_b128 v[0:3], v230 offset:2048
	ds_read_b128 v[4:7], v230 offset:3072
	v_lshl_add_u64 v[172:173], v[170:171], 0, s[2:3]
	s_add_i32 s92, s70, 0xc000
	v_lshl_add_u64 v[174:175], v[172:173], 0, s[8:9]
	s_mov_b32 m0, s92
	ds_read_b128 v[180:183], v227
	ds_read_b128 v[184:187], v227 offset:1024
	ds_read_b128 v[188:191], v227 offset:2048
	ds_read_b128 v[192:195], v227 offset:3072
	ds_read_b128 v[196:199], v227 offset:4096
	ds_read_b128 v[200:203], v227 offset:5120
	ds_read_b128 v[204:207], v227 offset:6144
	ds_read_b128 v[208:211], v227 offset:7168
	global_load_lds_dwordx4 v[174:175], off
	v_lshl_add_u64 v[174:175], v[168:169], 0, s[2:3]
	s_add_i32 s91, s70, 0xe000
	v_lshl_add_u64 v[176:177], v[174:175], 0, s[8:9]
	s_mov_b32 m0, s91
	s_nop 0
	global_load_lds_dwordx4 v[176:177], off
	s_waitcnt lgkmcnt(8)
	s_barrier
	s_waitcnt lgkmcnt(0)
	s_setprio 1
	s_waitcnt lgkmcnt(0)
	v_mfma_scale_f32_16x16x128_f8f6f4 v[16:19], v[8:15], v[180:187], v[16:19], v224, v224 op_sel_hi:[0,0,0]
	v_mfma_scale_f32_16x16x128_f8f6f4 v[20:23], v[0:7], v[180:187], v[20:23], v224, v224 op_sel_hi:[0,0,0]
	v_mfma_scale_f32_16x16x128_f8f6f4 v[24:27], v[8:15], v[188:195], v[24:27], v224, v224 op_sel_hi:[0,0,0]
	v_mfma_scale_f32_16x16x128_f8f6f4 v[28:31], v[0:7], v[188:195], v[28:31], v224, v224 op_sel_hi:[0,0,0]
	v_mfma_scale_f32_16x16x128_f8f6f4 v[32:35], v[8:15], v[196:203], v[32:35], v224, v224 op_sel_hi:[0,0,0]
	v_mfma_scale_f32_16x16x128_f8f6f4 v[36:39], v[0:7], v[196:203], v[36:39], v224, v224 op_sel_hi:[0,0,0]
	v_mfma_scale_f32_16x16x128_f8f6f4 v[40:43], v[8:15], v[204:211], v[40:43], v224, v224 op_sel_hi:[0,0,0]
	v_mfma_scale_f32_16x16x128_f8f6f4 v[44:47], v[0:7], v[204:211], v[44:47], v224, v224 op_sel_hi:[0,0,0]
	s_setprio 0
	s_barrier
	v_lshl_add_u64 v[176:177], v[146:147], 0, s[2:3]
	s_add_i32 s94, s80, s69
	v_lshl_add_u64 v[178:179], v[176:177], 0, s[10:11]
	s_mov_b32 m0, s94
	ds_read_b128 v[212:215], v231
	ds_read_b128 v[216:219], v231 offset:1024
	ds_read_b128 v[234:237], v231 offset:2048
	ds_read_b128 v[238:241], v231 offset:3072
	global_load_lds_dwordx4 v[178:179], off
	v_lshl_add_u64 v[178:179], v[144:145], 0, s[2:3]
	s_add_i32 s93, s94, 0x2000
	v_lshl_add_u64 v[220:221], v[178:179], 0, s[10:11]
	s_mov_b32 m0, s93
	s_nop 0
	global_load_lds_dwordx4 v[220:221], off
	s_barrier
	s_waitcnt lgkmcnt(0)
	s_setprio 1
	s_waitcnt lgkmcnt(0)
	v_mfma_scale_f32_16x16x128_f8f6f4 v[48:51], v[212:219], v[180:187], v[48:51], v224, v224 op_sel_hi:[0,0,0]
	v_mfma_scale_f32_16x16x128_f8f6f4 v[52:55], v[234:241], v[180:187], v[52:55], v224, v224 op_sel_hi:[0,0,0]
	v_mfma_scale_f32_16x16x128_f8f6f4 v[56:59], v[212:219], v[188:195], v[56:59], v224, v224 op_sel_hi:[0,0,0]
	v_mfma_scale_f32_16x16x128_f8f6f4 v[60:63], v[234:241], v[188:195], v[60:63], v224, v224 op_sel_hi:[0,0,0]
	v_mfma_scale_f32_16x16x128_f8f6f4 v[64:67], v[212:219], v[196:203], v[64:67], v224, v224 op_sel_hi:[0,0,0]
	v_mfma_scale_f32_16x16x128_f8f6f4 v[68:71], v[234:241], v[196:203], v[68:71], v224, v224 op_sel_hi:[0,0,0]
	v_mfma_scale_f32_16x16x128_f8f6f4 v[72:75], v[212:219], v[204:211], v[72:75], v224, v224 op_sel_hi:[0,0,0]
	v_mfma_scale_f32_16x16x128_f8f6f4 v[76:79], v[234:241], v[204:211], v[76:79], v224, v224 op_sel_hi:[0,0,0]
	s_setprio 0
	s_mov_b32 m0, s70
	v_lshl_add_u64 v[220:221], v[172:173], 0, s[10:11]
	s_barrier
	ds_read_b128 v[180:183], v227 offset:16384
	ds_read_b128 v[184:187], v227 offset:17408
	ds_read_b128 v[188:191], v227 offset:18432
	ds_read_b128 v[192:195], v227 offset:19456
	ds_read_b128 v[196:199], v227 offset:20480
	ds_read_b128 v[200:203], v227 offset:21504
	ds_read_b128 v[204:207], v227 offset:22528
	ds_read_b128 v[208:211], v227 offset:23552
	global_load_lds_dwordx4 v[220:221], off
	v_lshl_add_u64 v[220:221], v[174:175], 0, s[10:11]
	s_mov_b32 m0, s71
	s_nop 0
	global_load_lds_dwordx4 v[220:221], off
	s_barrier
	s_waitcnt lgkmcnt(0)
	s_setprio 1
	s_waitcnt lgkmcnt(0)
	v_mfma_scale_f32_16x16x128_f8f6f4 v[80:83], v[8:15], v[180:187], v[80:83], v224, v224 op_sel_hi:[0,0,0]
	v_mfma_scale_f32_16x16x128_f8f6f4 v[84:87], v[0:7], v[180:187], v[84:87], v224, v224 op_sel_hi:[0,0,0]
	v_mfma_scale_f32_16x16x128_f8f6f4 v[88:91], v[8:15], v[188:195], v[88:91], v224, v224 op_sel_hi:[0,0,0]
	v_mfma_scale_f32_16x16x128_f8f6f4 v[92:95], v[0:7], v[188:195], v[92:95], v224, v224 op_sel_hi:[0,0,0]
	v_mfma_scale_f32_16x16x128_f8f6f4 v[96:99], v[8:15], v[196:203], v[96:99], v224, v224 op_sel_hi:[0,0,0]
	v_mfma_scale_f32_16x16x128_f8f6f4 v[100:103], v[0:7], v[196:203], v[100:103], v224, v224 op_sel_hi:[0,0,0]
	v_mfma_scale_f32_16x16x128_f8f6f4 v[104:107], v[8:15], v[204:211], v[104:107], v224, v224 op_sel_hi:[0,0,0]
	v_mfma_scale_f32_16x16x128_f8f6f4 v[108:111], v[0:7], v[204:211], v[108:111], v224, v224 op_sel_hi:[0,0,0]
	s_setprio 0
	s_barrier
	s_add_i32 s52, s81, s69
	v_lshl_add_u64 v[0:1], v[176:177], 0, s[12:13]
	s_mov_b32 m0, s52
	s_add_i32 s95, s52, 0x2000
	global_load_lds_dwordx4 v[0:1], off
	v_lshl_add_u64 v[0:1], v[178:179], 0, s[12:13]
	s_mov_b32 m0, s95
	s_nop 0
	global_load_lds_dwordx4 v[0:1], off
	s_waitcnt vmcnt(6)
	s_barrier
	s_setprio 1
	v_mfma_scale_f32_16x16x128_f8f6f4 v[112:115], v[212:219], v[180:187], v[112:115], v224, v224 op_sel_hi:[0,0,0]
	v_mfma_scale_f32_16x16x128_f8f6f4 v[116:119], v[234:241], v[180:187], v[116:119], v224, v224 op_sel_hi:[0,0,0]
	v_mfma_scale_f32_16x16x128_f8f6f4 v[120:123], v[212:219], v[188:195], v[120:123], v224, v224 op_sel_hi:[0,0,0]
	v_mfma_scale_f32_16x16x128_f8f6f4 v[124:127], v[234:241], v[188:195], v[124:127], v224, v224 op_sel_hi:[0,0,0]
	v_mfma_scale_f32_16x16x128_f8f6f4 v[128:131], v[212:219], v[196:203], v[128:131], v224, v224 op_sel_hi:[0,0,0]
	v_mfma_scale_f32_16x16x128_f8f6f4 v[132:135], v[234:241], v[196:203], v[132:135], v224, v224 op_sel_hi:[0,0,0]
	v_mfma_scale_f32_16x16x128_f8f6f4 v[136:139], v[212:219], v[204:211], v[136:139], v224, v224 op_sel_hi:[0,0,0]
	v_mfma_scale_f32_16x16x128_f8f6f4 v[140:143], v[234:241], v[204:211], v[140:143], v224, v224 op_sel_hi:[0,0,0]
	s_setprio 0
	s_add_i32 s63, 0, 0x18000
	v_add_u32_e32 v234, s63, v226
	s_barrier
	ds_read_b128 v[0:3], v234
	ds_read_b128 v[4:7], v234 offset:1024
	ds_read_b128 v[8:11], v234 offset:2048
	ds_read_b128 v[12:15], v234 offset:3072
	s_mov_b32 m0, s72
	v_lshl_add_u64 v[212:213], v[172:173], 0, s[12:13]
	ds_read_b128 v[180:183], v227 offset:32768
	ds_read_b128 v[184:187], v227 offset:33792
	ds_read_b128 v[188:191], v227 offset:34816
	ds_read_b128 v[192:195], v227 offset:35840
	ds_read_b128 v[196:199], v227 offset:36864
	ds_read_b128 v[200:203], v227 offset:37888
	ds_read_b128 v[204:207], v227 offset:38912
	ds_read_b128 v[208:211], v227 offset:39936
	global_load_lds_dwordx4 v[212:213], off
	v_lshl_add_u64 v[212:213], v[174:175], 0, s[12:13]
	s_mov_b32 m0, s73
	s_nop 0
	global_load_lds_dwordx4 v[212:213], off
	s_waitcnt lgkmcnt(8)
	s_barrier
	s_waitcnt lgkmcnt(0)
	s_setprio 1
	s_waitcnt lgkmcnt(0)
	v_mfma_scale_f32_16x16x128_f8f6f4 v[16:19], v[0:7], v[180:187], v[16:19], v224, v224 op_sel_hi:[0,0,0]
	v_mfma_scale_f32_16x16x128_f8f6f4 v[20:23], v[8:15], v[180:187], v[20:23], v224, v224 op_sel_hi:[0,0,0]
	v_mfma_scale_f32_16x16x128_f8f6f4 v[24:27], v[0:7], v[188:195], v[24:27], v224, v224 op_sel_hi:[0,0,0]
	v_mfma_scale_f32_16x16x128_f8f6f4 v[28:31], v[8:15], v[188:195], v[28:31], v224, v224 op_sel_hi:[0,0,0]
	v_mfma_scale_f32_16x16x128_f8f6f4 v[32:35], v[0:7], v[196:203], v[32:35], v224, v224 op_sel_hi:[0,0,0]
	v_mfma_scale_f32_16x16x128_f8f6f4 v[36:39], v[8:15], v[196:203], v[36:39], v224, v224 op_sel_hi:[0,0,0]
	v_mfma_scale_f32_16x16x128_f8f6f4 v[40:43], v[0:7], v[204:211], v[40:43], v224, v224 op_sel_hi:[0,0,0]
	v_mfma_scale_f32_16x16x128_f8f6f4 v[44:47], v[8:15], v[204:211], v[44:47], v224, v224 op_sel_hi:[0,0,0]
	s_setprio 0
	s_barrier
	s_add_i32 s64, 0, 0x1c000
	s_add_i32 s63, s63, s69
	v_add_u32_e32 v233, s64, v226
	v_lshl_add_u64 v[220:221], v[176:177], 0, s[16:17]
	s_mov_b32 m0, s63
	s_add_i32 s62, s63, 0x2000
	ds_read_b128 v[212:215], v233
	ds_read_b128 v[216:219], v233 offset:1024
	ds_read_b128 v[236:239], v233 offset:2048
	ds_read_b128 v[240:243], v233 offset:3072
	global_load_lds_dwordx4 v[220:221], off
	v_lshl_add_u64 v[220:221], v[178:179], 0, s[16:17]
	s_mov_b32 m0, s62
	s_nop 0
	global_load_lds_dwordx4 v[220:221], off
	s_barrier
	s_waitcnt lgkmcnt(0)
	s_setprio 1
	s_waitcnt lgkmcnt(0)
	v_mfma_scale_f32_16x16x128_f8f6f4 v[48:51], v[212:219], v[180:187], v[48:51], v224, v224 op_sel_hi:[0,0,0]
	v_mfma_scale_f32_16x16x128_f8f6f4 v[52:55], v[236:243], v[180:187], v[52:55], v224, v224 op_sel_hi:[0,0,0]
	v_mfma_scale_f32_16x16x128_f8f6f4 v[56:59], v[212:219], v[188:195], v[56:59], v224, v224 op_sel_hi:[0,0,0]
	v_mfma_scale_f32_16x16x128_f8f6f4 v[60:63], v[236:243], v[188:195], v[60:63], v224, v224 op_sel_hi:[0,0,0]
	v_mfma_scale_f32_16x16x128_f8f6f4 v[64:67], v[212:219], v[196:203], v[64:67], v224, v224 op_sel_hi:[0,0,0]
	v_mfma_scale_f32_16x16x128_f8f6f4 v[68:71], v[236:243], v[196:203], v[68:71], v224, v224 op_sel_hi:[0,0,0]
	v_mfma_scale_f32_16x16x128_f8f6f4 v[72:75], v[212:219], v[204:211], v[72:75], v224, v224 op_sel_hi:[0,0,0]
	v_mfma_scale_f32_16x16x128_f8f6f4 v[76:79], v[236:243], v[204:211], v[76:79], v224, v224 op_sel_hi:[0,0,0]
	s_setprio 0
	s_mov_b32 m0, s77
	v_lshl_add_u64 v[172:173], v[172:173], 0, s[16:17]
	s_barrier
	ds_read_b128 v[180:183], v227 offset:49152
	ds_read_b128 v[184:187], v227 offset:50176
	ds_read_b128 v[188:191], v227 offset:51200
	ds_read_b128 v[192:195], v227 offset:52224
	ds_read_b128 v[196:199], v227 offset:53248
	ds_read_b128 v[200:203], v227 offset:54272
	ds_read_b128 v[204:207], v227 offset:55296
	ds_read_b128 v[208:211], v227 offset:56320
	global_load_lds_dwordx4 v[172:173], off
	v_lshl_add_u64 v[172:173], v[174:175], 0, s[16:17]
	s_mov_b32 m0, s78
	s_nop 0
	global_load_lds_dwordx4 v[172:173], off
	s_barrier
	s_waitcnt lgkmcnt(0)
	s_setprio 1
	s_waitcnt lgkmcnt(0)
	v_mfma_scale_f32_16x16x128_f8f6f4 v[80:83], v[0:7], v[180:187], v[80:83], v224, v224 op_sel_hi:[0,0,0]
	v_mfma_scale_f32_16x16x128_f8f6f4 v[84:87], v[8:15], v[180:187], v[84:87], v224, v224 op_sel_hi:[0,0,0]
	v_mfma_scale_f32_16x16x128_f8f6f4 v[88:91], v[0:7], v[188:195], v[88:91], v224, v224 op_sel_hi:[0,0,0]
	v_mfma_scale_f32_16x16x128_f8f6f4 v[92:95], v[8:15], v[188:195], v[92:95], v224, v224 op_sel_hi:[0,0,0]
	v_mfma_scale_f32_16x16x128_f8f6f4 v[96:99], v[0:7], v[196:203], v[96:99], v224, v224 op_sel_hi:[0,0,0]
	v_mfma_scale_f32_16x16x128_f8f6f4 v[100:103], v[8:15], v[196:203], v[100:103], v224, v224 op_sel_hi:[0,0,0]
	v_mfma_scale_f32_16x16x128_f8f6f4 v[104:107], v[0:7], v[204:211], v[104:107], v224, v224 op_sel_hi:[0,0,0]
	v_mfma_scale_f32_16x16x128_f8f6f4 v[108:111], v[8:15], v[204:211], v[108:111], v224, v224 op_sel_hi:[0,0,0]
	s_setprio 0
	s_barrier
	s_add_i32 s64, s64, s69
	v_lshl_add_u64 v[0:1], v[176:177], 0, s[18:19]
	s_mov_b32 m0, s64
	s_add_i32 s53, s64, 0x2000
	global_load_lds_dwordx4 v[0:1], off
	v_lshl_add_u64 v[0:1], v[178:179], 0, s[18:19]
	s_mov_b32 m0, s53
	s_nop 0
	global_load_lds_dwordx4 v[0:1], off
	s_waitcnt vmcnt(6)
	s_barrier
	s_setprio 1
	v_mfma_scale_f32_16x16x128_f8f6f4 v[112:115], v[212:219], v[180:187], v[112:115], v224, v224 op_sel_hi:[0,0,0]
	v_mfma_scale_f32_16x16x128_f8f6f4 v[116:119], v[236:243], v[180:187], v[116:119], v224, v224 op_sel_hi:[0,0,0]
	v_mfma_scale_f32_16x16x128_f8f6f4 v[120:123], v[212:219], v[188:195], v[120:123], v224, v224 op_sel_hi:[0,0,0]
	v_mfma_scale_f32_16x16x128_f8f6f4 v[124:127], v[236:243], v[188:195], v[124:127], v224, v224 op_sel_hi:[0,0,0]
	v_mfma_scale_f32_16x16x128_f8f6f4 v[128:131], v[212:219], v[196:203], v[128:131], v224, v224 op_sel_hi:[0,0,0]
	v_mfma_scale_f32_16x16x128_f8f6f4 v[132:135], v[236:243], v[196:203], v[132:135], v224, v224 op_sel_hi:[0,0,0]
	v_mfma_scale_f32_16x16x128_f8f6f4 v[136:139], v[212:219], v[204:211], v[136:139], v224, v224 op_sel_hi:[0,0,0]
	v_mfma_scale_f32_16x16x128_f8f6f4 v[140:143], v[236:243], v[204:211], v[140:143], v224, v224 op_sel_hi:[0,0,0]
	s_setprio 0
	s_add_i32 s42, s42, 2
	s_add_u32 s2, s2, 0x100
	s_addc_u32 s3, s3, 0
	s_cmp_gt_u32 s42, 5
	s_barrier
	s_cbranch_scc0 .LBB0_2191
	s_add_u32 s42, s65, s87
	s_addc_u32 s43, s66, 0
	s_add_u32 s44, s67, s88
	s_addc_u32 s45, s68, 0
	s_and_b64 s[2:3], vcc, exec
	s_mul_i32 s2, s90, 24
	s_cselect_b32 s51, s43, s47
	s_cselect_b32 s50, s42, s46
	s_add_i32 s56, s2, s89
	s_ashr_i32 s57, s56, 31
	s_lshl_b64 s[2:3], s[56:57], 16
	s_add_u32 s2, s75, s2
	s_addc_u32 s3, s76, s3
	s_add_i32 s54, s56, 8
	s_ashr_i32 s55, s54, 31
	v_mov_b32_e32 v156, v229
	s_lshl_b64 s[54:55], s[54:55], 16
	s_nop 7
	s_nop 7
	s_nop 7
	s_add_u32 s54, s75, s54
	s_addc_u32 s55, s76, s55
	global_load_dwordx2 v[210:211], v156, s[2:3]
	global_load_dwordx2 v[216:217], v156, s[54:55]
	global_load_dwordx2 v[206:207], v156, s[2:3] offset:512
	global_load_dwordx2 v[208:209], v156, s[54:55] offset:512
	global_load_dwordx2 v[202:203], v156, s[2:3] offset:1024
	global_load_dwordx2 v[204:205], v156, s[54:55] offset:1024
	global_load_dwordx2 v[198:199], v156, s[2:3] offset:1536
	global_load_dwordx2 v[200:201], v156, s[54:55] offset:1536
	global_load_dwordx2 v[194:195], v156, s[2:3] offset:2048
	global_load_dwordx2 v[196:197], v156, s[54:55] offset:2048
	global_load_dwordx2 v[190:191], v156, s[2:3] offset:2560
	global_load_dwordx2 v[192:193], v156, s[54:55] offset:2560
	global_load_dwordx2 v[186:187], v156, s[2:3] offset:3072
	global_load_dwordx2 v[188:189], v156, s[54:55] offset:3072
	global_load_dwordx2 v[182:183], v156, s[2:3] offset:3584
	global_load_dwordx2 v[184:185], v156, s[54:55] offset:3584
	v_lshl_add_u64 v[0:1], s[2:3], 0, v[156:157]
	v_lshl_add_u64 v[2:3], s[54:55], 0, v[156:157]
	v_add_co_u32_e64 v0, s[2:3], s82, v0
	s_waitcnt vmcnt(0)
	v_cvt_f32_ubyte3_e32 v237, v210
	v_cvt_f32_ubyte0_e32 v156, v216
	v_add_f32_e32 v156, 0.5, v156
	v_rcp_f32_e32 v218, v156
	v_cvt_f32_ubyte0_e32 v156, v217
	v_add_f32_e32 v156, 0.5, v156
	v_rcp_f32_e32 v212, v156
	v_cvt_f32_ubyte1_e32 v156, v216
	v_add_f32_e32 v156, 0.5, v156
	v_rcp_f32_e32 v219, v156
	v_cvt_f32_ubyte1_e32 v156, v217
	v_add_f32_e32 v156, 0.5, v156
	v_rcp_f32_e32 v213, v156
	v_cvt_f32_ubyte2_e32 v156, v216
	v_add_f32_e32 v156, 0.5, v156
	v_rcp_f32_e32 v220, v156
	v_cvt_f32_ubyte2_e32 v156, v217
	v_add_f32_e32 v156, 0.5, v156
	v_rcp_f32_e32 v214, v156
	v_cvt_f32_ubyte3_e32 v156, v216
	v_add_f32_e32 v156, 0.5, v156
	v_rcp_f32_e32 v221, v156
	v_cvt_f32_ubyte3_e32 v156, v217
	v_add_f32_e32 v156, 0.5, v156
	v_cvt_f32_ubyte1_e32 v217, v210
	v_cvt_f32_ubyte0_e32 v216, v210
	v_cvt_f32_ubyte2_e32 v236, v210
	v_rcp_f32_e32 v215, v156
	v_pk_add_f32 v[236:237], v[236:237], 0.5 op_sel_hi:[1,0]
	v_pk_add_f32 v[216:217], v[216:217], 0.5 op_sel_hi:[1,0]
	v_cvt_f32_ubyte0_e32 v156, v208
	v_pk_mul_f32 v[216:217], v[216:217], v[218:219]
	v_pk_mul_f32 v[218:219], v[236:237], v[220:221]
	v_pk_mul_f32 v[16:17], v[16:17], v[216:217]
	v_pk_mul_f32 v[18:19], v[18:19], v[218:219]
	v_cvt_f32_ubyte3_e32 v219, v211
	v_cvt_f32_ubyte2_e32 v218, v211
	v_cvt_f32_ubyte1_e32 v217, v211
	v_cvt_f32_ubyte0_e32 v216, v211
	v_pk_add_f32 v[210:211], v[218:219], 0.5 op_sel_hi:[1,0]
	v_add_f32_e32 v156, 0.5, v156
	v_pk_mul_f32 v[210:211], v[210:211], v[214:215]
	v_pk_add_f32 v[216:217], v[216:217], 0.5 op_sel_hi:[1,0]
	v_pk_mul_f32 v[22:23], v[22:23], v[210:211]
	v_rcp_f32_e32 v210, v156
	v_cvt_f32_ubyte0_e32 v156, v209
	v_pk_mul_f32 v[212:213], v[216:217], v[212:213]
	v_add_f32_e32 v156, 0.5, v156
	v_pk_mul_f32 v[20:21], v[20:21], v[212:213]
	v_rcp_f32_e32 v212, v156
	v_cvt_f32_ubyte1_e32 v156, v208
	v_add_f32_e32 v156, 0.5, v156
	v_rcp_f32_e32 v211, v156
	v_cvt_f32_ubyte1_e32 v156, v209
	v_add_f32_e32 v156, 0.5, v156
	v_rcp_f32_e32 v213, v156
	v_cvt_f32_ubyte2_e32 v156, v208
	v_add_f32_e32 v156, 0.5, v156
	v_rcp_f32_e32 v214, v156
	v_cvt_f32_ubyte2_e32 v156, v209
	v_add_f32_e32 v156, 0.5, v156
	v_rcp_f32_e32 v216, v156
	v_cvt_f32_ubyte3_e32 v156, v208
	v_add_f32_e32 v156, 0.5, v156
	v_rcp_f32_e32 v215, v156
	v_cvt_f32_ubyte3_e32 v156, v209
	v_add_f32_e32 v156, 0.5, v156
	v_cvt_f32_ubyte1_e32 v209, v206
	v_cvt_f32_ubyte0_e32 v208, v206
	v_cvt_f32_ubyte3_e32 v219, v206
	v_cvt_f32_ubyte2_e32 v218, v206
	v_rcp_f32_e32 v217, v156
	v_pk_add_f32 v[218:219], v[218:219], 0.5 op_sel_hi:[1,0]
	v_pk_add_f32 v[208:209], v[208:209], 0.5 op_sel_hi:[1,0]
	v_cvt_f32_ubyte0_e32 v156, v204
	v_pk_mul_f32 v[208:209], v[208:209], v[210:211]
	v_pk_mul_f32 v[210:211], v[218:219], v[214:215]
	v_pk_mul_f32 v[48:49], v[48:49], v[208:209]
	v_pk_mul_f32 v[50:51], v[50:51], v[210:211]
	v_cvt_f32_ubyte3_e32 v211, v207
	v_cvt_f32_ubyte2_e32 v210, v207
	v_cvt_f32_ubyte1_e32 v209, v207
	v_cvt_f32_ubyte0_e32 v208, v207
	v_pk_add_f32 v[206:207], v[210:211], 0.5 op_sel_hi:[1,0]
	v_add_f32_e32 v156, 0.5, v156
	v_pk_mul_f32 v[206:207], v[206:207], v[216:217]
	v_pk_add_f32 v[208:209], v[208:209], 0.5 op_sel_hi:[1,0]
	v_pk_mul_f32 v[54:55], v[54:55], v[206:207]
	v_rcp_f32_e32 v206, v156
	v_cvt_f32_ubyte0_e32 v156, v205
	v_pk_mul_f32 v[208:209], v[208:209], v[212:213]
	v_add_f32_e32 v156, 0.5, v156
	v_pk_mul_f32 v[52:53], v[52:53], v[208:209]
	v_rcp_f32_e32 v208, v156
	v_cvt_f32_ubyte1_e32 v156, v204
	v_add_f32_e32 v156, 0.5, v156
	v_rcp_f32_e32 v207, v156
	v_cvt_f32_ubyte1_e32 v156, v205
	v_add_f32_e32 v156, 0.5, v156
	v_rcp_f32_e32 v209, v156
	v_cvt_f32_ubyte2_e32 v156, v204
	v_add_f32_e32 v156, 0.5, v156
	v_rcp_f32_e32 v210, v156
	v_cvt_f32_ubyte2_e32 v156, v205
	v_add_f32_e32 v156, 0.5, v156
	v_rcp_f32_e32 v212, v156
	v_cvt_f32_ubyte3_e32 v156, v204
	v_add_f32_e32 v156, 0.5, v156
	v_rcp_f32_e32 v211, v156
	v_cvt_f32_ubyte3_e32 v156, v205
	v_add_f32_e32 v156, 0.5, v156
	v_cvt_f32_ubyte1_e32 v205, v202
	v_cvt_f32_ubyte0_e32 v204, v202
	v_cvt_f32_ubyte3_e32 v215, v202
	v_cvt_f32_ubyte2_e32 v214, v202
	v_rcp_f32_e32 v213, v156
	v_pk_add_f32 v[214:215], v[214:215], 0.5 op_sel_hi:[1,0]
	v_pk_add_f32 v[204:205], v[204:205], 0.5 op_sel_hi:[1,0]
	v_cvt_f32_ubyte0_e32 v156, v200
	v_pk_mul_f32 v[204:205], v[204:205], v[206:207]
	v_pk_mul_f32 v[206:207], v[214:215], v[210:211]
	v_pk_mul_f32 v[24:25], v[24:25], v[204:205]
	v_pk_mul_f32 v[26:27], v[26:27], v[206:207]
	v_cvt_f32_ubyte3_e32 v207, v203
	v_cvt_f32_ubyte2_e32 v206, v203
	v_cvt_f32_ubyte1_e32 v205, v203
	v_cvt_f32_ubyte0_e32 v204, v203
	v_pk_add_f32 v[202:203], v[206:207], 0.5 op_sel_hi:[1,0]
	v_add_f32_e32 v156, 0.5, v156
	v_pk_mul_f32 v[202:203], v[202:203], v[212:213]
	v_pk_add_f32 v[204:205], v[204:205], 0.5 op_sel_hi:[1,0]
	v_pk_mul_f32 v[30:31], v[30:31], v[202:203]
	v_rcp_f32_e32 v202, v156
	v_cvt_f32_ubyte0_e32 v156, v201
	v_pk_mul_f32 v[204:205], v[204:205], v[208:209]
	v_add_f32_e32 v156, 0.5, v156
	v_pk_mul_f32 v[28:29], v[28:29], v[204:205]
	v_rcp_f32_e32 v204, v156
	v_cvt_f32_ubyte1_e32 v156, v200
	v_add_f32_e32 v156, 0.5, v156
	v_rcp_f32_e32 v203, v156
	v_cvt_f32_ubyte1_e32 v156, v201
	v_add_f32_e32 v156, 0.5, v156
	v_rcp_f32_e32 v205, v156
	v_cvt_f32_ubyte2_e32 v156, v200
	v_add_f32_e32 v156, 0.5, v156
	v_rcp_f32_e32 v206, v156
	v_cvt_f32_ubyte2_e32 v156, v201
	v_add_f32_e32 v156, 0.5, v156
	v_rcp_f32_e32 v208, v156
	v_cvt_f32_ubyte3_e32 v156, v200
	v_add_f32_e32 v156, 0.5, v156
	v_rcp_f32_e32 v207, v156
	v_cvt_f32_ubyte3_e32 v156, v201
	v_add_f32_e32 v156, 0.5, v156
	v_cvt_f32_ubyte1_e32 v201, v198
	v_cvt_f32_ubyte0_e32 v200, v198
	v_cvt_f32_ubyte3_e32 v211, v198
	v_cvt_f32_ubyte2_e32 v210, v198
	v_rcp_f32_e32 v209, v156
	v_pk_add_f32 v[210:211], v[210:211], 0.5 op_sel_hi:[1,0]
	v_pk_add_f32 v[200:201], v[200:201], 0.5 op_sel_hi:[1,0]
	v_cvt_f32_ubyte0_e32 v156, v196
	v_pk_mul_f32 v[200:201], v[200:201], v[202:203]
	v_pk_mul_f32 v[202:203], v[210:211], v[206:207]
	v_pk_mul_f32 v[56:57], v[56:57], v[200:201]
	v_pk_mul_f32 v[58:59], v[58:59], v[202:203]
	v_cvt_f32_ubyte3_e32 v203, v199
	v_cvt_f32_ubyte2_e32 v202, v199
	v_cvt_f32_ubyte1_e32 v201, v199
	v_cvt_f32_ubyte0_e32 v200, v199
	v_pk_add_f32 v[198:199], v[202:203], 0.5 op_sel_hi:[1,0]
	v_add_f32_e32 v156, 0.5, v156
	v_pk_mul_f32 v[198:199], v[198:199], v[208:209]
	v_pk_add_f32 v[200:201], v[200:201], 0.5 op_sel_hi:[1,0]
	v_pk_mul_f32 v[62:63], v[62:63], v[198:199]
	v_rcp_f32_e32 v198, v156
	v_cvt_f32_ubyte0_e32 v156, v197
	v_pk_mul_f32 v[200:201], v[200:201], v[204:205]
	v_add_f32_e32 v156, 0.5, v156
	v_pk_mul_f32 v[60:61], v[60:61], v[200:201]
	v_rcp_f32_e32 v200, v156
	v_cvt_f32_ubyte1_e32 v156, v196
	v_add_f32_e32 v156, 0.5, v156
	v_rcp_f32_e32 v199, v156
	v_cvt_f32_ubyte1_e32 v156, v197
	v_add_f32_e32 v156, 0.5, v156
	v_rcp_f32_e32 v201, v156
	v_cvt_f32_ubyte2_e32 v156, v196
	v_add_f32_e32 v156, 0.5, v156
	v_rcp_f32_e32 v202, v156
	v_cvt_f32_ubyte2_e32 v156, v197
	v_addc_co_u32_e64 v1, s[2:3], 0, v1, s[2:3]
	v_add_f32_e32 v156, 0.5, v156
	v_add_co_u32_e64 v6, s[2:3], s82, v2
	v_rcp_f32_e32 v204, v156
	v_cvt_f32_ubyte3_e32 v156, v196
	v_addc_co_u32_e64 v7, s[2:3], 0, v3, s[2:3]
	v_add_f32_e32 v156, 0.5, v156
	global_load_dwordx2 v[178:179], v[0:1], off
	global_load_dwordx2 v[180:181], v[6:7], off
	global_load_dwordx2 v[174:175], v[0:1], off offset:512
	global_load_dwordx2 v[176:177], v[6:7], off offset:512
	global_load_dwordx2 v[170:171], v[0:1], off offset:1024
	global_load_dwordx2 v[172:173], v[6:7], off offset:1024
	global_load_dwordx2 v[144:145], v[0:1], off offset:1536
	global_load_dwordx2 v[146:147], v[6:7], off offset:1536
	global_load_dwordx2 v[12:13], v[0:1], off offset:2048
	global_load_dwordx2 v[14:15], v[6:7], off offset:2048
	global_load_dwordx2 v[8:9], v[0:1], off offset:2560
	global_load_dwordx2 v[10:11], v[6:7], off offset:2560
	global_load_dwordx2 v[2:3], v[0:1], off offset:3072
	global_load_dwordx2 v[4:5], v[6:7], off offset:3072
	s_nop 0
	global_load_dwordx2 v[0:1], v[0:1], off offset:3584
	s_nop 0
	global_load_dwordx2 v[6:7], v[6:7], off offset:3584
	v_rcp_f32_e32 v203, v156
	v_cvt_f32_ubyte3_e32 v156, v197
	v_add_f32_e32 v156, 0.5, v156
	v_cvt_f32_ubyte1_e32 v197, v194
	v_cvt_f32_ubyte0_e32 v196, v194
	v_cvt_f32_ubyte3_e32 v207, v194
	v_cvt_f32_ubyte2_e32 v206, v194
	v_rcp_f32_e32 v205, v156
	v_pk_add_f32 v[206:207], v[206:207], 0.5 op_sel_hi:[1,0]
	v_pk_add_f32 v[196:197], v[196:197], 0.5 op_sel_hi:[1,0]
	v_cvt_f32_ubyte0_e32 v156, v192
	v_pk_mul_f32 v[196:197], v[196:197], v[198:199]
	v_pk_mul_f32 v[198:199], v[206:207], v[202:203]
	v_pk_mul_f32 v[32:33], v[32:33], v[196:197]
	v_pk_mul_f32 v[34:35], v[34:35], v[198:199]
	v_cvt_f32_ubyte3_e32 v199, v195
	v_cvt_f32_ubyte2_e32 v198, v195
	v_cvt_f32_ubyte1_e32 v197, v195
	v_cvt_f32_ubyte0_e32 v196, v195
	v_pk_add_f32 v[194:195], v[198:199], 0.5 op_sel_hi:[1,0]
	v_add_f32_e32 v156, 0.5, v156
	v_pk_mul_f32 v[194:195], v[194:195], v[204:205]
	v_pk_add_f32 v[196:197], v[196:197], 0.5 op_sel_hi:[1,0]
	v_pk_mul_f32 v[38:39], v[38:39], v[194:195]
	v_rcp_f32_e32 v194, v156
	v_cvt_f32_ubyte0_e32 v156, v193
	v_pk_mul_f32 v[196:197], v[196:197], v[200:201]
	v_add_f32_e32 v156, 0.5, v156
	v_pk_mul_f32 v[36:37], v[36:37], v[196:197]
	v_rcp_f32_e32 v196, v156
	v_cvt_f32_ubyte1_e32 v156, v192
	v_add_f32_e32 v156, 0.5, v156
	v_rcp_f32_e32 v195, v156
	v_cvt_f32_ubyte1_e32 v156, v193
	v_add_f32_e32 v156, 0.5, v156
	v_rcp_f32_e32 v197, v156
	v_cvt_f32_ubyte2_e32 v156, v192
	v_add_f32_e32 v156, 0.5, v156
	v_rcp_f32_e32 v198, v156
	v_cvt_f32_ubyte2_e32 v156, v193
	v_add_f32_e32 v156, 0.5, v156
	v_rcp_f32_e32 v200, v156
	v_cvt_f32_ubyte3_e32 v156, v192
	v_add_f32_e32 v156, 0.5, v156
	v_rcp_f32_e32 v199, v156
	v_cvt_f32_ubyte3_e32 v156, v193
	v_add_f32_e32 v156, 0.5, v156
	v_cvt_f32_ubyte1_e32 v193, v190
	v_cvt_f32_ubyte0_e32 v192, v190
	v_cvt_f32_ubyte3_e32 v203, v190
	v_cvt_f32_ubyte2_e32 v202, v190
	v_rcp_f32_e32 v201, v156
	v_pk_add_f32 v[202:203], v[202:203], 0.5 op_sel_hi:[1,0]
	v_pk_add_f32 v[192:193], v[192:193], 0.5 op_sel_hi:[1,0]
	v_cvt_f32_ubyte0_e32 v156, v188
	v_pk_mul_f32 v[192:193], v[192:193], v[194:195]
	v_pk_mul_f32 v[194:195], v[202:203], v[198:199]
	v_pk_mul_f32 v[64:65], v[64:65], v[192:193]
	v_pk_mul_f32 v[66:67], v[66:67], v[194:195]
	v_cvt_f32_ubyte3_e32 v195, v191
	v_cvt_f32_ubyte2_e32 v194, v191
	v_cvt_f32_ubyte1_e32 v193, v191
	v_cvt_f32_ubyte0_e32 v192, v191
	v_pk_add_f32 v[190:191], v[194:195], 0.5 op_sel_hi:[1,0]
	v_add_f32_e32 v156, 0.5, v156
	v_pk_mul_f32 v[190:191], v[190:191], v[200:201]
	v_pk_add_f32 v[192:193], v[192:193], 0.5 op_sel_hi:[1,0]
	v_pk_mul_f32 v[70:71], v[70:71], v[190:191]
	v_rcp_f32_e32 v190, v156
	v_cvt_f32_ubyte0_e32 v156, v189
	v_pk_mul_f32 v[192:193], v[192:193], v[196:197]
	v_add_f32_e32 v156, 0.5, v156
	v_pk_mul_f32 v[68:69], v[68:69], v[192:193]
	v_rcp_f32_e32 v192, v156
	v_cvt_f32_ubyte1_e32 v156, v188
	v_add_f32_e32 v156, 0.5, v156
	v_rcp_f32_e32 v191, v156
	v_cvt_f32_ubyte1_e32 v156, v189
	v_add_f32_e32 v156, 0.5, v156
	v_rcp_f32_e32 v193, v156
	v_cvt_f32_ubyte2_e32 v156, v188
	v_add_f32_e32 v156, 0.5, v156
	v_rcp_f32_e32 v194, v156
	v_cvt_f32_ubyte2_e32 v156, v189
	v_add_f32_e32 v156, 0.5, v156
	v_rcp_f32_e32 v196, v156
	v_cvt_f32_ubyte3_e32 v156, v188
	v_add_f32_e32 v156, 0.5, v156
	v_rcp_f32_e32 v195, v156
	v_cvt_f32_ubyte3_e32 v156, v189
	v_add_f32_e32 v156, 0.5, v156
	v_cvt_f32_ubyte1_e32 v189, v186
	v_cvt_f32_ubyte0_e32 v188, v186
	v_cvt_f32_ubyte3_e32 v199, v186
	v_cvt_f32_ubyte2_e32 v198, v186
	v_rcp_f32_e32 v197, v156
	v_pk_add_f32 v[198:199], v[198:199], 0.5 op_sel_hi:[1,0]
	v_pk_add_f32 v[188:189], v[188:189], 0.5 op_sel_hi:[1,0]
	v_cvt_f32_ubyte0_e32 v156, v184
	v_pk_mul_f32 v[188:189], v[188:189], v[190:191]
	v_pk_mul_f32 v[190:191], v[198:199], v[194:195]
	v_pk_mul_f32 v[40:41], v[40:41], v[188:189]
	v_pk_mul_f32 v[42:43], v[42:43], v[190:191]
	v_cvt_f32_ubyte3_e32 v191, v187
	v_cvt_f32_ubyte2_e32 v190, v187
	v_cvt_f32_ubyte1_e32 v189, v187
	v_cvt_f32_ubyte0_e32 v188, v187
	v_pk_add_f32 v[186:187], v[190:191], 0.5 op_sel_hi:[1,0]
	v_add_f32_e32 v156, 0.5, v156
	v_pk_mul_f32 v[186:187], v[186:187], v[196:197]
	v_pk_add_f32 v[188:189], v[188:189], 0.5 op_sel_hi:[1,0]
	v_pk_mul_f32 v[46:47], v[46:47], v[186:187]
	v_rcp_f32_e32 v186, v156
	v_cvt_f32_ubyte0_e32 v156, v185
	v_pk_mul_f32 v[188:189], v[188:189], v[192:193]
	v_add_f32_e32 v156, 0.5, v156
	v_pk_mul_f32 v[44:45], v[44:45], v[188:189]
	v_rcp_f32_e32 v188, v156
	v_cvt_f32_ubyte1_e32 v156, v184
	v_add_f32_e32 v156, 0.5, v156
	v_rcp_f32_e32 v187, v156
	v_cvt_f32_ubyte1_e32 v156, v185
	v_add_f32_e32 v156, 0.5, v156
	v_rcp_f32_e32 v189, v156
	v_cvt_f32_ubyte2_e32 v156, v184
	v_add_f32_e32 v156, 0.5, v156
	v_rcp_f32_e32 v190, v156
	v_cvt_f32_ubyte2_e32 v156, v185
	v_add_f32_e32 v156, 0.5, v156
	v_rcp_f32_e32 v192, v156
	v_cvt_f32_ubyte3_e32 v156, v184
	v_add_f32_e32 v156, 0.5, v156
	v_rcp_f32_e32 v191, v156
	v_cvt_f32_ubyte3_e32 v156, v185
	v_add_f32_e32 v156, 0.5, v156
	v_cvt_f32_ubyte1_e32 v185, v182
	v_cvt_f32_ubyte0_e32 v184, v182
	v_cvt_f32_ubyte3_e32 v195, v182
	v_cvt_f32_ubyte2_e32 v194, v182
	v_rcp_f32_e32 v193, v156
	v_pk_add_f32 v[194:195], v[194:195], 0.5 op_sel_hi:[1,0]
	v_pk_add_f32 v[184:185], v[184:185], 0.5 op_sel_hi:[1,0]
	s_waitcnt vmcnt(0)
	v_cvt_f32_ubyte0_e32 v156, v180
	v_pk_mul_f32 v[184:185], v[184:185], v[186:187]
	v_pk_mul_f32 v[186:187], v[194:195], v[190:191]
	v_pk_mul_f32 v[72:73], v[72:73], v[184:185]
	v_pk_mul_f32 v[74:75], v[74:75], v[186:187]
	v_cvt_f32_ubyte3_e32 v187, v183
	v_cvt_f32_ubyte2_e32 v186, v183
	v_cvt_f32_ubyte1_e32 v185, v183
	v_cvt_f32_ubyte0_e32 v184, v183
	v_pk_add_f32 v[182:183], v[186:187], 0.5 op_sel_hi:[1,0]
	v_add_f32_e32 v156, 0.5, v156
	v_pk_mul_f32 v[182:183], v[182:183], v[192:193]
	v_pk_add_f32 v[184:185], v[184:185], 0.5 op_sel_hi:[1,0]
	v_pk_mul_f32 v[78:79], v[78:79], v[182:183]
	v_rcp_f32_e32 v182, v156
	v_cvt_f32_ubyte0_e32 v156, v181
	v_pk_mul_f32 v[184:185], v[184:185], v[188:189]
	v_add_f32_e32 v156, 0.5, v156
	v_pk_mul_f32 v[76:77], v[76:77], v[184:185]
	v_rcp_f32_e32 v184, v156
	v_cvt_f32_ubyte1_e32 v156, v180
	v_add_f32_e32 v156, 0.5, v156
	v_rcp_f32_e32 v183, v156
	v_cvt_f32_ubyte1_e32 v156, v181
	v_add_f32_e32 v156, 0.5, v156
	v_rcp_f32_e32 v185, v156
	v_cvt_f32_ubyte2_e32 v156, v180
	v_add_f32_e32 v156, 0.5, v156
	v_rcp_f32_e32 v186, v156
	v_cvt_f32_ubyte2_e32 v156, v181
	v_add_f32_e32 v156, 0.5, v156
	v_rcp_f32_e32 v188, v156
	v_cvt_f32_ubyte3_e32 v156, v180
	v_add_f32_e32 v156, 0.5, v156
	v_rcp_f32_e32 v187, v156
	v_cvt_f32_ubyte3_e32 v156, v181
	v_add_f32_e32 v156, 0.5, v156
	v_cvt_f32_ubyte1_e32 v181, v178
	v_cvt_f32_ubyte0_e32 v180, v178
	v_cvt_f32_ubyte3_e32 v191, v178
	v_cvt_f32_ubyte2_e32 v190, v178
	v_rcp_f32_e32 v189, v156
	v_pk_add_f32 v[190:191], v[190:191], 0.5 op_sel_hi:[1,0]
	v_pk_add_f32 v[180:181], v[180:181], 0.5 op_sel_hi:[1,0]
	v_cvt_f32_ubyte0_e32 v156, v176
	v_pk_mul_f32 v[180:181], v[180:181], v[182:183]
	v_pk_mul_f32 v[182:183], v[190:191], v[186:187]
	v_pk_mul_f32 v[80:81], v[80:81], v[180:181]
	v_pk_mul_f32 v[82:83], v[82:83], v[182:183]
	v_cvt_f32_ubyte3_e32 v183, v179
	v_cvt_f32_ubyte2_e32 v182, v179
	v_cvt_f32_ubyte1_e32 v181, v179
	v_cvt_f32_ubyte0_e32 v180, v179
	v_pk_add_f32 v[178:179], v[182:183], 0.5 op_sel_hi:[1,0]
	v_add_f32_e32 v156, 0.5, v156
	v_pk_mul_f32 v[178:179], v[178:179], v[188:189]
	v_pk_add_f32 v[180:181], v[180:181], 0.5 op_sel_hi:[1,0]
	v_pk_mul_f32 v[86:87], v[86:87], v[178:179]
	v_rcp_f32_e32 v178, v156
	v_cvt_f32_ubyte0_e32 v156, v177
	v_pk_mul_f32 v[180:181], v[180:181], v[184:185]
	v_add_f32_e32 v156, 0.5, v156
	v_pk_mul_f32 v[84:85], v[84:85], v[180:181]
	v_rcp_f32_e32 v180, v156
	v_cvt_f32_ubyte1_e32 v156, v176
	v_add_f32_e32 v156, 0.5, v156
	v_rcp_f32_e32 v179, v156
	v_cvt_f32_ubyte1_e32 v156, v177
	v_add_f32_e32 v156, 0.5, v156
	v_rcp_f32_e32 v181, v156
	v_cvt_f32_ubyte2_e32 v156, v176
	v_add_f32_e32 v156, 0.5, v156
	v_rcp_f32_e32 v182, v156
	v_cvt_f32_ubyte2_e32 v156, v177
	v_add_f32_e32 v156, 0.5, v156
	v_rcp_f32_e32 v184, v156
	v_cvt_f32_ubyte3_e32 v156, v176
	v_add_f32_e32 v156, 0.5, v156
	v_rcp_f32_e32 v183, v156
	v_cvt_f32_ubyte3_e32 v156, v177
	v_add_f32_e32 v156, 0.5, v156
	v_cvt_f32_ubyte1_e32 v177, v174
	v_cvt_f32_ubyte0_e32 v176, v174
	v_cvt_f32_ubyte3_e32 v187, v174
	v_cvt_f32_ubyte2_e32 v186, v174
	v_rcp_f32_e32 v185, v156
	v_pk_add_f32 v[186:187], v[186:187], 0.5 op_sel_hi:[1,0]
	v_pk_add_f32 v[176:177], v[176:177], 0.5 op_sel_hi:[1,0]
	v_cvt_f32_ubyte0_e32 v156, v172
	v_pk_mul_f32 v[176:177], v[176:177], v[178:179]
	v_pk_mul_f32 v[178:179], v[186:187], v[182:183]
	v_pk_mul_f32 v[112:113], v[112:113], v[176:177]
	v_pk_mul_f32 v[114:115], v[114:115], v[178:179]
	v_cvt_f32_ubyte3_e32 v179, v175
	v_cvt_f32_ubyte2_e32 v178, v175
	v_cvt_f32_ubyte1_e32 v177, v175
	v_cvt_f32_ubyte0_e32 v176, v175
	v_pk_add_f32 v[174:175], v[178:179], 0.5 op_sel_hi:[1,0]
	v_add_f32_e32 v156, 0.5, v156
	v_pk_mul_f32 v[174:175], v[174:175], v[184:185]
	v_pk_add_f32 v[176:177], v[176:177], 0.5 op_sel_hi:[1,0]
	v_pk_mul_f32 v[118:119], v[118:119], v[174:175]
	v_rcp_f32_e32 v174, v156
	v_cvt_f32_ubyte0_e32 v156, v173
	v_pk_mul_f32 v[176:177], v[176:177], v[180:181]
	v_add_f32_e32 v156, 0.5, v156
	v_pk_mul_f32 v[116:117], v[116:117], v[176:177]
	v_rcp_f32_e32 v176, v156
	v_cvt_f32_ubyte1_e32 v156, v172
	v_add_f32_e32 v156, 0.5, v156
	v_rcp_f32_e32 v175, v156
	v_cvt_f32_ubyte1_e32 v156, v173
	v_add_f32_e32 v156, 0.5, v156
	v_rcp_f32_e32 v177, v156
	v_cvt_f32_ubyte2_e32 v156, v172
	v_add_f32_e32 v156, 0.5, v156
	v_rcp_f32_e32 v178, v156
	v_cvt_f32_ubyte2_e32 v156, v173
	v_add_f32_e32 v156, 0.5, v156
	v_rcp_f32_e32 v180, v156
	v_cvt_f32_ubyte3_e32 v156, v172
	v_add_f32_e32 v156, 0.5, v156
	v_rcp_f32_e32 v179, v156
	v_cvt_f32_ubyte3_e32 v156, v173
	v_add_f32_e32 v156, 0.5, v156
	v_cvt_f32_ubyte1_e32 v173, v170
	v_cvt_f32_ubyte0_e32 v172, v170
	v_cvt_f32_ubyte3_e32 v183, v170
	v_cvt_f32_ubyte2_e32 v182, v170
	v_rcp_f32_e32 v181, v156
	v_pk_add_f32 v[182:183], v[182:183], 0.5 op_sel_hi:[1,0]
	v_pk_add_f32 v[172:173], v[172:173], 0.5 op_sel_hi:[1,0]
	v_cvt_f32_ubyte0_e32 v156, v146
	v_pk_mul_f32 v[172:173], v[172:173], v[174:175]
	v_pk_mul_f32 v[174:175], v[182:183], v[178:179]
	v_pk_mul_f32 v[88:89], v[88:89], v[172:173]
	v_pk_mul_f32 v[90:91], v[90:91], v[174:175]
	v_cvt_f32_ubyte3_e32 v175, v171
	v_cvt_f32_ubyte2_e32 v174, v171
	v_cvt_f32_ubyte1_e32 v173, v171
	v_cvt_f32_ubyte0_e32 v172, v171
	v_pk_add_f32 v[170:171], v[174:175], 0.5 op_sel_hi:[1,0]
	v_add_f32_e32 v156, 0.5, v156
	v_pk_mul_f32 v[170:171], v[170:171], v[180:181]
	v_pk_add_f32 v[172:173], v[172:173], 0.5 op_sel_hi:[1,0]
	v_pk_mul_f32 v[94:95], v[94:95], v[170:171]
	v_rcp_f32_e32 v170, v156
	v_cvt_f32_ubyte0_e32 v156, v147
	v_pk_mul_f32 v[172:173], v[172:173], v[176:177]
	v_add_f32_e32 v156, 0.5, v156
	v_pk_mul_f32 v[92:93], v[92:93], v[172:173]
	v_rcp_f32_e32 v172, v156
	v_cvt_f32_ubyte1_e32 v156, v146
	v_add_f32_e32 v156, 0.5, v156
	v_rcp_f32_e32 v171, v156
	v_cvt_f32_ubyte1_e32 v156, v147
	v_add_f32_e32 v156, 0.5, v156
	v_rcp_f32_e32 v173, v156
	v_cvt_f32_ubyte2_e32 v156, v146
	v_cvt_f32_ubyte3_e32 v146, v146
	v_add_f32_e32 v156, 0.5, v156
	v_add_f32_e32 v146, 0.5, v146
	v_rcp_f32_e32 v174, v156
	v_rcp_f32_e32 v175, v146
	v_cvt_f32_ubyte3_e32 v146, v147
	v_cvt_f32_ubyte2_e32 v156, v147
	v_add_f32_e32 v146, 0.5, v146
	v_add_f32_e32 v156, 0.5, v156
	v_rcp_f32_e32 v177, v146
	v_cvt_f32_ubyte1_e32 v147, v144
	v_cvt_f32_ubyte0_e32 v146, v144
	v_cvt_f32_ubyte3_e32 v179, v144
	v_cvt_f32_ubyte2_e32 v178, v144
	v_rcp_f32_e32 v176, v156
	v_pk_add_f32 v[178:179], v[178:179], 0.5 op_sel_hi:[1,0]
	v_pk_add_f32 v[146:147], v[146:147], 0.5 op_sel_hi:[1,0]
	v_cvt_f32_ubyte2_e32 v156, v14
	v_pk_mul_f32 v[146:147], v[146:147], v[170:171]
	v_pk_mul_f32 v[170:171], v[178:179], v[174:175]
	v_pk_mul_f32 v[120:121], v[120:121], v[146:147]
	v_pk_mul_f32 v[122:123], v[122:123], v[170:171]
	v_cvt_f32_ubyte3_e32 v171, v145
	v_cvt_f32_ubyte2_e32 v170, v145
	v_cvt_f32_ubyte1_e32 v147, v145
	v_cvt_f32_ubyte0_e32 v146, v145
	v_pk_add_f32 v[144:145], v[170:171], 0.5 op_sel_hi:[1,0]
	v_pk_add_f32 v[146:147], v[146:147], 0.5 op_sel_hi:[1,0]
	v_pk_mul_f32 v[144:145], v[144:145], v[176:177]
	v_pk_mul_f32 v[146:147], v[146:147], v[172:173]
	v_pk_mul_f32 v[126:127], v[126:127], v[144:145]
	v_cvt_f32_ubyte0_e32 v145, v15
	v_add_f32_e32 v145, 0.5, v145
	v_pk_mul_f32 v[124:125], v[124:125], v[146:147]
	v_cvt_f32_ubyte0_e32 v144, v14
	v_rcp_f32_e32 v146, v145
	v_cvt_f32_ubyte1_e32 v145, v14
	v_cvt_f32_ubyte3_e32 v14, v14
	v_add_f32_e32 v144, 0.5, v144
	v_add_f32_e32 v145, 0.5, v145
	v_add_f32_e32 v156, 0.5, v156
	v_add_f32_e32 v14, 0.5, v14
	v_rcp_f32_e32 v144, v144
	v_rcp_f32_e32 v145, v145
	v_rcp_f32_e32 v170, v156
	v_rcp_f32_e32 v171, v14
	v_cvt_f32_ubyte3_e32 v14, v15
	v_cvt_f32_ubyte2_e32 v156, v15
	v_add_f32_e32 v14, 0.5, v14
	v_cvt_f32_ubyte1_e32 v147, v15
	v_add_f32_e32 v156, 0.5, v156
	v_rcp_f32_e32 v173, v14
	v_cvt_f32_ubyte1_e32 v15, v12
	v_cvt_f32_ubyte0_e32 v14, v12
	v_cvt_f32_ubyte3_e32 v175, v12
	v_cvt_f32_ubyte2_e32 v174, v12
	v_rcp_f32_e32 v172, v156
	v_pk_add_f32 v[174:175], v[174:175], 0.5 op_sel_hi:[1,0]
	v_pk_add_f32 v[14:15], v[14:15], 0.5 op_sel_hi:[1,0]
	v_add_f32_e32 v147, 0.5, v147
	v_pk_mul_f32 v[14:15], v[14:15], v[144:145]
	v_pk_mul_f32 v[144:145], v[174:175], v[170:171]
	v_rcp_f32_e32 v147, v147
	v_pk_mul_f32 v[98:99], v[98:99], v[144:145]
	v_cvt_f32_ubyte3_e32 v145, v13
	v_cvt_f32_ubyte2_e32 v144, v13
	v_pk_mul_f32 v[96:97], v[96:97], v[14:15]
	v_cvt_f32_ubyte1_e32 v15, v13
	v_cvt_f32_ubyte0_e32 v14, v13
	v_pk_add_f32 v[12:13], v[144:145], 0.5 op_sel_hi:[1,0]
	v_pk_add_f32 v[14:15], v[14:15], 0.5 op_sel_hi:[1,0]
	v_pk_mul_f32 v[12:13], v[12:13], v[172:173]
	v_pk_mul_f32 v[14:15], v[14:15], v[146:147]
	v_pk_mul_f32 v[102:103], v[102:103], v[12:13]
	v_cvt_f32_ubyte0_e32 v13, v11
	v_add_f32_e32 v13, 0.5, v13
	v_pk_mul_f32 v[100:101], v[100:101], v[14:15]
	v_cvt_f32_ubyte0_e32 v12, v10
	v_rcp_f32_e32 v14, v13
	v_cvt_f32_ubyte1_e32 v13, v10
	v_cvt_f32_ubyte2_e32 v144, v10
	v_cvt_f32_ubyte2_e32 v145, v11
	v_cvt_f32_ubyte3_e32 v10, v10
	v_add_f32_e32 v12, 0.5, v12
	v_add_f32_e32 v13, 0.5, v13
	v_add_f32_e32 v144, 0.5, v144
	v_add_f32_e32 v145, 0.5, v145
	v_add_f32_e32 v10, 0.5, v10
	v_rcp_f32_e32 v12, v12
	v_rcp_f32_e32 v13, v13
	v_rcp_f32_e32 v144, v144
	v_rcp_f32_e32 v146, v145
	v_rcp_f32_e32 v145, v10
	v_cvt_f32_ubyte3_e32 v10, v11
	v_add_f32_e32 v10, 0.5, v10
	v_cvt_f32_ubyte1_e32 v15, v11
	v_rcp_f32_e32 v147, v10
	v_cvt_f32_ubyte1_e32 v11, v8
	v_cvt_f32_ubyte0_e32 v10, v8
	v_cvt_f32_ubyte3_e32 v171, v8
	v_cvt_f32_ubyte2_e32 v170, v8
	v_pk_add_f32 v[170:171], v[170:171], 0.5 op_sel_hi:[1,0]
	v_pk_add_f32 v[10:11], v[10:11], 0.5 op_sel_hi:[1,0]
	v_add_f32_e32 v15, 0.5, v15
	v_pk_mul_f32 v[10:11], v[10:11], v[12:13]
	v_pk_mul_f32 v[12:13], v[170:171], v[144:145]
	v_rcp_f32_e32 v15, v15
	v_pk_mul_f32 v[130:131], v[130:131], v[12:13]
	v_cvt_f32_ubyte3_e32 v13, v9
	v_cvt_f32_ubyte2_e32 v12, v9
	v_pk_mul_f32 v[128:129], v[128:129], v[10:11]
	v_cvt_f32_ubyte1_e32 v11, v9
	v_cvt_f32_ubyte0_e32 v10, v9
	v_pk_add_f32 v[8:9], v[12:13], 0.5 op_sel_hi:[1,0]
	v_pk_add_f32 v[10:11], v[10:11], 0.5 op_sel_hi:[1,0]
	v_pk_mul_f32 v[8:9], v[8:9], v[146:147]
	v_pk_mul_f32 v[10:11], v[10:11], v[14:15]
	v_pk_mul_f32 v[134:135], v[134:135], v[8:9]
	v_cvt_f32_ubyte0_e32 v9, v5
	v_add_f32_e32 v9, 0.5, v9
	v_pk_mul_f32 v[132:133], v[132:133], v[10:11]
	v_cvt_f32_ubyte0_e32 v8, v4
	v_rcp_f32_e32 v10, v9
	v_cvt_f32_ubyte1_e32 v9, v4
	v_cvt_f32_ubyte2_e32 v12, v4
	v_cvt_f32_ubyte2_e32 v13, v5
	v_cvt_f32_ubyte3_e32 v4, v4
	v_add_f32_e32 v8, 0.5, v8
	v_add_f32_e32 v9, 0.5, v9
	v_add_f32_e32 v12, 0.5, v12
	v_add_f32_e32 v13, 0.5, v13
	v_add_f32_e32 v4, 0.5, v4
	v_rcp_f32_e32 v8, v8
	v_rcp_f32_e32 v9, v9
	v_rcp_f32_e32 v12, v12
	v_rcp_f32_e32 v14, v13
	v_rcp_f32_e32 v13, v4
	v_cvt_f32_ubyte3_e32 v4, v5
	v_add_f32_e32 v4, 0.5, v4
	v_cvt_f32_ubyte1_e32 v11, v5
	v_rcp_f32_e32 v15, v4
	v_cvt_f32_ubyte1_e32 v5, v2
	v_cvt_f32_ubyte0_e32 v4, v2
	v_cvt_f32_ubyte3_e32 v145, v2
	v_cvt_f32_ubyte2_e32 v144, v2
	v_pk_add_f32 v[144:145], v[144:145], 0.5 op_sel_hi:[1,0]
	v_pk_add_f32 v[4:5], v[4:5], 0.5 op_sel_hi:[1,0]
	v_add_f32_e32 v11, 0.5, v11
	v_pk_mul_f32 v[4:5], v[4:5], v[8:9]
	v_pk_mul_f32 v[8:9], v[144:145], v[12:13]
	v_rcp_f32_e32 v11, v11
	v_pk_mul_f32 v[106:107], v[106:107], v[8:9]
	v_cvt_f32_ubyte3_e32 v9, v3
	v_cvt_f32_ubyte2_e32 v8, v3
	v_pk_mul_f32 v[104:105], v[104:105], v[4:5]
	v_cvt_f32_ubyte1_e32 v5, v3
	v_cvt_f32_ubyte0_e32 v4, v3
	v_pk_add_f32 v[2:3], v[8:9], 0.5 op_sel_hi:[1,0]
	v_pk_add_f32 v[4:5], v[4:5], 0.5 op_sel_hi:[1,0]
	v_pk_mul_f32 v[2:3], v[2:3], v[14:15]
	v_pk_mul_f32 v[4:5], v[4:5], v[10:11]
	v_pk_mul_f32 v[110:111], v[110:111], v[2:3]
	v_cvt_f32_ubyte0_e32 v3, v7
	v_add_f32_e32 v3, 0.5, v3
	v_pk_mul_f32 v[108:109], v[108:109], v[4:5]
	v_cvt_f32_ubyte0_e32 v2, v6
	v_rcp_f32_e32 v4, v3
	v_cvt_f32_ubyte1_e32 v3, v6
	v_cvt_f32_ubyte2_e32 v8, v6
	v_cvt_f32_ubyte2_e32 v9, v7
	v_cvt_f32_ubyte3_e32 v6, v6
	v_add_f32_e32 v2, 0.5, v2
	v_add_f32_e32 v3, 0.5, v3
	v_add_f32_e32 v8, 0.5, v8
	v_add_f32_e32 v9, 0.5, v9
	v_add_f32_e32 v6, 0.5, v6
	v_rcp_f32_e32 v2, v2
	v_rcp_f32_e32 v3, v3
	v_rcp_f32_e32 v8, v8
	v_rcp_f32_e32 v10, v9
	v_rcp_f32_e32 v9, v6
	v_cvt_f32_ubyte3_e32 v6, v7
	v_cvt_f32_ubyte1_e32 v5, v7
	v_add_f32_e32 v6, 0.5, v6
	v_add_f32_e32 v5, 0.5, v5
	v_rcp_f32_e32 v11, v6
	v_cvt_f32_ubyte1_e32 v7, v0
	v_cvt_f32_ubyte0_e32 v6, v0
	v_cvt_f32_ubyte3_e32 v13, v0
	v_cvt_f32_ubyte2_e32 v12, v0
	v_rcp_f32_e32 v5, v5
	v_pk_add_f32 v[12:13], v[12:13], 0.5 op_sel_hi:[1,0]
	v_pk_add_f32 v[6:7], v[6:7], 0.5 op_sel_hi:[1,0]
	s_nop 0
	v_pk_mul_f32 v[2:3], v[6:7], v[2:3]
	v_pk_mul_f32 v[6:7], v[12:13], v[8:9]
	v_pk_mul_f32 v[136:137], v[136:137], v[2:3]
	v_pk_mul_f32 v[138:139], v[138:139], v[6:7]
	v_cvt_f32_ubyte1_e32 v3, v1
	v_cvt_f32_ubyte0_e32 v2, v1
	v_cvt_f32_ubyte3_e32 v7, v1
	v_cvt_f32_ubyte2_e32 v6, v1
	v_pk_add_f32 v[0:1], v[6:7], 0.5 op_sel_hi:[1,0]
	v_pk_add_f32 v[2:3], v[2:3], 0.5 op_sel_hi:[1,0]
	v_pk_mul_f32 v[0:1], v[0:1], v[10:11]
	v_pk_mul_f32 v[2:3], v[2:3], v[4:5]
	v_pk_mul_f32 v[142:143], v[142:143], v[0:1]
	v_pk_mul_f32 v[140:141], v[140:141], v[2:3]
	ds_read_b128 v[8:11], v230
	ds_read_b128 v[12:15], v230 offset:1024
	ds_read_b128 v[0:3], v230 offset:2048
	ds_read_b128 v[4:7], v230 offset:3072
	s_add_u32 s2, s46, 0x40480
	s_addc_u32 s3, s47, 0
	s_mov_b32 m0, s92
	v_lshl_add_u64 v[144:145], s[2:3], 0, v[148:149]
	ds_read_b128 v[174:177], v227
	ds_read_b128 v[178:181], v227 offset:1024
	ds_read_b128 v[182:185], v227 offset:2048
	ds_read_b128 v[186:189], v227 offset:3072
	ds_read_b128 v[190:193], v227 offset:4096
	ds_read_b128 v[194:197], v227 offset:5120
	ds_read_b128 v[198:201], v227 offset:6144
	ds_read_b128 v[202:205], v227 offset:7168
	global_load_lds_dwordx4 v[144:145], off
	v_lshl_add_u64 v[144:145], s[2:3], 0, v[152:153]
	s_mov_b32 m0, s91
	s_nop 0
	global_load_lds_dwordx4 v[144:145], off
	s_waitcnt lgkmcnt(8)
	s_barrier
	s_waitcnt lgkmcnt(0)
	s_setprio 1
	s_waitcnt lgkmcnt(0)
	v_mfma_scale_f32_16x16x128_f8f6f4 v[16:19], v[8:15], v[174:181], v[16:19], v224, v224 op_sel_hi:[0,0,0]
	v_mfma_scale_f32_16x16x128_f8f6f4 v[20:23], v[0:7], v[174:181], v[20:23], v224, v224 op_sel_hi:[0,0,0]
	v_mfma_scale_f32_16x16x128_f8f6f4 v[24:27], v[8:15], v[182:189], v[24:27], v224, v224 op_sel_hi:[0,0,0]
	v_mfma_scale_f32_16x16x128_f8f6f4 v[28:31], v[0:7], v[182:189], v[28:31], v224, v224 op_sel_hi:[0,0,0]
	v_mfma_scale_f32_16x16x128_f8f6f4 v[32:35], v[8:15], v[190:197], v[32:35], v224, v224 op_sel_hi:[0,0,0]
	v_mfma_scale_f32_16x16x128_f8f6f4 v[36:39], v[0:7], v[190:197], v[36:39], v224, v224 op_sel_hi:[0,0,0]
	v_mfma_scale_f32_16x16x128_f8f6f4 v[40:43], v[8:15], v[198:205], v[40:43], v224, v224 op_sel_hi:[0,0,0]
	v_mfma_scale_f32_16x16x128_f8f6f4 v[44:47], v[0:7], v[198:205], v[44:47], v224, v224 op_sel_hi:[0,0,0]
	s_setprio 0
	s_barrier
	v_lshl_add_u64 v[170:171], s[48:49], 0, v[150:151]
	s_mov_b32 m0, s94
	v_lshl_add_u64 v[144:145], v[170:171], 0, s[20:21]
	v_lshl_add_u64 v[172:173], s[48:49], 0, v[154:155]
	ds_read_b128 v[206:209], v231
	ds_read_b128 v[210:213], v231 offset:1024
	ds_read_b128 v[214:217], v231 offset:2048
	ds_read_b128 v[218:221], v231 offset:3072
	global_load_lds_dwordx4 v[144:145], off
	v_lshl_add_u64 v[144:145], v[172:173], 0, s[20:21]
	s_mov_b32 m0, s93
	s_nop 0
	global_load_lds_dwordx4 v[144:145], off
	s_barrier
	s_waitcnt lgkmcnt(0)
	s_setprio 1
	s_waitcnt lgkmcnt(0)
	v_mfma_scale_f32_16x16x128_f8f6f4 v[48:51], v[206:213], v[174:181], v[48:51], v224, v224 op_sel_hi:[0,0,0]
	v_mfma_scale_f32_16x16x128_f8f6f4 v[52:55], v[214:221], v[174:181], v[52:55], v224, v224 op_sel_hi:[0,0,0]
	v_mfma_scale_f32_16x16x128_f8f6f4 v[56:59], v[206:213], v[182:189], v[56:59], v224, v224 op_sel_hi:[0,0,0]
	v_mfma_scale_f32_16x16x128_f8f6f4 v[60:63], v[214:221], v[182:189], v[60:63], v224, v224 op_sel_hi:[0,0,0]
	v_mfma_scale_f32_16x16x128_f8f6f4 v[64:67], v[206:213], v[190:197], v[64:67], v224, v224 op_sel_hi:[0,0,0]
	v_mfma_scale_f32_16x16x128_f8f6f4 v[68:71], v[214:221], v[190:197], v[68:71], v224, v224 op_sel_hi:[0,0,0]
	v_mfma_scale_f32_16x16x128_f8f6f4 v[72:75], v[206:213], v[198:205], v[72:75], v224, v224 op_sel_hi:[0,0,0]
	v_mfma_scale_f32_16x16x128_f8f6f4 v[76:79], v[214:221], v[198:205], v[76:79], v224, v224 op_sel_hi:[0,0,0]
	s_setprio 0
	v_lshl_add_u64 v[174:175], s[46:47], 0, v[148:149]
	s_mov_b32 m0, s70
	v_lshl_add_u64 v[144:145], v[174:175], 0, s[20:21]
	s_barrier
	ds_read_b128 v[176:179], v227 offset:16384
	ds_read_b128 v[180:183], v227 offset:17408
	ds_read_b128 v[184:187], v227 offset:18432
	ds_read_b128 v[188:191], v227 offset:19456
	ds_read_b128 v[192:195], v227 offset:20480
	ds_read_b128 v[196:199], v227 offset:21504
	ds_read_b128 v[236:239], v227 offset:22528
	ds_read_b128 v[240:243], v227 offset:23552
	global_load_lds_dwordx4 v[144:145], off
	v_lshl_add_u64 v[144:145], v[168:169], 0, s[20:21]
	s_mov_b32 m0, s71
	s_nop 0
	global_load_lds_dwordx4 v[144:145], off
	s_barrier
	s_waitcnt lgkmcnt(0)
	s_setprio 1
	s_waitcnt lgkmcnt(0)
	v_mfma_scale_f32_16x16x128_f8f6f4 v[80:83], v[8:15], v[176:183], v[80:83], v224, v224 op_sel_hi:[0,0,0]
	v_mfma_scale_f32_16x16x128_f8f6f4 v[84:87], v[0:7], v[176:183], v[84:87], v224, v224 op_sel_hi:[0,0,0]
	v_mfma_scale_f32_16x16x128_f8f6f4 v[88:91], v[8:15], v[184:191], v[88:91], v224, v224 op_sel_hi:[0,0,0]
	v_mfma_scale_f32_16x16x128_f8f6f4 v[92:95], v[0:7], v[184:191], v[92:95], v224, v224 op_sel_hi:[0,0,0]
	v_mfma_scale_f32_16x16x128_f8f6f4 v[96:99], v[8:15], v[192:199], v[96:99], v224, v224 op_sel_hi:[0,0,0]
	v_mfma_scale_f32_16x16x128_f8f6f4 v[100:103], v[0:7], v[192:199], v[100:103], v224, v224 op_sel_hi:[0,0,0]
	v_mfma_scale_f32_16x16x128_f8f6f4 v[104:107], v[8:15], v[236:243], v[104:107], v224, v224 op_sel_hi:[0,0,0]
	v_mfma_scale_f32_16x16x128_f8f6f4 v[108:111], v[0:7], v[236:243], v[108:111], v224, v224 op_sel_hi:[0,0,0]
	s_setprio 0
	s_barrier
	s_add_u32 s2, s48, 0x40500
	s_addc_u32 s3, s49, 0
	s_mov_b32 m0, s52
	v_lshl_add_u64 v[0:1], s[2:3], 0, v[150:151]
	global_load_lds_dwordx4 v[0:1], off
	v_lshl_add_u64 v[0:1], s[2:3], 0, v[154:155]
	s_mov_b32 m0, s95
	s_nop 0
	global_load_lds_dwordx4 v[0:1], off
	s_waitcnt vmcnt(6)
	s_barrier
	s_setprio 1
	v_mfma_scale_f32_16x16x128_f8f6f4 v[112:115], v[206:213], v[176:183], v[112:115], v224, v224 op_sel_hi:[0,0,0]
	v_mfma_scale_f32_16x16x128_f8f6f4 v[116:119], v[214:221], v[176:183], v[116:119], v224, v224 op_sel_hi:[0,0,0]
	v_mfma_scale_f32_16x16x128_f8f6f4 v[120:123], v[206:213], v[184:191], v[120:123], v224, v224 op_sel_hi:[0,0,0]
	v_mfma_scale_f32_16x16x128_f8f6f4 v[124:127], v[214:221], v[184:191], v[124:127], v224, v224 op_sel_hi:[0,0,0]
	v_mfma_scale_f32_16x16x128_f8f6f4 v[128:131], v[206:213], v[192:199], v[128:131], v224, v224 op_sel_hi:[0,0,0]
	v_mfma_scale_f32_16x16x128_f8f6f4 v[132:135], v[214:221], v[192:199], v[132:135], v224, v224 op_sel_hi:[0,0,0]
	v_mfma_scale_f32_16x16x128_f8f6f4 v[136:139], v[206:213], v[236:243], v[136:139], v224, v224 op_sel_hi:[0,0,0]
	v_mfma_scale_f32_16x16x128_f8f6f4 v[140:143], v[214:221], v[236:243], v[140:143], v224, v224 op_sel_hi:[0,0,0]
	s_setprio 0
	s_barrier
	ds_read_b128 v[0:3], v234
	ds_read_b128 v[4:7], v234 offset:1024
	ds_read_b128 v[8:11], v234 offset:2048
	ds_read_b128 v[12:15], v234 offset:3072
	s_add_u32 s2, s46, 0x40500
	s_addc_u32 s3, s47, 0
	s_mov_b32 m0, s72
	v_lshl_add_u64 v[144:145], s[2:3], 0, v[148:149]
	ds_read_b128 v[176:179], v227 offset:32768
	ds_read_b128 v[180:183], v227 offset:33792
	ds_read_b128 v[184:187], v227 offset:34816
	ds_read_b128 v[188:191], v227 offset:35840
	ds_read_b128 v[192:195], v227 offset:36864
	ds_read_b128 v[196:199], v227 offset:37888
	ds_read_b128 v[200:203], v227 offset:38912
	ds_read_b128 v[204:207], v227 offset:39936
	global_load_lds_dwordx4 v[144:145], off
	v_lshl_add_u64 v[144:145], s[2:3], 0, v[152:153]
	s_mov_b32 m0, s73
	s_nop 0
	global_load_lds_dwordx4 v[144:145], off
	s_waitcnt lgkmcnt(8)
	s_barrier
	s_waitcnt lgkmcnt(0)
	s_setprio 1
	s_waitcnt lgkmcnt(0)
	v_mfma_scale_f32_16x16x128_f8f6f4 v[16:19], v[0:7], v[176:183], v[16:19], v224, v224 op_sel_hi:[0,0,0]
	v_mfma_scale_f32_16x16x128_f8f6f4 v[20:23], v[8:15], v[176:183], v[20:23], v224, v224 op_sel_hi:[0,0,0]
	v_mfma_scale_f32_16x16x128_f8f6f4 v[24:27], v[0:7], v[184:191], v[24:27], v224, v224 op_sel_hi:[0,0,0]
	v_mfma_scale_f32_16x16x128_f8f6f4 v[28:31], v[8:15], v[184:191], v[28:31], v224, v224 op_sel_hi:[0,0,0]
	v_mfma_scale_f32_16x16x128_f8f6f4 v[32:35], v[0:7], v[192:199], v[32:35], v224, v224 op_sel_hi:[0,0,0]
	v_mfma_scale_f32_16x16x128_f8f6f4 v[36:39], v[8:15], v[192:199], v[36:39], v224, v224 op_sel_hi:[0,0,0]
	v_mfma_scale_f32_16x16x128_f8f6f4 v[40:43], v[0:7], v[200:207], v[40:43], v224, v224 op_sel_hi:[0,0,0]
	v_mfma_scale_f32_16x16x128_f8f6f4 v[44:47], v[8:15], v[200:207], v[44:47], v224, v224 op_sel_hi:[0,0,0]
	s_setprio 0
	s_barrier
	s_mov_b32 m0, s63
	v_lshl_add_u64 v[144:145], v[170:171], 0, s[22:23]
	ds_read_b128 v[208:211], v233
	ds_read_b128 v[212:215], v233 offset:1024
	ds_read_b128 v[236:239], v233 offset:2048
	ds_read_b128 v[240:243], v233 offset:3072
	global_load_lds_dwordx4 v[144:145], off
	v_lshl_add_u64 v[144:145], v[172:173], 0, s[22:23]
	s_mov_b32 m0, s62
	s_nop 0
	global_load_lds_dwordx4 v[144:145], off
	s_barrier
	s_waitcnt lgkmcnt(0)
	s_setprio 1
	s_waitcnt lgkmcnt(0)
	v_mfma_scale_f32_16x16x128_f8f6f4 v[48:51], v[208:215], v[176:183], v[48:51], v224, v224 op_sel_hi:[0,0,0]
	v_mfma_scale_f32_16x16x128_f8f6f4 v[52:55], v[236:243], v[176:183], v[52:55], v224, v224 op_sel_hi:[0,0,0]
	v_mfma_scale_f32_16x16x128_f8f6f4 v[56:59], v[208:215], v[184:191], v[56:59], v224, v224 op_sel_hi:[0,0,0]
	v_mfma_scale_f32_16x16x128_f8f6f4 v[60:63], v[236:243], v[184:191], v[60:63], v224, v224 op_sel_hi:[0,0,0]
	v_mfma_scale_f32_16x16x128_f8f6f4 v[64:67], v[208:215], v[192:199], v[64:67], v224, v224 op_sel_hi:[0,0,0]
	v_mfma_scale_f32_16x16x128_f8f6f4 v[68:71], v[236:243], v[192:199], v[68:71], v224, v224 op_sel_hi:[0,0,0]
	v_mfma_scale_f32_16x16x128_f8f6f4 v[72:75], v[208:215], v[200:207], v[72:75], v224, v224 op_sel_hi:[0,0,0]
	v_mfma_scale_f32_16x16x128_f8f6f4 v[76:79], v[236:243], v[200:207], v[76:79], v224, v224 op_sel_hi:[0,0,0]
	s_setprio 0
	s_mov_b32 m0, s77
	v_lshl_add_u64 v[144:145], v[174:175], 0, s[22:23]
	s_barrier
	ds_read_b128 v[176:179], v227 offset:49152
	ds_read_b128 v[180:183], v227 offset:50176
	ds_read_b128 v[184:187], v227 offset:51200
	ds_read_b128 v[188:191], v227 offset:52224
	ds_read_b128 v[192:195], v227 offset:53248
	ds_read_b128 v[196:199], v227 offset:54272
	ds_read_b128 v[200:203], v227 offset:55296
	ds_read_b128 v[204:207], v227 offset:56320
	global_load_lds_dwordx4 v[144:145], off
	v_lshl_add_u64 v[144:145], v[168:169], 0, s[22:23]
	s_mov_b32 m0, s78
	s_nop 0
	global_load_lds_dwordx4 v[144:145], off
	s_barrier
	s_waitcnt lgkmcnt(0)
	s_setprio 1
	s_waitcnt lgkmcnt(0)
	v_mfma_scale_f32_16x16x128_f8f6f4 v[80:83], v[0:7], v[176:183], v[80:83], v224, v224 op_sel_hi:[0,0,0]
	v_mfma_scale_f32_16x16x128_f8f6f4 v[84:87], v[8:15], v[176:183], v[84:87], v224, v224 op_sel_hi:[0,0,0]
	v_mfma_scale_f32_16x16x128_f8f6f4 v[88:91], v[0:7], v[184:191], v[88:91], v224, v224 op_sel_hi:[0,0,0]
	v_mfma_scale_f32_16x16x128_f8f6f4 v[92:95], v[8:15], v[184:191], v[92:95], v224, v224 op_sel_hi:[0,0,0]
	v_mfma_scale_f32_16x16x128_f8f6f4 v[96:99], v[0:7], v[192:199], v[96:99], v224, v224 op_sel_hi:[0,0,0]
	v_mfma_scale_f32_16x16x128_f8f6f4 v[100:103], v[8:15], v[192:199], v[100:103], v224, v224 op_sel_hi:[0,0,0]
	v_mfma_scale_f32_16x16x128_f8f6f4 v[104:107], v[0:7], v[200:207], v[104:107], v224, v224 op_sel_hi:[0,0,0]
	v_mfma_scale_f32_16x16x128_f8f6f4 v[108:111], v[8:15], v[200:207], v[108:111], v224, v224 op_sel_hi:[0,0,0]
	s_setprio 0
	s_barrier
	s_add_u32 s2, s48, 0x40580
	s_addc_u32 s3, s49, 0
	s_mov_b32 m0, s64
	v_lshl_add_u64 v[0:1], s[2:3], 0, v[150:151]
	global_load_lds_dwordx4 v[0:1], off
	v_lshl_add_u64 v[0:1], s[2:3], 0, v[154:155]
	s_mov_b32 m0, s53
	s_nop 0
	global_load_lds_dwordx4 v[0:1], off
	s_waitcnt vmcnt(6)
	s_barrier
	s_setprio 1
	v_mfma_scale_f32_16x16x128_f8f6f4 v[112:115], v[208:215], v[176:183], v[112:115], v224, v224 op_sel_hi:[0,0,0]
	v_mfma_scale_f32_16x16x128_f8f6f4 v[116:119], v[236:243], v[176:183], v[116:119], v224, v224 op_sel_hi:[0,0,0]
	v_mfma_scale_f32_16x16x128_f8f6f4 v[120:123], v[208:215], v[184:191], v[120:123], v224, v224 op_sel_hi:[0,0,0]
	v_mfma_scale_f32_16x16x128_f8f6f4 v[124:127], v[236:243], v[184:191], v[124:127], v224, v224 op_sel_hi:[0,0,0]
	v_mfma_scale_f32_16x16x128_f8f6f4 v[128:131], v[208:215], v[192:199], v[128:131], v224, v224 op_sel_hi:[0,0,0]
	v_mfma_scale_f32_16x16x128_f8f6f4 v[132:135], v[236:243], v[192:199], v[132:135], v224, v224 op_sel_hi:[0,0,0]
	v_mfma_scale_f32_16x16x128_f8f6f4 v[136:139], v[208:215], v[200:207], v[136:139], v224, v224 op_sel_hi:[0,0,0]
	v_mfma_scale_f32_16x16x128_f8f6f4 v[140:143], v[236:243], v[200:207], v[140:143], v224, v224 op_sel_hi:[0,0,0]
	s_setprio 0
	s_barrier
	ds_read_b128 v[0:3], v230
	ds_read_b128 v[4:7], v230 offset:1024
	ds_read_b128 v[8:11], v230 offset:2048
	ds_read_b128 v[12:15], v230 offset:3072
	s_add_u32 s2, s46, 0x40580
	s_addc_u32 s3, s47, 0
	s_mov_b32 m0, s92
	v_lshl_add_u64 v[144:145], s[2:3], 0, v[148:149]
	ds_read_b128 v[176:179], v227
	ds_read_b128 v[180:183], v227 offset:1024
	ds_read_b128 v[184:187], v227 offset:2048
	ds_read_b128 v[188:191], v227 offset:3072
	ds_read_b128 v[192:195], v227 offset:4096
	ds_read_b128 v[196:199], v227 offset:5120
	ds_read_b128 v[200:203], v227 offset:6144
	ds_read_b128 v[204:207], v227 offset:7168
	global_load_lds_dwordx4 v[144:145], off
	v_lshl_add_u64 v[144:145], s[2:3], 0, v[152:153]
	s_mov_b32 m0, s91
	s_nop 0
	global_load_lds_dwordx4 v[144:145], off
	s_waitcnt lgkmcnt(8)
	s_barrier
	s_waitcnt lgkmcnt(0)
	s_setprio 1
	s_waitcnt lgkmcnt(0)
	v_mfma_scale_f32_16x16x128_f8f6f4 v[16:19], v[0:7], v[176:183], v[16:19], v224, v224 op_sel_hi:[0,0,0]
	v_mfma_scale_f32_16x16x128_f8f6f4 v[20:23], v[8:15], v[176:183], v[20:23], v224, v224 op_sel_hi:[0,0,0]
	v_mfma_scale_f32_16x16x128_f8f6f4 v[24:27], v[0:7], v[184:191], v[24:27], v224, v224 op_sel_hi:[0,0,0]
	v_mfma_scale_f32_16x16x128_f8f6f4 v[28:31], v[8:15], v[184:191], v[28:31], v224, v224 op_sel_hi:[0,0,0]
	v_mfma_scale_f32_16x16x128_f8f6f4 v[32:35], v[0:7], v[192:199], v[32:35], v224, v224 op_sel_hi:[0,0,0]
	v_mfma_scale_f32_16x16x128_f8f6f4 v[36:39], v[8:15], v[192:199], v[36:39], v224, v224 op_sel_hi:[0,0,0]
	v_mfma_scale_f32_16x16x128_f8f6f4 v[40:43], v[0:7], v[200:207], v[40:43], v224, v224 op_sel_hi:[0,0,0]
	v_mfma_scale_f32_16x16x128_f8f6f4 v[44:47], v[8:15], v[200:207], v[44:47], v224, v224 op_sel_hi:[0,0,0]
	s_setprio 0
	s_barrier
	s_mov_b32 m0, s94
	v_lshl_add_u64 v[144:145], v[170:171], 0, s[24:25]
	ds_read_b128 v[208:211], v231
	ds_read_b128 v[212:215], v231 offset:1024
	ds_read_b128 v[236:239], v231 offset:2048
	ds_read_b128 v[240:243], v231 offset:3072
	global_load_lds_dwordx4 v[144:145], off
	v_lshl_add_u64 v[144:145], v[172:173], 0, s[24:25]
	s_mov_b32 m0, s93
	s_nop 0
	global_load_lds_dwordx4 v[144:145], off
	s_barrier
	s_waitcnt lgkmcnt(0)
	s_setprio 1
	s_waitcnt lgkmcnt(0)
	v_mfma_scale_f32_16x16x128_f8f6f4 v[48:51], v[208:215], v[176:183], v[48:51], v224, v224 op_sel_hi:[0,0,0]
	v_mfma_scale_f32_16x16x128_f8f6f4 v[52:55], v[236:243], v[176:183], v[52:55], v224, v224 op_sel_hi:[0,0,0]
	v_mfma_scale_f32_16x16x128_f8f6f4 v[56:59], v[208:215], v[184:191], v[56:59], v224, v224 op_sel_hi:[0,0,0]
	v_mfma_scale_f32_16x16x128_f8f6f4 v[60:63], v[236:243], v[184:191], v[60:63], v224, v224 op_sel_hi:[0,0,0]
	v_mfma_scale_f32_16x16x128_f8f6f4 v[64:67], v[208:215], v[192:199], v[64:67], v224, v224 op_sel_hi:[0,0,0]
	v_mfma_scale_f32_16x16x128_f8f6f4 v[68:71], v[236:243], v[192:199], v[68:71], v224, v224 op_sel_hi:[0,0,0]
	v_mfma_scale_f32_16x16x128_f8f6f4 v[72:75], v[208:215], v[200:207], v[72:75], v224, v224 op_sel_hi:[0,0,0]
	v_mfma_scale_f32_16x16x128_f8f6f4 v[76:79], v[236:243], v[200:207], v[76:79], v224, v224 op_sel_hi:[0,0,0]
	s_setprio 0
	s_mov_b32 m0, s70
	v_lshl_add_u64 v[144:145], v[174:175], 0, s[24:25]
	s_barrier
	ds_read_b128 v[176:179], v227 offset:16384
	ds_read_b128 v[180:183], v227 offset:17408
	ds_read_b128 v[184:187], v227 offset:18432
	ds_read_b128 v[188:191], v227 offset:19456
	ds_read_b128 v[192:195], v227 offset:20480
	ds_read_b128 v[196:199], v227 offset:21504
	ds_read_b128 v[200:203], v227 offset:22528
	ds_read_b128 v[204:207], v227 offset:23552
	global_load_lds_dwordx4 v[144:145], off
	v_lshl_add_u64 v[144:145], v[168:169], 0, s[24:25]
	s_mov_b32 m0, s71
	s_nop 0
	global_load_lds_dwordx4 v[144:145], off
	s_barrier
	s_waitcnt lgkmcnt(0)
	s_setprio 1
	s_waitcnt lgkmcnt(0)
	v_mfma_scale_f32_16x16x128_f8f6f4 v[80:83], v[0:7], v[176:183], v[80:83], v224, v224 op_sel_hi:[0,0,0]
	v_mfma_scale_f32_16x16x128_f8f6f4 v[84:87], v[8:15], v[176:183], v[84:87], v224, v224 op_sel_hi:[0,0,0]
	v_mfma_scale_f32_16x16x128_f8f6f4 v[88:91], v[0:7], v[184:191], v[88:91], v224, v224 op_sel_hi:[0,0,0]
	v_mfma_scale_f32_16x16x128_f8f6f4 v[92:95], v[8:15], v[184:191], v[92:95], v224, v224 op_sel_hi:[0,0,0]
	v_mfma_scale_f32_16x16x128_f8f6f4 v[96:99], v[0:7], v[192:199], v[96:99], v224, v224 op_sel_hi:[0,0,0]
	v_mfma_scale_f32_16x16x128_f8f6f4 v[100:103], v[8:15], v[192:199], v[100:103], v224, v224 op_sel_hi:[0,0,0]
	v_mfma_scale_f32_16x16x128_f8f6f4 v[104:107], v[0:7], v[200:207], v[104:107], v224, v224 op_sel_hi:[0,0,0]
	v_mfma_scale_f32_16x16x128_f8f6f4 v[108:111], v[8:15], v[200:207], v[108:111], v224, v224 op_sel_hi:[0,0,0]
	s_setprio 0
	s_barrier
	s_add_u32 s2, s48, 0x40600
	s_addc_u32 s3, s49, 0
	s_mov_b32 m0, s52
	v_lshl_add_u64 v[0:1], s[2:3], 0, v[150:151]
	global_load_lds_dwordx4 v[0:1], off
	v_lshl_add_u64 v[0:1], s[2:3], 0, v[154:155]
	s_mov_b32 m0, s95
	s_nop 0
	global_load_lds_dwordx4 v[0:1], off
	s_waitcnt vmcnt(6)
	s_barrier
	s_setprio 1
	v_mfma_scale_f32_16x16x128_f8f6f4 v[112:115], v[208:215], v[176:183], v[112:115], v224, v224 op_sel_hi:[0,0,0]
	v_mfma_scale_f32_16x16x128_f8f6f4 v[116:119], v[236:243], v[176:183], v[116:119], v224, v224 op_sel_hi:[0,0,0]
	v_mfma_scale_f32_16x16x128_f8f6f4 v[120:123], v[208:215], v[184:191], v[120:123], v224, v224 op_sel_hi:[0,0,0]
	v_mfma_scale_f32_16x16x128_f8f6f4 v[124:127], v[236:243], v[184:191], v[124:127], v224, v224 op_sel_hi:[0,0,0]
	v_mfma_scale_f32_16x16x128_f8f6f4 v[128:131], v[208:215], v[192:199], v[128:131], v224, v224 op_sel_hi:[0,0,0]
	v_mfma_scale_f32_16x16x128_f8f6f4 v[132:135], v[236:243], v[192:199], v[132:135], v224, v224 op_sel_hi:[0,0,0]
	v_mfma_scale_f32_16x16x128_f8f6f4 v[136:139], v[208:215], v[200:207], v[136:139], v224, v224 op_sel_hi:[0,0,0]
	v_mfma_scale_f32_16x16x128_f8f6f4 v[140:143], v[236:243], v[200:207], v[140:143], v224, v224 op_sel_hi:[0,0,0]
	s_setprio 0
	s_barrier
	ds_read_b128 v[0:3], v234
	ds_read_b128 v[4:7], v234 offset:1024
	ds_read_b128 v[8:11], v234 offset:2048
	ds_read_b128 v[12:15], v234 offset:3072
	s_add_u32 s2, s46, 0x40600
	s_addc_u32 s3, s47, 0
	s_mov_b32 m0, s72
	v_lshl_add_u64 v[144:145], s[2:3], 0, v[148:149]
	ds_read_b128 v[176:179], v227 offset:32768
	ds_read_b128 v[180:183], v227 offset:33792
	ds_read_b128 v[184:187], v227 offset:34816
	ds_read_b128 v[188:191], v227 offset:35840
	ds_read_b128 v[192:195], v227 offset:36864
	ds_read_b128 v[196:199], v227 offset:37888
	ds_read_b128 v[200:203], v227 offset:38912
	ds_read_b128 v[204:207], v227 offset:39936
	global_load_lds_dwordx4 v[144:145], off
	v_lshl_add_u64 v[144:145], s[2:3], 0, v[152:153]
	s_mov_b32 m0, s73
	s_nop 0
	global_load_lds_dwordx4 v[144:145], off
	s_waitcnt lgkmcnt(8)
	s_barrier
	s_waitcnt lgkmcnt(0)
	s_setprio 1
	s_waitcnt lgkmcnt(0)
	v_mfma_scale_f32_16x16x128_f8f6f4 v[16:19], v[0:7], v[176:183], v[16:19], v224, v224 op_sel_hi:[0,0,0]
	v_mfma_scale_f32_16x16x128_f8f6f4 v[20:23], v[8:15], v[176:183], v[20:23], v224, v224 op_sel_hi:[0,0,0]
	v_mfma_scale_f32_16x16x128_f8f6f4 v[24:27], v[0:7], v[184:191], v[24:27], v224, v224 op_sel_hi:[0,0,0]
	v_mfma_scale_f32_16x16x128_f8f6f4 v[28:31], v[8:15], v[184:191], v[28:31], v224, v224 op_sel_hi:[0,0,0]
	v_mfma_scale_f32_16x16x128_f8f6f4 v[32:35], v[0:7], v[192:199], v[32:35], v224, v224 op_sel_hi:[0,0,0]
	v_mfma_scale_f32_16x16x128_f8f6f4 v[36:39], v[8:15], v[192:199], v[36:39], v224, v224 op_sel_hi:[0,0,0]
	v_mfma_scale_f32_16x16x128_f8f6f4 v[40:43], v[0:7], v[200:207], v[40:43], v224, v224 op_sel_hi:[0,0,0]
	v_mfma_scale_f32_16x16x128_f8f6f4 v[44:47], v[8:15], v[200:207], v[44:47], v224, v224 op_sel_hi:[0,0,0]
	s_setprio 0
	s_barrier
	s_mov_b32 m0, s63
	v_lshl_add_u64 v[144:145], v[170:171], 0, s[26:27]
	ds_read_b128 v[208:211], v233
	ds_read_b128 v[212:215], v233 offset:1024
	ds_read_b128 v[236:239], v233 offset:2048
	ds_read_b128 v[240:243], v233 offset:3072
	global_load_lds_dwordx4 v[144:145], off
	v_lshl_add_u64 v[144:145], v[172:173], 0, s[26:27]
	s_mov_b32 m0, s62
	s_nop 0
	global_load_lds_dwordx4 v[144:145], off
	s_barrier
	s_waitcnt lgkmcnt(0)
	s_setprio 1
	s_waitcnt lgkmcnt(0)
	v_mfma_scale_f32_16x16x128_f8f6f4 v[48:51], v[208:215], v[176:183], v[48:51], v224, v224 op_sel_hi:[0,0,0]
	v_mfma_scale_f32_16x16x128_f8f6f4 v[52:55], v[236:243], v[176:183], v[52:55], v224, v224 op_sel_hi:[0,0,0]
	v_mfma_scale_f32_16x16x128_f8f6f4 v[56:59], v[208:215], v[184:191], v[56:59], v224, v224 op_sel_hi:[0,0,0]
	v_mfma_scale_f32_16x16x128_f8f6f4 v[60:63], v[236:243], v[184:191], v[60:63], v224, v224 op_sel_hi:[0,0,0]
	v_mfma_scale_f32_16x16x128_f8f6f4 v[64:67], v[208:215], v[192:199], v[64:67], v224, v224 op_sel_hi:[0,0,0]
	v_mfma_scale_f32_16x16x128_f8f6f4 v[68:71], v[236:243], v[192:199], v[68:71], v224, v224 op_sel_hi:[0,0,0]
	v_mfma_scale_f32_16x16x128_f8f6f4 v[72:75], v[208:215], v[200:207], v[72:75], v224, v224 op_sel_hi:[0,0,0]
	v_mfma_scale_f32_16x16x128_f8f6f4 v[76:79], v[236:243], v[200:207], v[76:79], v224, v224 op_sel_hi:[0,0,0]
	s_setprio 0
	s_mov_b32 m0, s77
	v_lshl_add_u64 v[144:145], v[174:175], 0, s[26:27]
	s_barrier
	ds_read_b128 v[176:179], v227 offset:49152
	ds_read_b128 v[180:183], v227 offset:50176
	ds_read_b128 v[184:187], v227 offset:51200
	ds_read_b128 v[188:191], v227 offset:52224
	ds_read_b128 v[192:195], v227 offset:53248
	ds_read_b128 v[196:199], v227 offset:54272
	ds_read_b128 v[200:203], v227 offset:55296
	ds_read_b128 v[204:207], v227 offset:56320
	global_load_lds_dwordx4 v[144:145], off
	v_lshl_add_u64 v[144:145], v[168:169], 0, s[26:27]
	s_mov_b32 m0, s78
	s_nop 0
	global_load_lds_dwordx4 v[144:145], off
	s_barrier
	s_waitcnt lgkmcnt(0)
	s_setprio 1
	s_waitcnt lgkmcnt(0)
	v_mfma_scale_f32_16x16x128_f8f6f4 v[80:83], v[0:7], v[176:183], v[80:83], v224, v224 op_sel_hi:[0,0,0]
	v_mfma_scale_f32_16x16x128_f8f6f4 v[84:87], v[8:15], v[176:183], v[84:87], v224, v224 op_sel_hi:[0,0,0]
	v_mfma_scale_f32_16x16x128_f8f6f4 v[88:91], v[0:7], v[184:191], v[88:91], v224, v224 op_sel_hi:[0,0,0]
	v_mfma_scale_f32_16x16x128_f8f6f4 v[92:95], v[8:15], v[184:191], v[92:95], v224, v224 op_sel_hi:[0,0,0]
	v_mfma_scale_f32_16x16x128_f8f6f4 v[96:99], v[0:7], v[192:199], v[96:99], v224, v224 op_sel_hi:[0,0,0]
	v_mfma_scale_f32_16x16x128_f8f6f4 v[100:103], v[8:15], v[192:199], v[100:103], v224, v224 op_sel_hi:[0,0,0]
	v_mfma_scale_f32_16x16x128_f8f6f4 v[104:107], v[0:7], v[200:207], v[104:107], v224, v224 op_sel_hi:[0,0,0]
	v_mfma_scale_f32_16x16x128_f8f6f4 v[108:111], v[8:15], v[200:207], v[108:111], v224, v224 op_sel_hi:[0,0,0]
	s_setprio 0
	s_barrier
	s_add_u32 s2, s48, 0x40680
	s_addc_u32 s3, s49, 0
	s_mov_b32 m0, s64
	v_lshl_add_u64 v[0:1], s[2:3], 0, v[150:151]
	global_load_lds_dwordx4 v[0:1], off
	v_lshl_add_u64 v[0:1], s[2:3], 0, v[154:155]
	s_mov_b32 m0, s53
	s_nop 0
	global_load_lds_dwordx4 v[0:1], off
	s_waitcnt vmcnt(6)
	s_barrier
	s_setprio 1
	v_mfma_scale_f32_16x16x128_f8f6f4 v[112:115], v[208:215], v[176:183], v[112:115], v224, v224 op_sel_hi:[0,0,0]
	v_mfma_scale_f32_16x16x128_f8f6f4 v[116:119], v[236:243], v[176:183], v[116:119], v224, v224 op_sel_hi:[0,0,0]
	v_mfma_scale_f32_16x16x128_f8f6f4 v[120:123], v[208:215], v[184:191], v[120:123], v224, v224 op_sel_hi:[0,0,0]
	v_mfma_scale_f32_16x16x128_f8f6f4 v[124:127], v[236:243], v[184:191], v[124:127], v224, v224 op_sel_hi:[0,0,0]
	v_mfma_scale_f32_16x16x128_f8f6f4 v[128:131], v[208:215], v[192:199], v[128:131], v224, v224 op_sel_hi:[0,0,0]
	v_mfma_scale_f32_16x16x128_f8f6f4 v[132:135], v[236:243], v[192:199], v[132:135], v224, v224 op_sel_hi:[0,0,0]
	v_mfma_scale_f32_16x16x128_f8f6f4 v[136:139], v[208:215], v[200:207], v[136:139], v224, v224 op_sel_hi:[0,0,0]
	v_mfma_scale_f32_16x16x128_f8f6f4 v[140:143], v[236:243], v[200:207], v[140:143], v224, v224 op_sel_hi:[0,0,0]
	s_setprio 0
	s_and_b64 s[2:3], vcc, exec
	s_cselect_b32 s59, s45, s49
	s_cselect_b32 s58, s44, s48
	s_add_i32 s2, s56, 16
	s_ashr_i32 s3, s2, 31
	v_mov_b32_e32 v156, v229
	s_lshl_b64 s[2:3], s[2:3], 16
	s_barrier
	s_nop 7
	s_nop 7
	s_nop 7
	s_add_u32 s2, s75, s2
	s_addc_u32 s3, s76, s3
	global_load_dwordx2 v[216:217], v156, s[54:55]
	global_load_dwordx2 v[236:237], v156, s[2:3]
	global_load_dwordx2 v[212:213], v156, s[54:55] offset:512
	global_load_dwordx2 v[214:215], v156, s[2:3] offset:512
	global_load_dwordx2 v[208:209], v156, s[54:55] offset:1024
	global_load_dwordx2 v[210:211], v156, s[2:3] offset:1024
	global_load_dwordx2 v[204:205], v156, s[54:55] offset:1536
	global_load_dwordx2 v[206:207], v156, s[2:3] offset:1536
	global_load_dwordx2 v[200:201], v156, s[54:55] offset:2048
	global_load_dwordx2 v[202:203], v156, s[2:3] offset:2048
	global_load_dwordx2 v[196:197], v156, s[54:55] offset:2560
	global_load_dwordx2 v[198:199], v156, s[2:3] offset:2560
	global_load_dwordx2 v[192:193], v156, s[54:55] offset:3072
	global_load_dwordx2 v[194:195], v156, s[2:3] offset:3072
	global_load_dwordx2 v[188:189], v156, s[54:55] offset:3584
	global_load_dwordx2 v[190:191], v156, s[2:3] offset:3584
	v_lshl_add_u64 v[0:1], s[54:55], 0, v[156:157]
	v_lshl_add_u64 v[2:3], s[2:3], 0, v[156:157]
	v_add_co_u32_e32 v0, vcc, s82, v0
	s_waitcnt vmcnt(0)
	v_cvt_f32_ubyte3_e32 v243, v216
	v_cvt_f32_ubyte0_e32 v156, v236
	v_add_f32_e32 v156, 0.5, v156
	v_rcp_f32_e32 v238, v156
	v_cvt_f32_ubyte0_e32 v156, v237
	v_add_f32_e32 v156, 0.5, v156
	v_rcp_f32_e32 v218, v156
	v_cvt_f32_ubyte1_e32 v156, v236
	v_add_f32_e32 v156, 0.5, v156
	v_rcp_f32_e32 v239, v156
	v_cvt_f32_ubyte1_e32 v156, v237
	v_add_f32_e32 v156, 0.5, v156
	v_rcp_f32_e32 v219, v156
	v_cvt_f32_ubyte2_e32 v156, v236
	v_add_f32_e32 v156, 0.5, v156
	v_rcp_f32_e32 v240, v156
	v_cvt_f32_ubyte2_e32 v156, v237
	v_add_f32_e32 v156, 0.5, v156
	v_rcp_f32_e32 v220, v156
	v_cvt_f32_ubyte3_e32 v156, v236
	v_add_f32_e32 v156, 0.5, v156
	v_rcp_f32_e32 v241, v156
	v_cvt_f32_ubyte3_e32 v156, v237
	v_add_f32_e32 v156, 0.5, v156
	v_cvt_f32_ubyte1_e32 v237, v216
	v_cvt_f32_ubyte0_e32 v236, v216
	v_cvt_f32_ubyte2_e32 v242, v216
	v_rcp_f32_e32 v221, v156
	v_pk_add_f32 v[242:243], v[242:243], 0.5 op_sel_hi:[1,0]
	v_pk_add_f32 v[236:237], v[236:237], 0.5 op_sel_hi:[1,0]
	v_cvt_f32_ubyte0_e32 v156, v214
	v_pk_mul_f32 v[236:237], v[236:237], v[238:239]
	v_pk_mul_f32 v[238:239], v[242:243], v[240:241]
	v_pk_mul_f32 v[16:17], v[16:17], v[236:237]
	v_pk_mul_f32 v[18:19], v[18:19], v[238:239]
	v_cvt_f32_ubyte3_e32 v239, v217
	v_cvt_f32_ubyte2_e32 v238, v217
	v_cvt_f32_ubyte1_e32 v237, v217
	v_cvt_f32_ubyte0_e32 v236, v217
	v_pk_add_f32 v[216:217], v[238:239], 0.5 op_sel_hi:[1,0]
	v_add_f32_e32 v156, 0.5, v156
	v_pk_mul_f32 v[216:217], v[216:217], v[220:221]
	v_pk_add_f32 v[236:237], v[236:237], 0.5 op_sel_hi:[1,0]
	v_pk_mul_f32 v[22:23], v[22:23], v[216:217]
	v_rcp_f32_e32 v216, v156
	v_cvt_f32_ubyte0_e32 v156, v215
	v_pk_mul_f32 v[218:219], v[236:237], v[218:219]
	v_add_f32_e32 v156, 0.5, v156
	v_pk_mul_f32 v[20:21], v[20:21], v[218:219]
	v_rcp_f32_e32 v218, v156
	v_cvt_f32_ubyte1_e32 v156, v214
	v_add_f32_e32 v156, 0.5, v156
	v_rcp_f32_e32 v217, v156
	v_cvt_f32_ubyte1_e32 v156, v215
	v_add_f32_e32 v156, 0.5, v156
	v_rcp_f32_e32 v219, v156
	v_cvt_f32_ubyte2_e32 v156, v214
	v_add_f32_e32 v156, 0.5, v156
	v_rcp_f32_e32 v220, v156
	v_cvt_f32_ubyte2_e32 v156, v215
	v_add_f32_e32 v156, 0.5, v156
	v_rcp_f32_e32 v236, v156
	v_cvt_f32_ubyte3_e32 v156, v214
	v_add_f32_e32 v156, 0.5, v156
	v_rcp_f32_e32 v221, v156
	v_cvt_f32_ubyte3_e32 v156, v215
	v_add_f32_e32 v156, 0.5, v156
	v_cvt_f32_ubyte1_e32 v215, v212
	v_cvt_f32_ubyte0_e32 v214, v212
	v_cvt_f32_ubyte3_e32 v239, v212
	v_cvt_f32_ubyte2_e32 v238, v212
	v_rcp_f32_e32 v237, v156
	v_pk_add_f32 v[238:239], v[238:239], 0.5 op_sel_hi:[1,0]
	v_pk_add_f32 v[214:215], v[214:215], 0.5 op_sel_hi:[1,0]
	v_cvt_f32_ubyte0_e32 v156, v210
	v_pk_mul_f32 v[214:215], v[214:215], v[216:217]
	v_pk_mul_f32 v[216:217], v[238:239], v[220:221]
	v_pk_mul_f32 v[48:49], v[48:49], v[214:215]
	v_pk_mul_f32 v[50:51], v[50:51], v[216:217]
	v_cvt_f32_ubyte3_e32 v217, v213
	v_cvt_f32_ubyte2_e32 v216, v213
	v_cvt_f32_ubyte1_e32 v215, v213
	v_cvt_f32_ubyte0_e32 v214, v213
	v_pk_add_f32 v[212:213], v[216:217], 0.5 op_sel_hi:[1,0]
	v_add_f32_e32 v156, 0.5, v156
	v_pk_mul_f32 v[212:213], v[212:213], v[236:237]
	v_pk_add_f32 v[214:215], v[214:215], 0.5 op_sel_hi:[1,0]
	v_pk_mul_f32 v[54:55], v[54:55], v[212:213]
	v_rcp_f32_e32 v212, v156
	v_cvt_f32_ubyte0_e32 v156, v211
	v_pk_mul_f32 v[214:215], v[214:215], v[218:219]
	v_add_f32_e32 v156, 0.5, v156
	v_pk_mul_f32 v[52:53], v[52:53], v[214:215]
	v_rcp_f32_e32 v214, v156
	v_cvt_f32_ubyte1_e32 v156, v210
	v_add_f32_e32 v156, 0.5, v156
	v_rcp_f32_e32 v213, v156
	v_cvt_f32_ubyte1_e32 v156, v211
	v_add_f32_e32 v156, 0.5, v156
	v_rcp_f32_e32 v215, v156
	v_cvt_f32_ubyte2_e32 v156, v210
	v_add_f32_e32 v156, 0.5, v156
	v_rcp_f32_e32 v216, v156
	v_cvt_f32_ubyte2_e32 v156, v211
	v_add_f32_e32 v156, 0.5, v156
	v_rcp_f32_e32 v218, v156
	v_cvt_f32_ubyte3_e32 v156, v210
	v_add_f32_e32 v156, 0.5, v156
	v_rcp_f32_e32 v217, v156
	v_cvt_f32_ubyte3_e32 v156, v211
	v_add_f32_e32 v156, 0.5, v156
	v_cvt_f32_ubyte1_e32 v211, v208
	v_cvt_f32_ubyte0_e32 v210, v208
	v_cvt_f32_ubyte3_e32 v221, v208
	v_cvt_f32_ubyte2_e32 v220, v208
	v_rcp_f32_e32 v219, v156
	v_pk_add_f32 v[220:221], v[220:221], 0.5 op_sel_hi:[1,0]
	v_pk_add_f32 v[210:211], v[210:211], 0.5 op_sel_hi:[1,0]
	v_cvt_f32_ubyte0_e32 v156, v206
	v_pk_mul_f32 v[210:211], v[210:211], v[212:213]
	v_pk_mul_f32 v[212:213], v[220:221], v[216:217]
	v_pk_mul_f32 v[24:25], v[24:25], v[210:211]
	v_pk_mul_f32 v[26:27], v[26:27], v[212:213]
	v_cvt_f32_ubyte3_e32 v213, v209
	v_cvt_f32_ubyte2_e32 v212, v209
	v_cvt_f32_ubyte1_e32 v211, v209
	v_cvt_f32_ubyte0_e32 v210, v209
	v_pk_add_f32 v[208:209], v[212:213], 0.5 op_sel_hi:[1,0]
	v_add_f32_e32 v156, 0.5, v156
	v_pk_mul_f32 v[208:209], v[208:209], v[218:219]
	v_pk_add_f32 v[210:211], v[210:211], 0.5 op_sel_hi:[1,0]
	v_pk_mul_f32 v[30:31], v[30:31], v[208:209]
	v_rcp_f32_e32 v208, v156
	v_cvt_f32_ubyte0_e32 v156, v207
	v_pk_mul_f32 v[210:211], v[210:211], v[214:215]
	v_add_f32_e32 v156, 0.5, v156
	v_pk_mul_f32 v[28:29], v[28:29], v[210:211]
	v_rcp_f32_e32 v210, v156
	v_cvt_f32_ubyte1_e32 v156, v206
	v_add_f32_e32 v156, 0.5, v156
	v_rcp_f32_e32 v209, v156
	v_cvt_f32_ubyte1_e32 v156, v207
	v_add_f32_e32 v156, 0.5, v156
	v_rcp_f32_e32 v211, v156
	v_cvt_f32_ubyte2_e32 v156, v206
	v_add_f32_e32 v156, 0.5, v156
	v_rcp_f32_e32 v212, v156
	v_cvt_f32_ubyte2_e32 v156, v207
	v_add_f32_e32 v156, 0.5, v156
	v_rcp_f32_e32 v214, v156
	v_cvt_f32_ubyte3_e32 v156, v206
	v_add_f32_e32 v156, 0.5, v156
	v_rcp_f32_e32 v213, v156
	v_cvt_f32_ubyte3_e32 v156, v207
	v_add_f32_e32 v156, 0.5, v156
	v_cvt_f32_ubyte1_e32 v207, v204
	v_cvt_f32_ubyte0_e32 v206, v204
	v_cvt_f32_ubyte3_e32 v217, v204
	v_cvt_f32_ubyte2_e32 v216, v204
	v_rcp_f32_e32 v215, v156
	v_pk_add_f32 v[216:217], v[216:217], 0.5 op_sel_hi:[1,0]
	v_pk_add_f32 v[206:207], v[206:207], 0.5 op_sel_hi:[1,0]
	v_cvt_f32_ubyte0_e32 v156, v202
	v_pk_mul_f32 v[206:207], v[206:207], v[208:209]
	v_pk_mul_f32 v[208:209], v[216:217], v[212:213]
	v_pk_mul_f32 v[56:57], v[56:57], v[206:207]
	v_pk_mul_f32 v[58:59], v[58:59], v[208:209]
	v_cvt_f32_ubyte3_e32 v209, v205
	v_cvt_f32_ubyte2_e32 v208, v205
	v_cvt_f32_ubyte1_e32 v207, v205
	v_cvt_f32_ubyte0_e32 v206, v205
	v_pk_add_f32 v[204:205], v[208:209], 0.5 op_sel_hi:[1,0]
	v_add_f32_e32 v156, 0.5, v156
	v_pk_mul_f32 v[204:205], v[204:205], v[214:215]
	v_pk_add_f32 v[206:207], v[206:207], 0.5 op_sel_hi:[1,0]
	v_pk_mul_f32 v[62:63], v[62:63], v[204:205]
	v_rcp_f32_e32 v204, v156
	v_cvt_f32_ubyte0_e32 v156, v203
	v_pk_mul_f32 v[206:207], v[206:207], v[210:211]
	v_add_f32_e32 v156, 0.5, v156
	v_pk_mul_f32 v[60:61], v[60:61], v[206:207]
	v_rcp_f32_e32 v206, v156
	v_cvt_f32_ubyte1_e32 v156, v202
	v_add_f32_e32 v156, 0.5, v156
	v_rcp_f32_e32 v205, v156
	v_cvt_f32_ubyte1_e32 v156, v203
	v_add_f32_e32 v156, 0.5, v156
	v_rcp_f32_e32 v207, v156
	v_cvt_f32_ubyte2_e32 v156, v202
	v_add_f32_e32 v156, 0.5, v156
	v_rcp_f32_e32 v208, v156
	v_cvt_f32_ubyte2_e32 v156, v203
	v_addc_co_u32_e32 v1, vcc, 0, v1, vcc
	v_add_f32_e32 v156, 0.5, v156
	v_add_co_u32_e32 v6, vcc, s82, v2
	v_rcp_f32_e32 v210, v156
	v_cvt_f32_ubyte3_e32 v156, v202
	v_addc_co_u32_e32 v7, vcc, 0, v3, vcc
	v_add_f32_e32 v156, 0.5, v156
	global_load_dwordx2 v[184:185], v[0:1], off
	global_load_dwordx2 v[186:187], v[6:7], off
	global_load_dwordx2 v[180:181], v[0:1], off offset:512
	global_load_dwordx2 v[182:183], v[6:7], off offset:512
	global_load_dwordx2 v[176:177], v[0:1], off offset:1024
	global_load_dwordx2 v[178:179], v[6:7], off offset:1024
	global_load_dwordx2 v[144:145], v[0:1], off offset:1536
	global_load_dwordx2 v[146:147], v[6:7], off offset:1536
	global_load_dwordx2 v[12:13], v[0:1], off offset:2048
	global_load_dwordx2 v[14:15], v[6:7], off offset:2048
	global_load_dwordx2 v[8:9], v[0:1], off offset:2560
	global_load_dwordx2 v[10:11], v[6:7], off offset:2560
	global_load_dwordx2 v[2:3], v[0:1], off offset:3072
	global_load_dwordx2 v[4:5], v[6:7], off offset:3072
	s_nop 0
	global_load_dwordx2 v[0:1], v[0:1], off offset:3584
	s_nop 0
	global_load_dwordx2 v[6:7], v[6:7], off offset:3584
	v_rcp_f32_e32 v209, v156
	v_cvt_f32_ubyte3_e32 v156, v203
	v_add_f32_e32 v156, 0.5, v156
	v_cvt_f32_ubyte1_e32 v203, v200
	v_cvt_f32_ubyte0_e32 v202, v200
	v_cvt_f32_ubyte3_e32 v213, v200
	v_cvt_f32_ubyte2_e32 v212, v200
	v_rcp_f32_e32 v211, v156
	v_pk_add_f32 v[212:213], v[212:213], 0.5 op_sel_hi:[1,0]
	v_pk_add_f32 v[202:203], v[202:203], 0.5 op_sel_hi:[1,0]
	v_cvt_f32_ubyte0_e32 v156, v198
	v_pk_mul_f32 v[202:203], v[202:203], v[204:205]
	v_pk_mul_f32 v[204:205], v[212:213], v[208:209]
	v_pk_mul_f32 v[32:33], v[32:33], v[202:203]
	v_pk_mul_f32 v[34:35], v[34:35], v[204:205]
	v_cvt_f32_ubyte3_e32 v205, v201
	v_cvt_f32_ubyte2_e32 v204, v201
	v_cvt_f32_ubyte1_e32 v203, v201
	v_cvt_f32_ubyte0_e32 v202, v201
	v_pk_add_f32 v[200:201], v[204:205], 0.5 op_sel_hi:[1,0]
	v_add_f32_e32 v156, 0.5, v156
	v_pk_mul_f32 v[200:201], v[200:201], v[210:211]
	v_pk_add_f32 v[202:203], v[202:203], 0.5 op_sel_hi:[1,0]
	v_pk_mul_f32 v[38:39], v[38:39], v[200:201]
	v_rcp_f32_e32 v200, v156
	v_cvt_f32_ubyte0_e32 v156, v199
	v_pk_mul_f32 v[202:203], v[202:203], v[206:207]
	v_add_f32_e32 v156, 0.5, v156
	v_pk_mul_f32 v[36:37], v[36:37], v[202:203]
	v_rcp_f32_e32 v202, v156
	v_cvt_f32_ubyte1_e32 v156, v198
	v_add_f32_e32 v156, 0.5, v156
	v_rcp_f32_e32 v201, v156
	v_cvt_f32_ubyte1_e32 v156, v199
	v_add_f32_e32 v156, 0.5, v156
	v_rcp_f32_e32 v203, v156
	v_cvt_f32_ubyte2_e32 v156, v198
	v_add_f32_e32 v156, 0.5, v156
	v_rcp_f32_e32 v204, v156
	v_cvt_f32_ubyte2_e32 v156, v199
	v_add_f32_e32 v156, 0.5, v156
	v_rcp_f32_e32 v206, v156
	v_cvt_f32_ubyte3_e32 v156, v198
	v_add_f32_e32 v156, 0.5, v156
	v_rcp_f32_e32 v205, v156
	v_cvt_f32_ubyte3_e32 v156, v199
	v_add_f32_e32 v156, 0.5, v156
	v_cvt_f32_ubyte1_e32 v199, v196
	v_cvt_f32_ubyte0_e32 v198, v196
	v_cvt_f32_ubyte3_e32 v209, v196
	v_cvt_f32_ubyte2_e32 v208, v196
	v_rcp_f32_e32 v207, v156
	v_pk_add_f32 v[208:209], v[208:209], 0.5 op_sel_hi:[1,0]
	v_pk_add_f32 v[198:199], v[198:199], 0.5 op_sel_hi:[1,0]
	v_cvt_f32_ubyte0_e32 v156, v194
	v_pk_mul_f32 v[198:199], v[198:199], v[200:201]
	v_pk_mul_f32 v[200:201], v[208:209], v[204:205]
	v_pk_mul_f32 v[64:65], v[64:65], v[198:199]
	v_pk_mul_f32 v[66:67], v[66:67], v[200:201]
	v_cvt_f32_ubyte3_e32 v201, v197
	v_cvt_f32_ubyte2_e32 v200, v197
	v_cvt_f32_ubyte1_e32 v199, v197
	v_cvt_f32_ubyte0_e32 v198, v197
	v_pk_add_f32 v[196:197], v[200:201], 0.5 op_sel_hi:[1,0]
	v_add_f32_e32 v156, 0.5, v156
	v_pk_mul_f32 v[196:197], v[196:197], v[206:207]
	v_pk_add_f32 v[198:199], v[198:199], 0.5 op_sel_hi:[1,0]
	v_pk_mul_f32 v[70:71], v[70:71], v[196:197]
	v_rcp_f32_e32 v196, v156
	v_cvt_f32_ubyte0_e32 v156, v195
	v_pk_mul_f32 v[198:199], v[198:199], v[202:203]
	v_add_f32_e32 v156, 0.5, v156
	v_pk_mul_f32 v[68:69], v[68:69], v[198:199]
	v_rcp_f32_e32 v198, v156
	v_cvt_f32_ubyte1_e32 v156, v194
	v_add_f32_e32 v156, 0.5, v156
	v_rcp_f32_e32 v197, v156
	v_cvt_f32_ubyte1_e32 v156, v195
	v_add_f32_e32 v156, 0.5, v156
	v_rcp_f32_e32 v199, v156
	v_cvt_f32_ubyte2_e32 v156, v194
	v_add_f32_e32 v156, 0.5, v156
	v_rcp_f32_e32 v200, v156
	v_cvt_f32_ubyte2_e32 v156, v195
	v_add_f32_e32 v156, 0.5, v156
	v_rcp_f32_e32 v202, v156
	v_cvt_f32_ubyte3_e32 v156, v194
	v_add_f32_e32 v156, 0.5, v156
	v_rcp_f32_e32 v201, v156
	v_cvt_f32_ubyte3_e32 v156, v195
	v_add_f32_e32 v156, 0.5, v156
	v_cvt_f32_ubyte1_e32 v195, v192
	v_cvt_f32_ubyte0_e32 v194, v192
	v_cvt_f32_ubyte3_e32 v205, v192
	v_cvt_f32_ubyte2_e32 v204, v192
	v_rcp_f32_e32 v203, v156
	v_pk_add_f32 v[204:205], v[204:205], 0.5 op_sel_hi:[1,0]
	v_pk_add_f32 v[194:195], v[194:195], 0.5 op_sel_hi:[1,0]
	v_cvt_f32_ubyte0_e32 v156, v190
	v_pk_mul_f32 v[194:195], v[194:195], v[196:197]
	v_pk_mul_f32 v[196:197], v[204:205], v[200:201]
	v_pk_mul_f32 v[40:41], v[40:41], v[194:195]
	v_pk_mul_f32 v[42:43], v[42:43], v[196:197]
	v_cvt_f32_ubyte3_e32 v197, v193
	v_cvt_f32_ubyte2_e32 v196, v193
	v_cvt_f32_ubyte1_e32 v195, v193
	v_cvt_f32_ubyte0_e32 v194, v193
	v_pk_add_f32 v[192:193], v[196:197], 0.5 op_sel_hi:[1,0]
	v_add_f32_e32 v156, 0.5, v156
	v_pk_mul_f32 v[192:193], v[192:193], v[202:203]
	v_pk_add_f32 v[194:195], v[194:195], 0.5 op_sel_hi:[1,0]
	v_pk_mul_f32 v[46:47], v[46:47], v[192:193]
	v_rcp_f32_e32 v192, v156
	v_cvt_f32_ubyte0_e32 v156, v191
	v_pk_mul_f32 v[194:195], v[194:195], v[198:199]
	v_add_f32_e32 v156, 0.5, v156
	v_pk_mul_f32 v[44:45], v[44:45], v[194:195]
	v_rcp_f32_e32 v194, v156
	v_cvt_f32_ubyte1_e32 v156, v190
	v_add_f32_e32 v156, 0.5, v156
	v_rcp_f32_e32 v193, v156
	v_cvt_f32_ubyte1_e32 v156, v191
	v_add_f32_e32 v156, 0.5, v156
	v_rcp_f32_e32 v195, v156
	v_cvt_f32_ubyte2_e32 v156, v190
	v_add_f32_e32 v156, 0.5, v156
	v_rcp_f32_e32 v196, v156
	v_cvt_f32_ubyte2_e32 v156, v191
	v_add_f32_e32 v156, 0.5, v156
	v_rcp_f32_e32 v198, v156
	v_cvt_f32_ubyte3_e32 v156, v190
	v_add_f32_e32 v156, 0.5, v156
	v_rcp_f32_e32 v197, v156
	v_cvt_f32_ubyte3_e32 v156, v191
	v_add_f32_e32 v156, 0.5, v156
	v_cvt_f32_ubyte1_e32 v191, v188
	v_cvt_f32_ubyte0_e32 v190, v188
	v_cvt_f32_ubyte3_e32 v201, v188
	v_cvt_f32_ubyte2_e32 v200, v188
	v_rcp_f32_e32 v199, v156
	v_pk_add_f32 v[200:201], v[200:201], 0.5 op_sel_hi:[1,0]
	v_pk_add_f32 v[190:191], v[190:191], 0.5 op_sel_hi:[1,0]
	s_waitcnt vmcnt(0)
	v_cvt_f32_ubyte0_e32 v156, v186
	v_pk_mul_f32 v[190:191], v[190:191], v[192:193]
	v_pk_mul_f32 v[192:193], v[200:201], v[196:197]
	v_pk_mul_f32 v[72:73], v[72:73], v[190:191]
	v_pk_mul_f32 v[74:75], v[74:75], v[192:193]
	v_cvt_f32_ubyte3_e32 v193, v189
	v_cvt_f32_ubyte2_e32 v192, v189
	v_cvt_f32_ubyte1_e32 v191, v189
	v_cvt_f32_ubyte0_e32 v190, v189
	v_pk_add_f32 v[188:189], v[192:193], 0.5 op_sel_hi:[1,0]
	v_add_f32_e32 v156, 0.5, v156
	v_pk_mul_f32 v[188:189], v[188:189], v[198:199]
	v_pk_add_f32 v[190:191], v[190:191], 0.5 op_sel_hi:[1,0]
	v_pk_mul_f32 v[78:79], v[78:79], v[188:189]
	v_rcp_f32_e32 v188, v156
	v_cvt_f32_ubyte0_e32 v156, v187
	v_pk_mul_f32 v[190:191], v[190:191], v[194:195]
	v_add_f32_e32 v156, 0.5, v156
	v_pk_mul_f32 v[76:77], v[76:77], v[190:191]
	v_rcp_f32_e32 v190, v156
	v_cvt_f32_ubyte1_e32 v156, v186
	v_add_f32_e32 v156, 0.5, v156
	v_rcp_f32_e32 v189, v156
	v_cvt_f32_ubyte1_e32 v156, v187
	v_add_f32_e32 v156, 0.5, v156
	v_rcp_f32_e32 v191, v156
	v_cvt_f32_ubyte2_e32 v156, v186
	v_add_f32_e32 v156, 0.5, v156
	v_rcp_f32_e32 v192, v156
	v_cvt_f32_ubyte2_e32 v156, v187
	v_add_f32_e32 v156, 0.5, v156
	v_rcp_f32_e32 v194, v156
	v_cvt_f32_ubyte3_e32 v156, v186
	v_add_f32_e32 v156, 0.5, v156
	v_rcp_f32_e32 v193, v156
	v_cvt_f32_ubyte3_e32 v156, v187
	v_add_f32_e32 v156, 0.5, v156
	v_cvt_f32_ubyte1_e32 v187, v184
	v_cvt_f32_ubyte0_e32 v186, v184
	v_cvt_f32_ubyte3_e32 v197, v184
	v_cvt_f32_ubyte2_e32 v196, v184
	v_rcp_f32_e32 v195, v156
	v_pk_add_f32 v[196:197], v[196:197], 0.5 op_sel_hi:[1,0]
	v_pk_add_f32 v[186:187], v[186:187], 0.5 op_sel_hi:[1,0]
	v_cvt_f32_ubyte0_e32 v156, v182
	v_pk_mul_f32 v[186:187], v[186:187], v[188:189]
	v_pk_mul_f32 v[188:189], v[196:197], v[192:193]
	v_pk_mul_f32 v[80:81], v[80:81], v[186:187]
	v_pk_mul_f32 v[82:83], v[82:83], v[188:189]
	v_cvt_f32_ubyte3_e32 v189, v185
	v_cvt_f32_ubyte2_e32 v188, v185
	v_cvt_f32_ubyte1_e32 v187, v185
	v_cvt_f32_ubyte0_e32 v186, v185
	v_pk_add_f32 v[184:185], v[188:189], 0.5 op_sel_hi:[1,0]
	v_add_f32_e32 v156, 0.5, v156
	v_pk_mul_f32 v[184:185], v[184:185], v[194:195]
	v_pk_add_f32 v[186:187], v[186:187], 0.5 op_sel_hi:[1,0]
	v_pk_mul_f32 v[86:87], v[86:87], v[184:185]
	v_rcp_f32_e32 v184, v156
	v_cvt_f32_ubyte0_e32 v156, v183
	v_pk_mul_f32 v[186:187], v[186:187], v[190:191]
	v_add_f32_e32 v156, 0.5, v156
	v_pk_mul_f32 v[84:85], v[84:85], v[186:187]
	v_rcp_f32_e32 v186, v156
	v_cvt_f32_ubyte1_e32 v156, v182
	v_add_f32_e32 v156, 0.5, v156
	v_rcp_f32_e32 v185, v156
	v_cvt_f32_ubyte1_e32 v156, v183
	v_add_f32_e32 v156, 0.5, v156
	v_rcp_f32_e32 v187, v156
	v_cvt_f32_ubyte2_e32 v156, v182
	v_add_f32_e32 v156, 0.5, v156
	v_rcp_f32_e32 v188, v156
	v_cvt_f32_ubyte2_e32 v156, v183
	v_add_f32_e32 v156, 0.5, v156
	v_rcp_f32_e32 v190, v156
	v_cvt_f32_ubyte3_e32 v156, v182
	v_add_f32_e32 v156, 0.5, v156
	v_rcp_f32_e32 v189, v156
	v_cvt_f32_ubyte3_e32 v156, v183
	v_add_f32_e32 v156, 0.5, v156
	v_cvt_f32_ubyte1_e32 v183, v180
	v_cvt_f32_ubyte0_e32 v182, v180
	v_cvt_f32_ubyte3_e32 v193, v180
	v_cvt_f32_ubyte2_e32 v192, v180
	v_rcp_f32_e32 v191, v156
	v_pk_add_f32 v[192:193], v[192:193], 0.5 op_sel_hi:[1,0]
	v_pk_add_f32 v[182:183], v[182:183], 0.5 op_sel_hi:[1,0]
	v_cvt_f32_ubyte0_e32 v156, v178
	v_pk_mul_f32 v[182:183], v[182:183], v[184:185]
	v_pk_mul_f32 v[184:185], v[192:193], v[188:189]
	v_pk_mul_f32 v[112:113], v[112:113], v[182:183]
	v_pk_mul_f32 v[114:115], v[114:115], v[184:185]
	v_cvt_f32_ubyte3_e32 v185, v181
	v_cvt_f32_ubyte2_e32 v184, v181
	v_cvt_f32_ubyte1_e32 v183, v181
	v_cvt_f32_ubyte0_e32 v182, v181
	v_pk_add_f32 v[180:181], v[184:185], 0.5 op_sel_hi:[1,0]
	v_add_f32_e32 v156, 0.5, v156
	v_pk_mul_f32 v[180:181], v[180:181], v[190:191]
	v_pk_add_f32 v[182:183], v[182:183], 0.5 op_sel_hi:[1,0]
	v_pk_mul_f32 v[118:119], v[118:119], v[180:181]
	v_rcp_f32_e32 v180, v156
	v_cvt_f32_ubyte0_e32 v156, v179
	v_pk_mul_f32 v[182:183], v[182:183], v[186:187]
	v_add_f32_e32 v156, 0.5, v156
	v_pk_mul_f32 v[116:117], v[116:117], v[182:183]
	v_rcp_f32_e32 v182, v156
	v_cvt_f32_ubyte1_e32 v156, v178
	v_add_f32_e32 v156, 0.5, v156
	v_rcp_f32_e32 v181, v156
	v_cvt_f32_ubyte1_e32 v156, v179
	v_add_f32_e32 v156, 0.5, v156
	v_rcp_f32_e32 v183, v156
	v_cvt_f32_ubyte2_e32 v156, v178
	v_add_f32_e32 v156, 0.5, v156
	v_rcp_f32_e32 v184, v156
	v_cvt_f32_ubyte2_e32 v156, v179
	v_add_f32_e32 v156, 0.5, v156
	v_rcp_f32_e32 v186, v156
	v_cvt_f32_ubyte3_e32 v156, v178
	v_add_f32_e32 v156, 0.5, v156
	v_rcp_f32_e32 v185, v156
	v_cvt_f32_ubyte3_e32 v156, v179
	v_add_f32_e32 v156, 0.5, v156
	v_cvt_f32_ubyte1_e32 v179, v176
	v_cvt_f32_ubyte0_e32 v178, v176
	v_cvt_f32_ubyte3_e32 v189, v176
	v_cvt_f32_ubyte2_e32 v188, v176
	v_rcp_f32_e32 v187, v156
	v_pk_add_f32 v[188:189], v[188:189], 0.5 op_sel_hi:[1,0]
	v_pk_add_f32 v[178:179], v[178:179], 0.5 op_sel_hi:[1,0]
	v_cvt_f32_ubyte0_e32 v156, v146
	v_pk_mul_f32 v[178:179], v[178:179], v[180:181]
	v_pk_mul_f32 v[180:181], v[188:189], v[184:185]
	v_pk_mul_f32 v[88:89], v[88:89], v[178:179]
	v_pk_mul_f32 v[90:91], v[90:91], v[180:181]
	v_cvt_f32_ubyte3_e32 v181, v177
	v_cvt_f32_ubyte2_e32 v180, v177
	v_cvt_f32_ubyte1_e32 v179, v177
	v_cvt_f32_ubyte0_e32 v178, v177
	v_pk_add_f32 v[176:177], v[180:181], 0.5 op_sel_hi:[1,0]
	v_add_f32_e32 v156, 0.5, v156
	v_pk_mul_f32 v[176:177], v[176:177], v[186:187]
	v_pk_add_f32 v[178:179], v[178:179], 0.5 op_sel_hi:[1,0]
	v_pk_mul_f32 v[94:95], v[94:95], v[176:177]
	v_rcp_f32_e32 v176, v156
	v_cvt_f32_ubyte0_e32 v156, v147
	v_pk_mul_f32 v[178:179], v[178:179], v[182:183]
	v_add_f32_e32 v156, 0.5, v156
	v_pk_mul_f32 v[92:93], v[92:93], v[178:179]
	v_rcp_f32_e32 v178, v156
	v_cvt_f32_ubyte1_e32 v156, v146
	v_add_f32_e32 v156, 0.5, v156
	v_rcp_f32_e32 v177, v156
	v_cvt_f32_ubyte1_e32 v156, v147
	v_add_f32_e32 v156, 0.5, v156
	v_rcp_f32_e32 v179, v156
	v_cvt_f32_ubyte2_e32 v156, v146
	v_cvt_f32_ubyte3_e32 v146, v146
	v_add_f32_e32 v156, 0.5, v156
	v_add_f32_e32 v146, 0.5, v146
	v_rcp_f32_e32 v180, v156
	v_rcp_f32_e32 v181, v146
	v_cvt_f32_ubyte3_e32 v146, v147
	v_cvt_f32_ubyte2_e32 v156, v147
	v_add_f32_e32 v146, 0.5, v146
	v_add_f32_e32 v156, 0.5, v156
	v_rcp_f32_e32 v183, v146
	v_cvt_f32_ubyte1_e32 v147, v144
	v_cvt_f32_ubyte0_e32 v146, v144
	v_cvt_f32_ubyte3_e32 v185, v144
	v_cvt_f32_ubyte2_e32 v184, v144
	v_rcp_f32_e32 v182, v156
	v_pk_add_f32 v[184:185], v[184:185], 0.5 op_sel_hi:[1,0]
	v_pk_add_f32 v[146:147], v[146:147], 0.5 op_sel_hi:[1,0]
	v_cvt_f32_ubyte2_e32 v156, v14
	v_pk_mul_f32 v[146:147], v[146:147], v[176:177]
	v_pk_mul_f32 v[176:177], v[184:185], v[180:181]
	v_pk_mul_f32 v[120:121], v[120:121], v[146:147]
	v_pk_mul_f32 v[122:123], v[122:123], v[176:177]
	v_cvt_f32_ubyte3_e32 v177, v145
	v_cvt_f32_ubyte2_e32 v176, v145
	v_cvt_f32_ubyte1_e32 v147, v145
	v_cvt_f32_ubyte0_e32 v146, v145
	v_pk_add_f32 v[144:145], v[176:177], 0.5 op_sel_hi:[1,0]
	v_pk_add_f32 v[146:147], v[146:147], 0.5 op_sel_hi:[1,0]
	v_pk_mul_f32 v[144:145], v[144:145], v[182:183]
	v_pk_mul_f32 v[146:147], v[146:147], v[178:179]
	v_pk_mul_f32 v[126:127], v[126:127], v[144:145]
	v_cvt_f32_ubyte0_e32 v145, v15
	v_add_f32_e32 v145, 0.5, v145
	v_pk_mul_f32 v[124:125], v[124:125], v[146:147]
	v_cvt_f32_ubyte0_e32 v144, v14
	v_rcp_f32_e32 v146, v145
	v_cvt_f32_ubyte1_e32 v145, v14
	v_cvt_f32_ubyte3_e32 v14, v14
	v_add_f32_e32 v144, 0.5, v144
	v_add_f32_e32 v145, 0.5, v145
	v_add_f32_e32 v156, 0.5, v156
	v_add_f32_e32 v14, 0.5, v14
	v_rcp_f32_e32 v144, v144
	v_rcp_f32_e32 v145, v145
	v_rcp_f32_e32 v176, v156
	v_rcp_f32_e32 v177, v14
	v_cvt_f32_ubyte3_e32 v14, v15
	v_cvt_f32_ubyte2_e32 v156, v15
	v_add_f32_e32 v14, 0.5, v14
	v_cvt_f32_ubyte1_e32 v147, v15
	v_add_f32_e32 v156, 0.5, v156
	v_rcp_f32_e32 v179, v14
	v_cvt_f32_ubyte1_e32 v15, v12
	v_cvt_f32_ubyte0_e32 v14, v12
	v_cvt_f32_ubyte3_e32 v181, v12
	v_cvt_f32_ubyte2_e32 v180, v12
	v_rcp_f32_e32 v178, v156
	v_pk_add_f32 v[180:181], v[180:181], 0.5 op_sel_hi:[1,0]
	v_pk_add_f32 v[14:15], v[14:15], 0.5 op_sel_hi:[1,0]
	v_add_f32_e32 v147, 0.5, v147
	v_pk_mul_f32 v[14:15], v[14:15], v[144:145]
	v_pk_mul_f32 v[144:145], v[180:181], v[176:177]
	v_rcp_f32_e32 v147, v147
	v_pk_mul_f32 v[98:99], v[98:99], v[144:145]
	v_cvt_f32_ubyte3_e32 v145, v13
	v_cvt_f32_ubyte2_e32 v144, v13
	v_pk_mul_f32 v[96:97], v[96:97], v[14:15]
	v_cvt_f32_ubyte1_e32 v15, v13
	v_cvt_f32_ubyte0_e32 v14, v13
	v_pk_add_f32 v[12:13], v[144:145], 0.5 op_sel_hi:[1,0]
	v_pk_add_f32 v[14:15], v[14:15], 0.5 op_sel_hi:[1,0]
	v_pk_mul_f32 v[12:13], v[12:13], v[178:179]
	v_pk_mul_f32 v[14:15], v[14:15], v[146:147]
	v_pk_mul_f32 v[102:103], v[102:103], v[12:13]
	v_cvt_f32_ubyte0_e32 v13, v11
	v_add_f32_e32 v13, 0.5, v13
	v_pk_mul_f32 v[100:101], v[100:101], v[14:15]
	v_cvt_f32_ubyte0_e32 v12, v10
	v_rcp_f32_e32 v14, v13
	v_cvt_f32_ubyte1_e32 v13, v10
	v_cvt_f32_ubyte2_e32 v144, v10
	v_cvt_f32_ubyte2_e32 v145, v11
	v_cvt_f32_ubyte3_e32 v10, v10
	v_add_f32_e32 v12, 0.5, v12
	v_add_f32_e32 v13, 0.5, v13
	v_add_f32_e32 v144, 0.5, v144
	v_add_f32_e32 v145, 0.5, v145
	v_add_f32_e32 v10, 0.5, v10
	v_rcp_f32_e32 v12, v12
	v_rcp_f32_e32 v13, v13
	v_rcp_f32_e32 v144, v144
	v_rcp_f32_e32 v146, v145
	v_rcp_f32_e32 v145, v10
	v_cvt_f32_ubyte3_e32 v10, v11
	v_add_f32_e32 v10, 0.5, v10
	v_cvt_f32_ubyte1_e32 v15, v11
	v_rcp_f32_e32 v147, v10
	v_cvt_f32_ubyte1_e32 v11, v8
	v_cvt_f32_ubyte0_e32 v10, v8
	v_cvt_f32_ubyte3_e32 v177, v8
	v_cvt_f32_ubyte2_e32 v176, v8
	v_pk_add_f32 v[176:177], v[176:177], 0.5 op_sel_hi:[1,0]
	v_pk_add_f32 v[10:11], v[10:11], 0.5 op_sel_hi:[1,0]
	v_add_f32_e32 v15, 0.5, v15
	v_pk_mul_f32 v[10:11], v[10:11], v[12:13]
	v_pk_mul_f32 v[12:13], v[176:177], v[144:145]
	v_rcp_f32_e32 v15, v15
	v_pk_mul_f32 v[130:131], v[130:131], v[12:13]
	v_cvt_f32_ubyte3_e32 v13, v9
	v_cvt_f32_ubyte2_e32 v12, v9
	v_pk_mul_f32 v[128:129], v[128:129], v[10:11]
	v_cvt_f32_ubyte1_e32 v11, v9
	v_cvt_f32_ubyte0_e32 v10, v9
	v_pk_add_f32 v[8:9], v[12:13], 0.5 op_sel_hi:[1,0]
	v_pk_add_f32 v[10:11], v[10:11], 0.5 op_sel_hi:[1,0]
	v_pk_mul_f32 v[8:9], v[8:9], v[146:147]
	v_pk_mul_f32 v[10:11], v[10:11], v[14:15]
	v_pk_mul_f32 v[134:135], v[134:135], v[8:9]
	v_cvt_f32_ubyte0_e32 v9, v5
	v_add_f32_e32 v9, 0.5, v9
	v_pk_mul_f32 v[132:133], v[132:133], v[10:11]
	v_cvt_f32_ubyte0_e32 v8, v4
	v_rcp_f32_e32 v10, v9
	v_cvt_f32_ubyte1_e32 v9, v4
	v_cvt_f32_ubyte2_e32 v12, v4
	v_cvt_f32_ubyte2_e32 v13, v5
	v_cvt_f32_ubyte3_e32 v4, v4
	v_add_f32_e32 v8, 0.5, v8
	v_add_f32_e32 v9, 0.5, v9
	v_add_f32_e32 v12, 0.5, v12
	v_add_f32_e32 v13, 0.5, v13
	v_add_f32_e32 v4, 0.5, v4
	v_rcp_f32_e32 v8, v8
	v_rcp_f32_e32 v9, v9
	v_rcp_f32_e32 v12, v12
	v_rcp_f32_e32 v14, v13
	v_rcp_f32_e32 v13, v4
	v_cvt_f32_ubyte3_e32 v4, v5
	v_add_f32_e32 v4, 0.5, v4
	v_cvt_f32_ubyte1_e32 v11, v5
	v_rcp_f32_e32 v15, v4
	v_cvt_f32_ubyte1_e32 v5, v2
	v_cvt_f32_ubyte0_e32 v4, v2
	v_cvt_f32_ubyte3_e32 v145, v2
	v_cvt_f32_ubyte2_e32 v144, v2
	v_pk_add_f32 v[144:145], v[144:145], 0.5 op_sel_hi:[1,0]
	v_pk_add_f32 v[4:5], v[4:5], 0.5 op_sel_hi:[1,0]
	v_add_f32_e32 v11, 0.5, v11
	v_pk_mul_f32 v[4:5], v[4:5], v[8:9]
	v_pk_mul_f32 v[8:9], v[144:145], v[12:13]
	v_rcp_f32_e32 v11, v11
	v_pk_mul_f32 v[106:107], v[106:107], v[8:9]
	v_cvt_f32_ubyte3_e32 v9, v3
	v_cvt_f32_ubyte2_e32 v8, v3
	v_pk_mul_f32 v[104:105], v[104:105], v[4:5]
	v_cvt_f32_ubyte1_e32 v5, v3
	v_cvt_f32_ubyte0_e32 v4, v3
	v_pk_add_f32 v[2:3], v[8:9], 0.5 op_sel_hi:[1,0]
	v_pk_add_f32 v[4:5], v[4:5], 0.5 op_sel_hi:[1,0]
	v_pk_mul_f32 v[2:3], v[2:3], v[14:15]
	v_pk_mul_f32 v[4:5], v[4:5], v[10:11]
	v_pk_mul_f32 v[110:111], v[110:111], v[2:3]
	v_cvt_f32_ubyte0_e32 v3, v7
	v_add_f32_e32 v3, 0.5, v3
	v_pk_mul_f32 v[108:109], v[108:109], v[4:5]
	v_cvt_f32_ubyte0_e32 v2, v6
	v_rcp_f32_e32 v4, v3
	v_cvt_f32_ubyte1_e32 v3, v6
	v_cvt_f32_ubyte2_e32 v8, v6
	v_cvt_f32_ubyte2_e32 v9, v7
	v_cvt_f32_ubyte3_e32 v6, v6
	v_add_f32_e32 v2, 0.5, v2
	v_add_f32_e32 v3, 0.5, v3
	v_add_f32_e32 v8, 0.5, v8
	v_add_f32_e32 v9, 0.5, v9
	v_add_f32_e32 v6, 0.5, v6
	v_rcp_f32_e32 v2, v2
	v_rcp_f32_e32 v3, v3
	v_rcp_f32_e32 v8, v8
	v_rcp_f32_e32 v10, v9
	v_rcp_f32_e32 v9, v6
	v_cvt_f32_ubyte3_e32 v6, v7
	v_cvt_f32_ubyte1_e32 v5, v7
	v_add_f32_e32 v6, 0.5, v6
	v_add_f32_e32 v5, 0.5, v5
	v_rcp_f32_e32 v11, v6
	v_cvt_f32_ubyte1_e32 v7, v0
	v_cvt_f32_ubyte0_e32 v6, v0
	v_cvt_f32_ubyte3_e32 v13, v0
	v_cvt_f32_ubyte2_e32 v12, v0
	v_rcp_f32_e32 v5, v5
	v_pk_add_f32 v[12:13], v[12:13], 0.5 op_sel_hi:[1,0]
	v_pk_add_f32 v[6:7], v[6:7], 0.5 op_sel_hi:[1,0]
	s_nop 0
	v_pk_mul_f32 v[2:3], v[6:7], v[2:3]
	v_pk_mul_f32 v[6:7], v[12:13], v[8:9]
	v_pk_mul_f32 v[144:145], v[136:137], v[2:3]
	v_pk_mul_f32 v[146:147], v[138:139], v[6:7]
	v_cvt_f32_ubyte1_e32 v3, v1
	v_cvt_f32_ubyte0_e32 v2, v1
	v_cvt_f32_ubyte3_e32 v7, v1
	v_cvt_f32_ubyte2_e32 v6, v1
	v_pk_add_f32 v[0:1], v[6:7], 0.5 op_sel_hi:[1,0]
	v_pk_add_f32 v[2:3], v[2:3], 0.5 op_sel_hi:[1,0]
	v_pk_mul_f32 v[0:1], v[0:1], v[10:11]
	v_pk_mul_f32 v[2:3], v[2:3], v[4:5]
	v_pk_mul_f32 v[138:139], v[142:143], v[0:1]
	v_pk_mul_f32 v[136:137], v[140:141], v[2:3]
	ds_read_b128 v[8:11], v230
	ds_read_b128 v[12:15], v230 offset:1024
	ds_read_b128 v[0:3], v230 offset:2048
	ds_read_b128 v[4:7], v230 offset:3072
	s_add_u32 s54, s46, 0x40680
	s_addc_u32 s55, s47, 0
	s_mov_b32 m0, s92
	v_lshl_add_u64 v[140:141], s[54:55], 0, v[148:149]
	ds_read_b128 v[176:179], v227
	ds_read_b128 v[180:183], v227 offset:1024
	ds_read_b128 v[184:187], v227 offset:2048
	ds_read_b128 v[188:191], v227 offset:3072
	ds_read_b128 v[192:195], v227 offset:4096
	ds_read_b128 v[196:199], v227 offset:5120
	ds_read_b128 v[200:203], v227 offset:6144
	ds_read_b128 v[204:207], v227 offset:7168
	global_load_lds_dwordx4 v[140:141], off
	v_lshl_add_u64 v[140:141], s[54:55], 0, v[152:153]
	s_mov_b32 m0, s91
	s_nop 0
	global_load_lds_dwordx4 v[140:141], off
	s_waitcnt lgkmcnt(8)
	s_barrier
	s_waitcnt lgkmcnt(0)
	s_setprio 1
	s_waitcnt lgkmcnt(0)
	v_mfma_scale_f32_16x16x128_f8f6f4 v[16:19], v[8:15], v[176:183], v[16:19], v224, v224 op_sel_hi:[0,0,0]
	v_mfma_scale_f32_16x16x128_f8f6f4 v[20:23], v[0:7], v[176:183], v[20:23], v224, v224 op_sel_hi:[0,0,0]
	v_mfma_scale_f32_16x16x128_f8f6f4 v[24:27], v[8:15], v[184:191], v[24:27], v224, v224 op_sel_hi:[0,0,0]
	v_mfma_scale_f32_16x16x128_f8f6f4 v[28:31], v[0:7], v[184:191], v[28:31], v224, v224 op_sel_hi:[0,0,0]
	v_mfma_scale_f32_16x16x128_f8f6f4 v[32:35], v[8:15], v[192:199], v[32:35], v224, v224 op_sel_hi:[0,0,0]
	v_mfma_scale_f32_16x16x128_f8f6f4 v[36:39], v[0:7], v[192:199], v[36:39], v224, v224 op_sel_hi:[0,0,0]
	v_mfma_scale_f32_16x16x128_f8f6f4 v[40:43], v[8:15], v[200:207], v[40:43], v224, v224 op_sel_hi:[0,0,0]
	v_mfma_scale_f32_16x16x128_f8f6f4 v[44:47], v[0:7], v[200:207], v[44:47], v224, v224 op_sel_hi:[0,0,0]
	s_setprio 0
	s_barrier
	s_mov_b32 m0, s94
	v_lshl_add_u64 v[140:141], v[170:171], 0, s[28:29]
	ds_read_b128 v[208:211], v231
	ds_read_b128 v[212:215], v231 offset:1024
	ds_read_b128 v[236:239], v231 offset:2048
	ds_read_b128 v[240:243], v231 offset:3072
	global_load_lds_dwordx4 v[140:141], off
	v_lshl_add_u64 v[140:141], v[172:173], 0, s[28:29]
	s_mov_b32 m0, s93
	s_nop 0
	global_load_lds_dwordx4 v[140:141], off
	s_barrier
	s_waitcnt lgkmcnt(0)
	s_setprio 1
	s_waitcnt lgkmcnt(0)
	v_mfma_scale_f32_16x16x128_f8f6f4 v[48:51], v[208:215], v[176:183], v[48:51], v224, v224 op_sel_hi:[0,0,0]
	v_mfma_scale_f32_16x16x128_f8f6f4 v[52:55], v[236:243], v[176:183], v[52:55], v224, v224 op_sel_hi:[0,0,0]
	v_mfma_scale_f32_16x16x128_f8f6f4 v[56:59], v[208:215], v[184:191], v[56:59], v224, v224 op_sel_hi:[0,0,0]
	v_mfma_scale_f32_16x16x128_f8f6f4 v[60:63], v[236:243], v[184:191], v[60:63], v224, v224 op_sel_hi:[0,0,0]
	v_mfma_scale_f32_16x16x128_f8f6f4 v[64:67], v[208:215], v[192:199], v[64:67], v224, v224 op_sel_hi:[0,0,0]
	v_mfma_scale_f32_16x16x128_f8f6f4 v[68:71], v[236:243], v[192:199], v[68:71], v224, v224 op_sel_hi:[0,0,0]
	v_mfma_scale_f32_16x16x128_f8f6f4 v[72:75], v[208:215], v[200:207], v[72:75], v224, v224 op_sel_hi:[0,0,0]
	v_mfma_scale_f32_16x16x128_f8f6f4 v[76:79], v[236:243], v[200:207], v[76:79], v224, v224 op_sel_hi:[0,0,0]
	s_setprio 0
	s_mov_b32 m0, s70
	v_lshl_add_u64 v[140:141], v[174:175], 0, s[28:29]
	s_barrier
	ds_read_b128 v[176:179], v227 offset:16384
	ds_read_b128 v[180:183], v227 offset:17408
	ds_read_b128 v[184:187], v227 offset:18432
	ds_read_b128 v[188:191], v227 offset:19456
	ds_read_b128 v[192:195], v227 offset:20480
	ds_read_b128 v[196:199], v227 offset:21504
	ds_read_b128 v[200:203], v227 offset:22528
	ds_read_b128 v[204:207], v227 offset:23552
	global_load_lds_dwordx4 v[140:141], off
	v_lshl_add_u64 v[140:141], v[168:169], 0, s[28:29]
	s_mov_b32 m0, s71
	s_nop 0
	global_load_lds_dwordx4 v[140:141], off
	s_barrier
	s_waitcnt lgkmcnt(0)
	s_setprio 1
	s_waitcnt lgkmcnt(0)
	v_mfma_scale_f32_16x16x128_f8f6f4 v[80:83], v[8:15], v[176:183], v[80:83], v224, v224 op_sel_hi:[0,0,0]
	v_mfma_scale_f32_16x16x128_f8f6f4 v[84:87], v[0:7], v[176:183], v[84:87], v224, v224 op_sel_hi:[0,0,0]
	v_mfma_scale_f32_16x16x128_f8f6f4 v[88:91], v[8:15], v[184:191], v[88:91], v224, v224 op_sel_hi:[0,0,0]
	v_mfma_scale_f32_16x16x128_f8f6f4 v[92:95], v[0:7], v[184:191], v[92:95], v224, v224 op_sel_hi:[0,0,0]
	v_mfma_scale_f32_16x16x128_f8f6f4 v[96:99], v[8:15], v[192:199], v[96:99], v224, v224 op_sel_hi:[0,0,0]
	v_mfma_scale_f32_16x16x128_f8f6f4 v[100:103], v[0:7], v[192:199], v[100:103], v224, v224 op_sel_hi:[0,0,0]
	v_mfma_scale_f32_16x16x128_f8f6f4 v[104:107], v[8:15], v[200:207], v[104:107], v224, v224 op_sel_hi:[0,0,0]
	v_mfma_scale_f32_16x16x128_f8f6f4 v[108:111], v[0:7], v[200:207], v[108:111], v224, v224 op_sel_hi:[0,0,0]
	s_setprio 0
	s_barrier
	s_add_u32 s54, s48, 0x40700
	s_addc_u32 s55, s49, 0
	s_mov_b32 m0, s52
	v_lshl_add_u64 v[0:1], s[54:55], 0, v[150:151]
	global_load_lds_dwordx4 v[0:1], off
	v_lshl_add_u64 v[0:1], s[54:55], 0, v[154:155]
	s_mov_b32 m0, s95
	s_nop 0
	global_load_lds_dwordx4 v[0:1], off
	s_waitcnt vmcnt(6)
	s_barrier
	s_setprio 1
	v_mfma_scale_f32_16x16x128_f8f6f4 v[112:115], v[208:215], v[176:183], v[112:115], v224, v224 op_sel_hi:[0,0,0]
	v_mfma_scale_f32_16x16x128_f8f6f4 v[116:119], v[236:243], v[176:183], v[116:119], v224, v224 op_sel_hi:[0,0,0]
	v_mfma_scale_f32_16x16x128_f8f6f4 v[120:123], v[208:215], v[184:191], v[120:123], v224, v224 op_sel_hi:[0,0,0]
	v_mfma_scale_f32_16x16x128_f8f6f4 v[124:127], v[236:243], v[184:191], v[124:127], v224, v224 op_sel_hi:[0,0,0]
	v_mfma_scale_f32_16x16x128_f8f6f4 v[128:131], v[208:215], v[192:199], v[128:131], v224, v224 op_sel_hi:[0,0,0]
	v_mfma_scale_f32_16x16x128_f8f6f4 v[132:135], v[236:243], v[192:199], v[132:135], v224, v224 op_sel_hi:[0,0,0]
	v_mfma_scale_f32_16x16x128_f8f6f4 v[144:147], v[208:215], v[200:207], v[144:147], v224, v224 op_sel_hi:[0,0,0]
	v_mfma_scale_f32_16x16x128_f8f6f4 v[136:139], v[236:243], v[200:207], v[136:139], v224, v224 op_sel_hi:[0,0,0]
	s_setprio 0
	s_barrier
	ds_read_b128 v[0:3], v234
	ds_read_b128 v[4:7], v234 offset:1024
	ds_read_b128 v[8:11], v234 offset:2048
	ds_read_b128 v[12:15], v234 offset:3072
	s_add_u32 s54, s46, 0x40700
	s_addc_u32 s55, s47, 0
	s_mov_b32 m0, s72
	v_lshl_add_u64 v[140:141], s[54:55], 0, v[148:149]
	ds_read_b128 v[176:179], v227 offset:32768
	ds_read_b128 v[180:183], v227 offset:33792
	ds_read_b128 v[184:187], v227 offset:34816
	ds_read_b128 v[188:191], v227 offset:35840
	ds_read_b128 v[192:195], v227 offset:36864
	ds_read_b128 v[196:199], v227 offset:37888
	ds_read_b128 v[200:203], v227 offset:38912
	ds_read_b128 v[204:207], v227 offset:39936
	global_load_lds_dwordx4 v[140:141], off
	v_lshl_add_u64 v[140:141], s[54:55], 0, v[152:153]
	s_mov_b32 m0, s73
	s_nop 0
	global_load_lds_dwordx4 v[140:141], off
	s_waitcnt lgkmcnt(8)
	s_barrier
	s_waitcnt lgkmcnt(0)
	s_setprio 1
	s_waitcnt lgkmcnt(0)
	v_mfma_scale_f32_16x16x128_f8f6f4 v[16:19], v[0:7], v[176:183], v[16:19], v224, v224 op_sel_hi:[0,0,0]
	v_mfma_scale_f32_16x16x128_f8f6f4 v[20:23], v[8:15], v[176:183], v[20:23], v224, v224 op_sel_hi:[0,0,0]
	v_mfma_scale_f32_16x16x128_f8f6f4 v[24:27], v[0:7], v[184:191], v[24:27], v224, v224 op_sel_hi:[0,0,0]
	v_mfma_scale_f32_16x16x128_f8f6f4 v[28:31], v[8:15], v[184:191], v[28:31], v224, v224 op_sel_hi:[0,0,0]
	v_mfma_scale_f32_16x16x128_f8f6f4 v[32:35], v[0:7], v[192:199], v[32:35], v224, v224 op_sel_hi:[0,0,0]
	v_mfma_scale_f32_16x16x128_f8f6f4 v[36:39], v[8:15], v[192:199], v[36:39], v224, v224 op_sel_hi:[0,0,0]
	v_mfma_scale_f32_16x16x128_f8f6f4 v[40:43], v[0:7], v[200:207], v[40:43], v224, v224 op_sel_hi:[0,0,0]
	v_mfma_scale_f32_16x16x128_f8f6f4 v[44:47], v[8:15], v[200:207], v[44:47], v224, v224 op_sel_hi:[0,0,0]
	s_setprio 0
	s_barrier
	s_mov_b32 m0, s63
	v_lshl_add_u64 v[140:141], v[170:171], 0, s[30:31]
	ds_read_b128 v[208:211], v233
	ds_read_b128 v[212:215], v233 offset:1024
	ds_read_b128 v[236:239], v233 offset:2048
	ds_read_b128 v[240:243], v233 offset:3072
	global_load_lds_dwordx4 v[140:141], off
	v_lshl_add_u64 v[140:141], v[172:173], 0, s[30:31]
	s_mov_b32 m0, s62
	s_nop 0
	global_load_lds_dwordx4 v[140:141], off
	s_barrier
	s_waitcnt lgkmcnt(0)
	s_setprio 1
	s_waitcnt lgkmcnt(0)
	v_mfma_scale_f32_16x16x128_f8f6f4 v[48:51], v[208:215], v[176:183], v[48:51], v224, v224 op_sel_hi:[0,0,0]
	v_mfma_scale_f32_16x16x128_f8f6f4 v[52:55], v[236:243], v[176:183], v[52:55], v224, v224 op_sel_hi:[0,0,0]
	v_mfma_scale_f32_16x16x128_f8f6f4 v[56:59], v[208:215], v[184:191], v[56:59], v224, v224 op_sel_hi:[0,0,0]
	v_mfma_scale_f32_16x16x128_f8f6f4 v[60:63], v[236:243], v[184:191], v[60:63], v224, v224 op_sel_hi:[0,0,0]
	v_mfma_scale_f32_16x16x128_f8f6f4 v[64:67], v[208:215], v[192:199], v[64:67], v224, v224 op_sel_hi:[0,0,0]
	v_mfma_scale_f32_16x16x128_f8f6f4 v[68:71], v[236:243], v[192:199], v[68:71], v224, v224 op_sel_hi:[0,0,0]
	v_mfma_scale_f32_16x16x128_f8f6f4 v[72:75], v[208:215], v[200:207], v[72:75], v224, v224 op_sel_hi:[0,0,0]
	v_mfma_scale_f32_16x16x128_f8f6f4 v[76:79], v[236:243], v[200:207], v[76:79], v224, v224 op_sel_hi:[0,0,0]
	s_setprio 0
	s_mov_b32 m0, s77
	v_lshl_add_u64 v[140:141], v[174:175], 0, s[30:31]
	s_barrier
	ds_read_b128 v[176:179], v227 offset:49152
	ds_read_b128 v[180:183], v227 offset:50176
	ds_read_b128 v[184:187], v227 offset:51200
	ds_read_b128 v[188:191], v227 offset:52224
	ds_read_b128 v[192:195], v227 offset:53248
	ds_read_b128 v[196:199], v227 offset:54272
	ds_read_b128 v[200:203], v227 offset:55296
	ds_read_b128 v[204:207], v227 offset:56320
	global_load_lds_dwordx4 v[140:141], off
	v_lshl_add_u64 v[140:141], v[168:169], 0, s[30:31]
	s_mov_b32 m0, s78
	s_nop 0
	global_load_lds_dwordx4 v[140:141], off
	s_barrier
	s_waitcnt lgkmcnt(0)
	s_setprio 1
	s_waitcnt lgkmcnt(0)
	v_mfma_scale_f32_16x16x128_f8f6f4 v[80:83], v[0:7], v[176:183], v[80:83], v224, v224 op_sel_hi:[0,0,0]
	v_mfma_scale_f32_16x16x128_f8f6f4 v[84:87], v[8:15], v[176:183], v[84:87], v224, v224 op_sel_hi:[0,0,0]
	v_mfma_scale_f32_16x16x128_f8f6f4 v[88:91], v[0:7], v[184:191], v[88:91], v224, v224 op_sel_hi:[0,0,0]
	v_mfma_scale_f32_16x16x128_f8f6f4 v[92:95], v[8:15], v[184:191], v[92:95], v224, v224 op_sel_hi:[0,0,0]
	v_mfma_scale_f32_16x16x128_f8f6f4 v[96:99], v[0:7], v[192:199], v[96:99], v224, v224 op_sel_hi:[0,0,0]
	v_mfma_scale_f32_16x16x128_f8f6f4 v[100:103], v[8:15], v[192:199], v[100:103], v224, v224 op_sel_hi:[0,0,0]
	v_mfma_scale_f32_16x16x128_f8f6f4 v[104:107], v[0:7], v[200:207], v[104:107], v224, v224 op_sel_hi:[0,0,0]
	v_mfma_scale_f32_16x16x128_f8f6f4 v[108:111], v[8:15], v[200:207], v[108:111], v224, v224 op_sel_hi:[0,0,0]
	s_setprio 0
	s_barrier
	s_add_u32 s48, s48, 0x40780
	s_addc_u32 s49, s49, 0
	s_mov_b32 m0, s64
	v_lshl_add_u64 v[0:1], s[48:49], 0, v[150:151]
	global_load_lds_dwordx4 v[0:1], off
	v_lshl_add_u64 v[0:1], s[48:49], 0, v[154:155]
	s_mov_b32 m0, s53
	s_nop 0
	global_load_lds_dwordx4 v[0:1], off
	s_waitcnt vmcnt(6)
	s_barrier
	s_setprio 1
	v_mfma_scale_f32_16x16x128_f8f6f4 v[112:115], v[208:215], v[176:183], v[112:115], v224, v224 op_sel_hi:[0,0,0]
	v_mfma_scale_f32_16x16x128_f8f6f4 v[116:119], v[236:243], v[176:183], v[116:119], v224, v224 op_sel_hi:[0,0,0]
	v_mfma_scale_f32_16x16x128_f8f6f4 v[120:123], v[208:215], v[184:191], v[120:123], v224, v224 op_sel_hi:[0,0,0]
	v_mfma_scale_f32_16x16x128_f8f6f4 v[124:127], v[236:243], v[184:191], v[124:127], v224, v224 op_sel_hi:[0,0,0]
	v_mfma_scale_f32_16x16x128_f8f6f4 v[128:131], v[208:215], v[192:199], v[128:131], v224, v224 op_sel_hi:[0,0,0]
	v_mfma_scale_f32_16x16x128_f8f6f4 v[132:135], v[236:243], v[192:199], v[132:135], v224, v224 op_sel_hi:[0,0,0]
	v_mfma_scale_f32_16x16x128_f8f6f4 v[144:147], v[208:215], v[200:207], v[144:147], v224, v224 op_sel_hi:[0,0,0]
	v_mfma_scale_f32_16x16x128_f8f6f4 v[136:139], v[236:243], v[200:207], v[136:139], v224, v224 op_sel_hi:[0,0,0]
	s_setprio 0
	s_barrier
	ds_read_b128 v[8:11], v230
	ds_read_b128 v[12:15], v230 offset:1024
	ds_read_b128 v[168:171], v230 offset:2048
	ds_read_b128 v[172:175], v230 offset:3072
	s_add_u32 s46, s46, 0x40780
	s_addc_u32 s47, s47, 0
	s_mov_b32 m0, s92
	v_lshl_add_u64 v[0:1], s[46:47], 0, v[148:149]
	ds_read_b128 v[176:179], v227
	ds_read_b128 v[180:183], v227 offset:1024
	ds_read_b128 v[184:187], v227 offset:2048
	ds_read_b128 v[188:191], v227 offset:3072
	ds_read_b128 v[192:195], v227 offset:4096
	ds_read_b128 v[196:199], v227 offset:5120
	ds_read_b128 v[200:203], v227 offset:6144
	ds_read_b128 v[204:207], v227 offset:7168
	global_load_lds_dwordx4 v[0:1], off
	v_lshl_add_u64 v[0:1], s[46:47], 0, v[152:153]
	s_mov_b32 m0, s91
	s_nop 0
	global_load_lds_dwordx4 v[0:1], off
	s_waitcnt lgkmcnt(8)
	s_barrier
	s_waitcnt lgkmcnt(0)
	s_setprio 1
	s_waitcnt lgkmcnt(0)
	v_mfma_scale_f32_16x16x128_f8f6f4 v[16:19], v[8:15], v[176:183], v[16:19], v224, v224 op_sel_hi:[0,0,0]
	v_mfma_scale_f32_16x16x128_f8f6f4 v[20:23], v[168:175], v[176:183], v[20:23], v224, v224 op_sel_hi:[0,0,0]
	v_mfma_scale_f32_16x16x128_f8f6f4 v[24:27], v[8:15], v[184:191], v[24:27], v224, v224 op_sel_hi:[0,0,0]
	v_mfma_scale_f32_16x16x128_f8f6f4 v[28:31], v[168:175], v[184:191], v[28:31], v224, v224 op_sel_hi:[0,0,0]
	v_mfma_scale_f32_16x16x128_f8f6f4 v[32:35], v[8:15], v[192:199], v[32:35], v224, v224 op_sel_hi:[0,0,0]
	v_mfma_scale_f32_16x16x128_f8f6f4 v[36:39], v[168:175], v[192:199], v[36:39], v224, v224 op_sel_hi:[0,0,0]
	v_mfma_scale_f32_16x16x128_f8f6f4 v[40:43], v[8:15], v[200:207], v[40:43], v224, v224 op_sel_hi:[0,0,0]
	v_mfma_scale_f32_16x16x128_f8f6f4 v[44:47], v[168:175], v[200:207], v[44:47], v224, v224 op_sel_hi:[0,0,0]
	s_setprio 0
	s_barrier
	s_mov_b32 m0, s94
	v_lshl_add_u64 v[0:1], s[58:59], 0, v[150:151]
	ds_read_b128 v[208:211], v231
	ds_read_b128 v[212:215], v231 offset:1024
	ds_read_b128 v[236:239], v231 offset:2048
	ds_read_b128 v[240:243], v231 offset:3072
	global_load_lds_dwordx4 v[0:1], off
	v_lshl_add_u64 v[2:3], s[58:59], 0, v[154:155]
	s_mov_b32 m0, s93
	s_nop 0
	global_load_lds_dwordx4 v[2:3], off
	s_barrier
	s_waitcnt lgkmcnt(0)
	s_setprio 1
	s_waitcnt lgkmcnt(0)
	v_mfma_scale_f32_16x16x128_f8f6f4 v[48:51], v[208:215], v[176:183], v[48:51], v224, v224 op_sel_hi:[0,0,0]
	v_mfma_scale_f32_16x16x128_f8f6f4 v[52:55], v[236:243], v[176:183], v[52:55], v224, v224 op_sel_hi:[0,0,0]
	v_mfma_scale_f32_16x16x128_f8f6f4 v[56:59], v[208:215], v[184:191], v[56:59], v224, v224 op_sel_hi:[0,0,0]
	v_mfma_scale_f32_16x16x128_f8f6f4 v[60:63], v[236:243], v[184:191], v[60:63], v224, v224 op_sel_hi:[0,0,0]
	v_mfma_scale_f32_16x16x128_f8f6f4 v[64:67], v[208:215], v[192:199], v[64:67], v224, v224 op_sel_hi:[0,0,0]
	v_mfma_scale_f32_16x16x128_f8f6f4 v[68:71], v[236:243], v[192:199], v[68:71], v224, v224 op_sel_hi:[0,0,0]
	v_mfma_scale_f32_16x16x128_f8f6f4 v[72:75], v[208:215], v[200:207], v[72:75], v224, v224 op_sel_hi:[0,0,0]
	v_mfma_scale_f32_16x16x128_f8f6f4 v[76:79], v[236:243], v[200:207], v[76:79], v224, v224 op_sel_hi:[0,0,0]
	s_setprio 0
	s_mov_b32 m0, s70
	v_lshl_add_u64 v[4:5], s[50:51], 0, v[148:149]
	s_barrier
	ds_read_b128 v[176:179], v227 offset:16384
	ds_read_b128 v[180:183], v227 offset:17408
	ds_read_b128 v[184:187], v227 offset:18432
	ds_read_b128 v[188:191], v227 offset:19456
	ds_read_b128 v[192:195], v227 offset:20480
	ds_read_b128 v[196:199], v227 offset:21504
	ds_read_b128 v[200:203], v227 offset:22528
	ds_read_b128 v[204:207], v227 offset:23552
	global_load_lds_dwordx4 v[4:5], off
	v_lshl_add_u64 v[6:7], s[50:51], 0, v[152:153]
	s_mov_b32 m0, s71
	s_nop 0
	global_load_lds_dwordx4 v[6:7], off
	s_barrier
	s_waitcnt lgkmcnt(0)
	s_setprio 1
	s_waitcnt lgkmcnt(0)
	v_mfma_scale_f32_16x16x128_f8f6f4 v[80:83], v[8:15], v[176:183], v[80:83], v224, v224 op_sel_hi:[0,0,0]
	v_mfma_scale_f32_16x16x128_f8f6f4 v[84:87], v[168:175], v[176:183], v[84:87], v224, v224 op_sel_hi:[0,0,0]
	v_mfma_scale_f32_16x16x128_f8f6f4 v[88:91], v[8:15], v[184:191], v[88:91], v224, v224 op_sel_hi:[0,0,0]
	v_mfma_scale_f32_16x16x128_f8f6f4 v[92:95], v[168:175], v[184:191], v[92:95], v224, v224 op_sel_hi:[0,0,0]
	v_mfma_scale_f32_16x16x128_f8f6f4 v[96:99], v[8:15], v[192:199], v[96:99], v224, v224 op_sel_hi:[0,0,0]
	v_mfma_scale_f32_16x16x128_f8f6f4 v[100:103], v[168:175], v[192:199], v[100:103], v224, v224 op_sel_hi:[0,0,0]
	v_mfma_scale_f32_16x16x128_f8f6f4 v[104:107], v[8:15], v[200:207], v[104:107], v224, v224 op_sel_hi:[0,0,0]
	v_mfma_scale_f32_16x16x128_f8f6f4 v[108:111], v[168:175], v[200:207], v[108:111], v224, v224 op_sel_hi:[0,0,0]
	s_setprio 0
	s_barrier
	s_add_u32 s46, s58, 0x40000
	s_addc_u32 s47, s59, 0
	s_mov_b32 m0, s52
	v_lshl_add_u64 v[8:9], s[46:47], 0, v[150:151]
	global_load_lds_dwordx4 v[8:9], off
	v_lshl_add_u64 v[8:9], s[46:47], 0, v[154:155]
	s_mov_b32 m0, s95
	s_nop 0
	global_load_lds_dwordx4 v[8:9], off
	s_waitcnt vmcnt(6)
	s_barrier
	s_setprio 1
	v_mfma_scale_f32_16x16x128_f8f6f4 v[112:115], v[208:215], v[176:183], v[112:115], v224, v224 op_sel_hi:[0,0,0]
	v_mfma_scale_f32_16x16x128_f8f6f4 v[116:119], v[236:243], v[176:183], v[116:119], v224, v224 op_sel_hi:[0,0,0]
	v_mfma_scale_f32_16x16x128_f8f6f4 v[120:123], v[208:215], v[184:191], v[120:123], v224, v224 op_sel_hi:[0,0,0]
	v_mfma_scale_f32_16x16x128_f8f6f4 v[124:127], v[236:243], v[184:191], v[124:127], v224, v224 op_sel_hi:[0,0,0]
	v_mfma_scale_f32_16x16x128_f8f6f4 v[128:131], v[208:215], v[192:199], v[128:131], v224, v224 op_sel_hi:[0,0,0]
	v_mfma_scale_f32_16x16x128_f8f6f4 v[132:135], v[236:243], v[192:199], v[132:135], v224, v224 op_sel_hi:[0,0,0]
	v_mfma_scale_f32_16x16x128_f8f6f4 v[144:147], v[208:215], v[200:207], v[144:147], v224, v224 op_sel_hi:[0,0,0]
	v_mfma_scale_f32_16x16x128_f8f6f4 v[136:139], v[236:243], v[200:207], v[136:139], v224, v224 op_sel_hi:[0,0,0]
	s_setprio 0
	s_barrier
	ds_read_b128 v[8:11], v234
	ds_read_b128 v[12:15], v234 offset:1024
	ds_read_b128 v[168:171], v234 offset:2048
	ds_read_b128 v[172:175], v234 offset:3072
	s_add_u32 s46, s50, 0x40000
	s_addc_u32 s47, s51, 0
	s_mov_b32 m0, s72
	v_lshl_add_u64 v[140:141], s[46:47], 0, v[148:149]
	ds_read_b128 v[176:179], v227 offset:32768
	ds_read_b128 v[180:183], v227 offset:33792
	ds_read_b128 v[184:187], v227 offset:34816
	ds_read_b128 v[188:191], v227 offset:35840
	ds_read_b128 v[192:195], v227 offset:36864
	ds_read_b128 v[196:199], v227 offset:37888
	ds_read_b128 v[200:203], v227 offset:38912
	ds_read_b128 v[204:207], v227 offset:39936
	global_load_lds_dwordx4 v[140:141], off
	v_lshl_add_u64 v[140:141], s[46:47], 0, v[152:153]
	s_mov_b32 m0, s73
	s_nop 0
	global_load_lds_dwordx4 v[140:141], off
	s_waitcnt lgkmcnt(8)
	s_barrier
	s_waitcnt lgkmcnt(0)
	s_setprio 1
	s_waitcnt lgkmcnt(0)
	v_mfma_scale_f32_16x16x128_f8f6f4 v[16:19], v[8:15], v[176:183], v[16:19], v224, v224 op_sel_hi:[0,0,0]
	v_mfma_scale_f32_16x16x128_f8f6f4 v[20:23], v[168:175], v[176:183], v[20:23], v224, v224 op_sel_hi:[0,0,0]
	v_mfma_scale_f32_16x16x128_f8f6f4 v[24:27], v[8:15], v[184:191], v[24:27], v224, v224 op_sel_hi:[0,0,0]
	v_mfma_scale_f32_16x16x128_f8f6f4 v[28:31], v[168:175], v[184:191], v[28:31], v224, v224 op_sel_hi:[0,0,0]
	v_mfma_scale_f32_16x16x128_f8f6f4 v[32:35], v[8:15], v[192:199], v[32:35], v224, v224 op_sel_hi:[0,0,0]
	v_mfma_scale_f32_16x16x128_f8f6f4 v[36:39], v[168:175], v[192:199], v[36:39], v224, v224 op_sel_hi:[0,0,0]
	v_mfma_scale_f32_16x16x128_f8f6f4 v[40:43], v[8:15], v[200:207], v[40:43], v224, v224 op_sel_hi:[0,0,0]
	v_mfma_scale_f32_16x16x128_f8f6f4 v[44:47], v[168:175], v[200:207], v[44:47], v224, v224 op_sel_hi:[0,0,0]
	s_setprio 0
	s_barrier
	s_mov_b32 m0, s63
	v_lshl_add_u64 v[0:1], v[0:1], 0, s[6:7]
	ds_read_b128 v[208:211], v233
	ds_read_b128 v[212:215], v233 offset:1024
	ds_read_b128 v[234:237], v233 offset:2048
	ds_read_b128 v[238:241], v233 offset:3072
	global_load_lds_dwordx4 v[0:1], off
	v_lshl_add_u64 v[0:1], v[2:3], 0, s[6:7]
	s_mov_b32 m0, s62
	s_nop 0
	global_load_lds_dwordx4 v[0:1], off
	s_barrier
	s_waitcnt lgkmcnt(0)
	s_setprio 1
	s_waitcnt lgkmcnt(0)
	v_mfma_scale_f32_16x16x128_f8f6f4 v[48:51], v[208:215], v[176:183], v[48:51], v224, v224 op_sel_hi:[0,0,0]
	v_mfma_scale_f32_16x16x128_f8f6f4 v[52:55], v[234:241], v[176:183], v[52:55], v224, v224 op_sel_hi:[0,0,0]
	v_mfma_scale_f32_16x16x128_f8f6f4 v[56:59], v[208:215], v[184:191], v[56:59], v224, v224 op_sel_hi:[0,0,0]
	v_mfma_scale_f32_16x16x128_f8f6f4 v[60:63], v[234:241], v[184:191], v[60:63], v224, v224 op_sel_hi:[0,0,0]
	v_mfma_scale_f32_16x16x128_f8f6f4 v[64:67], v[208:215], v[192:199], v[64:67], v224, v224 op_sel_hi:[0,0,0]
	v_mfma_scale_f32_16x16x128_f8f6f4 v[68:71], v[234:241], v[192:199], v[68:71], v224, v224 op_sel_hi:[0,0,0]
	v_mfma_scale_f32_16x16x128_f8f6f4 v[72:75], v[208:215], v[200:207], v[72:75], v224, v224 op_sel_hi:[0,0,0]
	v_mfma_scale_f32_16x16x128_f8f6f4 v[76:79], v[234:241], v[200:207], v[76:79], v224, v224 op_sel_hi:[0,0,0]
	s_setprio 0
	s_mov_b32 m0, s77
	v_lshl_add_u64 v[0:1], v[4:5], 0, s[6:7]
	s_barrier
	ds_read_b128 v[176:179], v227 offset:49152
	ds_read_b128 v[180:183], v227 offset:50176
	ds_read_b128 v[184:187], v227 offset:51200
	ds_read_b128 v[188:191], v227 offset:52224
	ds_read_b128 v[192:195], v227 offset:53248
	ds_read_b128 v[196:199], v227 offset:54272
	ds_read_b128 v[200:203], v227 offset:55296
	ds_read_b128 v[204:207], v227 offset:56320
	global_load_lds_dwordx4 v[0:1], off
	v_lshl_add_u64 v[0:1], v[6:7], 0, s[6:7]
	s_mov_b32 m0, s78
	s_nop 0
	global_load_lds_dwordx4 v[0:1], off
	s_barrier
	s_waitcnt lgkmcnt(0)
	s_setprio 1
	s_waitcnt lgkmcnt(0)
	v_mfma_scale_f32_16x16x128_f8f6f4 v[80:83], v[8:15], v[176:183], v[80:83], v224, v224 op_sel_hi:[0,0,0]
	v_mfma_scale_f32_16x16x128_f8f6f4 v[84:87], v[168:175], v[176:183], v[84:87], v224, v224 op_sel_hi:[0,0,0]
	v_mfma_scale_f32_16x16x128_f8f6f4 v[88:91], v[8:15], v[184:191], v[88:91], v224, v224 op_sel_hi:[0,0,0]
	v_mfma_scale_f32_16x16x128_f8f6f4 v[92:95], v[168:175], v[184:191], v[92:95], v224, v224 op_sel_hi:[0,0,0]
	v_mfma_scale_f32_16x16x128_f8f6f4 v[96:99], v[8:15], v[192:199], v[96:99], v224, v224 op_sel_hi:[0,0,0]
	v_mfma_scale_f32_16x16x128_f8f6f4 v[100:103], v[168:175], v[192:199], v[100:103], v224, v224 op_sel_hi:[0,0,0]
	v_mfma_scale_f32_16x16x128_f8f6f4 v[104:107], v[8:15], v[200:207], v[104:107], v224, v224 op_sel_hi:[0,0,0]
	v_mfma_scale_f32_16x16x128_f8f6f4 v[108:111], v[168:175], v[200:207], v[108:111], v224, v224 op_sel_hi:[0,0,0]
	s_setprio 0
	s_barrier
	s_add_u32 s46, s58, 0x40080
	s_addc_u32 s47, s59, 0
	s_mov_b32 m0, s64
	v_lshl_add_u64 v[0:1], s[46:47], 0, v[150:151]
	global_load_lds_dwordx4 v[0:1], off
	v_lshl_add_u64 v[0:1], s[46:47], 0, v[154:155]
	s_mov_b32 m0, s53
	s_nop 0
	global_load_lds_dwordx4 v[0:1], off
	s_waitcnt vmcnt(6)
	s_barrier
	s_setprio 1
	v_mfma_scale_f32_16x16x128_f8f6f4 v[112:115], v[208:215], v[176:183], v[112:115], v224, v224 op_sel_hi:[0,0,0]
	v_mfma_scale_f32_16x16x128_f8f6f4 v[116:119], v[234:241], v[176:183], v[116:119], v224, v224 op_sel_hi:[0,0,0]
	v_mfma_scale_f32_16x16x128_f8f6f4 v[120:123], v[208:215], v[184:191], v[120:123], v224, v224 op_sel_hi:[0,0,0]
	v_mfma_scale_f32_16x16x128_f8f6f4 v[124:127], v[234:241], v[184:191], v[124:127], v224, v224 op_sel_hi:[0,0,0]
	v_mfma_scale_f32_16x16x128_f8f6f4 v[128:131], v[208:215], v[192:199], v[128:131], v224, v224 op_sel_hi:[0,0,0]
	v_mfma_scale_f32_16x16x128_f8f6f4 v[132:135], v[234:241], v[192:199], v[132:135], v224, v224 op_sel_hi:[0,0,0]
	v_mfma_scale_f32_16x16x128_f8f6f4 v[144:147], v[208:215], v[200:207], v[144:147], v224, v224 op_sel_hi:[0,0,0]
	v_mfma_scale_f32_16x16x128_f8f6f4 v[136:139], v[234:241], v[200:207], v[136:139], v224, v224 op_sel_hi:[0,0,0]
	s_setprio 0
	v_mov_b32_e32 v156, v229
	s_barrier
	s_nop 7
	s_nop 7
	s_nop 7
	global_load_dwordx2 v[4:5], v156, s[2:3]
	global_load_dwordx2 v[6:7], v156, s[2:3] offset:512
	global_load_dwordx2 v[8:9], v156, s[2:3] offset:1024
	global_load_dwordx2 v[10:11], v156, s[2:3] offset:1536
	global_load_dwordx2 v[168:169], v156, s[2:3] offset:2048
	global_load_dwordx2 v[202:203], v156, s[2:3] offset:2560
	global_load_dwordx2 v[200:201], v156, s[2:3] offset:3072
	global_load_dwordx2 v[198:199], v156, s[2:3] offset:3584
	v_lshl_add_u64 v[0:1], s[2:3], 0, v[156:157]
	v_add_co_u32_e32 v0, vcc, s82, v0
	s_mov_b64 s[2:3], 0x40000
	s_nop 0
	v_addc_co_u32_e32 v1, vcc, 0, v1, vcc
	global_load_dwordx2 v[196:197], v[0:1], off
	global_load_dwordx2 v[194:195], v[0:1], off offset:512
	global_load_dwordx2 v[192:193], v[0:1], off offset:1024
	global_load_dwordx2 v[190:191], v[0:1], off offset:1536
	global_load_dwordx2 v[180:181], v[0:1], off offset:2048
	global_load_dwordx2 v[170:171], v[0:1], off offset:2560
	global_load_dwordx2 v[2:3], v[0:1], off offset:3072
	s_nop 0
	global_load_dwordx2 v[0:1], v[0:1], off offset:3584
	s_mov_b64 s[48:49], s[44:45]
	s_mov_b64 s[46:47], s[42:43]
	s_waitcnt vmcnt(0)
	v_cvt_f32_ubyte1_e32 v13, v4
	v_cvt_f32_ubyte0_e32 v12, v4
	v_cvt_f32_ubyte3_e32 v15, v4
	v_cvt_f32_ubyte2_e32 v14, v4
	v_cvt_f32_ubyte1_e32 v141, v5
	v_cvt_f32_ubyte0_e32 v140, v5
	v_cvt_f32_ubyte3_e32 v143, v5
	v_cvt_f32_ubyte2_e32 v142, v5
	v_cvt_f32_ubyte1_e32 v5, v6
	v_cvt_f32_ubyte0_e32 v4, v6
	v_cvt_f32_ubyte1_e32 v175, v7
	v_cvt_f32_ubyte0_e32 v174, v7
	v_pk_add_f32 v[4:5], v[4:5], 0.5 op_sel_hi:[1,0]
	v_cvt_f32_ubyte3_e32 v173, v6
	v_cvt_f32_ubyte2_e32 v172, v6
	v_cvt_f32_ubyte3_e32 v177, v7
	v_cvt_f32_ubyte2_e32 v176, v7
	v_cvt_f32_ubyte1_e32 v7, v8
	v_cvt_f32_ubyte0_e32 v6, v8
	v_pk_add_f32 v[174:175], v[174:175], 0.5 op_sel_hi:[1,0]
	v_pk_mul_f32 v[4:5], v[4:5], s[38:39] op_sel_hi:[1,0]
	v_pk_add_f32 v[172:173], v[172:173], 0.5 op_sel_hi:[1,0]
	v_pk_add_f32 v[6:7], v[6:7], 0.5 op_sel_hi:[1,0]
	v_pk_mul_f32 v[204:205], v[174:175], s[38:39] op_sel_hi:[1,0]
	v_pk_mul_f32 v[174:175], v[48:49], v[4:5]
	v_cvt_f32_ubyte3_e32 v5, v10
	v_cvt_f32_ubyte2_e32 v4, v10
	v_cvt_f32_ubyte3_e32 v179, v8
	v_cvt_f32_ubyte2_e32 v178, v8
	v_cvt_f32_ubyte1_e32 v183, v9
	v_cvt_f32_ubyte0_e32 v182, v9
	v_cvt_f32_ubyte3_e32 v185, v9
	v_cvt_f32_ubyte2_e32 v184, v9
	v_cvt_f32_ubyte1_e32 v9, v10
	v_pk_add_f32 v[12:13], v[12:13], 0.5 op_sel_hi:[1,0]
	v_pk_mul_f32 v[172:173], v[172:173], s[38:39] op_sel_hi:[1,0]
	v_pk_mul_f32 v[6:7], v[6:7], s[38:39] op_sel_hi:[1,0]
	v_cvt_f32_ubyte0_e32 v8, v10
	v_pk_add_f32 v[4:5], v[4:5], 0.5 op_sel_hi:[1,0]
	v_pk_add_f32 v[14:15], v[14:15], 0.5 op_sel_hi:[1,0]
	v_pk_add_f32 v[184:185], v[184:185], 0.5 op_sel_hi:[1,0]
	v_pk_mul_f32 v[12:13], v[12:13], s[38:39] op_sel_hi:[1,0]
	v_pk_mul_f32 v[172:173], v[50:51], v[172:173]
	v_pk_mul_f32 v[50:51], v[24:25], v[6:7]
	v_pk_add_f32 v[6:7], v[8:9], 0.5 op_sel_hi:[1,0]
	v_pk_mul_f32 v[4:5], v[4:5], s[38:39] op_sel_hi:[1,0]
	v_pk_add_f32 v[182:183], v[182:183], 0.5 op_sel_hi:[1,0]
	v_pk_mul_f32 v[14:15], v[14:15], s[38:39] op_sel_hi:[1,0]
	v_pk_mul_f32 v[210:211], v[184:185], s[38:39] op_sel_hi:[1,0]
	v_pk_mul_f32 v[184:185], v[16:17], v[12:13]
	v_pk_mul_f32 v[6:7], v[6:7], s[38:39] op_sel_hi:[1,0]
	v_pk_mul_f32 v[12:13], v[58:59], v[4:5]
	v_cvt_f32_ubyte1_e32 v5, v11
	v_cvt_f32_ubyte0_e32 v4, v11
	v_pk_add_f32 v[142:143], v[142:143], 0.5 op_sel_hi:[1,0]
	v_pk_mul_f32 v[208:209], v[182:183], s[38:39] op_sel_hi:[1,0]
	v_pk_mul_f32 v[182:183], v[18:19], v[14:15]
	v_pk_mul_f32 v[14:15], v[56:57], v[6:7]
	v_cvt_f32_ubyte3_e32 v7, v11
	v_cvt_f32_ubyte2_e32 v6, v11
	v_pk_add_f32 v[4:5], v[4:5], 0.5 op_sel_hi:[1,0]
	v_pk_add_f32 v[140:141], v[140:141], 0.5 op_sel_hi:[1,0]
	v_pk_mul_f32 v[142:143], v[142:143], s[38:39] op_sel_hi:[1,0]
	v_pk_add_f32 v[6:7], v[6:7], 0.5 op_sel_hi:[1,0]
	v_pk_mul_f32 v[4:5], v[4:5], s[38:39] op_sel_hi:[1,0]
	v_pk_mul_f32 v[140:141], v[140:141], s[38:39] op_sel_hi:[1,0]
	v_pk_mul_f32 v[186:187], v[22:23], v[142:143]
	v_pk_mul_f32 v[6:7], v[6:7], s[38:39] op_sel_hi:[1,0]
	v_pk_mul_f32 v[142:143], v[60:61], v[4:5]
	v_cvt_f32_ubyte1_e32 v5, v168
	v_cvt_f32_ubyte0_e32 v4, v168
	v_pk_mul_f32 v[188:189], v[20:21], v[140:141]
	v_pk_mul_f32 v[140:141], v[62:63], v[6:7]
	v_cvt_f32_ubyte3_e32 v7, v168
	v_cvt_f32_ubyte2_e32 v6, v168
	v_pk_add_f32 v[4:5], v[4:5], 0.5 op_sel_hi:[1,0]
	v_pk_add_f32 v[6:7], v[6:7], 0.5 op_sel_hi:[1,0]
	v_pk_mul_f32 v[8:9], v[4:5], s[38:39] op_sel_hi:[1,0]
	v_pk_mul_f32 v[4:5], v[6:7], s[38:39] op_sel_hi:[1,0]
	v_pk_mul_f32 v[6:7], v[32:33], v[8:9]
	v_cvt_f32_ubyte1_e32 v9, v169
	v_cvt_f32_ubyte0_e32 v8, v169
	v_cvt_f32_ubyte3_e32 v11, v169
	v_cvt_f32_ubyte2_e32 v10, v169
	v_pk_add_f32 v[8:9], v[8:9], 0.5 op_sel_hi:[1,0]
	v_pk_add_f32 v[10:11], v[10:11], 0.5 op_sel_hi:[1,0]
	v_pk_mul_f32 v[8:9], v[8:9], s[38:39] op_sel_hi:[1,0]
	v_pk_mul_f32 v[10:11], v[10:11], s[38:39] op_sel_hi:[1,0]
	v_pk_mul_f32 v[58:59], v[36:37], v[8:9]
	v_cvt_f32_ubyte1_e32 v9, v202
	v_cvt_f32_ubyte0_e32 v8, v202
	v_pk_mul_f32 v[56:57], v[38:39], v[10:11]
	v_cvt_f32_ubyte3_e32 v11, v202
	v_cvt_f32_ubyte2_e32 v10, v202
	v_pk_add_f32 v[8:9], v[8:9], 0.5 op_sel_hi:[1,0]
	v_pk_add_f32 v[10:11], v[10:11], 0.5 op_sel_hi:[1,0]
	v_pk_mul_f32 v[8:9], v[8:9], s[38:39] op_sel_hi:[1,0]
	v_pk_mul_f32 v[10:11], v[10:11], s[38:39] op_sel_hi:[1,0]
	v_pk_mul_f32 v[18:19], v[64:65], v[8:9]
	v_cvt_f32_ubyte1_e32 v9, v203
	v_cvt_f32_ubyte0_e32 v8, v203
	v_pk_mul_f32 v[16:17], v[66:67], v[10:11]
	v_cvt_f32_ubyte3_e32 v11, v203
	v_cvt_f32_ubyte2_e32 v10, v203
	v_pk_add_f32 v[8:9], v[8:9], 0.5 op_sel_hi:[1,0]
	v_pk_add_f32 v[10:11], v[10:11], 0.5 op_sel_hi:[1,0]
	v_pk_mul_f32 v[8:9], v[8:9], s[38:39] op_sel_hi:[1,0]
	v_pk_mul_f32 v[10:11], v[10:11], s[38:39] op_sel_hi:[1,0]
	v_pk_mul_f32 v[168:169], v[68:69], v[8:9]
	v_cvt_f32_ubyte1_e32 v9, v200
	v_cvt_f32_ubyte0_e32 v8, v200
	v_pk_mul_f32 v[70:71], v[70:71], v[10:11]
	v_cvt_f32_ubyte3_e32 v11, v200
	v_cvt_f32_ubyte2_e32 v10, v200
	v_pk_add_f32 v[8:9], v[8:9], 0.5 op_sel_hi:[1,0]
	v_pk_add_f32 v[10:11], v[10:11], 0.5 op_sel_hi:[1,0]
	v_pk_mul_f32 v[20:21], v[8:9], s[38:39] op_sel_hi:[1,0]
	v_pk_mul_f32 v[8:9], v[10:11], s[38:39] op_sel_hi:[1,0]
	v_pk_mul_f32 v[10:11], v[40:41], v[20:21]
	v_cvt_f32_ubyte1_e32 v21, v201
	v_cvt_f32_ubyte0_e32 v20, v201
	v_cvt_f32_ubyte3_e32 v23, v201
	v_cvt_f32_ubyte2_e32 v22, v201
	v_pk_add_f32 v[20:21], v[20:21], 0.5 op_sel_hi:[1,0]
	v_pk_add_f32 v[22:23], v[22:23], 0.5 op_sel_hi:[1,0]
	v_pk_mul_f32 v[20:21], v[20:21], s[38:39] op_sel_hi:[1,0]
	v_pk_mul_f32 v[22:23], v[22:23], s[38:39] op_sel_hi:[1,0]
	v_pk_mul_f32 v[66:67], v[44:45], v[20:21]
	v_cvt_f32_ubyte1_e32 v21, v198
	v_cvt_f32_ubyte0_e32 v20, v198
	v_pk_mul_f32 v[64:65], v[46:47], v[22:23]
	v_cvt_f32_ubyte3_e32 v23, v198
	v_cvt_f32_ubyte2_e32 v22, v198
	v_pk_add_f32 v[20:21], v[20:21], 0.5 op_sel_hi:[1,0]
	v_pk_add_f32 v[178:179], v[178:179], 0.5 op_sel_hi:[1,0]
	v_pk_add_f32 v[22:23], v[22:23], 0.5 op_sel_hi:[1,0]
	v_pk_mul_f32 v[24:25], v[20:21], s[38:39] op_sel_hi:[1,0]
	v_pk_mul_f32 v[206:207], v[178:179], s[38:39] op_sel_hi:[1,0]
	v_pk_mul_f32 v[20:21], v[22:23], s[38:39] op_sel_hi:[1,0]
	v_pk_mul_f32 v[22:23], v[72:73], v[24:25]
	v_cvt_f32_ubyte1_e32 v25, v199
	v_cvt_f32_ubyte0_e32 v24, v199
	v_pk_mul_f32 v[48:49], v[26:27], v[206:207]
	v_cvt_f32_ubyte3_e32 v27, v199
	v_cvt_f32_ubyte2_e32 v26, v199
	v_pk_add_f32 v[24:25], v[24:25], 0.5 op_sel_hi:[1,0]
	v_pk_add_f32 v[26:27], v[26:27], 0.5 op_sel_hi:[1,0]
	v_pk_mul_f32 v[24:25], v[24:25], s[38:39] op_sel_hi:[1,0]
	v_pk_add_f32 v[176:177], v[176:177], 0.5 op_sel_hi:[1,0]
	v_pk_mul_f32 v[20:21], v[74:75], v[20:21]
	v_pk_mul_f32 v[26:27], v[26:27], s[38:39] op_sel_hi:[1,0]
	v_pk_mul_f32 v[74:75], v[76:77], v[24:25]
	v_cvt_f32_ubyte1_e32 v25, v196
	v_cvt_f32_ubyte0_e32 v24, v196
	v_pk_mul_f32 v[176:177], v[176:177], s[38:39] op_sel_hi:[1,0]
	v_pk_mul_f32 v[72:73], v[78:79], v[26:27]
	v_cvt_f32_ubyte3_e32 v27, v196
	v_cvt_f32_ubyte2_e32 v26, v196
	v_pk_add_f32 v[24:25], v[24:25], 0.5 op_sel_hi:[1,0]
	v_pk_mul_f32 v[176:177], v[54:55], v[176:177]
	v_pk_mul_f32 v[54:55], v[28:29], v[208:209]
	v_pk_add_f32 v[26:27], v[26:27], 0.5 op_sel_hi:[1,0]
	v_pk_mul_f32 v[28:29], v[24:25], s[38:39] op_sel_hi:[1,0]
	v_pk_mul_f32 v[24:25], v[26:27], s[38:39] op_sel_hi:[1,0]
	v_pk_mul_f32 v[26:27], v[80:81], v[28:29]
	v_cvt_f32_ubyte1_e32 v29, v197
	v_cvt_f32_ubyte0_e32 v28, v197
	v_pk_mul_f32 v[178:179], v[52:53], v[204:205]
	v_pk_mul_f32 v[52:53], v[30:31], v[210:211]
	v_cvt_f32_ubyte3_e32 v31, v197
	v_cvt_f32_ubyte2_e32 v30, v197
	v_pk_add_f32 v[28:29], v[28:29], 0.5 op_sel_hi:[1,0]
	v_pk_add_f32 v[30:31], v[30:31], 0.5 op_sel_hi:[1,0]
	v_pk_mul_f32 v[28:29], v[28:29], s[38:39] op_sel_hi:[1,0]
	v_pk_mul_f32 v[30:31], v[30:31], s[38:39] op_sel_hi:[1,0]
	v_pk_mul_f32 v[78:79], v[84:85], v[28:29]
	v_cvt_f32_ubyte1_e32 v29, v194
	v_cvt_f32_ubyte0_e32 v28, v194
	v_pk_mul_f32 v[76:77], v[86:87], v[30:31]
	v_cvt_f32_ubyte3_e32 v31, v194
	v_cvt_f32_ubyte2_e32 v30, v194
	v_pk_add_f32 v[28:29], v[28:29], 0.5 op_sel_hi:[1,0]
	v_pk_add_f32 v[30:31], v[30:31], 0.5 op_sel_hi:[1,0]
	v_pk_mul_f32 v[32:33], v[28:29], s[38:39] op_sel_hi:[1,0]
	v_pk_mul_f32 v[28:29], v[30:31], s[38:39] op_sel_hi:[1,0]
	v_pk_mul_f32 v[30:31], v[112:113], v[32:33]
	v_cvt_f32_ubyte1_e32 v33, v195
	v_cvt_f32_ubyte0_e32 v32, v195
	v_pk_mul_f32 v[4:5], v[34:35], v[4:5]
	v_cvt_f32_ubyte3_e32 v35, v195
	v_cvt_f32_ubyte2_e32 v34, v195
	v_pk_add_f32 v[32:33], v[32:33], 0.5 op_sel_hi:[1,0]
	v_pk_add_f32 v[34:35], v[34:35], 0.5 op_sel_hi:[1,0]
	v_pk_mul_f32 v[32:33], v[32:33], s[38:39] op_sel_hi:[1,0]
	v_pk_mul_f32 v[24:25], v[82:83], v[24:25]
	v_pk_mul_f32 v[34:35], v[34:35], s[38:39] op_sel_hi:[1,0]
	v_pk_mul_f32 v[82:83], v[116:117], v[32:33]
	v_cvt_f32_ubyte1_e32 v33, v192
	v_cvt_f32_ubyte0_e32 v32, v192
	v_pk_mul_f32 v[80:81], v[118:119], v[34:35]
	v_cvt_f32_ubyte3_e32 v35, v192
	v_cvt_f32_ubyte2_e32 v34, v192
	v_pk_add_f32 v[32:33], v[32:33], 0.5 op_sel_hi:[1,0]
	v_pk_add_f32 v[34:35], v[34:35], 0.5 op_sel_hi:[1,0]
	v_pk_mul_f32 v[36:37], v[32:33], s[38:39] op_sel_hi:[1,0]
	v_pk_mul_f32 v[32:33], v[34:35], s[38:39] op_sel_hi:[1,0]
	v_pk_mul_f32 v[34:35], v[88:89], v[36:37]
	v_cvt_f32_ubyte1_e32 v37, v193
	v_cvt_f32_ubyte0_e32 v36, v193
	v_cvt_f32_ubyte3_e32 v39, v193
	v_cvt_f32_ubyte2_e32 v38, v193
	v_pk_add_f32 v[36:37], v[36:37], 0.5 op_sel_hi:[1,0]
	v_pk_add_f32 v[38:39], v[38:39], 0.5 op_sel_hi:[1,0]
	v_pk_mul_f32 v[36:37], v[36:37], s[38:39] op_sel_hi:[1,0]
	v_pk_mul_f32 v[38:39], v[38:39], s[38:39] op_sel_hi:[1,0]
	v_pk_mul_f32 v[86:87], v[92:93], v[36:37]
	v_cvt_f32_ubyte1_e32 v37, v190
	v_cvt_f32_ubyte0_e32 v36, v190
	v_pk_mul_f32 v[84:85], v[94:95], v[38:39]
	v_cvt_f32_ubyte3_e32 v39, v190
	v_cvt_f32_ubyte2_e32 v38, v190
	v_pk_add_f32 v[36:37], v[36:37], 0.5 op_sel_hi:[1,0]
	v_pk_add_f32 v[38:39], v[38:39], 0.5 op_sel_hi:[1,0]
	v_pk_mul_f32 v[40:41], v[36:37], s[38:39] op_sel_hi:[1,0]
	v_pk_mul_f32 v[36:37], v[38:39], s[38:39] op_sel_hi:[1,0]
	v_pk_mul_f32 v[38:39], v[120:121], v[40:41]
	v_cvt_f32_ubyte1_e32 v41, v191
	v_cvt_f32_ubyte0_e32 v40, v191
	v_pk_mul_f32 v[8:9], v[42:43], v[8:9]
	v_cvt_f32_ubyte3_e32 v43, v191
	v_cvt_f32_ubyte2_e32 v42, v191
	v_pk_add_f32 v[40:41], v[40:41], 0.5 op_sel_hi:[1,0]
	v_pk_add_f32 v[42:43], v[42:43], 0.5 op_sel_hi:[1,0]
	v_pk_mul_f32 v[40:41], v[40:41], s[38:39] op_sel_hi:[1,0]
	v_pk_mul_f32 v[32:33], v[90:91], v[32:33]
	v_pk_mul_f32 v[42:43], v[42:43], s[38:39] op_sel_hi:[1,0]
	v_pk_mul_f32 v[90:91], v[124:125], v[40:41]
	v_cvt_f32_ubyte1_e32 v41, v180
	v_cvt_f32_ubyte0_e32 v40, v180
	v_pk_mul_f32 v[88:89], v[126:127], v[42:43]
	v_cvt_f32_ubyte3_e32 v43, v180
	v_cvt_f32_ubyte2_e32 v42, v180
	v_pk_add_f32 v[40:41], v[40:41], 0.5 op_sel_hi:[1,0]
	v_pk_add_f32 v[42:43], v[42:43], 0.5 op_sel_hi:[1,0]
	v_pk_mul_f32 v[44:45], v[40:41], s[38:39] op_sel_hi:[1,0]
	v_pk_mul_f32 v[40:41], v[42:43], s[38:39] op_sel_hi:[1,0]
	v_pk_mul_f32 v[42:43], v[96:97], v[44:45]
	v_cvt_f32_ubyte1_e32 v45, v181
	v_cvt_f32_ubyte0_e32 v44, v181
	v_cvt_f32_ubyte3_e32 v47, v181
	v_cvt_f32_ubyte2_e32 v46, v181
	v_pk_add_f32 v[44:45], v[44:45], 0.5 op_sel_hi:[1,0]
	v_pk_add_f32 v[46:47], v[46:47], 0.5 op_sel_hi:[1,0]
	v_pk_mul_f32 v[44:45], v[44:45], s[38:39] op_sel_hi:[1,0]
	v_pk_mul_f32 v[46:47], v[46:47], s[38:39] op_sel_hi:[1,0]
	v_pk_mul_f32 v[94:95], v[100:101], v[44:45]
	v_cvt_f32_ubyte1_e32 v45, v170
	v_cvt_f32_ubyte0_e32 v44, v170
	v_pk_mul_f32 v[92:93], v[102:103], v[46:47]
	v_cvt_f32_ubyte3_e32 v47, v170
	v_cvt_f32_ubyte2_e32 v46, v170
	v_pk_add_f32 v[44:45], v[44:45], 0.5 op_sel_hi:[1,0]
	v_pk_add_f32 v[46:47], v[46:47], 0.5 op_sel_hi:[1,0]
	v_pk_mul_f32 v[60:61], v[44:45], s[38:39] op_sel_hi:[1,0]
	v_pk_mul_f32 v[44:45], v[46:47], s[38:39] op_sel_hi:[1,0]
	v_pk_mul_f32 v[46:47], v[128:129], v[60:61]
	v_cvt_f32_ubyte1_e32 v61, v171
	v_cvt_f32_ubyte0_e32 v60, v171
	v_cvt_f32_ubyte3_e32 v63, v171
	v_cvt_f32_ubyte2_e32 v62, v171
	v_pk_add_f32 v[60:61], v[60:61], 0.5 op_sel_hi:[1,0]
	v_pk_add_f32 v[62:63], v[62:63], 0.5 op_sel_hi:[1,0]
	v_pk_mul_f32 v[60:61], v[60:61], s[38:39] op_sel_hi:[1,0]
	v_pk_mul_f32 v[40:41], v[98:99], v[40:41]
	v_pk_mul_f32 v[62:63], v[62:63], s[38:39] op_sel_hi:[1,0]
	v_pk_mul_f32 v[98:99], v[132:133], v[60:61]
	v_cvt_f32_ubyte1_e32 v61, v2
	v_cvt_f32_ubyte0_e32 v60, v2
	v_pk_mul_f32 v[96:97], v[134:135], v[62:63]
	v_cvt_f32_ubyte3_e32 v63, v2
	v_cvt_f32_ubyte2_e32 v62, v2
	v_pk_add_f32 v[60:61], v[60:61], 0.5 op_sel_hi:[1,0]
	v_pk_add_f32 v[62:63], v[62:63], 0.5 op_sel_hi:[1,0]
	v_pk_mul_f32 v[68:69], v[60:61], s[38:39] op_sel_hi:[1,0]
	v_cvt_f32_ubyte3_e32 v101, v3
	v_cvt_f32_ubyte2_e32 v100, v3
	v_pk_mul_f32 v[60:61], v[62:63], s[38:39] op_sel_hi:[1,0]
	v_pk_mul_f32 v[62:63], v[104:105], v[68:69]
	v_cvt_f32_ubyte1_e32 v69, v3
	v_cvt_f32_ubyte0_e32 v68, v3
	v_pk_add_f32 v[2:3], v[100:101], 0.5 op_sel_hi:[1,0]
	v_pk_add_f32 v[68:69], v[68:69], 0.5 op_sel_hi:[1,0]
	v_pk_mul_f32 v[2:3], v[2:3], s[38:39] op_sel_hi:[1,0]
	v_pk_mul_f32 v[68:69], v[68:69], s[38:39] op_sel_hi:[1,0]
	v_pk_mul_f32 v[100:101], v[110:111], v[2:3]
	v_cvt_f32_ubyte1_e32 v3, v0
	v_cvt_f32_ubyte0_e32 v2, v0
	v_pk_mul_f32 v[102:103], v[108:109], v[68:69]
	v_cvt_f32_ubyte3_e32 v69, v0
	v_cvt_f32_ubyte2_e32 v68, v0
	v_pk_add_f32 v[2:3], v[2:3], 0.5 op_sel_hi:[1,0]
	v_lshl_add_u32 v108, s90, 8, v225
	v_pk_mul_f32 v[28:29], v[114:115], v[28:29]
	v_pk_mul_f32 v[60:61], v[106:107], v[60:61]
	v_pk_add_f32 v[68:69], v[68:69], 0.5 op_sel_hi:[1,0]
	v_pk_mul_f32 v[104:105], v[2:3], s[38:39] op_sel_hi:[1,0]
	v_cvt_f32_ubyte3_e32 v107, v1
	v_cvt_f32_ubyte2_e32 v106, v1
	v_ashrrev_i32_e32 v109, 31, v108
	v_pk_mul_f32 v[112:113], v[182:183], s[40:41] op_sel_hi:[1,0]
	v_pk_mul_f32 v[114:115], v[184:185], s[40:41] op_sel_hi:[1,0]
	v_pk_mul_f32 v[2:3], v[68:69], s[38:39] op_sel_hi:[1,0]
	v_pk_mul_f32 v[68:69], v[144:145], v[104:105]
	v_cvt_f32_ubyte1_e32 v105, v1
	v_cvt_f32_ubyte0_e32 v104, v1
	v_pk_add_f32 v[0:1], v[106:107], 0.5 op_sel_hi:[1,0]
	v_lshlrev_b64 v[106:107], 11, v[108:109]
	v_pk_mul_f32 v[118:119], v[188:189], s[40:41] op_sel_hi:[1,0]
	v_med3_f32 v109, v114, s83, v232
	v_med3_f32 v114, v115, s83, v232
	v_med3_f32 v115, v112, s83, v232
	v_mov_b32_e32 v112, v157
	v_med3_f32 v120, v113, s83, v232
	v_cvt_pk_fp8_f32 v112, v109, v114
	v_med3_f32 v109, v118, s83, v232
	v_med3_f32 v114, v119, s83, v232
	v_mov_b32_e32 v113, v157
	v_cvt_pk_fp8_f32 v113, v109, v114
	v_pk_mul_f32 v[116:117], v[186:187], s[40:41] op_sel_hi:[1,0]
	v_cvt_pk_fp8_f32 v112, v115, v120 op_sel:[0,0,1]
	v_med3_f32 v109, v116, s83, v232
	v_med3_f32 v114, v117, s83, v232
	v_cvt_pk_fp8_f32 v113, v109, v114 op_sel:[0,0,1]
	v_pk_mul_f32 v[114:115], v[172:173], s[40:41] op_sel_hi:[1,0]
	v_pk_mul_f32 v[116:117], v[174:175], s[40:41] op_sel_hi:[1,0]
	v_pk_mul_f32 v[120:121], v[178:179], s[40:41] op_sel_hi:[1,0]
	v_med3_f32 v109, v116, s83, v232
	v_med3_f32 v116, v117, s83, v232
	v_med3_f32 v117, v114, s83, v232
	v_mov_b32_e32 v114, v157
	v_pk_mul_f32 v[36:37], v[122:123], v[36:37]
	v_med3_f32 v122, v115, s83, v232
	v_cvt_pk_fp8_f32 v114, v109, v116
	v_med3_f32 v109, v120, s83, v232
	v_med3_f32 v116, v121, s83, v232
	v_mov_b32_e32 v115, v157
	v_cvt_pk_fp8_f32 v115, v109, v116
	v_pk_mul_f32 v[118:119], v[176:177], s[40:41] op_sel_hi:[1,0]
	v_lshl_or_b32 v110, s89, 8, v228
	v_med3_f32 v109, v118, s83, v232
	v_med3_f32 v116, v119, s83, v232
	v_cvt_pk_fp8_f32 v114, v117, v122 op_sel:[0,0,1]
	v_cvt_pk_fp8_f32 v115, v109, v116 op_sel:[0,0,1]
	v_ashrrev_i32_e32 v111, 31, v110
	v_lshl_add_u64 v[106:107], s[4:5], 0, v[106:107]
	v_pk_mul_f32 v[48:49], v[48:49], s[40:41] op_sel_hi:[1,0]
	v_pk_mul_f32 v[50:51], v[50:51], s[40:41] op_sel_hi:[1,0]
	v_lshl_add_u64 v[106:107], v[106:107], 0, v[110:111]
	v_pk_mul_f32 v[54:55], v[54:55], s[40:41] op_sel_hi:[1,0]
	v_med3_f32 v50, v50, s83, v232
	v_med3_f32 v51, v51, s83, v232
	v_med3_f32 v109, v48, s83, v232
	v_mov_b32_e32 v48, v157
	global_store_dwordx2 v[106:107], v[112:113], off
	global_store_dwordx2 v[106:107], v[114:115], off offset:128
	v_pk_mul_f32 v[52:53], v[52:53], s[40:41] op_sel_hi:[1,0]
	v_med3_f32 v114, v49, s83, v232
	v_cvt_pk_fp8_f32 v48, v50, v51
	v_med3_f32 v50, v54, s83, v232
	v_med3_f32 v51, v55, s83, v232
	v_mov_b32_e32 v49, v157
	v_pk_mul_f32 v[12:13], v[12:13], s[40:41] op_sel_hi:[1,0]
	v_pk_mul_f32 v[14:15], v[14:15], s[40:41] op_sel_hi:[1,0]
	v_cvt_pk_fp8_f32 v49, v50, v51
	v_med3_f32 v50, v52, s83, v232
	v_med3_f32 v51, v53, s83, v232
	v_pk_mul_f32 v[52:53], v[142:143], s[40:41] op_sel_hi:[1,0]
	v_med3_f32 v14, v14, s83, v232
	v_med3_f32 v15, v15, s83, v232
	v_med3_f32 v54, v12, s83, v232
	v_mov_b32_e32 v12, v157
	v_med3_f32 v55, v13, s83, v232
	v_cvt_pk_fp8_f32 v12, v14, v15
	v_med3_f32 v14, v52, s83, v232
	v_med3_f32 v15, v53, s83, v232
	v_mov_b32_e32 v13, v157
	v_cvt_pk_fp8_f32 v13, v14, v15
	v_or_b32_e32 v112, 16, v108
	v_cvt_pk_fp8_f32 v49, v50, v51 op_sel:[0,0,1]
	v_pk_mul_f32 v[50:51], v[140:141], s[40:41] op_sel_hi:[1,0]
	v_ashrrev_i32_e32 v113, 31, v112
	v_cvt_pk_fp8_f32 v48, v109, v114 op_sel:[0,0,1]
	v_med3_f32 v14, v50, s83, v232
	v_med3_f32 v15, v51, s83, v232
	v_lshlrev_b64 v[112:113], 11, v[112:113]
	v_cvt_pk_fp8_f32 v12, v54, v55 op_sel:[0,0,1]
	v_cvt_pk_fp8_f32 v13, v14, v15 op_sel:[0,0,1]
	v_lshl_add_u64 v[14:15], s[4:5], 0, v[112:113]
	v_lshl_add_u64 v[14:15], v[14:15], 0, v[110:111]
	v_pk_mul_f32 v[4:5], v[4:5], s[40:41] op_sel_hi:[1,0]
	v_pk_mul_f32 v[6:7], v[6:7], s[40:41] op_sel_hi:[1,0]
	global_store_dwordx2 v[14:15], v[48:49], off
	global_store_dwordx2 v[14:15], v[12:13], off offset:128
	v_pk_mul_f32 v[48:49], v[58:59], s[40:41] op_sel_hi:[1,0]
	v_med3_f32 v6, v6, s83, v232
	v_med3_f32 v7, v7, s83, v232
	v_med3_f32 v50, v4, s83, v232
	v_mov_b32_e32 v4, v157
	v_med3_f32 v51, v5, s83, v232
	v_cvt_pk_fp8_f32 v4, v6, v7
	v_med3_f32 v6, v48, s83, v232
	v_med3_f32 v7, v49, s83, v232
	v_mov_b32_e32 v5, v157
	v_cvt_pk_fp8_f32 v5, v6, v7
	v_pk_mul_f32 v[14:15], v[56:57], s[40:41] op_sel_hi:[1,0]
	v_or_b32_e32 v12, 32, v108
	v_med3_f32 v6, v14, s83, v232
	v_med3_f32 v7, v15, s83, v232
	v_cvt_pk_fp8_f32 v5, v6, v7 op_sel:[0,0,1]
	v_pk_mul_f32 v[6:7], v[16:17], s[40:41] op_sel_hi:[1,0]
	v_pk_mul_f32 v[14:15], v[18:19], s[40:41] op_sel_hi:[1,0]
	v_pk_mul_f32 v[18:19], v[168:169], s[40:41] op_sel_hi:[1,0]
	v_med3_f32 v14, v14, s83, v232
	v_med3_f32 v15, v15, s83, v232
	v_med3_f32 v48, v6, s83, v232
	v_mov_b32_e32 v6, v157
	v_med3_f32 v49, v7, s83, v232
	v_cvt_pk_fp8_f32 v6, v14, v15
	v_med3_f32 v14, v18, s83, v232
	v_med3_f32 v15, v19, s83, v232
	v_mov_b32_e32 v7, v157
	v_cvt_pk_fp8_f32 v7, v14, v15
	v_pk_mul_f32 v[16:17], v[70:71], s[40:41] op_sel_hi:[1,0]
	v_ashrrev_i32_e32 v13, 31, v12
	v_cvt_pk_fp8_f32 v4, v50, v51 op_sel:[0,0,1]
	v_med3_f32 v14, v16, s83, v232
	v_med3_f32 v15, v17, s83, v232
	v_lshlrev_b64 v[12:13], 11, v[12:13]
	v_cvt_pk_fp8_f32 v6, v48, v49 op_sel:[0,0,1]
	v_cvt_pk_fp8_f32 v7, v14, v15 op_sel:[0,0,1]
	v_lshl_add_u64 v[12:13], s[4:5], 0, v[12:13]
	v_lshl_add_u64 v[12:13], v[12:13], 0, v[110:111]
	global_store_dwordx2 v[12:13], v[4:5], off
	global_store_dwordx2 v[12:13], v[6:7], off offset:128
	v_pk_mul_f32 v[6:7], v[8:9], s[40:41] op_sel_hi:[1,0]
	v_pk_mul_f32 v[8:9], v[10:11], s[40:41] op_sel_hi:[1,0]
	v_pk_mul_f32 v[12:13], v[66:67], s[40:41] op_sel_hi:[1,0]
	v_med3_f32 v8, v8, s83, v232
	v_med3_f32 v9, v9, s83, v232
	v_med3_f32 v14, v6, s83, v232
	v_mov_b32_e32 v6, v157
	v_med3_f32 v15, v7, s83, v232
	v_cvt_pk_fp8_f32 v6, v8, v9
	v_med3_f32 v8, v12, s83, v232
	v_med3_f32 v9, v13, s83, v232
	v_mov_b32_e32 v7, v157
	v_cvt_pk_fp8_f32 v7, v8, v9
	v_pk_mul_f32 v[10:11], v[64:65], s[40:41] op_sel_hi:[1,0]
	v_cvt_pk_fp8_f32 v6, v14, v15 op_sel:[0,0,1]
	v_med3_f32 v8, v10, s83, v232
	v_med3_f32 v9, v11, s83, v232
	v_cvt_pk_fp8_f32 v7, v8, v9 op_sel:[0,0,1]
	v_pk_mul_f32 v[8:9], v[20:21], s[40:41] op_sel_hi:[1,0]
	v_pk_mul_f32 v[10:11], v[22:23], s[40:41] op_sel_hi:[1,0]
	v_pk_mul_f32 v[14:15], v[74:75], s[40:41] op_sel_hi:[1,0]
	v_med3_f32 v10, v10, s83, v232
	v_med3_f32 v11, v11, s83, v232
	v_med3_f32 v16, v8, s83, v232
	v_mov_b32_e32 v8, v157
	v_med3_f32 v17, v9, s83, v232
	v_cvt_pk_fp8_f32 v8, v10, v11
	v_med3_f32 v10, v14, s83, v232
	v_med3_f32 v11, v15, s83, v232
	v_mov_b32_e32 v9, v157
	v_cvt_pk_fp8_f32 v9, v10, v11
	v_or_b32_e32 v4, 48, v108
	v_pk_mul_f32 v[12:13], v[72:73], s[40:41] op_sel_hi:[1,0]
	v_ashrrev_i32_e32 v5, 31, v4
	v_med3_f32 v10, v12, s83, v232
	v_med3_f32 v11, v13, s83, v232
	v_lshlrev_b64 v[4:5], 11, v[4:5]
	v_cvt_pk_fp8_f32 v8, v16, v17 op_sel:[0,0,1]
	v_cvt_pk_fp8_f32 v9, v10, v11 op_sel:[0,0,1]
	v_lshl_add_u64 v[4:5], s[4:5], 0, v[4:5]
	v_lshl_add_u64 v[4:5], v[4:5], 0, v[110:111]
	global_store_dwordx2 v[4:5], v[6:7], off
	global_store_dwordx2 v[4:5], v[8:9], off offset:128
	v_pk_mul_f32 v[6:7], v[24:25], s[40:41] op_sel_hi:[1,0]
	v_pk_mul_f32 v[8:9], v[26:27], s[40:41] op_sel_hi:[1,0]
	v_pk_mul_f32 v[12:13], v[78:79], s[40:41] op_sel_hi:[1,0]
	v_med3_f32 v8, v8, s83, v232
	v_med3_f32 v9, v9, s83, v232
	v_med3_f32 v14, v6, s83, v232
	v_mov_b32_e32 v6, v157
	v_med3_f32 v15, v7, s83, v232
	v_cvt_pk_fp8_f32 v6, v8, v9
	v_med3_f32 v8, v12, s83, v232
	v_med3_f32 v9, v13, s83, v232
	v_mov_b32_e32 v7, v157
	v_cvt_pk_fp8_f32 v7, v8, v9
	v_pk_mul_f32 v[10:11], v[76:77], s[40:41] op_sel_hi:[1,0]
	v_cvt_pk_fp8_f32 v6, v14, v15 op_sel:[0,0,1]
	v_med3_f32 v8, v10, s83, v232
	v_med3_f32 v9, v11, s83, v232
	v_cvt_pk_fp8_f32 v7, v8, v9 op_sel:[0,0,1]
	v_pk_mul_f32 v[8:9], v[28:29], s[40:41] op_sel_hi:[1,0]
	v_pk_mul_f32 v[10:11], v[30:31], s[40:41] op_sel_hi:[1,0]
	v_pk_mul_f32 v[14:15], v[82:83], s[40:41] op_sel_hi:[1,0]
	v_med3_f32 v10, v10, s83, v232
	v_med3_f32 v11, v11, s83, v232
	v_med3_f32 v16, v8, s83, v232
	v_mov_b32_e32 v8, v157
	v_med3_f32 v17, v9, s83, v232
	v_cvt_pk_fp8_f32 v8, v10, v11
	v_med3_f32 v10, v14, s83, v232
	v_med3_f32 v11, v15, s83, v232
	v_mov_b32_e32 v9, v157
	v_cvt_pk_fp8_f32 v9, v10, v11
	v_pk_mul_f32 v[12:13], v[80:81], s[40:41] op_sel_hi:[1,0]
	v_lshl_add_u64 v[4:5], v[106:107], 0, s[2:3]
	v_med3_f32 v10, v12, s83, v232
	v_med3_f32 v11, v13, s83, v232
	v_cvt_pk_fp8_f32 v8, v16, v17 op_sel:[0,0,1]
	v_cvt_pk_fp8_f32 v9, v10, v11 op_sel:[0,0,1]
	s_mov_b32 s2, 0x40000
	v_add_co_u32_e32 v10, vcc, s2, v106
	v_pk_mul_f32 v[12:13], v[86:87], s[40:41] op_sel_hi:[1,0]
	s_nop 0
	v_addc_co_u32_e32 v11, vcc, 0, v107, vcc
	global_store_dwordx2 v[10:11], v[6:7], off
	global_store_dwordx2 v[4:5], v[8:9], off offset:128
	v_pk_mul_f32 v[6:7], v[32:33], s[40:41] op_sel_hi:[1,0]
	v_pk_mul_f32 v[8:9], v[34:35], s[40:41] op_sel_hi:[1,0]
	v_med3_f32 v14, v6, s83, v232
	v_med3_f32 v8, v8, s83, v232
	v_med3_f32 v9, v9, s83, v232
	v_mov_b32_e32 v6, v157
	v_med3_f32 v15, v7, s83, v232
	v_cvt_pk_fp8_f32 v6, v8, v9
	v_med3_f32 v8, v12, s83, v232
	v_med3_f32 v9, v13, s83, v232
	v_mov_b32_e32 v7, v157
	v_cvt_pk_fp8_f32 v7, v8, v9
	v_pk_mul_f32 v[10:11], v[84:85], s[40:41] op_sel_hi:[1,0]
	v_cvt_pk_fp8_f32 v6, v14, v15 op_sel:[0,0,1]
	v_med3_f32 v8, v10, s83, v232
	v_med3_f32 v9, v11, s83, v232
	v_cvt_pk_fp8_f32 v7, v8, v9 op_sel:[0,0,1]
	v_pk_mul_f32 v[8:9], v[36:37], s[40:41] op_sel_hi:[1,0]
	v_pk_mul_f32 v[10:11], v[38:39], s[40:41] op_sel_hi:[1,0]
	v_pk_mul_f32 v[14:15], v[90:91], s[40:41] op_sel_hi:[1,0]
	v_med3_f32 v10, v10, s83, v232
	v_med3_f32 v11, v11, s83, v232
	v_med3_f32 v16, v8, s83, v232
	v_mov_b32_e32 v8, v157
	v_med3_f32 v17, v9, s83, v232
	v_cvt_pk_fp8_f32 v8, v10, v11
	v_med3_f32 v10, v14, s83, v232
	v_med3_f32 v11, v15, s83, v232
	v_mov_b32_e32 v9, v157
	v_cvt_pk_fp8_f32 v9, v10, v11
	v_pk_mul_f32 v[12:13], v[88:89], s[40:41] op_sel_hi:[1,0]
	s_mov_b64 s[2:3], 0x48000
	v_med3_f32 v10, v12, s83, v232
	v_med3_f32 v11, v13, s83, v232
	v_lshl_add_u64 v[4:5], v[106:107], 0, s[2:3]
	v_cvt_pk_fp8_f32 v8, v16, v17 op_sel:[0,0,1]
	v_cvt_pk_fp8_f32 v9, v10, v11 op_sel:[0,0,1]
	s_mov_b32 s2, 0x48000
	v_add_co_u32_e32 v10, vcc, s2, v106
	v_pk_mul_f32 v[12:13], v[94:95], s[40:41] op_sel_hi:[1,0]
	s_nop 0
	v_addc_co_u32_e32 v11, vcc, 0, v107, vcc
	global_store_dwordx2 v[10:11], v[6:7], off
	global_store_dwordx2 v[4:5], v[8:9], off offset:128
	v_pk_mul_f32 v[6:7], v[40:41], s[40:41] op_sel_hi:[1,0]
	v_pk_mul_f32 v[8:9], v[42:43], s[40:41] op_sel_hi:[1,0]
	v_med3_f32 v14, v6, s83, v232
	v_med3_f32 v8, v8, s83, v232
	v_med3_f32 v9, v9, s83, v232
	v_mov_b32_e32 v6, v157
	v_med3_f32 v15, v7, s83, v232
	v_cvt_pk_fp8_f32 v6, v8, v9
	v_med3_f32 v8, v12, s83, v232
	v_med3_f32 v9, v13, s83, v232
	v_mov_b32_e32 v7, v157
	v_cvt_pk_fp8_f32 v7, v8, v9
	v_pk_mul_f32 v[10:11], v[92:93], s[40:41] op_sel_hi:[1,0]
	v_pk_mul_f32 v[44:45], v[130:131], v[44:45]
	v_med3_f32 v8, v10, s83, v232
	v_med3_f32 v9, v11, s83, v232
	v_cvt_pk_fp8_f32 v7, v8, v9 op_sel:[0,0,1]
	v_pk_mul_f32 v[8:9], v[44:45], s[40:41] op_sel_hi:[1,0]
	v_pk_mul_f32 v[10:11], v[46:47], s[40:41] op_sel_hi:[1,0]
	v_cvt_pk_fp8_f32 v6, v14, v15 op_sel:[0,0,1]
	v_pk_mul_f32 v[14:15], v[98:99], s[40:41] op_sel_hi:[1,0]
	v_med3_f32 v10, v10, s83, v232
	v_med3_f32 v11, v11, s83, v232
	v_med3_f32 v16, v8, s83, v232
	v_mov_b32_e32 v8, v157
	v_med3_f32 v17, v9, s83, v232
	v_cvt_pk_fp8_f32 v8, v10, v11
	v_med3_f32 v10, v14, s83, v232
	v_med3_f32 v11, v15, s83, v232
	v_mov_b32_e32 v9, v157
	v_cvt_pk_fp8_f32 v9, v10, v11
	v_pk_mul_f32 v[12:13], v[96:97], s[40:41] op_sel_hi:[1,0]
	s_mov_b64 s[2:3], 0x50000
	v_med3_f32 v10, v12, s83, v232
	v_med3_f32 v11, v13, s83, v232
	v_lshl_add_u64 v[4:5], v[106:107], 0, s[2:3]
	v_cvt_pk_fp8_f32 v8, v16, v17 op_sel:[0,0,1]
	v_cvt_pk_fp8_f32 v9, v10, v11 op_sel:[0,0,1]
	s_mov_b32 s2, 0x50000
	v_add_co_u32_e32 v10, vcc, s2, v106
	v_pk_mul_f32 v[12:13], v[102:103], s[40:41] op_sel_hi:[1,0]
	s_nop 0
	v_addc_co_u32_e32 v11, vcc, 0, v107, vcc
	global_store_dwordx2 v[10:11], v[6:7], off
	global_store_dwordx2 v[4:5], v[8:9], off offset:128
	v_pk_mul_f32 v[6:7], v[60:61], s[40:41] op_sel_hi:[1,0]
	v_pk_mul_f32 v[8:9], v[62:63], s[40:41] op_sel_hi:[1,0]
	v_med3_f32 v14, v6, s83, v232
	v_med3_f32 v8, v8, s83, v232
	v_med3_f32 v9, v9, s83, v232
	v_mov_b32_e32 v6, v157
	v_med3_f32 v15, v7, s83, v232
	v_cvt_pk_fp8_f32 v6, v8, v9
	v_med3_f32 v8, v12, s83, v232
	v_med3_f32 v9, v13, s83, v232
	v_mov_b32_e32 v7, v157
	v_cvt_pk_fp8_f32 v7, v8, v9
	v_pk_add_f32 v[104:105], v[104:105], 0.5 op_sel_hi:[1,0]
	v_pk_mul_f32 v[10:11], v[100:101], s[40:41] op_sel_hi:[1,0]
	v_pk_mul_f32 v[2:3], v[146:147], v[2:3]
	v_pk_mul_f32 v[104:105], v[104:105], s[38:39] op_sel_hi:[1,0]
	v_med3_f32 v8, v10, s83, v232
	v_med3_f32 v9, v11, s83, v232
	v_pk_mul_f32 v[104:105], v[136:137], v[104:105]
	v_cvt_pk_fp8_f32 v7, v8, v9 op_sel:[0,0,1]
	v_pk_mul_f32 v[2:3], v[2:3], s[40:41] op_sel_hi:[1,0]
	v_pk_mul_f32 v[8:9], v[68:69], s[40:41] op_sel_hi:[1,0]
	v_pk_mul_f32 v[10:11], v[104:105], s[40:41] op_sel_hi:[1,0]
	v_med3_f32 v8, v8, s83, v232
	v_med3_f32 v9, v9, s83, v232
	v_med3_f32 v12, v2, s83, v232
	v_mov_b32_e32 v2, v157
	v_med3_f32 v13, v3, s83, v232
	v_cvt_pk_fp8_f32 v2, v8, v9
	v_med3_f32 v8, v10, s83, v232
	v_med3_f32 v9, v11, s83, v232
	v_mov_b32_e32 v3, v157
	v_pk_mul_f32 v[0:1], v[0:1], s[38:39] op_sel_hi:[1,0]
	v_cvt_pk_fp8_f32 v3, v8, v9
	v_pk_mul_f32 v[0:1], v[138:139], v[0:1]
	v_cvt_pk_fp8_f32 v6, v14, v15 op_sel:[0,0,1]
	v_pk_mul_f32 v[0:1], v[0:1], s[40:41] op_sel_hi:[1,0]
	v_cvt_pk_fp8_f32 v2, v12, v13 op_sel:[0,0,1]
	v_med3_f32 v0, v0, s83, v232
	v_med3_f32 v1, v1, s83, v232
	v_cvt_pk_fp8_f32 v3, v0, v1 op_sel:[0,0,1]
	v_add_co_u32_e32 v0, vcc, s84, v106
	s_mov_b64 s[2:3], 0x58000
	s_nop 0
	v_addc_co_u32_e32 v1, vcc, 0, v107, vcc
	s_and_b64 vcc, exec, s[0:1]
	s_mov_b32 s89, s85
	s_mov_b32 s90, s86
	v_lshl_add_u64 v[4:5], v[106:107], 0, s[2:3]
	global_store_dwordx2 v[0:1], v[6:7], off
	global_store_dwordx2 v[4:5], v[2:3], off offset:128
	s_cbranch_vccz .LBB0_2184
	s_waitcnt vmcnt(0)
	s_cmpk_lt_u32 s60, 0x100
	s_cbranch_scc1 .LBB0_2195
	s_barrier

.LBB0_2252:
	v_ashrrev_i32_e32 v1, 31, v8
	v_lshrrev_b32_e32 v1, 26, v1
	v_add_u32_e32 v1, v8, v1
	v_ashrrev_i32_e32 v9, 6, v1
	v_bfe_i32 v1, v8, 27, 1
	v_lshlrev_b32_e32 v0, 4, v8
	v_lshrrev_b32_e32 v1, 22, v1
	v_add_u32_e32 v1, v0, v1
	v_and_b32_e32 v1, 0xfffffc00, v1
	v_sub_u32_e32 v1, v0, v1
	s_waitcnt lgkmcnt(0)
	v_lshrrev_b32_e32 v2, 4, v1
	v_bitop3_b32 v1, v2, v1, 32 bitop3:0x6c
	v_ashrrev_i32_e32 v3, 31, v1
	v_lshrrev_b32_e32 v3, 26, v3
	v_add_u32_e32 v3, v1, v3
	v_lshlrev_b32_e32 v2, 3, v9
	v_ashrrev_i32_e32 v10, 6, v3
	v_and_b32_e32 v3, 0xc0, v3
	v_and_b32_e32 v2, -16, v2
	v_sub_u32_e32 v1, v1, v3
	v_mov_b32_e32 v3, 1
	v_add_u32_e32 v2, v10, v2
	v_ashrrev_i16_sdwa v1, v3, sext(v1) dst_sel:DWORD dst_unused:UNUSED_PAD src0_sel:DWORD src1_sel:BYTE_0
	v_lshlrev_b32_e32 v4, 5, v9
	v_bfe_i32 v11, v1, 0, 16
	v_lshlrev_b32_e32 v1, 1, v2
	v_lshrrev_b32_e32 v5, 2, v2
	v_and_b32_e32 v6, 3, v10
	s_mov_b32 s1, 0x1fffe0
	v_and_b32_e32 v4, 32, v4
	v_and_b32_e32 v1, 24, v1
	v_and_b32_e32 v5, 4, v5
	v_and_or_b32 v6, v2, s1, v6
	s_add_u32 s25, s2, 0x3660c000
	v_or3_b32 v1, v6, v5, v1
	v_add_lshl_u32 v4, v4, v11, 1
	v_add_u32_e32 v0, 0x2000, v0
	s_addc_u32 s26, s3, 0
	v_lshl_add_u32 v146, v1, 11, v4
	v_ashrrev_i32_e32 v1, 31, v0
	s_add_u32 s27, s2, 0x3620c000
	v_lshrrev_b32_e32 v1, 22, v1
	s_addc_u32 s28, s3, 0
	v_add_u32_e32 v1, v0, v1
	s_add_i32 s4, s4, s5
	v_ashrrev_i32_e32 v12, 10, v1
	s_ashr_i32 s5, s4, 31
	v_mul_i32_i24_e32 v1, 0x400, v12
	s_lshr_b32 s5, s5, 26
	v_sub_u32_e32 v0, v0, v1
	s_add_i32 s5, s4, s5
	v_lshrrev_b32_e32 v1, 4, v0
	s_ashr_i32 s6, s5, 6
	s_and_b32 s5, s5, 0xffc0
	v_bitop3_b32 v0, v1, v0, 32 bitop3:0x6c
	s_sub_i32 s4, s4, s5
	v_lshl_add_u32 v144, v2, 11, v4
	v_ashrrev_i32_e32 v2, 31, v0
	s_bfe_i32 s5, s4, 0x80000
	v_lshrrev_b32_e32 v2, 26, v2
	s_bfe_u32 s5, s5, 0x3000c
	v_add_u32_e32 v2, v0, v2
	s_add_i32 s5, s4, s5
	v_lshlrev_b32_e32 v1, 3, v12
	v_ashrrev_i32_e32 v13, 6, v2
	v_and_b32_e32 v2, 0xc0, v2
	s_bfe_i32 s7, s5, 0x80000
	s_and_b32 s5, s5, 0xf8
	v_and_b32_e32 v1, -16, v1
	v_sub_u32_e32 v0, v0, v2
	s_sub_i32 s4, s4, s5
	v_add_u32_e32 v1, v13, v1
	v_ashrrev_i16_sdwa v0, v3, sext(v0) dst_sel:DWORD dst_unused:UNUSED_PAD src0_sel:DWORD src1_sel:BYTE_0
	v_and_b32_e32 v3, 3, v13
	s_lshl_b32 s6, s6, 3
	s_sext_i32_i16 s7, s7
	s_sext_i32_i8 s4, s4
	v_and_or_b32 v3, v1, s1, v3
	s_ashr_i32 s1, s23, 6
	s_add_i32 s55, s6, s4
	s_ashr_i32 s54, s7, 3
	s_ashr_i32 s0, s23, 8
	s_lshl_b32 s29, s1, 10
	s_lshl_b32 s4, s54, 19
	s_lshl_b32 s5, s55, 19
	s_add_u32 s16, s27, s4
	v_lshlrev_b32_e32 v4, 5, v12
	v_bfe_i32 v14, v0, 0, 16
	v_lshlrev_b32_e32 v0, 1, v1
	v_lshrrev_b32_e32 v2, 2, v1
	s_addc_u32 s17, s28, 0
	s_add_i32 s30, s29, 0
	v_and_b32_e32 v4, 32, v4
	v_and_b32_e32 v0, 24, v0
	v_and_b32_e32 v2, 4, v2
	s_add_i32 m0, s30, 0x10000
	v_or3_b32 v0, v3, v2, v0
	v_add_lshl_u32 v2, v4, v14, 1
	global_load_lds_dwordx4 v146, s[16:17]
	s_add_i32 m0, s30, 0x12000
	v_lshl_add_u32 v150, v0, 11, v2
	s_add_u32 s18, s25, s5
	global_load_lds_dwordx4 v150, s[16:17]
	s_addc_u32 s19, s26, 0
	s_mov_b32 m0, s30
	s_add_i32 s31, s30, 0x2000
	v_lshl_add_u32 v148, v1, 11, v2
	global_load_lds_dwordx4 v144, s[18:19]
	s_mov_b32 m0, s31
	s_add_u32 s4, s16, 0x40000
	global_load_lds_dwordx4 v148, s[18:19]
	s_addc_u32 s5, s17, 0
	s_add_i32 m0, s30, 0x14000
	v_mov_b32_e32 v153, 0
	global_load_lds_dwordx4 v146, s[4:5]
	s_add_i32 m0, s30, 0x16000
	v_mov_b32_e32 v147, v153
	global_load_lds_dwordx4 v150, s[4:5]
	s_add_u32 s4, s18, 0x40000
	s_addc_u32 s5, s19, 0
	s_add_i32 s38, s30, 0x4000
	s_mov_b32 m0, s38
	s_add_i32 s39, s30, 0x6000
	global_load_lds_dwordx4 v144, s[4:5]
	s_mov_b32 m0, s39
	v_mov_b32_e32 v151, v153
	global_load_lds_dwordx4 v148, s[4:5]
	v_mov_b32_e32 v145, v153
	v_mov_b32_e32 v149, v153
	s_mov_b32 s40, 0
	v_lshl_add_u64 v[6:7], s[16:17], 0, v[146:147]
	v_lshl_add_u64 v[4:5], s[16:17], 0, v[150:151]
	v_lshl_add_u64 v[2:3], s[18:19], 0, v[144:145]
	s_cmp_lg_u32 s0, 0
	v_lshl_add_u64 v[0:1], s[18:19], 0, v[148:149]
	s_cbranch_scc1 .LBB0_2254
	s_barrier

.LBB0_2262:
	ds_read_b128 v[8:11], v179
	ds_read_b128 v[12:15], v179 offset:1024
	ds_read_b128 v[0:3], v179 offset:2048
	ds_read_b128 v[4:7], v179 offset:3072
	s_add_u32 s18, s16, 0xfffc0080
	s_addc_u32 s19, s17, -1
	s_cmp_eq_u32 s62, 12
	s_cselect_b32 s21, s56, s19
	s_cselect_b32 s20, s57, s18
	s_cselect_b32 s19, s58, s61
	s_cselect_b32 s18, s59, s60
	v_lshl_add_u64 v[162:163], s[16:17], 0, v[156:157]
	s_add_i32 m0, s30, 0xc000
	ds_read_b128 v[166:169], v180
	ds_read_b128 v[170:173], v180 offset:1024
	ds_read_b128 v[182:185], v180 offset:2048
	ds_read_b128 v[186:189], v180 offset:3072
	ds_read_b128 v[190:193], v180 offset:4096
	ds_read_b128 v[194:197], v180 offset:5120
	ds_read_b128 v[198:201], v180 offset:6144
	ds_read_b128 v[202:205], v180 offset:7168
	global_load_lds_dwordx4 v[162:163], off
	v_lshl_add_u64 v[162:163], s[16:17], 0, v[154:155]
	s_add_i32 m0, s30, 0xe000
	s_nop 0
	global_load_lds_dwordx4 v[162:163], off
	s_waitcnt lgkmcnt(8)
	s_barrier
	s_waitcnt lgkmcnt(0)
	s_setprio 1
	s_waitcnt lgkmcnt(0)
	v_mfma_scale_f32_16x16x128_f8f6f4 v[140:143], v[8:15], v[166:173], v[140:143], v175, v175 op_sel_hi:[0,0,0]
	v_mfma_scale_f32_16x16x128_f8f6f4 v[136:139], v[0:7], v[166:173], v[136:139], v175, v175 op_sel_hi:[0,0,0]
	v_mfma_scale_f32_16x16x128_f8f6f4 v[128:131], v[8:15], v[182:189], v[128:131], v175, v175 op_sel_hi:[0,0,0]
	v_mfma_scale_f32_16x16x128_f8f6f4 v[120:123], v[0:7], v[182:189], v[120:123], v175, v175 op_sel_hi:[0,0,0]
	v_mfma_scale_f32_16x16x128_f8f6f4 v[112:115], v[8:15], v[190:197], v[112:115], v175, v175 op_sel_hi:[0,0,0]
	v_mfma_scale_f32_16x16x128_f8f6f4 v[104:107], v[0:7], v[190:197], v[104:107], v175, v175 op_sel_hi:[0,0,0]
	v_mfma_scale_f32_16x16x128_f8f6f4 v[96:99], v[8:15], v[198:205], v[96:99], v175, v175 op_sel_hi:[0,0,0]
	v_mfma_scale_f32_16x16x128_f8f6f4 v[88:91], v[0:7], v[198:205], v[88:91], v175, v175 op_sel_hi:[0,0,0]
	s_setprio 0
	s_barrier
	s_add_i32 s63, s46, s29
	v_lshl_add_u64 v[162:163], s[18:19], 0, v[146:147]
	s_mov_b32 m0, s63
	ds_read_b128 v[206:209], v181
	ds_read_b128 v[210:213], v181 offset:1024
	ds_read_b128 v[214:217], v181 offset:2048
	ds_read_b128 v[218:221], v181 offset:3072
	global_load_lds_dwordx4 v[162:163], off
	v_lshl_add_u64 v[164:165], s[18:19], 0, v[150:151]
	s_add_i32 m0, s63, 0x2000
	s_nop 0
	global_load_lds_dwordx4 v[164:165], off
	s_barrier
	s_waitcnt lgkmcnt(0)
	s_setprio 1
	s_waitcnt lgkmcnt(0)
	v_mfma_scale_f32_16x16x128_f8f6f4 v[132:135], v[206:213], v[166:173], v[132:135], v175, v175 op_sel_hi:[0,0,0]
	v_mfma_scale_f32_16x16x128_f8f6f4 v[124:127], v[214:221], v[166:173], v[124:127], v175, v175 op_sel_hi:[0,0,0]
	v_mfma_scale_f32_16x16x128_f8f6f4 v[116:119], v[206:213], v[182:189], v[116:119], v175, v175 op_sel_hi:[0,0,0]
	v_mfma_scale_f32_16x16x128_f8f6f4 v[108:111], v[214:221], v[182:189], v[108:111], v175, v175 op_sel_hi:[0,0,0]
	v_mfma_scale_f32_16x16x128_f8f6f4 v[100:103], v[206:213], v[190:197], v[100:103], v175, v175 op_sel_hi:[0,0,0]
	v_mfma_scale_f32_16x16x128_f8f6f4 v[92:95], v[214:221], v[190:197], v[92:95], v175, v175 op_sel_hi:[0,0,0]
	v_mfma_scale_f32_16x16x128_f8f6f4 v[84:87], v[206:213], v[198:205], v[84:87], v175, v175 op_sel_hi:[0,0,0]
	v_mfma_scale_f32_16x16x128_f8f6f4 v[80:83], v[214:221], v[198:205], v[80:83], v175, v175 op_sel_hi:[0,0,0]
	s_setprio 0
	s_mov_b32 m0, s30
	v_lshl_add_u64 v[166:167], s[20:21], 0, v[144:145]
	s_barrier
	ds_read_b128 v[182:185], v180 offset:16384
	ds_read_b128 v[186:189], v180 offset:17408
	ds_read_b128 v[190:193], v180 offset:18432
	ds_read_b128 v[194:197], v180 offset:19456
	ds_read_b128 v[198:201], v180 offset:20480
	ds_read_b128 v[202:205], v180 offset:21504
	ds_read_b128 v[224:227], v180 offset:22528
	ds_read_b128 v[228:231], v180 offset:23552
	global_load_lds_dwordx4 v[166:167], off
	v_lshl_add_u64 v[168:169], s[20:21], 0, v[148:149]
	s_mov_b32 m0, s31
	s_nop 0
	global_load_lds_dwordx4 v[168:169], off
	s_barrier
	s_waitcnt lgkmcnt(0)
	s_setprio 1
	s_waitcnt lgkmcnt(0)
	v_mfma_scale_f32_16x16x128_f8f6f4 v[76:79], v[8:15], v[182:189], v[76:79], v175, v175 op_sel_hi:[0,0,0]
	v_mfma_scale_f32_16x16x128_f8f6f4 v[72:75], v[0:7], v[182:189], v[72:75], v175, v175 op_sel_hi:[0,0,0]
	v_mfma_scale_f32_16x16x128_f8f6f4 v[64:67], v[8:15], v[190:197], v[64:67], v175, v175 op_sel_hi:[0,0,0]
	v_mfma_scale_f32_16x16x128_f8f6f4 v[56:59], v[0:7], v[190:197], v[56:59], v175, v175 op_sel_hi:[0,0,0]
	v_mfma_scale_f32_16x16x128_f8f6f4 v[48:51], v[8:15], v[198:205], v[48:51], v175, v175 op_sel_hi:[0,0,0]
	v_mfma_scale_f32_16x16x128_f8f6f4 v[40:43], v[0:7], v[198:205], v[40:43], v175, v175 op_sel_hi:[0,0,0]
	v_mfma_scale_f32_16x16x128_f8f6f4 v[32:35], v[8:15], v[224:231], v[32:35], v175, v175 op_sel_hi:[0,0,0]
	v_mfma_scale_f32_16x16x128_f8f6f4 v[24:27], v[0:7], v[224:231], v[24:27], v175, v175 op_sel_hi:[0,0,0]
	s_setprio 0
	s_barrier
	s_add_u32 s64, s18, 0x40000
	s_addc_u32 s65, s19, 0
	s_add_i32 s63, s47, s29
	v_lshl_add_u64 v[0:1], s[64:65], 0, v[146:147]
	s_mov_b32 m0, s63
	s_nop 0
	global_load_lds_dwordx4 v[0:1], off
	v_lshl_add_u64 v[0:1], s[64:65], 0, v[150:151]
	s_add_i32 m0, s63, 0x2000
	s_nop 0
	global_load_lds_dwordx4 v[0:1], off
	s_waitcnt vmcnt(6)
	s_barrier
	s_setprio 1
	v_mfma_scale_f32_16x16x128_f8f6f4 v[68:71], v[206:213], v[182:189], v[68:71], v175, v175 op_sel_hi:[0,0,0]
	v_mfma_scale_f32_16x16x128_f8f6f4 v[60:63], v[214:221], v[182:189], v[60:63], v175, v175 op_sel_hi:[0,0,0]
	v_mfma_scale_f32_16x16x128_f8f6f4 v[52:55], v[206:213], v[190:197], v[52:55], v175, v175 op_sel_hi:[0,0,0]
	v_mfma_scale_f32_16x16x128_f8f6f4 v[44:47], v[214:221], v[190:197], v[44:47], v175, v175 op_sel_hi:[0,0,0]
	v_mfma_scale_f32_16x16x128_f8f6f4 v[36:39], v[206:213], v[198:205], v[36:39], v175, v175 op_sel_hi:[0,0,0]
	v_mfma_scale_f32_16x16x128_f8f6f4 v[28:31], v[214:221], v[198:205], v[28:31], v175, v175 op_sel_hi:[0,0,0]
	v_mfma_scale_f32_16x16x128_f8f6f4 v[20:23], v[206:213], v[224:231], v[20:23], v175, v175 op_sel_hi:[0,0,0]
	v_mfma_scale_f32_16x16x128_f8f6f4 v[16:19], v[214:221], v[224:231], v[16:19], v175, v175 op_sel_hi:[0,0,0]
	s_setprio 0
	s_add_i32 s63, 0, 0x18000
	v_add_u32_e32 v12, s63, v176
	s_barrier
	ds_read_b128 v[0:3], v12
	ds_read_b128 v[4:7], v12 offset:1024
	ds_read_b128 v[8:11], v12 offset:2048
	ds_read_b128 v[12:15], v12 offset:3072
	s_add_u32 s20, s20, 0x40000
	s_addc_u32 s21, s21, 0
	s_mov_b32 m0, s38
	v_lshl_add_u64 v[170:171], s[20:21], 0, v[144:145]
	ds_read_b128 v[182:185], v180 offset:32768
	ds_read_b128 v[186:189], v180 offset:33792
	ds_read_b128 v[190:193], v180 offset:34816
	ds_read_b128 v[194:197], v180 offset:35840
	ds_read_b128 v[198:201], v180 offset:36864
	ds_read_b128 v[202:205], v180 offset:37888
	ds_read_b128 v[206:209], v180 offset:38912
	ds_read_b128 v[210:213], v180 offset:39936
	global_load_lds_dwordx4 v[170:171], off
	v_lshl_add_u64 v[170:171], s[20:21], 0, v[148:149]
	s_mov_b32 m0, s39
	s_nop 0
	global_load_lds_dwordx4 v[170:171], off
	s_waitcnt lgkmcnt(8)
	s_barrier
	s_waitcnt lgkmcnt(0)
	s_setprio 1
	s_waitcnt lgkmcnt(0)
	v_mfma_scale_f32_16x16x128_f8f6f4 v[140:143], v[0:7], v[182:189], v[140:143], v175, v175 op_sel_hi:[0,0,0]
	v_mfma_scale_f32_16x16x128_f8f6f4 v[136:139], v[8:15], v[182:189], v[136:139], v175, v175 op_sel_hi:[0,0,0]
	v_mfma_scale_f32_16x16x128_f8f6f4 v[128:131], v[0:7], v[190:197], v[128:131], v175, v175 op_sel_hi:[0,0,0]
	v_mfma_scale_f32_16x16x128_f8f6f4 v[120:123], v[8:15], v[190:197], v[120:123], v175, v175 op_sel_hi:[0,0,0]
	v_mfma_scale_f32_16x16x128_f8f6f4 v[112:115], v[0:7], v[198:205], v[112:115], v175, v175 op_sel_hi:[0,0,0]
	v_mfma_scale_f32_16x16x128_f8f6f4 v[104:107], v[8:15], v[198:205], v[104:107], v175, v175 op_sel_hi:[0,0,0]
	v_mfma_scale_f32_16x16x128_f8f6f4 v[96:99], v[0:7], v[206:213], v[96:99], v175, v175 op_sel_hi:[0,0,0]
	v_mfma_scale_f32_16x16x128_f8f6f4 v[88:91], v[8:15], v[206:213], v[88:91], v175, v175 op_sel_hi:[0,0,0]
	s_setprio 0
	s_barrier
	s_add_i32 s20, 0, 0x1c000
	s_add_i32 s21, s63, s29
	v_add_u32_e32 v152, s20, v176
	v_lshl_add_u64 v[162:163], v[162:163], 0, s[4:5]
	s_mov_b32 m0, s21
	ds_read_b128 v[214:217], v152
	ds_read_b128 v[218:221], v152 offset:1024
	ds_read_b128 v[224:227], v152 offset:2048
	ds_read_b128 v[228:231], v152 offset:3072
	global_load_lds_dwordx4 v[162:163], off
	v_lshl_add_u64 v[162:163], v[164:165], 0, s[4:5]
	s_add_i32 m0, s21, 0x2000
	s_nop 0
	global_load_lds_dwordx4 v[162:163], off
	s_barrier
	s_waitcnt lgkmcnt(0)
	s_setprio 1
	s_waitcnt lgkmcnt(0)
	v_mfma_scale_f32_16x16x128_f8f6f4 v[132:135], v[214:221], v[182:189], v[132:135], v175, v175 op_sel_hi:[0,0,0]
	v_mfma_scale_f32_16x16x128_f8f6f4 v[124:127], v[224:231], v[182:189], v[124:127], v175, v175 op_sel_hi:[0,0,0]
	v_mfma_scale_f32_16x16x128_f8f6f4 v[116:119], v[214:221], v[190:197], v[116:119], v175, v175 op_sel_hi:[0,0,0]
	v_mfma_scale_f32_16x16x128_f8f6f4 v[108:111], v[224:231], v[190:197], v[108:111], v175, v175 op_sel_hi:[0,0,0]
	v_mfma_scale_f32_16x16x128_f8f6f4 v[100:103], v[214:221], v[198:205], v[100:103], v175, v175 op_sel_hi:[0,0,0]
	v_mfma_scale_f32_16x16x128_f8f6f4 v[92:95], v[224:231], v[198:205], v[92:95], v175, v175 op_sel_hi:[0,0,0]
	v_mfma_scale_f32_16x16x128_f8f6f4 v[84:87], v[214:221], v[206:213], v[84:87], v175, v175 op_sel_hi:[0,0,0]
	v_mfma_scale_f32_16x16x128_f8f6f4 v[80:83], v[224:231], v[206:213], v[80:83], v175, v175 op_sel_hi:[0,0,0]
	s_setprio 0
	s_mov_b32 m0, s43
	v_lshl_add_u64 v[162:163], v[166:167], 0, s[4:5]
	s_barrier
	ds_read_b128 v[182:185], v180 offset:49152
	ds_read_b128 v[186:189], v180 offset:50176
	ds_read_b128 v[190:193], v180 offset:51200
	ds_read_b128 v[194:197], v180 offset:52224
	ds_read_b128 v[198:201], v180 offset:53248
	ds_read_b128 v[202:205], v180 offset:54272
	ds_read_b128 v[206:209], v180 offset:55296
	ds_read_b128 v[210:213], v180 offset:56320
	global_load_lds_dwordx4 v[162:163], off
	v_lshl_add_u64 v[162:163], v[168:169], 0, s[4:5]
	s_mov_b32 m0, s44
	s_nop 0
	global_load_lds_dwordx4 v[162:163], off
	s_barrier
	s_waitcnt lgkmcnt(0)
	s_setprio 1
	s_waitcnt lgkmcnt(0)
	v_mfma_scale_f32_16x16x128_f8f6f4 v[76:79], v[0:7], v[182:189], v[76:79], v175, v175 op_sel_hi:[0,0,0]
	v_mfma_scale_f32_16x16x128_f8f6f4 v[72:75], v[8:15], v[182:189], v[72:75], v175, v175 op_sel_hi:[0,0,0]
	v_mfma_scale_f32_16x16x128_f8f6f4 v[64:67], v[0:7], v[190:197], v[64:67], v175, v175 op_sel_hi:[0,0,0]
	v_mfma_scale_f32_16x16x128_f8f6f4 v[56:59], v[8:15], v[190:197], v[56:59], v175, v175 op_sel_hi:[0,0,0]
	v_mfma_scale_f32_16x16x128_f8f6f4 v[48:51], v[0:7], v[198:205], v[48:51], v175, v175 op_sel_hi:[0,0,0]
	v_mfma_scale_f32_16x16x128_f8f6f4 v[40:43], v[8:15], v[198:205], v[40:43], v175, v175 op_sel_hi:[0,0,0]
	v_mfma_scale_f32_16x16x128_f8f6f4 v[32:35], v[0:7], v[206:213], v[32:35], v175, v175 op_sel_hi:[0,0,0]
	v_mfma_scale_f32_16x16x128_f8f6f4 v[24:27], v[8:15], v[206:213], v[24:27], v175, v175 op_sel_hi:[0,0,0]
	s_setprio 0
	s_barrier
	s_add_u32 s18, s18, 0x40080
	s_addc_u32 s19, s19, 0
	s_add_i32 s20, s20, s29
	v_lshl_add_u64 v[0:1], s[18:19], 0, v[146:147]
	s_mov_b32 m0, s20
	s_nop 0
	global_load_lds_dwordx4 v[0:1], off
	v_lshl_add_u64 v[0:1], s[18:19], 0, v[150:151]
	s_add_i32 m0, s20, 0x2000
	s_nop 0
	global_load_lds_dwordx4 v[0:1], off
	s_waitcnt vmcnt(6)
	s_barrier
	s_setprio 1
	v_mfma_scale_f32_16x16x128_f8f6f4 v[68:71], v[214:221], v[182:189], v[68:71], v175, v175 op_sel_hi:[0,0,0]
	v_mfma_scale_f32_16x16x128_f8f6f4 v[60:63], v[224:231], v[182:189], v[60:63], v175, v175 op_sel_hi:[0,0,0]
	v_mfma_scale_f32_16x16x128_f8f6f4 v[52:55], v[214:221], v[190:197], v[52:55], v175, v175 op_sel_hi:[0,0,0]
	v_mfma_scale_f32_16x16x128_f8f6f4 v[44:47], v[224:231], v[190:197], v[44:47], v175, v175 op_sel_hi:[0,0,0]
	v_mfma_scale_f32_16x16x128_f8f6f4 v[36:39], v[214:221], v[198:205], v[36:39], v175, v175 op_sel_hi:[0,0,0]
	v_mfma_scale_f32_16x16x128_f8f6f4 v[28:31], v[224:231], v[198:205], v[28:31], v175, v175 op_sel_hi:[0,0,0]
	v_mfma_scale_f32_16x16x128_f8f6f4 v[20:23], v[214:221], v[206:213], v[20:23], v175, v175 op_sel_hi:[0,0,0]
	v_mfma_scale_f32_16x16x128_f8f6f4 v[16:19], v[224:231], v[206:213], v[16:19], v175, v175 op_sel_hi:[0,0,0]
	s_setprio 0
	s_add_i32 s62, s62, 2
	s_add_u32 s60, s60, 0x100
	s_addc_u32 s61, s61, 0
	s_add_u32 s16, s16, 0x100
	s_addc_u32 s17, s17, 0
	s_cmp_gt_u32 s62, 13
	s_barrier
	s_cbranch_scc0 .LBB0_2262
	s_lshl_b32 s16, s55, 8
	s_min_i32 s17, s55, 32
	s_ashr_i32 s20, s17, 4
	s_add_i32 s17, s16, 0xffffe000
	s_cmp_lt_i32 s55, 32
	s_cselect_b32 s19, s48, 0x302b8000
	s_cselect_b32 s18, s16, s17
	s_add_u32 s55, s2, s19
	s_mul_i32 s20, s20, 6
	s_addc_u32 s56, s3, 0
	s_ashr_i32 s19, s18, 31
	s_ashr_i32 s17, s16, 31
	s_ashr_i32 s21, s20, 31
	s_lshl_b64 s[18:19], s[18:19], 12
	s_lshl_b64 s[16:17], s[16:17], 12
	s_lshl_b64 s[20:21], s[20:21], 13
	v_lshl_or_b32 v8, s54, 8, v178
	s_add_u32 s20, s2, s20
	s_addc_u32 s21, s3, s21
	v_ashrrev_i32_e32 v9, 31, v8
	v_lshl_add_u64 v[0:1], v[8:9], 2, s[20:21]
	v_lshl_add_u64 v[10:11], v[0:1], 0, s[6:7]
	v_add_co_u32_e32 v0, vcc, s49, v0
	s_nop 7
	s_nop 7
	s_nop 7
	s_add_u32 s18, s55, s18
	s_nop 0
	v_addc_co_u32_e32 v1, vcc, 0, v1, vcc
	v_add_u32_e32 v152, v177, v8
	global_load_dwordx4 v[0:3], v[0:1], off
	s_nop 0
	global_load_dwordx4 v[182:185], v[10:11], off offset:528
	global_load_dwordx4 v[4:7], v[10:11], off offset:16
	global_load_dwordx4 v[186:189], v[10:11], off offset:512
	s_addc_u32 s19, s56, s19
	s_add_u32 s16, s41, s16
	v_lshlrev_b64 v[222:223], 1, v[152:153]
	v_lshl_add_u64 v[8:9], s[18:19], 0, v[222:223]
	global_load_dwordx4 v[190:193], v[8:9], off
	v_add_u32_e32 v8, 0x80, v152
	v_mov_b32_e32 v9, v153
	v_lshlrev_b64 v[224:225], 1, v[8:9]
	v_lshl_add_u64 v[8:9], s[18:19], 0, v[224:225]
	global_load_dwordx4 v[194:197], v[8:9], off
	v_add_u32_e32 v8, 0x8000, v152
	v_mov_b32_e32 v9, v153
	v_lshlrev_b64 v[226:227], 1, v[8:9]
	v_lshl_add_u64 v[8:9], s[18:19], 0, v[226:227]
	global_load_dwordx4 v[198:201], v[8:9], off
	v_add_u32_e32 v8, 0x8080, v152
	v_mov_b32_e32 v9, v153
	v_lshlrev_b64 v[170:171], 1, v[8:9]
	v_lshl_add_u64 v[8:9], s[18:19], 0, v[170:171]
	global_load_dwordx4 v[202:205], v[8:9], off
	v_add_u32_e32 v8, 0x10000, v152
	v_mov_b32_e32 v9, v153
	v_lshlrev_b64 v[168:169], 1, v[8:9]
	v_lshl_add_u64 v[8:9], s[18:19], 0, v[168:169]
	global_load_dwordx4 v[206:209], v[8:9], off
	v_add_u32_e32 v8, 0x10080, v152
	v_mov_b32_e32 v9, v153
	v_lshlrev_b64 v[166:167], 1, v[8:9]
	v_lshl_add_u64 v[8:9], s[18:19], 0, v[166:167]
	global_load_dwordx4 v[210:213], v[8:9], off
	v_mov_b32_e32 v9, v153
	v_add_u32_e32 v8, 0x18000, v152
	v_lshlrev_b64 v[164:165], 1, v[8:9]
	v_lshl_add_u64 v[8:9], s[18:19], 0, v[164:165]
	global_load_dwordx4 v[214:217], v[8:9], off
	v_mov_b32_e32 v9, v153
	v_add_u32_e32 v8, 0x18080, v152
	v_lshlrev_b64 v[162:163], 1, v[8:9]
	v_lshl_add_u64 v[8:9], s[18:19], 0, v[162:163]
	global_load_dwordx4 v[218:221], v[8:9], off
	s_addc_u32 s17, s42, s17
	s_and_b64 vcc, exec, s[0:1]
	s_mov_b32 s54, s50
	s_mov_b32 s55, s51
	s_waitcnt vmcnt(0)
	v_pk_mul_f32 v[12:13], v[0:1], s[8:9] op_sel_hi:[1,0]
	v_pk_mul_f32 v[0:1], v[182:183], s[8:9] op_sel_hi:[1,0]
	v_pk_mul_f32 v[14:15], v[2:3], s[8:9] op_sel_hi:[1,0]
	v_pk_mul_f32 v[10:11], v[6:7], s[8:9] op_sel_hi:[1,0]
	v_pk_mul_f32 v[8:9], v[4:5], s[8:9] op_sel_hi:[1,0]
	v_pk_mul_f32 v[6:7], v[188:189], s[8:9] op_sel_hi:[1,0]
	v_pk_mul_f32 v[4:5], v[186:187], s[8:9] op_sel_hi:[1,0]
	v_pk_mul_f32 v[2:3], v[184:185], s[8:9] op_sel_hi:[1,0]
	v_lshlrev_b32_e32 v182, 16, v190
	v_and_b32_e32 v183, 0xffff0000, v190
	v_lshlrev_b32_e32 v184, 16, v191
	v_and_b32_e32 v185, 0xffff0000, v191
	v_lshlrev_b32_e32 v186, 16, v192
	v_and_b32_e32 v187, 0xffff0000, v192
	v_lshlrev_b32_e32 v188, 16, v193
	v_and_b32_e32 v189, 0xffff0000, v193
	v_lshlrev_b32_e32 v190, 16, v194
	v_and_b32_e32 v191, 0xffff0000, v194
	v_pk_fma_f32 v[140:141], v[140:141], v[12:13], v[182:183]
	v_lshlrev_b32_e32 v192, 16, v195
	v_and_b32_e32 v193, 0xffff0000, v195
	v_lshlrev_b32_e32 v194, 16, v196
	v_and_b32_e32 v195, 0xffff0000, v196
	v_lshlrev_b32_e32 v196, 16, v197
	v_and_b32_e32 v197, 0xffff0000, v197
	v_pk_fma_f32 v[142:143], v[142:143], v[14:15], v[184:185]
	v_pk_fma_f32 v[182:183], v[138:139], v[10:11], v[188:189]
	v_pk_fma_f32 v[138:139], v[136:137], v[8:9], v[186:187]
	v_cvt_pk_bf16_f32 v136, v140, v141
	v_cvt_pk_bf16_f32 v137, v142, v143
	v_lshl_add_u64 v[140:141], s[16:17], 0, v[222:223]
	v_pk_fma_f32 v[132:133], v[132:133], v[4:5], v[190:191]
	v_lshlrev_b32_e32 v228, 16, v198
	v_and_b32_e32 v229, 0xffff0000, v198
	v_lshlrev_b32_e32 v198, 16, v199
	v_and_b32_e32 v199, 0xffff0000, v199
	v_cvt_pk_bf16_f32 v138, v138, v139
	v_cvt_pk_bf16_f32 v139, v182, v183
	global_store_dwordx4 v[140:141], v[136:139], off
	v_pk_fma_f32 v[134:135], v[134:135], v[6:7], v[192:193]
	v_lshlrev_b32_e32 v230, 16, v200
	v_pk_fma_f32 v[136:137], v[126:127], v[2:3], v[196:197]
	v_pk_fma_f32 v[126:127], v[124:125], v[0:1], v[194:195]
	v_cvt_pk_bf16_f32 v124, v132, v133
	v_cvt_pk_bf16_f32 v125, v134, v135
	v_lshl_add_u64 v[132:133], s[16:17], 0, v[224:225]
	v_and_b32_e32 v231, 0xffff0000, v200
	v_lshlrev_b32_e32 v200, 16, v201
	v_and_b32_e32 v201, 0xffff0000, v201
	v_lshlrev_b32_e32 v232, 16, v202
	v_and_b32_e32 v233, 0xffff0000, v202
	v_cvt_pk_bf16_f32 v126, v126, v127
	v_cvt_pk_bf16_f32 v127, v136, v137
	global_store_dwordx4 v[132:133], v[124:127], off
	v_lshlrev_b32_e32 v202, 16, v203
	v_and_b32_e32 v203, 0xffff0000, v203
	v_pk_fma_f32 v[124:125], v[130:131], v[14:15], v[198:199]
	v_lshlrev_b32_e32 v234, 16, v204
	v_and_b32_e32 v235, 0xffff0000, v204
	v_lshlrev_b32_e32 v204, 16, v205
	v_and_b32_e32 v205, 0xffff0000, v205
	v_pk_fma_f32 v[126:127], v[128:129], v[12:13], v[228:229]
	v_pk_fma_f32 v[128:129], v[122:123], v[10:11], v[200:201]
	v_pk_fma_f32 v[122:123], v[120:121], v[8:9], v[230:231]
	v_cvt_pk_bf16_f32 v120, v126, v127
	v_cvt_pk_bf16_f32 v121, v124, v125
	v_lshl_add_u64 v[124:125], s[16:17], 0, v[226:227]
	v_pk_fma_f32 v[116:117], v[116:117], v[4:5], v[232:233]
	v_lshlrev_b32_e32 v236, 16, v206
	v_and_b32_e32 v237, 0xffff0000, v206
	v_lshlrev_b32_e32 v206, 16, v207
	v_and_b32_e32 v207, 0xffff0000, v207
	v_cvt_pk_bf16_f32 v122, v122, v123
	v_cvt_pk_bf16_f32 v123, v128, v129
	global_store_dwordx4 v[124:125], v[120:123], off
	v_pk_fma_f32 v[118:119], v[118:119], v[6:7], v[202:203]
	v_lshlrev_b32_e32 v238, 16, v208
	v_pk_fma_f32 v[120:121], v[110:111], v[2:3], v[204:205]
	v_pk_fma_f32 v[110:111], v[108:109], v[0:1], v[234:235]
	v_cvt_pk_bf16_f32 v108, v116, v117
	v_cvt_pk_bf16_f32 v109, v118, v119
	v_lshl_add_u64 v[116:117], s[16:17], 0, v[170:171]
	v_and_b32_e32 v239, 0xffff0000, v208
	v_lshlrev_b32_e32 v208, 16, v209
	v_and_b32_e32 v209, 0xffff0000, v209
	v_lshlrev_b32_e32 v240, 16, v210
	v_and_b32_e32 v241, 0xffff0000, v210
	v_cvt_pk_bf16_f32 v110, v110, v111
	v_cvt_pk_bf16_f32 v111, v120, v121
	global_store_dwordx4 v[116:117], v[108:111], off
	v_lshlrev_b32_e32 v210, 16, v211
	v_and_b32_e32 v211, 0xffff0000, v211
	v_pk_fma_f32 v[108:109], v[114:115], v[14:15], v[206:207]
	v_lshlrev_b32_e32 v242, 16, v212
	v_and_b32_e32 v243, 0xffff0000, v212
	v_lshlrev_b32_e32 v212, 16, v213
	v_and_b32_e32 v213, 0xffff0000, v213
	v_pk_fma_f32 v[110:111], v[112:113], v[12:13], v[236:237]
	v_pk_fma_f32 v[112:113], v[106:107], v[10:11], v[208:209]
	v_pk_fma_f32 v[106:107], v[104:105], v[8:9], v[238:239]
	v_cvt_pk_bf16_f32 v104, v110, v111
	v_cvt_pk_bf16_f32 v105, v108, v109
	v_lshl_add_u64 v[108:109], s[16:17], 0, v[168:169]
	v_pk_fma_f32 v[100:101], v[100:101], v[4:5], v[240:241]
	v_lshlrev_b32_e32 v244, 16, v214
	v_and_b32_e32 v245, 0xffff0000, v214
	v_lshlrev_b32_e32 v214, 16, v215
	v_and_b32_e32 v215, 0xffff0000, v215
	v_cvt_pk_bf16_f32 v106, v106, v107
	v_cvt_pk_bf16_f32 v107, v112, v113
	global_store_dwordx4 v[108:109], v[104:107], off
	v_pk_fma_f32 v[102:103], v[102:103], v[6:7], v[210:211]
	v_lshlrev_b32_e32 v246, 16, v216
	v_pk_fma_f32 v[104:105], v[94:95], v[2:3], v[212:213]
	v_pk_fma_f32 v[94:95], v[92:93], v[0:1], v[242:243]
	v_cvt_pk_bf16_f32 v92, v100, v101
	v_cvt_pk_bf16_f32 v93, v102, v103
	v_lshl_add_u64 v[100:101], s[16:17], 0, v[166:167]
	v_and_b32_e32 v247, 0xffff0000, v216
	v_lshlrev_b32_e32 v216, 16, v217
	v_and_b32_e32 v217, 0xffff0000, v217
	v_lshlrev_b32_e32 v248, 16, v218
	v_and_b32_e32 v249, 0xffff0000, v218
	v_cvt_pk_bf16_f32 v94, v94, v95
	v_cvt_pk_bf16_f32 v95, v104, v105
	global_store_dwordx4 v[100:101], v[92:95], off
	v_lshlrev_b32_e32 v218, 16, v219
	v_and_b32_e32 v219, 0xffff0000, v219
	v_pk_fma_f32 v[92:93], v[98:99], v[14:15], v[214:215]
	v_lshlrev_b32_e32 v172, 16, v220
	v_and_b32_e32 v173, 0xffff0000, v220
	v_lshlrev_b32_e32 v220, 16, v221
	v_and_b32_e32 v221, 0xffff0000, v221
	v_pk_fma_f32 v[94:95], v[96:97], v[12:13], v[244:245]
	v_pk_fma_f32 v[96:97], v[90:91], v[10:11], v[216:217]
	v_pk_fma_f32 v[90:91], v[88:89], v[8:9], v[246:247]
	v_cvt_pk_bf16_f32 v88, v94, v95
	v_cvt_pk_bf16_f32 v89, v92, v93
	v_lshl_add_u64 v[92:93], s[16:17], 0, v[164:165]
	v_pk_fma_f32 v[84:85], v[84:85], v[4:5], v[248:249]
	v_cvt_pk_bf16_f32 v90, v90, v91
	v_cvt_pk_bf16_f32 v91, v96, v97
	global_store_dwordx4 v[92:93], v[88:91], off
	v_pk_fma_f32 v[86:87], v[86:87], v[6:7], v[218:219]
	s_nop 0
	v_pk_fma_f32 v[88:89], v[82:83], v[2:3], v[220:221]
	v_pk_fma_f32 v[82:83], v[80:81], v[0:1], v[172:173]
	v_cvt_pk_bf16_f32 v80, v84, v85
	v_cvt_pk_bf16_f32 v81, v86, v87
	v_lshl_add_u64 v[84:85], s[16:17], 0, v[162:163]
	v_cvt_pk_bf16_f32 v82, v82, v83
	v_cvt_pk_bf16_f32 v83, v88, v89
	global_store_dwordx4 v[84:85], v[80:83], off
	s_nop 1
	v_add_u32_e32 v80, 0x40000, v152
	v_mov_b32_e32 v81, v153
	v_lshlrev_b64 v[122:123], 1, v[80:81]
	v_lshl_add_u64 v[80:81], s[18:19], 0, v[122:123]
	global_load_dwordx4 v[90:93], v[80:81], off
	v_add_u32_e32 v80, 0x40080, v152
	v_mov_b32_e32 v81, v153
	v_lshlrev_b64 v[124:125], 1, v[80:81]
	v_lshl_add_u64 v[80:81], s[18:19], 0, v[124:125]
	global_load_dwordx4 v[94:97], v[80:81], off
	v_add_u32_e32 v80, 0x48000, v152
	v_mov_b32_e32 v81, v153
	v_lshlrev_b64 v[126:127], 1, v[80:81]
	v_lshl_add_u64 v[80:81], s[18:19], 0, v[126:127]
	global_load_dwordx4 v[98:101], v[80:81], off
	v_add_u32_e32 v80, 0x48080, v152
	v_mov_b32_e32 v81, v153
	v_lshlrev_b64 v[88:89], 1, v[80:81]
	v_lshl_add_u64 v[80:81], s[18:19], 0, v[88:89]
	global_load_dwordx4 v[102:105], v[80:81], off
	v_add_u32_e32 v80, 0x50000, v152
	v_mov_b32_e32 v81, v153
	v_lshlrev_b64 v[86:87], 1, v[80:81]
	v_lshl_add_u64 v[80:81], s[18:19], 0, v[86:87]
	global_load_dwordx4 v[106:109], v[80:81], off
	v_add_u32_e32 v80, 0x50080, v152
	v_mov_b32_e32 v81, v153
	v_lshlrev_b64 v[84:85], 1, v[80:81]
	v_lshl_add_u64 v[80:81], s[18:19], 0, v[84:85]
	global_load_dwordx4 v[110:113], v[80:81], off
	v_add_u32_e32 v80, 0x58000, v152
	v_mov_b32_e32 v81, v153
	v_lshlrev_b64 v[82:83], 1, v[80:81]
	v_lshl_add_u64 v[80:81], s[18:19], 0, v[82:83]
	v_add_u32_e32 v152, 0x58080, v152
	global_load_dwordx4 v[114:117], v[80:81], off
	v_lshlrev_b64 v[80:81], 1, v[152:153]
	v_lshl_add_u64 v[118:119], s[18:19], 0, v[80:81]
	global_load_dwordx4 v[118:121], v[118:119], off
	s_mov_b64 s[18:19], s[10:11]
	s_waitcnt vmcnt(0)
	v_lshlrev_b32_e32 v128, 16, v90
	v_and_b32_e32 v129, 0xffff0000, v90
	v_lshlrev_b32_e32 v130, 16, v91
	v_and_b32_e32 v131, 0xffff0000, v91
	v_lshlrev_b32_e32 v132, 16, v92
	v_and_b32_e32 v133, 0xffff0000, v92
	v_lshlrev_b32_e32 v92, 16, v93
	v_and_b32_e32 v93, 0xffff0000, v93
	v_lshlrev_b32_e32 v134, 16, v94
	v_and_b32_e32 v135, 0xffff0000, v94
	v_pk_fma_f32 v[76:77], v[76:77], v[12:13], v[128:129]
	v_lshlrev_b32_e32 v94, 16, v95
	v_and_b32_e32 v95, 0xffff0000, v95
	v_lshlrev_b32_e32 v136, 16, v96
	v_and_b32_e32 v137, 0xffff0000, v96
	v_lshlrev_b32_e32 v96, 16, v97
	v_and_b32_e32 v97, 0xffff0000, v97
	v_pk_fma_f32 v[78:79], v[78:79], v[14:15], v[130:131]
	v_pk_fma_f32 v[92:93], v[74:75], v[10:11], v[92:93]
	v_pk_fma_f32 v[74:75], v[72:73], v[8:9], v[132:133]
	v_cvt_pk_bf16_f32 v72, v76, v77
	v_cvt_pk_bf16_f32 v73, v78, v79
	v_lshl_add_u64 v[76:77], s[16:17], 0, v[122:123]
	v_pk_fma_f32 v[68:69], v[68:69], v[4:5], v[134:135]
	v_lshlrev_b32_e32 v138, 16, v98
	v_and_b32_e32 v139, 0xffff0000, v98
	v_lshlrev_b32_e32 v98, 16, v99
	v_and_b32_e32 v99, 0xffff0000, v99
	v_cvt_pk_bf16_f32 v74, v74, v75
	v_cvt_pk_bf16_f32 v75, v92, v93
	global_store_dwordx4 v[76:77], v[72:75], off
	v_pk_fma_f32 v[70:71], v[70:71], v[6:7], v[94:95]
	v_lshlrev_b32_e32 v140, 16, v100
	v_pk_fma_f32 v[72:73], v[62:63], v[2:3], v[96:97]
	v_pk_fma_f32 v[62:63], v[60:61], v[0:1], v[136:137]
	v_cvt_pk_bf16_f32 v60, v68, v69
	v_cvt_pk_bf16_f32 v61, v70, v71
	v_lshl_add_u64 v[68:69], s[16:17], 0, v[124:125]
	v_and_b32_e32 v141, 0xffff0000, v100
	v_lshlrev_b32_e32 v100, 16, v101
	v_and_b32_e32 v101, 0xffff0000, v101
	v_lshlrev_b32_e32 v142, 16, v102
	v_and_b32_e32 v143, 0xffff0000, v102
	v_cvt_pk_bf16_f32 v62, v62, v63
	v_cvt_pk_bf16_f32 v63, v72, v73
	global_store_dwordx4 v[68:69], v[60:63], off
	v_lshlrev_b32_e32 v102, 16, v103
	v_and_b32_e32 v103, 0xffff0000, v103
	v_pk_fma_f32 v[60:61], v[66:67], v[14:15], v[98:99]
	v_lshlrev_b32_e32 v162, 16, v104
	v_and_b32_e32 v163, 0xffff0000, v104
	v_lshlrev_b32_e32 v104, 16, v105
	v_and_b32_e32 v105, 0xffff0000, v105
	v_pk_fma_f32 v[62:63], v[64:65], v[12:13], v[138:139]
	v_pk_fma_f32 v[64:65], v[58:59], v[10:11], v[100:101]
	v_pk_fma_f32 v[58:59], v[56:57], v[8:9], v[140:141]
	v_cvt_pk_bf16_f32 v56, v62, v63
	v_cvt_pk_bf16_f32 v57, v60, v61
	v_lshl_add_u64 v[60:61], s[16:17], 0, v[126:127]
	v_pk_fma_f32 v[52:53], v[52:53], v[4:5], v[142:143]
	v_lshlrev_b32_e32 v164, 16, v106
	v_and_b32_e32 v165, 0xffff0000, v106
	v_lshlrev_b32_e32 v106, 16, v107
	v_and_b32_e32 v107, 0xffff0000, v107
	v_cvt_pk_bf16_f32 v58, v58, v59
	v_cvt_pk_bf16_f32 v59, v64, v65
	global_store_dwordx4 v[60:61], v[56:59], off
	v_pk_fma_f32 v[54:55], v[54:55], v[6:7], v[102:103]
	v_lshlrev_b32_e32 v166, 16, v108
	v_pk_fma_f32 v[56:57], v[46:47], v[2:3], v[104:105]
	v_pk_fma_f32 v[46:47], v[44:45], v[0:1], v[162:163]
	v_cvt_pk_bf16_f32 v44, v52, v53
	v_cvt_pk_bf16_f32 v45, v54, v55
	v_lshl_add_u64 v[52:53], s[16:17], 0, v[88:89]
	v_and_b32_e32 v167, 0xffff0000, v108
	v_lshlrev_b32_e32 v108, 16, v109
	v_and_b32_e32 v109, 0xffff0000, v109
	v_lshlrev_b32_e32 v168, 16, v110
	v_and_b32_e32 v169, 0xffff0000, v110
	v_cvt_pk_bf16_f32 v46, v46, v47
	v_cvt_pk_bf16_f32 v47, v56, v57
	global_store_dwordx4 v[52:53], v[44:47], off
	v_lshlrev_b32_e32 v170, 16, v112
	v_and_b32_e32 v171, 0xffff0000, v112
	v_pk_fma_f32 v[44:45], v[50:51], v[14:15], v[106:107]
	v_lshlrev_b32_e32 v112, 16, v113
	v_and_b32_e32 v113, 0xffff0000, v113
	v_lshlrev_b32_e32 v172, 16, v114
	v_and_b32_e32 v173, 0xffff0000, v114
	v_pk_fma_f32 v[46:47], v[48:49], v[12:13], v[164:165]
	v_pk_fma_f32 v[48:49], v[42:43], v[10:11], v[108:109]
	v_pk_fma_f32 v[42:43], v[40:41], v[8:9], v[166:167]
	v_cvt_pk_bf16_f32 v40, v46, v47
	v_cvt_pk_bf16_f32 v41, v44, v45
	v_lshl_add_u64 v[44:45], s[16:17], 0, v[86:87]
	v_pk_fma_f32 v[36:37], v[36:37], v[4:5], v[168:169]
	v_lshlrev_b32_e32 v110, 16, v111
	v_and_b32_e32 v111, 0xffff0000, v111
	v_lshlrev_b32_e32 v114, 16, v115
	v_and_b32_e32 v115, 0xffff0000, v115
	v_lshlrev_b32_e32 v182, 16, v116
	v_and_b32_e32 v183, 0xffff0000, v116
	v_lshlrev_b32_e32 v116, 16, v117
	v_and_b32_e32 v117, 0xffff0000, v117
	v_lshlrev_b32_e32 v184, 16, v118
	v_and_b32_e32 v185, 0xffff0000, v118
	v_cvt_pk_bf16_f32 v42, v42, v43
	v_cvt_pk_bf16_f32 v43, v48, v49
	global_store_dwordx4 v[44:45], v[40:43], off
	v_pk_fma_f32 v[12:13], v[32:33], v[12:13], v[172:173]
	v_lshlrev_b32_e32 v90, 16, v120
	v_pk_fma_f32 v[40:41], v[30:31], v[2:3], v[112:113]
	v_pk_fma_f32 v[30:31], v[28:29], v[0:1], v[170:171]
	v_cvt_pk_bf16_f32 v28, v36, v37
	v_lshl_add_u64 v[36:37], s[16:17], 0, v[84:85]
	v_and_b32_e32 v91, 0xffff0000, v120
	v_lshlrev_b32_e32 v120, 16, v121
	v_and_b32_e32 v121, 0xffff0000, v121
	v_pk_fma_f32 v[38:39], v[38:39], v[6:7], v[110:111]
	v_pk_fma_f32 v[14:15], v[34:35], v[14:15], v[114:115]
	v_cvt_pk_bf16_f32 v29, v38, v39
	v_cvt_pk_bf16_f32 v30, v30, v31
	v_cvt_pk_bf16_f32 v31, v40, v41
	global_store_dwordx4 v[36:37], v[28:31], off
	v_pk_fma_f32 v[26:27], v[26:27], v[10:11], v[116:117]
	v_pk_fma_f32 v[10:11], v[24:25], v[8:9], v[182:183]
	v_cvt_pk_bf16_f32 v8, v12, v13
	v_cvt_pk_bf16_f32 v9, v14, v15
	v_lshl_add_u64 v[12:13], s[16:17], 0, v[82:83]
	v_pk_fma_f32 v[4:5], v[20:21], v[4:5], v[184:185]
	v_lshlrev_b32_e32 v118, 16, v119
	v_and_b32_e32 v119, 0xffff0000, v119
	v_cvt_pk_bf16_f32 v10, v10, v11
	v_cvt_pk_bf16_f32 v11, v26, v27
	global_store_dwordx4 v[12:13], v[8:11], off
	v_pk_fma_f32 v[6:7], v[22:23], v[6:7], v[118:119]
	s_nop 0
	v_pk_fma_f32 v[8:9], v[18:19], v[2:3], v[120:121]
	v_pk_fma_f32 v[2:3], v[16:17], v[0:1], v[90:91]
	v_cvt_pk_bf16_f32 v0, v4, v5
	v_lshl_add_u64 v[4:5], s[16:17], 0, v[80:81]
	v_cvt_pk_bf16_f32 v1, v6, v7
	v_cvt_pk_bf16_f32 v2, v2, v3
	v_cvt_pk_bf16_f32 v3, v8, v9
	global_store_dwordx4 v[4:5], v[0:3], off
	s_mov_b64 s[16:17], s[12:13]
	s_cbranch_vccz .LBB0_2255
	s_waitcnt vmcnt(0)
	s_cmpk_lt_u32 s23, 0x100
	s_cbranch_scc1 .LBB0_2266
	s_barrier

.LBB0_2472:
	s_cmp_gt_i32 s36, 25
	s_cselect_b64 s[0:1], -1, 0
	s_cmp_lt_i32 s37, 26
	s_cselect_b64 s[2:3], -1, 0
	s_or_b64 s[0:1], s[0:1], s[2:3]
	s_and_b64 vcc, exec, s[0:1]
	s_cbranch_vccnz .LBB0_2616
	s_and_b32 s0, s81, 0xffffffc0
	v_mbcnt_hi_u32_b32 v186, -1, v253
	v_add_u32_e32 v187, s0, v186
	s_mov_b64 s[4:5], s[34:35]
	s_mov_b32 s6, s14
	s_mov_b32 s23, s15
	v_mov_b32_e32 v0, 0x4000
	global_load_dword v0, v0, s[4:5] offset:3072
	v_readfirstlane_b32 s40, v187
	s_and_b32 s0, s40, 0xffffffc0
	s_waitcnt vmcnt(0) lgkmcnt(0)
	v_add_u32_e32 v4, s0, v186
	s_ashr_i32 s7, s6, 31
	s_mov_b32 s2, 0
	v_mov_b32_e32 v188, 0x7f7f7f7f
	v_readfirstlane_b32 s0, v0
	s_ashr_i32 s1, s0, 31
	s_lshl_b64 s[0:1], s[0:1], 2
	v_mov_b64_e32 v[0:1], s[6:7]
	v_cmp_le_i64_e32 vcc, s[0:1], v[0:1]
	v_readfirstlane_b32 s41, v4
	s_cbranch_vccnz .LBB0_2489
	s_add_u32 s42, s4, 0x4a00
	s_addc_u32 s43, s5, 0
	s_add_u32 s44, s4, 0x3bf0c000
	s_addc_u32 s45, s5, 0
	s_add_u32 s46, s4, 0x4080
	s_addc_u32 s47, s5, 0
	s_add_u32 s8, s4, 0x3280c000
	s_addc_u32 s9, s5, 0
	s_add_u32 s48, s4, 0xf458000
	s_addc_u32 s49, s5, 0
	s_ashr_i32 s16, s41, 6
	s_ashr_i32 s20, s41, 8
	s_lshl_b32 s50, s16, 10
	s_ashr_i64 s[28:29], s[6:7], 2
	s_and_b32 s66, s6, 3
	s_and_b32 s3, s6, -4
	s_add_u32 s10, s42, s3
	s_addc_u32 s11, s43, s7
	v_mov_b32_e32 v161, 0
	global_load_dword v0, v161, s[10:11]
	s_lshl_b32 s11, s66, 19
	s_add_i32 s3, s28, 0xa0
	s_ashr_i64 s[2:3], s[2:3], 30
	v_lshlrev_b32_e32 v2, 4, v4
	v_ashrrev_i32_e32 v3, 31, v4
	v_bfe_i32 v5, v4, 27, 1
	v_lshrrev_b32_e32 v3, 26, v3
	v_lshrrev_b32_e32 v5, 22, v5
	v_add_u32_e32 v6, 0x2000, v2
	v_add_u32_e32 v3, v4, v3
	v_add_u32_e32 v5, v2, v5
	v_ashrrev_i32_e32 v7, 31, v6
	v_ashrrev_i32_e32 v10, 6, v3
	v_and_b32_e32 v3, 0xfffffc00, v5
	v_lshrrev_b32_e32 v5, 22, v7
	v_sub_u32_e32 v2, v2, v3
	v_add_u32_e32 v5, v6, v5
	v_lshrrev_b32_e32 v7, 4, v2
	v_ashrrev_i32_e32 v5, 10, v5
	v_bitop3_b32 v11, v7, v2, 32 bitop3:0x6c
	v_mul_i32_i24_e32 v2, 0x400, v5
	v_lshlrev_b32_e32 v7, 3, v5
	v_ashrrev_i32_e32 v8, 31, v11
	v_sub_u32_e32 v2, v6, v2
	v_and_b32_e32 v6, -16, v7
	v_lshrrev_b32_e32 v7, 26, v8
	v_lshrrev_b32_e32 v8, 4, v2
	v_bitop3_b32 v13, v8, v2, 32 bitop3:0x6c
	v_ashrrev_i32_e32 v2, 31, v13
	v_lshlrev_b32_e32 v3, 3, v10
	v_add_u32_e32 v12, v11, v7
	v_lshrrev_b32_e32 v2, 26, v2
	v_and_b32_e32 v3, -16, v3
	v_ashrrev_i32_e32 v14, 6, v12
	v_add_u32_e32 v15, v13, v2
	v_add_u32_e32 v189, v14, v3
	v_ashrrev_i32_e32 v16, 6, v15
	v_add_u32_e32 v190, v16, v6
	v_mov_b32_e32 v163, v161
	v_mov_b32_e32 v165, v161
	s_mov_b32 s54, 0x10000
	s_mov_b32 s55, 0x12000
	v_mov_b32_e32 v173, v161
	s_mov_b32 s56, 0x14000
	s_waitcnt vmcnt(0)
	v_readfirstlane_b32 s10, v0
	s_lshl_b32 s12, s10, 21
	s_or_b32 s12, s12, s11
	s_add_u32 s2, s42, s2
	s_addc_u32 s3, s43, s3
	s_ashr_i32 s11, s10, 31
	global_load_dword v0, v161, s[2:3]
	s_lshl_b64 s[2:3], s[10:11], 2
	s_add_u32 s2, s46, s2
	s_addc_u32 s3, s47, s3
	global_load_dword v1, v161, s[2:3]
	s_mul_i32 s2, s10, 0x8800
	s_mul_hi_i32 s3, s10, 0x8800
	s_waitcnt vmcnt(1)
	v_readfirstlane_b32 s21, v0
	s_lshl_b32 s11, s21, 8
	s_add_u32 s2, s44, s2
	v_add_u32_e32 v0, s11, v189
	s_waitcnt vmcnt(0)
	v_readfirstlane_b32 s25, v1
	v_add_u32_e32 v2, s11, v190
	s_addc_u32 s3, s45, s3
	s_bitset1_b32 s11, 7
	v_cmp_gt_i32_e32 vcc, s25, v0
	v_add_u32_e32 v6, s11, v189
	v_add_u32_e32 v7, s11, v190
	v_cndmask_b32_e32 v0, 0, v0, vcc
	v_cmp_gt_i32_e32 vcc, s25, v2
	v_ashrrev_i32_e32 v1, 31, v0
	v_lshl_add_u64 v[0:1], v[0:1], 2, s[2:3]
	v_cndmask_b32_e32 v2, 0, v2, vcc
	v_cmp_gt_i32_e32 vcc, s25, v6
	v_ashrrev_i32_e32 v3, 31, v2
	v_lshl_add_u64 v[2:3], v[2:3], 2, s[2:3]
	v_cndmask_b32_e32 v6, 0, v6, vcc
	v_cmp_gt_i32_e32 vcc, s25, v7
	s_add_u32 s30, s48, s12
	s_addc_u32 s31, s49, 0
	v_cndmask_b32_e32 v8, 0, v7, vcc
	v_ashrrev_i32_e32 v7, 31, v6
	v_ashrrev_i32_e32 v9, 31, v8
	v_lshl_add_u64 v[6:7], v[6:7], 2, s[2:3]
	v_lshl_add_u64 v[8:9], v[8:9], 2, s[2:3]
	global_load_dword v17, v[0:1], off
	global_load_dword v18, v[2:3], off
	global_load_dword v19, v[6:7], off
	global_load_dword v20, v[8:9], off
	v_and_b32_e32 v3, 0xc0, v12
	v_mov_b32_e32 v0, 1
	v_sub_u32_e32 v3, v11, v3
	v_lshlrev_b32_e32 v1, 5, v10
	v_ashrrev_i16_sdwa v3, v0, sext(v3) dst_sel:DWORD dst_unused:UNUSED_PAD src0_sel:DWORD src1_sel:BYTE_0
	s_mov_b32 s2, 0x1fffe0
	v_and_b32_e32 v1, 32, v1
	v_lshlrev_b32_e32 v2, 5, v5
	v_and_b32_e32 v5, 3, v14
	v_lshrrev_b32_e32 v6, 2, v189
	v_lshlrev_b32_e32 v7, 1, v189
	v_bfe_i32 v3, v3, 0, 16
	v_and_b32_e32 v8, 0xc0, v15
	v_and_or_b32 v5, v189, s2, v5
	v_and_b32_e32 v6, 4, v6
	v_and_b32_e32 v7, 24, v7
	v_add_lshl_u32 v191, v1, v3, 1
	v_sub_u32_e32 v1, v13, v8
	v_and_b32_e32 v3, 3, v16
	v_or3_b32 v5, v5, v6, v7
	v_ashrrev_i16_sdwa v0, v0, sext(v1) dst_sel:DWORD dst_unused:UNUSED_PAD src0_sel:DWORD src1_sel:BYTE_0
	v_and_or_b32 v1, v190, s2, v3
	v_lshrrev_b32_e32 v3, 2, v190
	v_lshlrev_b32_e32 v6, 1, v190
	v_and_b32_e32 v2, 32, v2
	v_lshl_add_u32 v162, v5, 11, v191
	v_bfe_i32 v0, v0, 0, 16
	v_and_b32_e32 v3, 4, v3
	v_and_b32_e32 v5, 24, v6
	s_add_i32 s29, s50, 0
	v_add_lshl_u32 v192, v2, v0, 1
	v_or3_b32 v0, v1, v3, v5
	s_add_i32 m0, s29, 0x10000
	v_lshl_add_u32 v164, v0, 11, v192
	global_load_lds_dwordx4 v162, s[30:31]
	s_add_i32 m0, s29, 0x12000
	s_add_i32 s51, s29, 0x2000
	global_load_lds_dwordx4 v164, s[30:31]
	s_mov_b32 m0, s29
	s_add_u32 s2, s30, 0x40000
	s_addc_u32 s3, s31, 0
	s_add_i32 s52, s29, 0x4000
	s_add_i32 s53, s29, 0x6000
	v_lshl_add_u64 v[2:3], s[30:31], 0, v[162:163]
	v_lshl_add_u64 v[0:1], s[30:31], 0, v[164:165]
	s_waitcnt vmcnt(0)
	v_lshl_add_u32 v160, v17, 11, v191
	v_lshl_add_u32 v172, v18, 11, v192
	global_load_lds_dwordx4 v160, s[8:9]
	s_mov_b32 m0, s51
	v_lshl_add_u32 v170, v19, 11, v191
	global_load_lds_dwordx4 v172, s[8:9]
	s_add_i32 m0, s29, 0x14000
	v_lshl_add_u32 v168, v20, 11, v192
	global_load_lds_dwordx4 v162, s[2:3]
	s_add_i32 m0, s29, 0x16000
	s_cmp_lg_u32 s20, 0
	global_load_lds_dwordx4 v164, s[2:3]
	s_mov_b32 m0, s52
	s_nop 0
	global_load_lds_dwordx4 v170, s[8:9]
	s_mov_b32 m0, s53
	s_nop 0
	global_load_lds_dwordx4 v168, s[8:9]
	s_cbranch_scc1 .LBB0_2476
	s_barrier

.LBB0_2486:
	s_waitcnt vmcnt(0)
	s_cmpk_lt_u32 s41, 0x100
	s_cbranch_scc1 .LBB0_2488
	s_barrier

.LBB0_2616:
	s_cmp_gt_i32 s36, 26
	s_cselect_b64 s[0:1], -1, 0
	s_cmp_lt_i32 s37, 27
	s_cselect_b64 s[2:3], -1, 0
	s_or_b64 s[0:1], s[0:1], s[2:3]
	s_and_b64 vcc, exec, s[0:1]
	s_cbranch_vccnz .LBB0_2677
	s_and_b32 s0, s81, 0xffffffc0
	v_mbcnt_hi_u32_b32 v152, -1, v253
	v_add_u32_e32 v0, s0, v152
	s_mov_b64 s[2:3], s[34:35]
	s_mov_b32 s8, s14
	s_mov_b32 s19, s15
	v_mov_b32_e32 v1, 0x4000
	global_load_dword v1, v1, s[2:3] offset:3072
	v_readfirstlane_b32 s0, v0
	s_andn2_b32 s0, s0, 63
	s_ashr_i32 s9, s8, 31
	s_waitcnt vmcnt(0)
	v_add_u32_e32 v8, s0, v152
	v_mov_b32_e32 v153, 0x7f7f7f7f
	v_readfirstlane_b32 s0, v1
	s_ashr_i32 s1, s0, 31
	s_lshl_b64 s[0:1], s[0:1], 3
	v_mov_b64_e32 v[0:1], s[8:9]
	v_cmp_le_i64_e32 vcc, s[0:1], v[0:1]
	v_readfirstlane_b32 s40, v8
	s_cbranch_vccnz .LBB0_2627
	s_add_u32 s41, s2, 0x4a00
	s_addc_u32 s42, s3, 0
	s_add_u32 s43, s2, 0x4241c000
	s_addc_u32 s44, s3, 0
	s_add_u32 s45, s2, 0x1b458000
	s_addc_u32 s46, s3, 0
	s_ashr_i32 s5, s40, 6
	s_ashr_i64 s[26:27], s[8:9], 3
	s_ashr_i32 s4, s40, 8
	s_lshl_b32 s47, s5, 10
	s_and_b32 s68, s8, 7
	s_lshl_b64 s[6:7], s[26:27], 2
	s_add_u32 s6, s41, s6
	s_addc_u32 s7, s42, s7
	v_mov_b32_e32 v133, 0
	global_load_dword v0, v133, s[6:7]
	v_lshlrev_b32_e32 v1, 4, v8
	v_bfe_i32 v3, v8, 27, 1
	v_add_u32_e32 v5, 0x2000, v1
	v_lshrrev_b32_e32 v3, 22, v3
	v_ashrrev_i32_e32 v6, 31, v5
	v_add_u32_e32 v3, v1, v3
	v_lshrrev_b32_e32 v6, 22, v6
	v_and_b32_e32 v3, 0xfffffc00, v3
	v_add_u32_e32 v6, v5, v6
	v_sub_u32_e32 v1, v1, v3
	v_ashrrev_i32_e32 v6, 10, v6
	v_lshrrev_b32_e32 v7, 4, v1
	v_mul_i32_i24_e32 v9, 0x400, v6
	v_lshlrev_b32_e32 v10, 3, v6
	v_bitop3_b32 v1, v7, v1, 32 bitop3:0x6c
	v_sub_u32_e32 v5, v5, v9
	s_waitcnt lgkmcnt(0)
	v_ashrrev_i32_e32 v4, 31, v8
	v_and_b32_e32 v7, -16, v10
	v_ashrrev_i32_e32 v9, 31, v1
	v_lshrrev_b32_e32 v10, 4, v5
	v_lshrrev_b32_e32 v4, 26, v4
	v_lshrrev_b32_e32 v9, 26, v9
	v_bitop3_b32 v5, v10, v5, 32 bitop3:0x6c
	v_add_u32_e32 v4, v8, v4
	v_add_u32_e32 v9, v1, v9
	v_ashrrev_i32_e32 v10, 31, v5
	v_ashrrev_i32_e32 v4, 6, v4
	v_ashrrev_i32_e32 v11, 6, v9
	v_and_b32_e32 v9, 0xc0, v9
	v_lshrrev_b32_e32 v10, 26, v10
	v_mov_b32_e32 v2, 1
	v_lshlrev_b32_e32 v3, 3, v4
	v_sub_u32_e32 v1, v1, v9
	v_add_u32_e32 v9, v5, v10
	v_lshlrev_b32_e32 v4, 5, v4
	v_and_b32_e32 v3, -16, v3
	v_ashrrev_i16_sdwa v1, v2, sext(v1) dst_sel:DWORD dst_unused:UNUSED_PAD src0_sel:DWORD src1_sel:BYTE_0
	v_ashrrev_i32_e32 v13, 6, v9
	s_mov_b32 s6, 0x7fffe0
	v_and_b32_e32 v4, 32, v4
	v_add_u32_e32 v3, v11, v3
	v_and_b32_e32 v11, 3, v11
	v_bfe_i32 v1, v1, 0, 16
	v_add_u32_e32 v7, v13, v7
	v_and_b32_e32 v13, 3, v13
	v_and_or_b32 v10, v3, s6, v11
	v_add_lshl_u32 v1, v4, v1, 1
	v_and_or_b32 v4, v7, s6, v13
	s_lshl_b32 s10, s68, 17
	s_lshl_b32 s7, s26, 17
	v_lshrrev_b32_e32 v11, 2, v3
	v_lshlrev_b32_e32 v12, 1, v3
	v_and_b32_e32 v9, 0xc0, v9
	v_and_b32_e32 v11, 4, v11
	v_and_b32_e32 v12, 24, v12
	v_sub_u32_e32 v5, v5, v9
	v_lshlrev_b32_e32 v6, 5, v6
	v_or3_b32 v9, v10, v11, v12
	v_lshrrev_b32_e32 v10, 2, v7
	v_lshlrev_b32_e32 v11, 1, v7
	v_ashrrev_i16_sdwa v2, v2, sext(v5) dst_sel:DWORD dst_unused:UNUSED_PAD src0_sel:DWORD src1_sel:BYTE_0
	v_and_b32_e32 v6, 32, v6
	v_lshl_add_u32 v132, v9, 9, v1
	v_lshl_add_u32 v134, v3, 9, v1
	v_and_b32_e32 v1, 4, v10
	v_and_b32_e32 v3, 24, v11
	v_bfe_i32 v2, v2, 0, 16
	v_or3_b32 v1, v4, v1, v3
	v_add_lshl_u32 v2, v6, v2, 1
	v_lshl_add_u32 v136, v1, 9, v2
	v_lshl_add_u32 v138, v7, 9, v2
	v_mov_b32_e32 v137, v133
	v_mov_b32_e32 v135, v133
	v_mov_b32_e32 v139, v133
	s_mov_b32 s51, 0x10000
	s_waitcnt vmcnt(0)
	v_readfirstlane_b32 s6, v0
	s_lshl_b32 s6, s6, 20
	s_or_b32 s6, s6, s10
	s_add_u32 s38, s45, s6
	s_addc_u32 s39, s46, 0
	s_add_i32 s27, s47, 0
	s_add_i32 m0, s27, 0x10000
	v_lshl_add_u64 v[6:7], s[38:39], 0, v[132:133]
	global_load_lds_dwordx4 v132, s[38:39]
	s_add_i32 m0, s27, 0x12000
	s_add_u32 s30, s43, s7
	global_load_lds_dwordx4 v136, s[38:39]
	s_addc_u32 s31, s44, 0
	s_mov_b32 m0, s27
	s_add_i32 s48, s27, 0x2000
	global_load_lds_dwordx4 v134, s[30:31]
	s_mov_b32 m0, s48
	s_add_u32 s6, s38, 0x10000
	global_load_lds_dwordx4 v138, s[30:31]
	s_addc_u32 s7, s39, 0
	s_add_i32 m0, s27, 0x14000
	v_lshl_add_u64 v[4:5], s[38:39], 0, v[136:137]
	global_load_lds_dwordx4 v132, s[6:7]
	s_add_i32 m0, s27, 0x16000
	v_lshl_add_u64 v[2:3], s[30:31], 0, v[134:135]
	global_load_lds_dwordx4 v136, s[6:7]
	s_add_u32 s6, s30, 0x10000
	s_addc_u32 s7, s31, 0
	s_add_i32 s49, s27, 0x4000
	s_mov_b32 m0, s49
	s_add_i32 s50, s27, 0x6000
	global_load_lds_dwordx4 v134, s[6:7]
	s_mov_b32 m0, s50
	s_cmp_lg_u32 s4, 0
	global_load_lds_dwordx4 v138, s[6:7]
	v_lshl_add_u64 v[0:1], s[30:31], 0, v[138:139]
	s_cbranch_scc1 .LBB0_2620
	s_barrier
